# weight transpose-convert items: the 16 transposing LDS reads issued in two batches of 8 (was one lgkmcnt(0) per read) in all 60 inlined copies; plus GEMM2 epilogue, router, combine, diff-combine load
# speedup vs baseline: 1.0046x; 1.0046x over previous
; __device__ __forceinline__ unsigned pk2(float lo, float hi) { unsigned r; asm volatile("v_cvt_pk_bf16_f32 %0, %1, %2" : "=v"(r) : "v"(lo), "v"(hi)); return r; }
; __device__ __forceinline__ void transpose_item(const float* W, int K, int N, bf16_t* WT, int rstep, int roff, float* scr, int item, int lane) {
;   const int nblk = N / 32, kb = item / nblk, nb = item % nblk, k0 = 64 * kb, n0 = 32 * nb;
;   f32x4 v[8];
; #pragma unroll
;   for (int i = 0; i < 8; ++i) v[i] = __builtin_nontemporal_load((const f32x4*)(W + (size_t)(k0 + i * 8 + (lane >> 3)) * N + n0 + (lane & 7) * 4));
; #pragma unroll
;   for (int i = 0; i < 8; ++i) { float* d = scr + (i * 8 + (lane >> 3)) * 33 + (lane & 7) * 4; d[0] = v[i].x; d[1] = v[i].y; d[2] = v[i].z; d[3] = v[i].w; }
;   __builtin_amdgcn_wave_barrier(); asm volatile("s_waitcnt lgkmcnt(0)" ::: "memory");
;   const int c = lane & 7;
; #pragma unroll
;   for (int j = 0; j < 4; ++j) { const int nl = (lane >> 3) + 8 * j, n = n0 + nl; const float* s = scr + (8 * c) * 33 + nl;
;     u32x4 o; o.x = pk2(s[0 * 33], s[1 * 33]); o.y = pk2(s[2 * 33], s[3 * 33]); o.z = pk2(s[4 * 33], s[5 * 33]); o.w = pk2(s[6 * 33], s[7 * 33]);
;     const int row = n + (n >> 7) * rstep + roff;
;     __builtin_nontemporal_store(o, (u32x4*)(WT + (size_t)row * K + k0 + 8 * c)); }
;   __builtin_amdgcn_wave_barrier(); asm volatile("s_waitcnt lgkmcnt(0)" ::: "memory");
; }
; __device__ __forceinline__ void convert_item(const P& p, int it, float* scr, int lane) {
;   if (it < IT_DENSE) {
;     const int l = it / (IT_WIN + IT_WOUT), r = it % (IT_WIN + IT_WOUT);
;     if (r < IT_WIN) transpose_item(p.w_in + (size_t)l * DM * INW, DM, INW, WSP(bf16_t, WS_WIN) + (size_t)l * INW * DM, 0, 0, scr, r, lane);
;     else transpose_item(p.w_out + (size_t)l * DM * DM, DM, DM, WSP(bf16_t, WS_WOUT) + (size_t)l * DM * DM, 0, 0, scr, r - IT_WIN, lane);
.LBB0_121:
	s_lshl_b64 s[6:7], s[4:5], 24
	s_add_u32 s28, s10, s6
	s_addc_u32 s29, s11, s7
	s_lshl_b64 s[6:7], s[4:5], 23
	s_add_u32 s5, s12, s6
	s_addc_u32 s31, s13, s7
	s_add_i32 s6, s27, 0xe800
	s_and_b32 s34, s16, 0x7e0
	s_and_b32 s33, s6, 0xffc0
	s_lshl_b32 s6, s34, 2
	v_add_u32_e32 v24, s33, v4
	s_add_u32 s6, s28, s6
	s_addc_u32 s7, s29, 0
	v_ashrrev_i32_e32 v25, 31, v24
	v_lshl_add_u64 v[26:27], s[6:7], 0, v[0:1]
	v_lshlrev_b64 v[24:25], 13, v[24:25]
	v_lshl_add_u64 v[52:53], v[26:27], 0, v[24:25]
	v_add_co_u32_e32 v32, vcc, s18, v52
	s_lshl_b32 s6, s33, 1
	s_nop 0
	v_addc_co_u32_e32 v33, vcc, 0, v53, vcc
	global_load_dwordx4 v[24:27], v[52:53], off nt
	global_load_dwordx4 v[28:31], v[32:33], off nt
	v_add_co_u32_e32 v32, vcc, s19, v52
	s_add_u32 s6, s5, s6
	s_nop 0
	v_addc_co_u32_e32 v33, vcc, 0, v53, vcc
	v_add_co_u32_e32 v36, vcc, s20, v52
	v_mov_b32_e32 v3, v1
	s_nop 0
	v_addc_co_u32_e32 v37, vcc, 0, v53, vcc
	v_add_co_u32_e32 v40, vcc, s21, v52
	global_load_dwordx4 v[32:35], v[32:33], off nt
	s_nop 0
	global_load_dwordx4 v[36:39], v[36:37], off nt
	v_addc_co_u32_e32 v41, vcc, 0, v53, vcc
	v_add_co_u32_e32 v44, vcc, s22, v52
	s_addc_u32 s7, s31, 0
	s_nop 0
	v_addc_co_u32_e32 v45, vcc, 0, v53, vcc
	global_load_dwordx4 v[40:43], v[40:41], off nt
	s_nop 0
	global_load_dwordx4 v[44:47], v[44:45], off nt
	v_add_co_u32_e32 v48, vcc, s23, v52
	s_nop 1
	v_addc_co_u32_e32 v49, vcc, 0, v53, vcc
	global_load_dwordx4 v[48:51], v[48:49], off nt
	v_add_co_u32_e32 v52, vcc, s24, v52
	s_nop 1
	v_addc_co_u32_e32 v53, vcc, 0, v53, vcc
	global_load_dwordx4 v[52:55], v[52:53], off nt
	s_waitcnt vmcnt(7)
	ds_write2_b32 v9, v24, v25 offset1:1
	ds_write2_b32 v9, v26, v27 offset0:2 offset1:3
	s_waitcnt vmcnt(6)
	ds_write2_b32 v10, v28, v29 offset1:1
	ds_write2_b32 v11, v30, v31 offset1:1
	s_waitcnt vmcnt(5)
	ds_write2_b32 v12, v32, v33 offset1:1
	ds_write2_b32 v13, v34, v35 offset1:1
	s_waitcnt vmcnt(4)
	ds_write2_b32 v14, v36, v37 offset1:1
	ds_write2_b32 v15, v38, v39 offset1:1
	s_waitcnt vmcnt(3)
	ds_write2_b32 v16, v40, v41 offset1:1
	ds_write2_b32 v17, v42, v43 offset1:1
	s_waitcnt vmcnt(2)
	ds_write2_b32 v18, v44, v45 offset1:1
	ds_write2_b32 v19, v46, v47 offset1:1
	s_waitcnt vmcnt(1)
	ds_write2_b32 v20, v48, v49 offset1:1
	ds_write2_b32 v21, v50, v51 offset1:1
	s_waitcnt vmcnt(0)
	ds_write2_b32 v22, v52, v53 offset1:1
	ds_write2_b32 v23, v54, v55 offset1:1
	s_waitcnt lgkmcnt(0)
	ds_read2_b32 v[220:221], v8 offset1:33
	ds_read2_b32 v[222:223], v8 offset0:66 offset1:99
	ds_read2_b32 v[224:225], v8 offset0:132 offset1:165
	ds_read2_b32 v[226:227], v8 offset0:198 offset1:231
	ds_read2_b32 v[228:229], v8 offset0:8 offset1:41
	ds_read2_b32 v[230:231], v8 offset0:74 offset1:107
	ds_read2_b32 v[232:233], v8 offset0:140 offset1:173
	ds_read2_b32 v[234:235], v8 offset0:206 offset1:239
	s_waitcnt lgkmcnt(0)
	ds_read2_b32 v[236:237], v8 offset0:16 offset1:49
	ds_read2_b32 v[238:239], v8 offset0:82 offset1:115
	ds_read2_b32 v[240:241], v8 offset0:148 offset1:181
	ds_read2_b32 v[242:243], v8 offset0:214 offset1:247
	ds_read2_b32 v[244:245], v8 offset0:24 offset1:57
	ds_read2_b32 v[246:247], v8 offset0:90 offset1:123
	ds_read2_b32 v[248:249], v8 offset0:156 offset1:189
	ds_read2_b32 v[250:251], v8 offset0:222 offset1:255
	v_cvt_pk_bf16_f32 v24, v220, v221
	v_add_u32_e32 v28, s34, v4
	v_cvt_pk_bf16_f32 v25, v222, v223
	v_ashrrev_i32_e32 v29, 31, v28
	v_cvt_pk_bf16_f32 v26, v224, v225
	v_lshlrev_b64 v[28:29], 12, v[28:29]
	v_lshl_add_u64 v[32:33], s[6:7], 0, v[2:3]
	v_cvt_pk_bf16_f32 v27, v226, v227
	v_lshl_add_u64 v[28:29], v[32:33], 0, v[28:29]
	global_store_dwordx4 v[28:29], v[24:27], off nt
	s_nop 1
	s_nop 0
	v_cvt_pk_bf16_f32 v24, v228, v229
	v_add_u32_e32 v30, s34, v5
	v_ashrrev_i32_e32 v31, 31, v30
	v_lshlrev_b64 v[30:31], 12, v[30:31]
	v_cvt_pk_bf16_f32 v25, v230, v231
	v_lshl_add_u64 v[30:31], v[32:33], 0, v[30:31]
	v_cvt_pk_bf16_f32 v26, v232, v233
	v_cvt_pk_bf16_f32 v27, v234, v235
	global_store_dwordx4 v[30:31], v[24:27], off nt
	s_nop 1
	v_add_u32_e32 v30, s34, v6
	v_ashrrev_i32_e32 v31, 31, v30
	s_waitcnt lgkmcnt(0)
	v_cvt_pk_bf16_f32 v24, v236, v237
	v_lshlrev_b64 v[30:31], 12, v[30:31]
	v_cvt_pk_bf16_f32 v25, v238, v239
	v_lshl_add_u64 v[30:31], v[32:33], 0, v[30:31]
	v_cvt_pk_bf16_f32 v26, v240, v241
	v_cvt_pk_bf16_f32 v27, v242, v243
	global_store_dwordx4 v[30:31], v[24:27], off nt
	s_nop 1
	v_add_u32_e32 v30, s34, v7
	v_ashrrev_i32_e32 v31, 31, v30
	v_cvt_pk_bf16_f32 v24, v244, v245
	v_lshlrev_b64 v[30:31], 12, v[30:31]
	v_cvt_pk_bf16_f32 v25, v246, v247
	v_lshl_add_u64 v[30:31], v[32:33], 0, v[30:31]
	v_cvt_pk_bf16_f32 v26, v248, v249
	v_cvt_pk_bf16_f32 v27, v250, v251
	global_store_dwordx4 v[30:31], v[24:27], off nt
	s_nop 1
	s_waitcnt lgkmcnt(0)
	s_cbranch_execnz .LBB0_118
; __device__ __forceinline__ unsigned pk2(float lo, float hi) { unsigned r; asm volatile("v_cvt_pk_bf16_f32 %0, %1, %2" : "=v"(r) : "v"(lo), "v"(hi)); return r; }
; __device__ __forceinline__ void transpose_item(const float* W, int K, int N, bf16_t* WT, int rstep, int roff, float* scr, int item, int lane) {
;   const int nblk = N / 32, kb = item / nblk, nb = item % nblk, k0 = 64 * kb, n0 = 32 * nb;
;   f32x4 v[8];
; #pragma unroll
;   for (int i = 0; i < 8; ++i) v[i] = __builtin_nontemporal_load((const f32x4*)(W + (size_t)(k0 + i * 8 + (lane >> 3)) * N + n0 + (lane & 7) * 4));
; #pragma unroll
;   for (int i = 0; i < 8; ++i) { float* d = scr + (i * 8 + (lane >> 3)) * 33 + (lane & 7) * 4; d[0] = v[i].x; d[1] = v[i].y; d[2] = v[i].z; d[3] = v[i].w; }
;   __builtin_amdgcn_wave_barrier(); asm volatile("s_waitcnt lgkmcnt(0)" ::: "memory");
;   const int c = lane & 7;
; #pragma unroll
;   for (int j = 0; j < 4; ++j) { const int nl = (lane >> 3) + 8 * j, n = n0 + nl; const float* s = scr + (8 * c) * 33 + nl;
;     u32x4 o; o.x = pk2(s[0 * 33], s[1 * 33]); o.y = pk2(s[2 * 33], s[3 * 33]); o.z = pk2(s[4 * 33], s[5 * 33]); o.w = pk2(s[6 * 33], s[7 * 33]);
;     const int row = n + (n >> 7) * rstep + roff;
;     __builtin_nontemporal_store(o, (u32x4*)(WT + (size_t)row * K + k0 + 8 * c)); }
;   __builtin_amdgcn_wave_barrier(); asm volatile("s_waitcnt lgkmcnt(0)" ::: "memory");
; }
; __device__ __forceinline__ void convert_item(const P& p, int it, float* scr, int lane) {
;   if (it < IT_DENSE) {
;     const int l = it / (IT_WIN + IT_WOUT), r = it % (IT_WIN + IT_WOUT);
;     if (r < IT_WIN) transpose_item(p.w_in + (size_t)l * DM * INW, DM, INW, WSP(bf16_t, WS_WIN) + (size_t)l * INW * DM, 0, 0, scr, r, lane);
.LBB0_122:
	s_mul_i32 s6, s4, 0x3000000
	s_mul_hi_i32 s5, s4, 0x3000000
	s_add_u32 s7, s8, s6
	s_addc_u32 s31, s9, s5
	s_mul_hi_i32 s5, s4, 0x1800000
	s_mul_i32 s4, s4, 0x1800000
	s_add_u32 s33, s14, s4
	s_mul_i32 s4, s27, 0x2aab
	s_addc_u32 s34, s15, s5
	s_lshr_b32 s5, s4, 31
	s_ashr_i32 s4, s4, 21
	s_add_i32 s4, s4, s5
	s_sext_i32_i16 s5, s4
	s_mulk_i32 s4, 0xc0
	s_sub_i32 s4, s27, s4
	s_sext_i32_i16 s4, s4
	s_lshl_b32 s4, s4, 5
	s_lshl_b32 s6, s5, 6
	s_ashr_i32 s5, s4, 31
	s_lshl_b64 s[28:29], s[4:5], 2
	s_add_u32 s28, s7, s28
	s_addc_u32 s29, s31, s29
	v_add_u32_e32 v3, s6, v4
	v_lshl_add_u64 v[52:53], s[28:29], 0, v[0:1]
	v_mad_i64_i32 v[32:33], s[28:29], v3, s25, v[52:53]
	v_add_u32_e32 v24, 8, v3
	v_mad_i64_i32 v[34:35], s[28:29], v24, s25, v[52:53]
	global_load_dwordx4 v[24:27], v[32:33], off nt
	global_load_dwordx4 v[28:31], v[34:35], off nt
	v_add_u32_e32 v32, 16, v3
	v_mad_i64_i32 v[40:41], s[28:29], v32, s25, v[52:53]
	v_add_u32_e32 v32, 24, v3
	v_mad_i64_i32 v[42:43], s[28:29], v32, s25, v[52:53]
	global_load_dwordx4 v[32:35], v[40:41], off nt
	global_load_dwordx4 v[36:39], v[42:43], off nt
	v_add_u32_e32 v40, 32, v3
	v_mad_i64_i32 v[48:49], s[28:29], v40, s25, v[52:53]
	v_add_u32_e32 v40, 40, v3
	v_mad_i64_i32 v[50:51], s[28:29], v40, s25, v[52:53]
	global_load_dwordx4 v[40:43], v[48:49], off nt
	global_load_dwordx4 v[44:47], v[50:51], off nt
	v_add_u32_e32 v48, 48, v3
	v_mad_i64_i32 v[48:49], s[28:29], v48, s25, v[52:53]
	global_load_dwordx4 v[48:51], v[48:49], off nt
	v_add_u32_e32 v3, 56, v3
	v_mad_i64_i32 v[52:53], s[28:29], v3, s25, v[52:53]
	global_load_dwordx4 v[52:55], v[52:53], off nt
	s_ashr_i32 s7, s6, 31
	s_lshl_b64 s[6:7], s[6:7], 1
	s_add_u32 s6, s33, s6
	v_mov_b32_e32 v3, v1
	s_addc_u32 s7, s34, s7
	s_waitcnt vmcnt(7)
	ds_write2_b32 v9, v24, v25 offset1:1
	ds_write2_b32 v9, v26, v27 offset0:2 offset1:3
	s_waitcnt vmcnt(6)
	ds_write2_b32 v10, v28, v29 offset1:1
	ds_write2_b32 v11, v30, v31 offset1:1
	s_waitcnt vmcnt(5)
	ds_write2_b32 v12, v32, v33 offset1:1
	ds_write2_b32 v13, v34, v35 offset1:1
	s_waitcnt vmcnt(4)
	ds_write2_b32 v14, v36, v37 offset1:1
	ds_write2_b32 v15, v38, v39 offset1:1
	s_waitcnt vmcnt(3)
	ds_write2_b32 v16, v40, v41 offset1:1
	ds_write2_b32 v17, v42, v43 offset1:1
	s_waitcnt vmcnt(2)
	ds_write2_b32 v18, v44, v45 offset1:1
	ds_write2_b32 v19, v46, v47 offset1:1
	s_waitcnt vmcnt(1)
	ds_write2_b32 v20, v48, v49 offset1:1
	ds_write2_b32 v21, v50, v51 offset1:1
	s_waitcnt vmcnt(0)
	ds_write2_b32 v22, v52, v53 offset1:1
	ds_write2_b32 v23, v54, v55 offset1:1
	s_waitcnt lgkmcnt(0)
	ds_read2_b32 v[220:221], v8 offset1:33
	ds_read2_b32 v[222:223], v8 offset0:66 offset1:99
	ds_read2_b32 v[224:225], v8 offset0:132 offset1:165
	ds_read2_b32 v[226:227], v8 offset0:198 offset1:231
	ds_read2_b32 v[228:229], v8 offset0:8 offset1:41
	ds_read2_b32 v[230:231], v8 offset0:74 offset1:107
	ds_read2_b32 v[232:233], v8 offset0:140 offset1:173
	ds_read2_b32 v[234:235], v8 offset0:206 offset1:239
	s_waitcnt lgkmcnt(0)
	ds_read2_b32 v[236:237], v8 offset0:16 offset1:49
	ds_read2_b32 v[238:239], v8 offset0:82 offset1:115
	ds_read2_b32 v[240:241], v8 offset0:148 offset1:181
	ds_read2_b32 v[242:243], v8 offset0:214 offset1:247
	ds_read2_b32 v[244:245], v8 offset0:24 offset1:57
	ds_read2_b32 v[246:247], v8 offset0:90 offset1:123
	ds_read2_b32 v[248:249], v8 offset0:156 offset1:189
	ds_read2_b32 v[250:251], v8 offset0:222 offset1:255
	v_cvt_pk_bf16_f32 v24, v220, v221
	v_add_u32_e32 v28, s4, v4
	v_cvt_pk_bf16_f32 v25, v222, v223
	v_ashrrev_i32_e32 v29, 31, v28
	v_cvt_pk_bf16_f32 v26, v224, v225
	v_lshlrev_b64 v[28:29], 12, v[28:29]
	v_lshl_add_u64 v[32:33], s[6:7], 0, v[2:3]
	v_cvt_pk_bf16_f32 v27, v226, v227
	v_lshl_add_u64 v[28:29], v[32:33], 0, v[28:29]
	global_store_dwordx4 v[28:29], v[24:27], off nt
	s_nop 1
	s_nop 0
	v_cvt_pk_bf16_f32 v24, v228, v229
	v_add_u32_e32 v30, s4, v5
	v_ashrrev_i32_e32 v31, 31, v30
	v_lshlrev_b64 v[30:31], 12, v[30:31]
	v_cvt_pk_bf16_f32 v25, v230, v231
	v_lshl_add_u64 v[30:31], v[32:33], 0, v[30:31]
	v_cvt_pk_bf16_f32 v26, v232, v233
	v_cvt_pk_bf16_f32 v27, v234, v235
	global_store_dwordx4 v[30:31], v[24:27], off nt
	s_nop 1
	v_add_u32_e32 v30, s4, v6
	v_ashrrev_i32_e32 v31, 31, v30
	s_waitcnt lgkmcnt(0)
	v_cvt_pk_bf16_f32 v24, v236, v237
	v_lshlrev_b64 v[30:31], 12, v[30:31]
	v_cvt_pk_bf16_f32 v25, v238, v239
	v_lshl_add_u64 v[30:31], v[32:33], 0, v[30:31]
	v_cvt_pk_bf16_f32 v26, v240, v241
	v_cvt_pk_bf16_f32 v27, v242, v243
	global_store_dwordx4 v[30:31], v[24:27], off nt
	s_nop 1
	v_add_u32_e32 v30, s4, v7
	v_ashrrev_i32_e32 v31, 31, v30
	v_cvt_pk_bf16_f32 v24, v244, v245
	v_lshlrev_b64 v[30:31], 12, v[30:31]
	v_cvt_pk_bf16_f32 v25, v246, v247
	v_lshl_add_u64 v[30:31], v[32:33], 0, v[30:31]
	v_cvt_pk_bf16_f32 v26, v248, v249
	v_cvt_pk_bf16_f32 v27, v250, v251
	global_store_dwordx4 v[30:31], v[24:27], off nt
	s_nop 1
	s_waitcnt lgkmcnt(0)
	s_branch .LBB0_118

; __device__ __forceinline__ unsigned pk2(float lo, float hi) { unsigned r; asm volatile("v_cvt_pk_bf16_f32 %0, %1, %2" : "=v"(r) : "v"(lo), "v"(hi)); return r; }
; __device__ __forceinline__ void transpose_item(const float* W, int K, int N, bf16_t* WT, int rstep, int roff, float* scr, int item, int lane) {
;   const int nblk = N / 32, kb = item / nblk, nb = item % nblk, k0 = 64 * kb, n0 = 32 * nb;
;   f32x4 v[8];
; #pragma unroll
;   for (int i = 0; i < 8; ++i) v[i] = __builtin_nontemporal_load((const f32x4*)(W + (size_t)(k0 + i * 8 + (lane >> 3)) * N + n0 + (lane & 7) * 4));
; #pragma unroll
;   for (int i = 0; i < 8; ++i) { float* d = scr + (i * 8 + (lane >> 3)) * 33 + (lane & 7) * 4; d[0] = v[i].x; d[1] = v[i].y; d[2] = v[i].z; d[3] = v[i].w; }
;   __builtin_amdgcn_wave_barrier(); asm volatile("s_waitcnt lgkmcnt(0)" ::: "memory");
;   const int c = lane & 7;
; #pragma unroll
;   for (int j = 0; j < 4; ++j) { const int nl = (lane >> 3) + 8 * j, n = n0 + nl; const float* s = scr + (8 * c) * 33 + nl;
;     u32x4 o; o.x = pk2(s[0 * 33], s[1 * 33]); o.y = pk2(s[2 * 33], s[3 * 33]); o.z = pk2(s[4 * 33], s[5 * 33]); o.w = pk2(s[6 * 33], s[7 * 33]);
;     const int row = n + (n >> 7) * rstep + roff;
;     __builtin_nontemporal_store(o, (u32x4*)(WT + (size_t)row * K + k0 + 8 * c)); }
;   __builtin_amdgcn_wave_barrier(); asm volatile("s_waitcnt lgkmcnt(0)" ::: "memory");
; }
; __device__ __forceinline__ void convert_item(const P& p, int it, float* scr, int lane) {
;     ...
;     const int idx = it - IT_DENSE, m = idx / IT_EXP, sub = idx % IT_EXP, le = m / 3, which = m % 3;
;     if (which == 0) transpose_item(p.wg + (size_t)le * DM * EFF, DM, EFF, WSP(bf16_t, WS_WGU) + (size_t)le * 1024 * DM, 128, 0, scr, sub, lane);
;     else if (which == 1) transpose_item(p.wu + (size_t)le * DM * EFF, DM, EFF, WSP(bf16_t, WS_WGU) + (size_t)le * 1024 * DM, 128, 128, scr, sub, lane);
;     else transpose_item(p.wd + (size_t)le * EFF * DM, EFF, DM, WSP(bf16_t, WS_WD) + (size_t)le * DM * EFF, 0, 0, scr, sub, lane);
.LBB0_220:
	s_cmpk_gt_i32 s16, 0x3fff
	s_mov_b64 s[0:1], -1
	s_cbranch_scc0 .LBB0_230
	s_add_i32 s0, s16, 0xffffc000
	s_lshr_b32 s1, s0, 9
	s_mul_hi_u32 s0, s0, 0xaaaaaaab
	s_lshr_b32 s64, s0, 10
	s_mul_hi_u32 s0, s1, 0x55555556
	s_mul_i32 s0, s0, 3
	s_and_b32 s17, s16, 0x1ff
	s_sub_i32 s19, s1, s0
	s_lshl_b64 s[0:1], s[64:65], 22
	s_lshl_b32 s18, s16, 5
	s_cmp_lt_i32 s19, 1
	s_mov_b64 s[6:7], -1
	s_cbranch_scc1 .LBB0_227
	s_cmp_lg_u32 s19, 1
	s_cbranch_scc0 .LBB0_224
	s_add_u32 s22, s74, s0
	s_addc_u32 s23, s75, s1
	s_lshl_b64 s[20:21], s[64:65], 21
	s_add_u32 s7, s9, s20
	s_addc_u32 s19, s12, s21
	s_and_b32 s6, s18, 0x7e0
	s_and_b32 s20, s16, 0x1c0
	s_lshl_b32 s21, s6, 2
	v_add_u32_e32 v4, s20, v1
	s_add_u32 s22, s22, s21
	s_addc_u32 s23, s23, 0
	v_lshlrev_b32_e32 v96, 2, v0
	v_ashrrev_i32_e32 v5, 31, v4
	v_lshl_add_u64 v[12:13], s[22:23], 0, v[96:97]
	v_lshlrev_b64 v[4:5], 13, v[4:5]
	v_lshl_add_u64 v[4:5], v[12:13], 0, v[4:5]
	s_mov_b32 s21, 0x10000
	v_add_co_u32_e32 v16, vcc, s21, v4
	s_mov_b32 s21, 0x20000
	s_nop 0
	v_addc_co_u32_e32 v17, vcc, 0, v5, vcc
	global_load_dwordx4 v[12:15], v[4:5], off nt
	v_add_co_u32_e32 v20, vcc, s21, v4
	global_load_dwordx4 v[16:19], v[16:17], off nt
	s_nop 0
	v_addc_co_u32_e32 v21, vcc, 0, v5, vcc
	s_mov_b32 s21, 0x30000
	global_load_dwordx4 v[20:23], v[20:21], off nt
	v_add_co_u32_e32 v24, vcc, s21, v4
	s_mov_b32 s21, 0x40000
	s_nop 0
	v_addc_co_u32_e32 v25, vcc, 0, v5, vcc
	global_load_dwordx4 v[24:27], v[24:25], off nt
	v_add_co_u32_e32 v28, vcc, s21, v4
	s_mov_b32 s21, 0x50000
	s_nop 0
	v_addc_co_u32_e32 v29, vcc, 0, v5, vcc
	global_load_dwordx4 v[28:31], v[28:29], off nt
	v_add_co_u32_e32 v32, vcc, s21, v4
	s_mov_b32 s21, 0x60000
	s_nop 0
	v_addc_co_u32_e32 v33, vcc, 0, v5, vcc
	global_load_dwordx4 v[32:35], v[32:33], off nt
	v_add_co_u32_e32 v36, vcc, s21, v4
	s_mov_b32 s21, 0x70000
	s_nop 0
	v_addc_co_u32_e32 v37, vcc, 0, v5, vcc
	global_load_dwordx4 v[36:39], v[36:37], off nt
	v_add_co_u32_e32 v4, vcc, s21, v4
	s_lshl_b32 s20, s20, 1
	s_nop 0
	v_addc_co_u32_e32 v5, vcc, 0, v5, vcc
	global_load_dwordx4 v[40:43], v[4:5], off nt
	v_add_u32_e32 v4, v3, v6
	v_add_u32_e32 v5, 0x420, v4
	s_add_u32 s20, s7, s20
	s_addc_u32 s21, s19, 0
	v_lshlrev_b32_e32 v96, 1, v2
	s_waitcnt vmcnt(7)
	ds_write2_b32 v4, v12, v13 offset1:1
	ds_write2_b32 v4, v14, v15 offset0:2 offset1:3
	s_waitcnt vmcnt(6)
	ds_write2_b32 v5, v16, v17 offset1:1
	v_add_u32_e32 v5, 0x428, v4
	ds_write2_b32 v5, v18, v19 offset1:1
	v_add_u32_e32 v5, 0x840, v4
	s_waitcnt vmcnt(5)
	ds_write2_b32 v5, v20, v21 offset1:1
	v_add_u32_e32 v5, 0x848, v4
	ds_write2_b32 v5, v22, v23 offset1:1
	v_add_u32_e32 v5, 0xc60, v4
	v_add_u32_e32 v16, s6, v1
	v_ashrrev_i32_e32 v17, 31, v16
	s_waitcnt vmcnt(4)
	ds_write2_b32 v5, v24, v25 offset1:1
	v_add_u32_e32 v5, 0xc68, v4
	ds_write2_b32 v5, v26, v27 offset1:1
	v_add_u32_e32 v5, 0x1080, v4
	v_lshlrev_b64 v[16:17], 10, v[16:17]
	s_waitcnt vmcnt(3)
	ds_write2_b32 v5, v28, v29 offset1:1
	v_add_u32_e32 v5, 0x1088, v4
	ds_write2_b32 v5, v30, v31 offset1:1
	v_add_u32_e32 v5, 0x14a0, v4
	s_waitcnt vmcnt(2)
	ds_write2_b32 v5, v32, v33 offset1:1
	v_add_u32_e32 v5, 0x14a8, v4
	ds_write2_b32 v5, v34, v35 offset1:1
	v_add_u32_e32 v5, 0x18c0, v4
	s_waitcnt vmcnt(1)
	ds_write2_b32 v5, v36, v37 offset1:1
	v_add_u32_e32 v5, 0x18c8, v4
	ds_write2_b32 v5, v38, v39 offset1:1
	v_add_u32_e32 v5, 0x1ce0, v4
	v_add_u32_e32 v4, 0x1ce8, v4
	s_waitcnt vmcnt(0)
	ds_write2_b32 v5, v40, v41 offset1:1
	ds_write2_b32 v4, v42, v43 offset1:1
	s_waitcnt lgkmcnt(0)
	ds_read2_b32 v[214:215], v10 offset1:33
	ds_read2_b32 v[222:223], v10 offset0:66 offset1:99
	ds_read2_b32 v[224:225], v10 offset0:132 offset1:165
	ds_read2_b32 v[226:227], v10 offset0:198 offset1:231
	ds_read2_b32 v[228:229], v10 offset0:8 offset1:41
	ds_read2_b32 v[230:231], v10 offset0:74 offset1:107
	ds_read2_b32 v[232:233], v10 offset0:140 offset1:173
	ds_read2_b32 v[234:235], v10 offset0:206 offset1:239
	s_waitcnt lgkmcnt(0)
	ds_read2_b32 v[236:237], v10 offset0:16 offset1:49
	ds_read2_b32 v[238:239], v10 offset0:82 offset1:115
	ds_read2_b32 v[240:241], v10 offset0:148 offset1:181
	ds_read2_b32 v[242:243], v10 offset0:214 offset1:247
	ds_read2_b32 v[244:245], v10 offset0:24 offset1:57
	ds_read2_b32 v[246:247], v10 offset0:90 offset1:123
	ds_read2_b32 v[248:249], v10 offset0:156 offset1:189
	ds_read2_b32 v[250:251], v10 offset0:222 offset1:255
	v_lshl_add_u64 v[4:5], s[20:21], 0, v[96:97]
	v_cvt_pk_bf16_f32 v12, v214, v215
	v_cvt_pk_bf16_f32 v13, v222, v223
	v_lshl_add_u64 v[16:17], v[4:5], 0, v[16:17]
	v_cvt_pk_bf16_f32 v14, v224, v225
	v_cvt_pk_bf16_f32 v15, v226, v227
	global_store_dwordx4 v[16:17], v[12:15], off nt
	s_nop 1
	v_add_u32_e32 v16, s6, v7
	v_ashrrev_i32_e32 v17, 31, v16
	v_cvt_pk_bf16_f32 v12, v228, v229
	v_lshlrev_b64 v[16:17], 10, v[16:17]
	v_cvt_pk_bf16_f32 v13, v230, v231
	v_lshl_add_u64 v[16:17], v[4:5], 0, v[16:17]
	v_cvt_pk_bf16_f32 v14, v232, v233
	v_cvt_pk_bf16_f32 v15, v234, v235
	global_store_dwordx4 v[16:17], v[12:15], off nt
	s_nop 1
	v_add_u32_e32 v16, s6, v8
	s_waitcnt lgkmcnt(0)
	v_ashrrev_i32_e32 v17, 31, v16
	v_cvt_pk_bf16_f32 v12, v236, v237
	v_lshlrev_b64 v[16:17], 10, v[16:17]
	v_cvt_pk_bf16_f32 v13, v238, v239
	v_lshl_add_u64 v[16:17], v[4:5], 0, v[16:17]
	v_cvt_pk_bf16_f32 v14, v240, v241
	v_cvt_pk_bf16_f32 v15, v242, v243
	global_store_dwordx4 v[16:17], v[12:15], off nt
	s_nop 1
	v_add_u32_e32 v16, s6, v9
	v_ashrrev_i32_e32 v17, 31, v16
	v_cvt_pk_bf16_f32 v12, v244, v245
	v_lshlrev_b64 v[16:17], 10, v[16:17]
	v_cvt_pk_bf16_f32 v13, v246, v247
	v_lshl_add_u64 v[4:5], v[4:5], 0, v[16:17]
	v_cvt_pk_bf16_f32 v14, v248, v249
	v_cvt_pk_bf16_f32 v15, v250, v251
	global_store_dwordx4 v[4:5], v[12:15], off nt
	s_nop 1
	s_waitcnt lgkmcnt(0)
	s_mov_b64 s[6:7], 0
; __device__ __forceinline__ unsigned pk2(float lo, float hi) { unsigned r; asm volatile("v_cvt_pk_bf16_f32 %0, %1, %2" : "=v"(r) : "v"(lo), "v"(hi)); return r; }
; __device__ __forceinline__ void transpose_item(const float* W, int K, int N, bf16_t* WT, int rstep, int roff, float* scr, int item, int lane) {
;   const int nblk = N / 32, kb = item / nblk, nb = item % nblk, k0 = 64 * kb, n0 = 32 * nb;
;   f32x4 v[8];
; #pragma unroll
;   for (int i = 0; i < 8; ++i) v[i] = __builtin_nontemporal_load((const f32x4*)(W + (size_t)(k0 + i * 8 + (lane >> 3)) * N + n0 + (lane & 7) * 4));
; #pragma unroll
;   for (int i = 0; i < 8; ++i) { float* d = scr + (i * 8 + (lane >> 3)) * 33 + (lane & 7) * 4; d[0] = v[i].x; d[1] = v[i].y; d[2] = v[i].z; d[3] = v[i].w; }
;   __builtin_amdgcn_wave_barrier(); asm volatile("s_waitcnt lgkmcnt(0)" ::: "memory");
;   const int c = lane & 7;
; #pragma unroll
;   for (int j = 0; j < 4; ++j) { const int nl = (lane >> 3) + 8 * j, n = n0 + nl; const float* s = scr + (8 * c) * 33 + nl;
;     u32x4 o; o.x = pk2(s[0 * 33], s[1 * 33]); o.y = pk2(s[2 * 33], s[3 * 33]); o.z = pk2(s[4 * 33], s[5 * 33]); o.w = pk2(s[6 * 33], s[7 * 33]);
;     const int row = n + (n >> 7) * rstep + roff;
;     __builtin_nontemporal_store(o, (u32x4*)(WT + (size_t)row * K + k0 + 8 * c)); }
;   __builtin_amdgcn_wave_barrier(); asm volatile("s_waitcnt lgkmcnt(0)" ::: "memory");
; }
; __device__ __forceinline__ void convert_item(const P& p, int it, float* scr, int lane) {
;     ...
;     else if (which == 1) transpose_item(p.wu + (size_t)le * DM * EFF, DM, EFF, WSP(bf16_t, WS_WGU) + (size_t)le * 1024 * DM, 128, 128, scr, sub, lane);
.LBB0_224:
	s_andn2_b64 vcc, exec, s[6:7]
	s_cbranch_vccnz .LBB0_226
	s_add_u32 s21, s42, s0
	s_addc_u32 s23, s43, s1
	s_add_u32 s7, s4, s0
	s_addc_u32 s19, s5, s1
	s_lshl_b32 s6, s17, 2
	s_and_b32 s20, s6, 0x7c0
	s_and_b32 s6, s18, 0x1e0
	s_lshl_b32 s22, s6, 2
	v_add_u32_e32 v4, s20, v1
	s_add_u32 s22, s21, s22
	s_addc_u32 s23, s23, 0
	v_lshlrev_b32_e32 v96, 2, v0
	v_ashrrev_i32_e32 v5, 31, v4
	v_lshl_add_u64 v[12:13], s[22:23], 0, v[96:97]
	v_lshlrev_b64 v[4:5], 11, v[4:5]
	v_lshl_add_u64 v[4:5], v[12:13], 0, v[4:5]
	s_movk_i32 s21, 0x4000
	v_add_co_u32_e32 v16, vcc, s21, v4
	s_mov_b32 s21, 0x8000
	s_nop 0
	v_addc_co_u32_e32 v17, vcc, 0, v5, vcc
	global_load_dwordx4 v[12:15], v[4:5], off nt
	v_add_co_u32_e32 v20, vcc, s21, v4
	global_load_dwordx4 v[16:19], v[16:17], off nt
	s_nop 0
	v_addc_co_u32_e32 v21, vcc, 0, v5, vcc
	s_mov_b32 s21, 0xc000
	global_load_dwordx4 v[20:23], v[20:21], off nt
	v_add_co_u32_e32 v24, vcc, s21, v4
	s_mov_b32 s21, 0x10000
	s_nop 0
	v_addc_co_u32_e32 v25, vcc, 0, v5, vcc
	global_load_dwordx4 v[24:27], v[24:25], off nt
	v_add_co_u32_e32 v28, vcc, s21, v4
	s_mov_b32 s21, 0x14000
	s_nop 0
	v_addc_co_u32_e32 v29, vcc, 0, v5, vcc
	global_load_dwordx4 v[28:31], v[28:29], off nt
	v_add_co_u32_e32 v32, vcc, s21, v4
	s_lshl_b32 s20, s20, 1
	s_nop 0
	v_addc_co_u32_e32 v33, vcc, 0, v5, vcc
	global_load_dwordx4 v[32:35], v[32:33], off nt
	v_add_co_u32_e32 v36, vcc, s93, v4
	v_add_u32_e32 v11, s6, v1
	s_nop 0
	v_addc_co_u32_e32 v37, vcc, 0, v5, vcc
	global_load_dwordx4 v[36:39], v[36:37], off nt
	v_add_co_u32_e32 v4, vcc, s96, v4
	s_add_u32 s20, s7, s20
	s_nop 0
	v_addc_co_u32_e32 v5, vcc, 0, v5, vcc
	global_load_dwordx4 v[40:43], v[4:5], off nt
	v_add_u32_e32 v4, v3, v6
	v_add_u32_e32 v5, 0x420, v4
	s_movk_i32 s7, 0x80
	s_addc_u32 s21, s19, 0
	v_lshlrev_b32_e32 v96, 1, v2
	s_waitcnt vmcnt(7)
	ds_write2_b32 v4, v12, v13 offset1:1
	ds_write2_b32 v4, v14, v15 offset0:2 offset1:3
	s_waitcnt vmcnt(6)
	ds_write2_b32 v5, v16, v17 offset1:1
	v_add_u32_e32 v5, 0x428, v4
	ds_write2_b32 v5, v18, v19 offset1:1
	v_add_u32_e32 v5, 0x840, v4
	s_waitcnt vmcnt(5)
	ds_write2_b32 v5, v20, v21 offset1:1
	v_add_u32_e32 v5, 0x848, v4
	ds_write2_b32 v5, v22, v23 offset1:1
	v_add_u32_e32 v5, 0xc60, v4
	s_waitcnt vmcnt(4)
	ds_write2_b32 v5, v24, v25 offset1:1
	v_add_u32_e32 v5, 0xc68, v4
	ds_write2_b32 v5, v26, v27 offset1:1
	v_add_u32_e32 v5, 0x1080, v4
	s_waitcnt vmcnt(3)
	ds_write2_b32 v5, v28, v29 offset1:1
	v_add_u32_e32 v5, 0x1088, v4
	ds_write2_b32 v5, v30, v31 offset1:1
	v_add_u32_e32 v5, 0x14a0, v4
	s_waitcnt vmcnt(2)
	ds_write2_b32 v5, v32, v33 offset1:1
	v_add_u32_e32 v5, 0x14a8, v4
	ds_write2_b32 v5, v34, v35 offset1:1
	v_add_u32_e32 v5, 0x18c0, v4
	s_waitcnt vmcnt(1)
	ds_write2_b32 v5, v36, v37 offset1:1
	v_add_u32_e32 v5, 0x18c8, v4
	ds_write2_b32 v5, v38, v39 offset1:1
	v_add_u32_e32 v5, 0x1ce0, v4
	v_add_u32_e32 v4, 0x1ce8, v4
	s_waitcnt vmcnt(0)
	ds_write2_b32 v5, v40, v41 offset1:1
	ds_write2_b32 v4, v42, v43 offset1:1
	s_waitcnt lgkmcnt(0)
	ds_read2_b32 v[214:215], v10 offset1:33
	ds_read2_b32 v[222:223], v10 offset0:66 offset1:99
	ds_read2_b32 v[224:225], v10 offset0:132 offset1:165
	ds_read2_b32 v[226:227], v10 offset0:198 offset1:231
	ds_read2_b32 v[228:229], v10 offset0:8 offset1:41
	ds_read2_b32 v[230:231], v10 offset0:74 offset1:107
	ds_read2_b32 v[232:233], v10 offset0:140 offset1:173
	ds_read2_b32 v[234:235], v10 offset0:206 offset1:239
	s_waitcnt lgkmcnt(0)
	ds_read2_b32 v[236:237], v10 offset0:16 offset1:49
	ds_read2_b32 v[238:239], v10 offset0:82 offset1:115
	ds_read2_b32 v[240:241], v10 offset0:148 offset1:181
	ds_read2_b32 v[242:243], v10 offset0:214 offset1:247
	ds_read2_b32 v[244:245], v10 offset0:24 offset1:57
	ds_read2_b32 v[246:247], v10 offset0:90 offset1:123
	ds_read2_b32 v[248:249], v10 offset0:156 offset1:189
	ds_read2_b32 v[250:251], v10 offset0:222 offset1:255
	v_cvt_pk_bf16_f32 v12, v214, v215
	v_cvt_pk_bf16_f32 v13, v222, v223
	v_cvt_pk_bf16_f32 v14, v224, v225
	v_cvt_pk_bf16_f32 v15, v226, v227
	v_and_b32_e32 v16, 0xffffff80, v11
	v_add3_u32 v16, v11, v16, s7
	v_ashrrev_i32_e32 v17, 31, v16
	v_lshl_add_u64 v[4:5], s[20:21], 0, v[96:97]
	v_lshlrev_b64 v[16:17], 12, v[16:17]
	v_lshl_add_u64 v[16:17], v[4:5], 0, v[16:17]
	global_store_dwordx4 v[16:17], v[12:15], off nt
	s_nop 1
	v_add_u32_e32 v11, s6, v7
	v_cvt_pk_bf16_f32 v12, v228, v229
	v_cvt_pk_bf16_f32 v13, v230, v231
	v_cvt_pk_bf16_f32 v14, v232, v233
	v_cvt_pk_bf16_f32 v15, v234, v235
	v_and_b32_e32 v16, 0xffffff80, v11
	v_add3_u32 v16, v11, v16, s7
	v_ashrrev_i32_e32 v17, 31, v16
	v_lshlrev_b64 v[16:17], 12, v[16:17]
	v_lshl_add_u64 v[16:17], v[4:5], 0, v[16:17]
	global_store_dwordx4 v[16:17], v[12:15], off nt
	s_nop 1
	s_waitcnt lgkmcnt(0)
	v_add_u32_e32 v11, s6, v8
	v_cvt_pk_bf16_f32 v12, v236, v237
	v_cvt_pk_bf16_f32 v13, v238, v239
	v_cvt_pk_bf16_f32 v14, v240, v241
	v_cvt_pk_bf16_f32 v15, v242, v243
	v_and_b32_e32 v16, 0xffffff80, v11
	v_add3_u32 v16, v11, v16, s7
	v_ashrrev_i32_e32 v17, 31, v16
	v_lshlrev_b64 v[16:17], 12, v[16:17]
	v_lshl_add_u64 v[16:17], v[4:5], 0, v[16:17]
	global_store_dwordx4 v[16:17], v[12:15], off nt
	s_nop 1
	v_add_u32_e32 v11, s6, v9
	v_cvt_pk_bf16_f32 v12, v244, v245
	v_cvt_pk_bf16_f32 v13, v246, v247
	v_cvt_pk_bf16_f32 v14, v248, v249
	v_cvt_pk_bf16_f32 v15, v250, v251
	v_and_b32_e32 v16, 0xffffff80, v11
	v_add3_u32 v16, v11, v16, s7
	v_ashrrev_i32_e32 v17, 31, v16
	v_lshlrev_b64 v[16:17], 12, v[16:17]
	v_lshl_add_u64 v[4:5], v[4:5], 0, v[16:17]
	global_store_dwordx4 v[4:5], v[12:15], off nt
	s_nop 1
	s_waitcnt lgkmcnt(0)

; __device__ __forceinline__ unsigned pk2(float lo, float hi) { unsigned r; asm volatile("v_cvt_pk_bf16_f32 %0, %1, %2" : "=v"(r) : "v"(lo), "v"(hi)); return r; }
; __device__ __forceinline__ void transpose_item(const float* W, int K, int N, bf16_t* WT, int rstep, int roff, float* scr, int item, int lane) {
;   const int nblk = N / 32, kb = item / nblk, nb = item % nblk, k0 = 64 * kb, n0 = 32 * nb;
;   f32x4 v[8];
; #pragma unroll
;   for (int i = 0; i < 8; ++i) v[i] = __builtin_nontemporal_load((const f32x4*)(W + (size_t)(k0 + i * 8 + (lane >> 3)) * N + n0 + (lane & 7) * 4));
; #pragma unroll
;   for (int i = 0; i < 8; ++i) { float* d = scr + (i * 8 + (lane >> 3)) * 33 + (lane & 7) * 4; d[0] = v[i].x; d[1] = v[i].y; d[2] = v[i].z; d[3] = v[i].w; }
;   __builtin_amdgcn_wave_barrier(); asm volatile("s_waitcnt lgkmcnt(0)" ::: "memory");
;   const int c = lane & 7;
; #pragma unroll
;   for (int j = 0; j < 4; ++j) { const int nl = (lane >> 3) + 8 * j, n = n0 + nl; const float* s = scr + (8 * c) * 33 + nl;
;     u32x4 o; o.x = pk2(s[0 * 33], s[1 * 33]); o.y = pk2(s[2 * 33], s[3 * 33]); o.z = pk2(s[4 * 33], s[5 * 33]); o.w = pk2(s[6 * 33], s[7 * 33]);
;     const int row = n + (n >> 7) * rstep + roff;
;     __builtin_nontemporal_store(o, (u32x4*)(WT + (size_t)row * K + k0 + 8 * c)); }
;   __builtin_amdgcn_wave_barrier(); asm volatile("s_waitcnt lgkmcnt(0)" ::: "memory");
; }
; __device__ __forceinline__ void convert_item(const P& p, int it, float* scr, int lane) {
;     ...
;     if (which == 0) transpose_item(p.wg + (size_t)le * DM * EFF, DM, EFF, WSP(bf16_t, WS_WGU) + (size_t)le * 1024 * DM, 128, 0, scr, sub, lane);
.LBB0_227:
	s_andn2_b64 vcc, exec, s[6:7]
	s_cbranch_vccnz .LBB0_229
	s_add_u32 s19, s40, s0
	s_addc_u32 s20, s41, s1
	s_add_u32 s6, s4, s0
	s_addc_u32 s1, s5, s1
	s_lshl_b32 s0, s17, 2
	s_and_b32 s7, s0, 0x7c0
	s_and_b32 s0, s18, 0x1e0
	s_lshl_b32 s17, s0, 2
	v_add_u32_e32 v4, s7, v1
	s_add_u32 s18, s19, s17
	s_addc_u32 s19, s20, 0
	v_lshlrev_b32_e32 v96, 2, v0
	v_ashrrev_i32_e32 v5, 31, v4
	v_lshl_add_u64 v[12:13], s[18:19], 0, v[96:97]
	v_lshlrev_b64 v[4:5], 11, v[4:5]
	v_lshl_add_u64 v[4:5], v[12:13], 0, v[4:5]
	s_movk_i32 s17, 0x4000
	v_add_co_u32_e32 v16, vcc, s17, v4
	s_mov_b32 s17, 0x8000
	s_nop 0
	v_addc_co_u32_e32 v17, vcc, 0, v5, vcc
	global_load_dwordx4 v[12:15], v[4:5], off nt
	v_add_co_u32_e32 v20, vcc, s17, v4
	global_load_dwordx4 v[16:19], v[16:17], off nt
	s_nop 0
	v_addc_co_u32_e32 v21, vcc, 0, v5, vcc
	s_mov_b32 s17, 0xc000
	global_load_dwordx4 v[20:23], v[20:21], off nt
	v_add_co_u32_e32 v24, vcc, s17, v4
	s_mov_b32 s17, 0x10000
	s_nop 0
	v_addc_co_u32_e32 v25, vcc, 0, v5, vcc
	global_load_dwordx4 v[24:27], v[24:25], off nt
	v_add_co_u32_e32 v28, vcc, s17, v4
	s_mov_b32 s17, 0x14000
	s_nop 0
	v_addc_co_u32_e32 v29, vcc, 0, v5, vcc
	global_load_dwordx4 v[28:31], v[28:29], off nt
	v_add_co_u32_e32 v32, vcc, s17, v4
	v_add_u32_e32 v11, s0, v1
	s_nop 0
	v_addc_co_u32_e32 v33, vcc, 0, v5, vcc
	global_load_dwordx4 v[32:35], v[32:33], off nt
	v_add_co_u32_e32 v36, vcc, s93, v4
	s_lshl_b32 s7, s7, 1
	s_nop 0
	v_addc_co_u32_e32 v37, vcc, 0, v5, vcc
	global_load_dwordx4 v[36:39], v[36:37], off nt
	v_add_co_u32_e32 v4, vcc, s96, v4
	s_add_u32 s6, s6, s7
	s_nop 0
	v_addc_co_u32_e32 v5, vcc, 0, v5, vcc
	global_load_dwordx4 v[40:43], v[4:5], off nt
	v_add_u32_e32 v4, v3, v6
	v_add_u32_e32 v5, 0x420, v4
	s_addc_u32 s7, s1, 0
	v_lshlrev_b32_e32 v96, 1, v2
	s_waitcnt vmcnt(7)
	ds_write2_b32 v4, v12, v13 offset1:1
	ds_write2_b32 v4, v14, v15 offset0:2 offset1:3
	s_waitcnt vmcnt(6)
	ds_write2_b32 v5, v16, v17 offset1:1
	v_add_u32_e32 v5, 0x428, v4
	ds_write2_b32 v5, v18, v19 offset1:1
	v_add_u32_e32 v5, 0x840, v4
	s_waitcnt vmcnt(5)
	ds_write2_b32 v5, v20, v21 offset1:1
	v_add_u32_e32 v5, 0x848, v4
	ds_write2_b32 v5, v22, v23 offset1:1
	v_add_u32_e32 v5, 0xc60, v4
	s_waitcnt vmcnt(4)
	ds_write2_b32 v5, v24, v25 offset1:1
	v_add_u32_e32 v5, 0xc68, v4
	ds_write2_b32 v5, v26, v27 offset1:1
	v_add_u32_e32 v5, 0x1080, v4
	s_waitcnt vmcnt(3)
	ds_write2_b32 v5, v28, v29 offset1:1
	v_add_u32_e32 v5, 0x1088, v4
	ds_write2_b32 v5, v30, v31 offset1:1
	v_add_u32_e32 v5, 0x14a0, v4
	s_waitcnt vmcnt(2)
	ds_write2_b32 v5, v32, v33 offset1:1
	v_add_u32_e32 v5, 0x14a8, v4
	ds_write2_b32 v5, v34, v35 offset1:1
	v_add_u32_e32 v5, 0x18c0, v4
	s_waitcnt vmcnt(1)
	ds_write2_b32 v5, v36, v37 offset1:1
	v_add_u32_e32 v5, 0x18c8, v4
	ds_write2_b32 v5, v38, v39 offset1:1
	v_add_u32_e32 v5, 0x1ce0, v4
	v_add_u32_e32 v4, 0x1ce8, v4
	s_waitcnt vmcnt(0)
	ds_write2_b32 v5, v40, v41 offset1:1
	ds_write2_b32 v4, v42, v43 offset1:1
	s_waitcnt lgkmcnt(0)
	ds_read2_b32 v[214:215], v10 offset1:33
	ds_read2_b32 v[222:223], v10 offset0:66 offset1:99
	ds_read2_b32 v[224:225], v10 offset0:132 offset1:165
	ds_read2_b32 v[226:227], v10 offset0:198 offset1:231
	ds_read2_b32 v[228:229], v10 offset0:8 offset1:41
	ds_read2_b32 v[230:231], v10 offset0:74 offset1:107
	ds_read2_b32 v[232:233], v10 offset0:140 offset1:173
	ds_read2_b32 v[234:235], v10 offset0:206 offset1:239
	s_waitcnt lgkmcnt(0)
	ds_read2_b32 v[236:237], v10 offset0:16 offset1:49
	ds_read2_b32 v[238:239], v10 offset0:82 offset1:115
	ds_read2_b32 v[240:241], v10 offset0:148 offset1:181
	ds_read2_b32 v[242:243], v10 offset0:214 offset1:247
	ds_read2_b32 v[244:245], v10 offset0:24 offset1:57
	ds_read2_b32 v[246:247], v10 offset0:90 offset1:123
	ds_read2_b32 v[248:249], v10 offset0:156 offset1:189
	ds_read2_b32 v[250:251], v10 offset0:222 offset1:255
	v_cvt_pk_bf16_f32 v12, v214, v215
	v_cvt_pk_bf16_f32 v13, v222, v223
	v_cvt_pk_bf16_f32 v14, v224, v225
	v_cvt_pk_bf16_f32 v15, v226, v227
	v_and_b32_e32 v16, 0xffffff80, v11
	v_add_u32_e32 v16, v16, v11
	v_ashrrev_i32_e32 v17, 31, v16
	v_lshl_add_u64 v[4:5], s[6:7], 0, v[96:97]
	v_lshlrev_b64 v[16:17], 12, v[16:17]
	v_lshl_add_u64 v[16:17], v[4:5], 0, v[16:17]
	global_store_dwordx4 v[16:17], v[12:15], off nt
	s_nop 1
	v_add_u32_e32 v11, s0, v7
	v_cvt_pk_bf16_f32 v12, v228, v229
	v_cvt_pk_bf16_f32 v13, v230, v231
	v_cvt_pk_bf16_f32 v14, v232, v233
	v_cvt_pk_bf16_f32 v15, v234, v235
	v_and_b32_e32 v16, 0xffffff80, v11
	v_add_u32_e32 v16, v16, v11
	v_ashrrev_i32_e32 v17, 31, v16
	v_lshlrev_b64 v[16:17], 12, v[16:17]
	v_lshl_add_u64 v[16:17], v[4:5], 0, v[16:17]
	global_store_dwordx4 v[16:17], v[12:15], off nt
	s_nop 1
	s_waitcnt lgkmcnt(0)
	v_add_u32_e32 v11, s0, v8
	v_cvt_pk_bf16_f32 v12, v236, v237
	v_cvt_pk_bf16_f32 v13, v238, v239
	v_cvt_pk_bf16_f32 v14, v240, v241
	v_cvt_pk_bf16_f32 v15, v242, v243
	v_and_b32_e32 v16, 0xffffff80, v11
	v_add_u32_e32 v16, v16, v11
	v_ashrrev_i32_e32 v17, 31, v16
	v_lshlrev_b64 v[16:17], 12, v[16:17]
	v_lshl_add_u64 v[16:17], v[4:5], 0, v[16:17]
	global_store_dwordx4 v[16:17], v[12:15], off nt
	s_nop 1
	v_add_u32_e32 v11, s0, v9
	v_cvt_pk_bf16_f32 v12, v244, v245
	v_cvt_pk_bf16_f32 v13, v246, v247
	v_cvt_pk_bf16_f32 v14, v248, v249
	v_cvt_pk_bf16_f32 v15, v250, v251
	v_and_b32_e32 v16, 0xffffff80, v11
	v_add_u32_e32 v16, v16, v11
	v_ashrrev_i32_e32 v17, 31, v16
	v_lshlrev_b64 v[16:17], 12, v[16:17]
	v_lshl_add_u64 v[4:5], v[4:5], 0, v[16:17]
	global_store_dwordx4 v[4:5], v[12:15], off nt
	s_nop 1
	s_waitcnt lgkmcnt(0)

; __device__ __forceinline__ unsigned pk2(float lo, float hi) { unsigned r; asm volatile("v_cvt_pk_bf16_f32 %0, %1, %2" : "=v"(r) : "v"(lo), "v"(hi)); return r; }
; __device__ __forceinline__ void transpose_item(const float* W, int K, int N, bf16_t* WT, int rstep, int roff, float* scr, int item, int lane) {
;   const int nblk = N / 32, kb = item / nblk, nb = item % nblk, k0 = 64 * kb, n0 = 32 * nb;
;   f32x4 v[8];
; #pragma unroll
;   for (int i = 0; i < 8; ++i) v[i] = __builtin_nontemporal_load((const f32x4*)(W + (size_t)(k0 + i * 8 + (lane >> 3)) * N + n0 + (lane & 7) * 4));
; #pragma unroll
;   for (int i = 0; i < 8; ++i) { float* d = scr + (i * 8 + (lane >> 3)) * 33 + (lane & 7) * 4; d[0] = v[i].x; d[1] = v[i].y; d[2] = v[i].z; d[3] = v[i].w; }
;   __builtin_amdgcn_wave_barrier(); asm volatile("s_waitcnt lgkmcnt(0)" ::: "memory");
;   const int c = lane & 7;
; #pragma unroll
;   for (int j = 0; j < 4; ++j) { const int nl = (lane >> 3) + 8 * j, n = n0 + nl; const float* s = scr + (8 * c) * 33 + nl;
;     u32x4 o; o.x = pk2(s[0 * 33], s[1 * 33]); o.y = pk2(s[2 * 33], s[3 * 33]); o.z = pk2(s[4 * 33], s[5 * 33]); o.w = pk2(s[6 * 33], s[7 * 33]);
;     const int row = n + (n >> 7) * rstep + roff;
;     __builtin_nontemporal_store(o, (u32x4*)(WT + (size_t)row * K + k0 + 8 * c)); }
;   __builtin_amdgcn_wave_barrier(); asm volatile("s_waitcnt lgkmcnt(0)" ::: "memory");
; }
; __device__ __forceinline__ void convert_item(const P& p, int it, float* scr, int lane) {
;   if (it < IT_DENSE) {
;     const int l = it / (IT_WIN + IT_WOUT), r = it % (IT_WIN + IT_WOUT);
;     if (r < IT_WIN) transpose_item(p.w_in + (size_t)l * DM * INW, DM, INW, WSP(bf16_t, WS_WIN) + (size_t)l * INW * DM, 0, 0, scr, r, lane);
;     else transpose_item(p.w_out + (size_t)l * DM * DM, DM, DM, WSP(bf16_t, WS_WOUT) + (size_t)l * DM * DM, 0, 0, scr, r - IT_WIN, lane);
.LBB0_230:
	s_and_b64 vcc, exec, s[0:1]
	s_cbranch_vccz .LBB0_210
	s_ashr_i32 s0, s16, 31
	s_lshr_b32 s0, s0, 19
	s_add_i32 s1, s16, s0
	s_ashr_i32 s0, s1, 13
	s_and_b32 s1, s1, 0xffffe000
	s_sub_i32 s16, s16, s1
	s_ashr_i32 s1, s0, 31
	v_add_u32_e32 v11, v3, v6
	s_cmpk_gt_i32 s16, 0x17ff
	s_mov_b64 s[6:7], -1
	v_lshlrev_b32_e32 v96, 2, v0
	v_add_u32_e32 v12, 0x420, v11
	v_add_u32_e32 v13, 0x428, v11
	v_add_u32_e32 v14, 0x840, v11
	v_add_u32_e32 v15, 0x848, v11
	v_add_u32_e32 v16, 0xc60, v11
	v_add_u32_e32 v17, 0xc68, v11
	v_add_u32_e32 v18, 0x1080, v11
	v_add_u32_e32 v19, 0x1088, v11
	v_add_u32_e32 v20, 0x14a0, v11
	v_add_u32_e32 v21, 0x14a8, v11
	v_add_u32_e32 v22, 0x18c0, v11
	v_add_u32_e32 v23, 0x18c8, v11
	v_add_u32_e32 v24, 0x1ce0, v11
	v_add_u32_e32 v25, 0x1ce8, v11
	v_lshlrev_b32_e32 v4, 1, v2
	s_cbranch_scc0 .LBB0_233
	s_lshl_b64 s[6:7], s[0:1], 24
	s_add_u32 s17, s70, s6
	s_addc_u32 s18, s71, s7
	s_lshl_b64 s[6:7], s[0:1], 23
	s_add_u32 s1, s13, s6
	s_addc_u32 s19, s14, s7
	s_add_i32 s6, s16, 0xe800
	s_and_b32 s20, s6, 0xffc0
	s_lshl_b32 s6, s16, 5
	s_and_b32 s21, s6, 0x7e0
	s_lshl_b32 s6, s21, 2
	v_add_u32_e32 v26, s20, v1
	s_add_u32 s6, s17, s6
	s_addc_u32 s7, s18, 0
	v_ashrrev_i32_e32 v27, 31, v26
	v_lshl_add_u64 v[28:29], s[6:7], 0, v[96:97]
	v_lshlrev_b64 v[26:27], 13, v[26:27]
	v_lshl_add_u64 v[54:55], v[28:29], 0, v[26:27]
	s_mov_b32 s6, 0x10000
	v_add_co_u32_e32 v30, vcc, s6, v54
	s_mov_b32 s6, 0x20000
	s_nop 0
	v_addc_co_u32_e32 v31, vcc, 0, v55, vcc
	v_add_co_u32_e32 v34, vcc, s6, v54
	s_mov_b32 s6, 0x30000
	s_nop 0
	v_addc_co_u32_e32 v35, vcc, 0, v55, vcc
	v_add_co_u32_e32 v38, vcc, s6, v54
	s_mov_b32 s6, 0x40000
	s_nop 0
	v_addc_co_u32_e32 v39, vcc, 0, v55, vcc
	v_add_co_u32_e32 v42, vcc, s6, v54
	s_mov_b32 s6, 0x50000
	s_nop 0
	v_addc_co_u32_e32 v43, vcc, 0, v55, vcc
	v_add_co_u32_e32 v46, vcc, s6, v54
	global_load_dwordx4 v[26:29], v[54:55], off nt
	s_nop 0
	global_load_dwordx4 v[30:33], v[30:31], off nt
	v_addc_co_u32_e32 v47, vcc, 0, v55, vcc
	global_load_dwordx4 v[34:37], v[34:35], off nt
	s_nop 0
	global_load_dwordx4 v[38:41], v[38:39], off nt
	s_nop 0
	global_load_dwordx4 v[42:45], v[42:43], off nt
	s_nop 0
	global_load_dwordx4 v[46:49], v[46:47], off nt
	s_mov_b32 s6, 0x60000
	v_add_co_u32_e32 v50, vcc, s6, v54
	s_mov_b32 s6, 0x70000
	s_nop 0
	v_addc_co_u32_e32 v51, vcc, 0, v55, vcc
	global_load_dwordx4 v[50:53], v[50:51], off nt
	v_add_co_u32_e32 v54, vcc, s6, v54
	s_lshl_b32 s6, s20, 1
	s_nop 0
	v_addc_co_u32_e32 v55, vcc, 0, v55, vcc
	global_load_dwordx4 v[54:57], v[54:55], off nt
	s_add_u32 s6, s1, s6
	v_mov_b32_e32 v5, v97
	s_addc_u32 s7, s19, 0
	s_waitcnt vmcnt(7)
	ds_write2_b32 v11, v26, v27 offset1:1
	ds_write2_b32 v11, v28, v29 offset0:2 offset1:3
	s_waitcnt vmcnt(6)
	ds_write2_b32 v12, v30, v31 offset1:1
	ds_write2_b32 v13, v32, v33 offset1:1
	s_waitcnt vmcnt(5)
	ds_write2_b32 v14, v34, v35 offset1:1
	ds_write2_b32 v15, v36, v37 offset1:1
	s_waitcnt vmcnt(4)
	ds_write2_b32 v16, v38, v39 offset1:1
	ds_write2_b32 v17, v40, v41 offset1:1
	s_waitcnt vmcnt(3)
	ds_write2_b32 v18, v42, v43 offset1:1
	ds_write2_b32 v19, v44, v45 offset1:1
	s_waitcnt vmcnt(2)
	ds_write2_b32 v20, v46, v47 offset1:1
	ds_write2_b32 v21, v48, v49 offset1:1
	s_waitcnt vmcnt(1)
	ds_write2_b32 v22, v50, v51 offset1:1
	ds_write2_b32 v23, v52, v53 offset1:1
	s_waitcnt vmcnt(0)
	ds_write2_b32 v24, v54, v55 offset1:1
	ds_write2_b32 v25, v56, v57 offset1:1
	s_waitcnt lgkmcnt(0)
	ds_read2_b32 v[214:215], v10 offset1:33
	ds_read2_b32 v[222:223], v10 offset0:66 offset1:99
	ds_read2_b32 v[224:225], v10 offset0:132 offset1:165
	ds_read2_b32 v[226:227], v10 offset0:198 offset1:231
	ds_read2_b32 v[228:229], v10 offset0:8 offset1:41
	ds_read2_b32 v[230:231], v10 offset0:74 offset1:107
	ds_read2_b32 v[232:233], v10 offset0:140 offset1:173
	ds_read2_b32 v[234:235], v10 offset0:206 offset1:239
	s_waitcnt lgkmcnt(0)
	ds_read2_b32 v[236:237], v10 offset0:16 offset1:49
	ds_read2_b32 v[238:239], v10 offset0:82 offset1:115
	ds_read2_b32 v[240:241], v10 offset0:148 offset1:181
	ds_read2_b32 v[242:243], v10 offset0:214 offset1:247
	ds_read2_b32 v[244:245], v10 offset0:24 offset1:57
	ds_read2_b32 v[246:247], v10 offset0:90 offset1:123
	ds_read2_b32 v[248:249], v10 offset0:156 offset1:189
	ds_read2_b32 v[250:251], v10 offset0:222 offset1:255
	v_cvt_pk_bf16_f32 v26, v214, v215
	v_add_u32_e32 v30, s21, v1
	v_cvt_pk_bf16_f32 v27, v222, v223
	v_ashrrev_i32_e32 v31, 31, v30
	v_cvt_pk_bf16_f32 v28, v224, v225
	v_lshlrev_b64 v[30:31], 12, v[30:31]
	v_lshl_add_u64 v[34:35], s[6:7], 0, v[4:5]
	v_cvt_pk_bf16_f32 v29, v226, v227
	v_lshl_add_u64 v[30:31], v[34:35], 0, v[30:31]
	global_store_dwordx4 v[30:31], v[26:29], off nt
	s_nop 1
	s_mov_b64 s[6:7], 0
	v_cvt_pk_bf16_f32 v26, v228, v229
	v_add_u32_e32 v32, s21, v7
	v_ashrrev_i32_e32 v33, 31, v32
	v_lshlrev_b64 v[32:33], 12, v[32:33]
	v_cvt_pk_bf16_f32 v27, v230, v231
	v_lshl_add_u64 v[32:33], v[34:35], 0, v[32:33]
	v_cvt_pk_bf16_f32 v28, v232, v233
	v_cvt_pk_bf16_f32 v29, v234, v235
	global_store_dwordx4 v[32:33], v[26:29], off nt
	s_nop 1
	v_add_u32_e32 v32, s21, v8
	v_ashrrev_i32_e32 v33, 31, v32
	s_waitcnt lgkmcnt(0)
	v_cvt_pk_bf16_f32 v26, v236, v237
	v_lshlrev_b64 v[32:33], 12, v[32:33]
	v_cvt_pk_bf16_f32 v27, v238, v239
	v_lshl_add_u64 v[32:33], v[34:35], 0, v[32:33]
	v_cvt_pk_bf16_f32 v28, v240, v241
	v_cvt_pk_bf16_f32 v29, v242, v243
	global_store_dwordx4 v[32:33], v[26:29], off nt
	s_nop 1
	v_add_u32_e32 v32, s21, v9
	v_ashrrev_i32_e32 v33, 31, v32
	v_cvt_pk_bf16_f32 v26, v244, v245
	v_lshlrev_b64 v[32:33], 12, v[32:33]
	v_cvt_pk_bf16_f32 v27, v246, v247
	v_lshl_add_u64 v[32:33], v[34:35], 0, v[32:33]
	v_cvt_pk_bf16_f32 v28, v248, v249
	v_cvt_pk_bf16_f32 v29, v250, v251
	global_store_dwordx4 v[32:33], v[26:29], off nt
	s_nop 1
	s_waitcnt lgkmcnt(0)
; __device__ __forceinline__ unsigned pk2(float lo, float hi) { unsigned r; asm volatile("v_cvt_pk_bf16_f32 %0, %1, %2" : "=v"(r) : "v"(lo), "v"(hi)); return r; }
; __device__ __forceinline__ void transpose_item(const float* W, int K, int N, bf16_t* WT, int rstep, int roff, float* scr, int item, int lane) {
;   const int nblk = N / 32, kb = item / nblk, nb = item % nblk, k0 = 64 * kb, n0 = 32 * nb;
;   f32x4 v[8];
; #pragma unroll
;   for (int i = 0; i < 8; ++i) v[i] = __builtin_nontemporal_load((const f32x4*)(W + (size_t)(k0 + i * 8 + (lane >> 3)) * N + n0 + (lane & 7) * 4));
; #pragma unroll
;   for (int i = 0; i < 8; ++i) { float* d = scr + (i * 8 + (lane >> 3)) * 33 + (lane & 7) * 4; d[0] = v[i].x; d[1] = v[i].y; d[2] = v[i].z; d[3] = v[i].w; }
;   __builtin_amdgcn_wave_barrier(); asm volatile("s_waitcnt lgkmcnt(0)" ::: "memory");
;   const int c = lane & 7;
; #pragma unroll
;   for (int j = 0; j < 4; ++j) { const int nl = (lane >> 3) + 8 * j, n = n0 + nl; const float* s = scr + (8 * c) * 33 + nl;
;     u32x4 o; o.x = pk2(s[0 * 33], s[1 * 33]); o.y = pk2(s[2 * 33], s[3 * 33]); o.z = pk2(s[4 * 33], s[5 * 33]); o.w = pk2(s[6 * 33], s[7 * 33]);
;     const int row = n + (n >> 7) * rstep + roff;
;     __builtin_nontemporal_store(o, (u32x4*)(WT + (size_t)row * K + k0 + 8 * c)); }
;   __builtin_amdgcn_wave_barrier(); asm volatile("s_waitcnt lgkmcnt(0)" ::: "memory");
; }
; __device__ __forceinline__ void convert_item(const P& p, int it, float* scr, int lane) {
;     ...
;     if (r < IT_WIN) transpose_item(p.w_in + (size_t)l * DM * INW, DM, INW, WSP(bf16_t, WS_WIN) + (size_t)l * INW * DM, 0, 0, scr, r, lane);
.LBB0_233:
	s_andn2_b64 vcc, exec, s[6:7]
	s_cbranch_vccnz .LBB0_210
	s_mul_i32 s6, s0, 0x3000000
	s_mul_hi_i32 s1, s0, 0x3000000
	s_add_u32 s7, s68, s6
	s_addc_u32 s18, s69, s1
	s_mul_hi_i32 s1, s0, 0x1800000
	s_mul_i32 s0, s0, 0x1800000
	s_add_u32 s19, s24, s0
	s_mul_i32 s0, s16, 0x2aab
	s_addc_u32 s20, s30, s1
	s_lshr_b32 s1, s0, 31
	s_ashr_i32 s0, s0, 21
	s_add_i32 s0, s0, s1
	s_sext_i32_i16 s1, s0
	s_mulk_i32 s0, 0xc0
	s_sub_i32 s0, s16, s0
	s_sext_i32_i16 s0, s0
	s_lshl_b32 s0, s0, 5
	s_lshl_b32 s6, s1, 6
	s_ashr_i32 s1, s0, 31
	s_lshl_b64 s[16:17], s[0:1], 2
	s_add_u32 s16, s7, s16
	v_add_u32_e32 v5, s6, v1
	s_addc_u32 s17, s18, s17
	v_lshl_add_u64 v[54:55], s[16:17], 0, v[96:97]
	s_movk_i32 s1, 0x6000
	v_add_u32_e32 v28, 8, v5
	v_add_u32_e32 v34, 16, v5
	v_add_u32_e32 v36, 24, v5
	v_add_u32_e32 v42, 32, v5
	v_add_u32_e32 v44, 40, v5
	v_mad_i64_i32 v[26:27], s[16:17], v5, s1, v[54:55]
	v_mad_i64_i32 v[30:31], s[16:17], v28, s1, v[54:55]
	v_mad_i64_i32 v[34:35], s[16:17], v34, s1, v[54:55]
	v_mad_i64_i32 v[38:39], s[16:17], v36, s1, v[54:55]
	v_mad_i64_i32 v[42:43], s[16:17], v42, s1, v[54:55]
	v_mad_i64_i32 v[46:47], s[16:17], v44, s1, v[54:55]
	global_load_dwordx4 v[26:29], v[26:27], off nt
	s_nop 0
	global_load_dwordx4 v[30:33], v[30:31], off nt
	s_nop 0
	global_load_dwordx4 v[34:37], v[34:35], off nt
	s_nop 0
	global_load_dwordx4 v[38:41], v[38:39], off nt
	s_nop 0
	global_load_dwordx4 v[42:45], v[42:43], off nt
	s_nop 0
	global_load_dwordx4 v[46:49], v[46:47], off nt
	v_add_u32_e32 v50, 48, v5
	v_mad_i64_i32 v[50:51], s[16:17], v50, s1, v[54:55]
	global_load_dwordx4 v[50:53], v[50:51], off nt
	v_add_u32_e32 v5, 56, v5
	v_mad_i64_i32 v[54:55], s[16:17], v5, s1, v[54:55]
	global_load_dwordx4 v[54:57], v[54:55], off nt
	s_ashr_i32 s7, s6, 31
	s_lshl_b64 s[6:7], s[6:7], 1
	s_add_u32 s6, s19, s6
	v_mov_b32_e32 v5, v97
	s_addc_u32 s7, s20, s7
	v_lshl_add_u64 v[4:5], s[6:7], 0, v[4:5]
	s_movk_i32 s82, 0x6000
	s_waitcnt vmcnt(7)
	ds_write2_b32 v11, v26, v27 offset1:1
	ds_write2_b32 v11, v28, v29 offset0:2 offset1:3
	s_waitcnt vmcnt(6)
	ds_write2_b32 v12, v30, v31 offset1:1
	ds_write2_b32 v13, v32, v33 offset1:1
	s_waitcnt vmcnt(5)
	ds_write2_b32 v14, v34, v35 offset1:1
	ds_write2_b32 v15, v36, v37 offset1:1
	s_waitcnt vmcnt(4)
	ds_write2_b32 v16, v38, v39 offset1:1
	ds_write2_b32 v17, v40, v41 offset1:1
	s_waitcnt vmcnt(3)
	ds_write2_b32 v18, v42, v43 offset1:1
	ds_write2_b32 v19, v44, v45 offset1:1
	s_waitcnt vmcnt(2)
	ds_write2_b32 v20, v46, v47 offset1:1
	ds_write2_b32 v21, v48, v49 offset1:1
	s_waitcnt vmcnt(1)
	ds_write2_b32 v22, v50, v51 offset1:1
	ds_write2_b32 v23, v52, v53 offset1:1
	s_waitcnt vmcnt(0)
	ds_write2_b32 v24, v54, v55 offset1:1
	ds_write2_b32 v25, v56, v57 offset1:1
	s_waitcnt lgkmcnt(0)
	ds_read2_b32 v[214:215], v10 offset1:33
	ds_read2_b32 v[222:223], v10 offset0:66 offset1:99
	ds_read2_b32 v[224:225], v10 offset0:132 offset1:165
	ds_read2_b32 v[226:227], v10 offset0:198 offset1:231
	ds_read2_b32 v[228:229], v10 offset0:8 offset1:41
	ds_read2_b32 v[230:231], v10 offset0:74 offset1:107
	ds_read2_b32 v[232:233], v10 offset0:140 offset1:173
	ds_read2_b32 v[234:235], v10 offset0:206 offset1:239
	s_waitcnt lgkmcnt(0)
	ds_read2_b32 v[236:237], v10 offset0:16 offset1:49
	ds_read2_b32 v[238:239], v10 offset0:82 offset1:115
	ds_read2_b32 v[240:241], v10 offset0:148 offset1:181
	ds_read2_b32 v[242:243], v10 offset0:214 offset1:247
	ds_read2_b32 v[244:245], v10 offset0:24 offset1:57
	ds_read2_b32 v[246:247], v10 offset0:90 offset1:123
	ds_read2_b32 v[248:249], v10 offset0:156 offset1:189
	ds_read2_b32 v[250:251], v10 offset0:222 offset1:255
	v_cvt_pk_bf16_f32 v12, v214, v215
	v_add_u32_e32 v16, s0, v1
	v_cvt_pk_bf16_f32 v13, v222, v223
	v_ashrrev_i32_e32 v17, 31, v16
	v_cvt_pk_bf16_f32 v14, v224, v225
	v_lshlrev_b64 v[16:17], 12, v[16:17]
	v_cvt_pk_bf16_f32 v15, v226, v227
	v_lshl_add_u64 v[16:17], v[4:5], 0, v[16:17]
	global_store_dwordx4 v[16:17], v[12:15], off nt
	s_nop 1
	s_nop 0
	v_cvt_pk_bf16_f32 v12, v228, v229
	v_add_u32_e32 v18, s0, v7
	v_ashrrev_i32_e32 v19, 31, v18
	v_lshlrev_b64 v[18:19], 12, v[18:19]
	v_cvt_pk_bf16_f32 v13, v230, v231
	v_lshl_add_u64 v[18:19], v[4:5], 0, v[18:19]
	v_cvt_pk_bf16_f32 v14, v232, v233
	v_cvt_pk_bf16_f32 v15, v234, v235
	global_store_dwordx4 v[18:19], v[12:15], off nt
	s_nop 1
	v_add_u32_e32 v18, s0, v8
	v_ashrrev_i32_e32 v19, 31, v18
	s_waitcnt lgkmcnt(0)
	v_cvt_pk_bf16_f32 v12, v236, v237
	v_lshlrev_b64 v[18:19], 12, v[18:19]
	v_cvt_pk_bf16_f32 v13, v238, v239
	v_lshl_add_u64 v[18:19], v[4:5], 0, v[18:19]
	v_cvt_pk_bf16_f32 v14, v240, v241
	v_cvt_pk_bf16_f32 v15, v242, v243
	global_store_dwordx4 v[18:19], v[12:15], off nt
	s_nop 1
	v_add_u32_e32 v18, s0, v9
	v_ashrrev_i32_e32 v19, 31, v18
	v_cvt_pk_bf16_f32 v12, v244, v245
	v_lshlrev_b64 v[18:19], 12, v[18:19]
	v_cvt_pk_bf16_f32 v13, v246, v247
	v_lshl_add_u64 v[4:5], v[4:5], 0, v[18:19]
	v_cvt_pk_bf16_f32 v14, v248, v249
	v_cvt_pk_bf16_f32 v15, v250, v251
	global_store_dwordx4 v[4:5], v[12:15], off nt
	s_nop 1
	s_waitcnt lgkmcnt(0)
	s_branch .LBB0_210

; __device__ __forceinline__ unsigned pk2(float lo, float hi) { unsigned r; asm volatile("v_cvt_pk_bf16_f32 %0, %1, %2" : "=v"(r) : "v"(lo), "v"(hi)); return r; }
; __device__ __forceinline__ void transpose_item(const float* W, int K, int N, bf16_t* WT, int rstep, int roff, float* scr, int item, int lane) {
;   const int nblk = N / 32, kb = item / nblk, nb = item % nblk, k0 = 64 * kb, n0 = 32 * nb;
;   f32x4 v[8];
; #pragma unroll
;   for (int i = 0; i < 8; ++i) v[i] = __builtin_nontemporal_load((const f32x4*)(W + (size_t)(k0 + i * 8 + (lane >> 3)) * N + n0 + (lane & 7) * 4));
; #pragma unroll
;   for (int i = 0; i < 8; ++i) { float* d = scr + (i * 8 + (lane >> 3)) * 33 + (lane & 7) * 4; d[0] = v[i].x; d[1] = v[i].y; d[2] = v[i].z; d[3] = v[i].w; }
;   __builtin_amdgcn_wave_barrier(); asm volatile("s_waitcnt lgkmcnt(0)" ::: "memory");
;   const int c = lane & 7;
; #pragma unroll
;   for (int j = 0; j < 4; ++j) { const int nl = (lane >> 3) + 8 * j, n = n0 + nl; const float* s = scr + (8 * c) * 33 + nl;
;     u32x4 o; o.x = pk2(s[0 * 33], s[1 * 33]); o.y = pk2(s[2 * 33], s[3 * 33]); o.z = pk2(s[4 * 33], s[5 * 33]); o.w = pk2(s[6 * 33], s[7 * 33]);
;     const int row = n + (n >> 7) * rstep + roff;
;     __builtin_nontemporal_store(o, (u32x4*)(WT + (size_t)row * K + k0 + 8 * c)); }
;   __builtin_amdgcn_wave_barrier(); asm volatile("s_waitcnt lgkmcnt(0)" ::: "memory");
; }
; __device__ __forceinline__ void convert_item(const P& p, int it, float* scr, int lane) {
;     ...
;     const int idx = it - IT_DENSE, m = idx / IT_EXP, sub = idx % IT_EXP, le = m / 3, which = m % 3;
;     if (which == 0) transpose_item(p.wg + (size_t)le * DM * EFF, DM, EFF, WSP(bf16_t, WS_WGU) + (size_t)le * 1024 * DM, 128, 0, scr, sub, lane);
;     else if (which == 1) transpose_item(p.wu + (size_t)le * DM * EFF, DM, EFF, WSP(bf16_t, WS_WGU) + (size_t)le * 1024 * DM, 128, 128, scr, sub, lane);
;     else transpose_item(p.wd + (size_t)le * EFF * DM, EFF, DM, WSP(bf16_t, WS_WD) + (size_t)le * DM * EFF, 0, 0, scr, sub, lane);
.LBB0_240:
	s_add_i32 s0, s13, 0x2000
	s_cmpk_lt_i32 s13, 0x2000
	s_cselect_b32 s6, s13, s0
	s_cmpk_gt_i32 s6, 0x3fff
	s_mov_b64 s[0:1], -1
	s_cbranch_scc0 .LBB0_250
	s_add_i32 s0, s6, 0xffffc000
	s_lshr_b32 s1, s0, 9
	s_mul_i32 s0, s0, 0xaaab
	s_lshr_b32 s16, s0, 26
	s_mul_i32 s0, s1, 0xab
	s_bfe_u32 s0, s0, 0x70009
	s_mul_i32 s0, s0, 3
	s_sub_i32 s0, s1, s0
	s_and_b32 s7, s6, 0x1ff
	s_lshl_b32 s15, s16, 22
	s_lshl_b32 s14, s6, 5
	s_and_b32 s17, s0, 0xff
	s_cmp_lt_i32 s17, 1
	s_mov_b64 s[0:1], -1
	s_cbranch_scc1 .LBB0_247
	s_and_b32 s0, 0xffff, s17
	s_cmp_lg_u32 s0, 1
	s_mov_b64 s[0:1], -1
	s_cbranch_scc0 .LBB0_244
	s_add_u32 s18, s74, s15
	s_addc_u32 s19, s75, 0
	s_lshl_b32 s0, s16, 21
	s_add_u32 s1, s4, s0
	s_addc_u32 s16, s5, 0
	s_and_b32 s0, s14, 0x7e0
	s_and_b32 s17, s6, 0x1c0
	s_lshl_b32 s20, s0, 2
	v_add_u32_e32 v4, s17, v1
	s_add_u32 s18, s18, s20
	s_addc_u32 s19, s19, 0
	v_lshlrev_b32_e32 v96, 2, v0
	v_ashrrev_i32_e32 v5, 31, v4
	v_lshl_add_u64 v[12:13], s[18:19], 0, v[96:97]
	v_lshlrev_b64 v[4:5], 13, v[4:5]
	v_lshl_add_u64 v[4:5], v[12:13], 0, v[4:5]
	s_mov_b32 s18, 0x10000
	v_add_co_u32_e32 v16, vcc, s18, v4
	s_mov_b32 s18, 0x20000
	s_nop 0
	v_addc_co_u32_e32 v17, vcc, 0, v5, vcc
	global_load_dwordx4 v[12:15], v[4:5], off nt
	v_add_co_u32_e32 v20, vcc, s18, v4
	global_load_dwordx4 v[16:19], v[16:17], off nt
	s_nop 0
	v_addc_co_u32_e32 v21, vcc, 0, v5, vcc
	s_mov_b32 s18, 0x30000
	global_load_dwordx4 v[20:23], v[20:21], off nt
	v_add_co_u32_e32 v24, vcc, s18, v4
	s_mov_b32 s18, 0x40000
	s_nop 0
	v_addc_co_u32_e32 v25, vcc, 0, v5, vcc
	global_load_dwordx4 v[24:27], v[24:25], off nt
	v_add_co_u32_e32 v28, vcc, s18, v4
	s_mov_b32 s18, 0x50000
	s_nop 0
	v_addc_co_u32_e32 v29, vcc, 0, v5, vcc
	global_load_dwordx4 v[28:31], v[28:29], off nt
	v_add_co_u32_e32 v32, vcc, s18, v4
	s_mov_b32 s18, 0x60000
	s_nop 0
	v_addc_co_u32_e32 v33, vcc, 0, v5, vcc
	global_load_dwordx4 v[32:35], v[32:33], off nt
	v_add_co_u32_e32 v36, vcc, s18, v4
	s_mov_b32 s18, 0x70000
	s_nop 0
	v_addc_co_u32_e32 v37, vcc, 0, v5, vcc
	global_load_dwordx4 v[36:39], v[36:37], off nt
	v_add_co_u32_e32 v4, vcc, s18, v4
	s_lshl_b32 s17, s17, 1
	s_nop 0
	v_addc_co_u32_e32 v5, vcc, 0, v5, vcc
	global_load_dwordx4 v[40:43], v[4:5], off nt
	v_add_u32_e32 v4, v3, v6
	v_add_u32_e32 v5, 0x420, v4
	s_add_u32 s18, s1, s17
	s_addc_u32 s19, s16, 0
	v_lshlrev_b32_e32 v96, 1, v2
	s_waitcnt vmcnt(0)
	ds_write2_b32 v4, v12, v13 offset1:1
	ds_write2_b32 v4, v14, v15 offset0:2 offset1:3
	ds_write2_b32 v5, v16, v17 offset1:1
	v_add_u32_e32 v5, 0x428, v4
	ds_write2_b32 v5, v18, v19 offset1:1
	v_add_u32_e32 v5, 0x840, v4
	ds_write2_b32 v5, v20, v21 offset1:1
	v_add_u32_e32 v5, 0x848, v4
	ds_write2_b32 v5, v22, v23 offset1:1
	v_add_u32_e32 v5, 0xc60, v4
	v_add_u32_e32 v16, s0, v1
	v_ashrrev_i32_e32 v17, 31, v16
	ds_write2_b32 v5, v24, v25 offset1:1
	v_add_u32_e32 v5, 0xc68, v4
	ds_write2_b32 v5, v26, v27 offset1:1
	v_add_u32_e32 v5, 0x1080, v4
	v_lshlrev_b64 v[16:17], 10, v[16:17]
	ds_write2_b32 v5, v28, v29 offset1:1
	v_add_u32_e32 v5, 0x1088, v4
	ds_write2_b32 v5, v30, v31 offset1:1
	v_add_u32_e32 v5, 0x14a0, v4
	ds_write2_b32 v5, v32, v33 offset1:1
	v_add_u32_e32 v5, 0x14a8, v4
	ds_write2_b32 v5, v34, v35 offset1:1
	v_add_u32_e32 v5, 0x18c0, v4
	ds_write2_b32 v5, v36, v37 offset1:1
	v_add_u32_e32 v5, 0x18c8, v4
	ds_write2_b32 v5, v38, v39 offset1:1
	v_add_u32_e32 v5, 0x1ce0, v4
	v_add_u32_e32 v4, 0x1ce8, v4
	ds_write2_b32 v5, v40, v41 offset1:1
	ds_write2_b32 v4, v42, v43 offset1:1
	s_waitcnt lgkmcnt(0)
	ds_read2_b32 v[214:215], v10 offset1:33
	ds_read2_b32 v[222:223], v10 offset0:66 offset1:99
	ds_read2_b32 v[224:225], v10 offset0:132 offset1:165
	ds_read2_b32 v[226:227], v10 offset0:198 offset1:231
	ds_read2_b32 v[228:229], v10 offset0:8 offset1:41
	ds_read2_b32 v[230:231], v10 offset0:74 offset1:107
	ds_read2_b32 v[232:233], v10 offset0:140 offset1:173
	ds_read2_b32 v[234:235], v10 offset0:206 offset1:239
	s_waitcnt lgkmcnt(0)
	ds_read2_b32 v[236:237], v10 offset0:16 offset1:49
	ds_read2_b32 v[238:239], v10 offset0:82 offset1:115
	ds_read2_b32 v[240:241], v10 offset0:148 offset1:181
	ds_read2_b32 v[242:243], v10 offset0:214 offset1:247
	ds_read2_b32 v[244:245], v10 offset0:24 offset1:57
	ds_read2_b32 v[246:247], v10 offset0:90 offset1:123
	ds_read2_b32 v[248:249], v10 offset0:156 offset1:189
	ds_read2_b32 v[250:251], v10 offset0:222 offset1:255
	v_lshl_add_u64 v[4:5], s[18:19], 0, v[96:97]
	v_cvt_pk_bf16_f32 v12, v214, v215
	v_cvt_pk_bf16_f32 v13, v222, v223
	v_lshl_add_u64 v[16:17], v[4:5], 0, v[16:17]
	v_cvt_pk_bf16_f32 v14, v224, v225
	v_cvt_pk_bf16_f32 v15, v226, v227
	global_store_dwordx4 v[16:17], v[12:15], off nt
	s_nop 1
	v_add_u32_e32 v16, s0, v7
	v_ashrrev_i32_e32 v17, 31, v16
	v_cvt_pk_bf16_f32 v12, v228, v229
	v_lshlrev_b64 v[16:17], 10, v[16:17]
	v_cvt_pk_bf16_f32 v13, v230, v231
	v_lshl_add_u64 v[16:17], v[4:5], 0, v[16:17]
	v_cvt_pk_bf16_f32 v14, v232, v233
	v_cvt_pk_bf16_f32 v15, v234, v235
	global_store_dwordx4 v[16:17], v[12:15], off nt
	s_nop 1
	v_add_u32_e32 v16, s0, v8
	s_waitcnt lgkmcnt(0)
	v_ashrrev_i32_e32 v17, 31, v16
	v_cvt_pk_bf16_f32 v12, v236, v237
	v_lshlrev_b64 v[16:17], 10, v[16:17]
	v_cvt_pk_bf16_f32 v13, v238, v239
	v_lshl_add_u64 v[16:17], v[4:5], 0, v[16:17]
	v_cvt_pk_bf16_f32 v14, v240, v241
	v_cvt_pk_bf16_f32 v15, v242, v243
	global_store_dwordx4 v[16:17], v[12:15], off nt
	s_nop 1
	v_add_u32_e32 v16, s0, v9
	v_ashrrev_i32_e32 v17, 31, v16
	v_cvt_pk_bf16_f32 v12, v244, v245
	v_lshlrev_b64 v[16:17], 10, v[16:17]
	v_cvt_pk_bf16_f32 v13, v246, v247
	v_lshl_add_u64 v[4:5], v[4:5], 0, v[16:17]
	v_cvt_pk_bf16_f32 v14, v248, v249
	v_cvt_pk_bf16_f32 v15, v250, v251
	global_store_dwordx4 v[4:5], v[12:15], off nt
	s_nop 1
	s_waitcnt lgkmcnt(0)
	s_mov_b64 s[0:1], 0
; __device__ __forceinline__ unsigned pk2(float lo, float hi) { unsigned r; asm volatile("v_cvt_pk_bf16_f32 %0, %1, %2" : "=v"(r) : "v"(lo), "v"(hi)); return r; }
; __device__ __forceinline__ void transpose_item(const float* W, int K, int N, bf16_t* WT, int rstep, int roff, float* scr, int item, int lane) {
;   const int nblk = N / 32, kb = item / nblk, nb = item % nblk, k0 = 64 * kb, n0 = 32 * nb;
;   f32x4 v[8];
; #pragma unroll
;   for (int i = 0; i < 8; ++i) v[i] = __builtin_nontemporal_load((const f32x4*)(W + (size_t)(k0 + i * 8 + (lane >> 3)) * N + n0 + (lane & 7) * 4));
; #pragma unroll
;   for (int i = 0; i < 8; ++i) { float* d = scr + (i * 8 + (lane >> 3)) * 33 + (lane & 7) * 4; d[0] = v[i].x; d[1] = v[i].y; d[2] = v[i].z; d[3] = v[i].w; }
;   __builtin_amdgcn_wave_barrier(); asm volatile("s_waitcnt lgkmcnt(0)" ::: "memory");
;   const int c = lane & 7;
; #pragma unroll
;   for (int j = 0; j < 4; ++j) { const int nl = (lane >> 3) + 8 * j, n = n0 + nl; const float* s = scr + (8 * c) * 33 + nl;
;     u32x4 o; o.x = pk2(s[0 * 33], s[1 * 33]); o.y = pk2(s[2 * 33], s[3 * 33]); o.z = pk2(s[4 * 33], s[5 * 33]); o.w = pk2(s[6 * 33], s[7 * 33]);
;     const int row = n + (n >> 7) * rstep + roff;
;     __builtin_nontemporal_store(o, (u32x4*)(WT + (size_t)row * K + k0 + 8 * c)); }
;   __builtin_amdgcn_wave_barrier(); asm volatile("s_waitcnt lgkmcnt(0)" ::: "memory");
; }
; __device__ __forceinline__ void convert_item(const P& p, int it, float* scr, int lane) {
;     ...
;     else if (which == 1) transpose_item(p.wu + (size_t)le * DM * EFF, DM, EFF, WSP(bf16_t, WS_WGU) + (size_t)le * 1024 * DM, 128, 128, scr, sub, lane);
.LBB0_244:
	s_andn2_b64 vcc, exec, s[0:1]
	s_cbranch_vccnz .LBB0_246
	s_add_u32 s18, s42, s15
	s_addc_u32 s19, s43, 0
	s_add_u32 s1, s2, s15
	s_addc_u32 s16, s3, 0
	s_lshl_b32 s0, s7, 2
	s_and_b32 s17, s0, 0x7c0
	s_and_b32 s0, s14, 0x1e0
	s_lshl_b32 s20, s0, 2
	v_add_u32_e32 v4, s17, v1
	s_add_u32 s18, s18, s20
	s_addc_u32 s19, s19, 0
	v_lshlrev_b32_e32 v96, 2, v0
	v_ashrrev_i32_e32 v5, 31, v4
	v_lshl_add_u64 v[12:13], s[18:19], 0, v[96:97]
	v_lshlrev_b64 v[4:5], 11, v[4:5]
	v_lshl_add_u64 v[4:5], v[12:13], 0, v[4:5]
	s_movk_i32 s18, 0x4000
	v_add_co_u32_e32 v16, vcc, s18, v4
	s_mov_b32 s18, 0x8000
	s_nop 0
	v_addc_co_u32_e32 v17, vcc, 0, v5, vcc
	global_load_dwordx4 v[12:15], v[4:5], off nt
	v_add_co_u32_e32 v20, vcc, s18, v4
	global_load_dwordx4 v[16:19], v[16:17], off nt
	s_nop 0
	v_addc_co_u32_e32 v21, vcc, 0, v5, vcc
	s_mov_b32 s18, 0xc000
	global_load_dwordx4 v[20:23], v[20:21], off nt
	v_add_co_u32_e32 v24, vcc, s18, v4
	s_mov_b32 s18, 0x10000
	s_nop 0
	v_addc_co_u32_e32 v25, vcc, 0, v5, vcc
	global_load_dwordx4 v[24:27], v[24:25], off nt
	v_add_co_u32_e32 v28, vcc, s18, v4
	s_mov_b32 s18, 0x14000
	s_nop 0
	v_addc_co_u32_e32 v29, vcc, 0, v5, vcc
	global_load_dwordx4 v[28:31], v[28:29], off nt
	v_add_co_u32_e32 v32, vcc, s18, v4
	s_lshl_b32 s17, s17, 1
	s_nop 0
	v_addc_co_u32_e32 v33, vcc, 0, v5, vcc
	global_load_dwordx4 v[32:35], v[32:33], off nt
	v_add_co_u32_e32 v36, vcc, s93, v4
	v_add_u32_e32 v11, s0, v1
	s_nop 0
	v_addc_co_u32_e32 v37, vcc, 0, v5, vcc
	global_load_dwordx4 v[36:39], v[36:37], off nt
	v_add_co_u32_e32 v4, vcc, s96, v4
	s_add_u32 s18, s1, s17
	s_nop 0
	v_addc_co_u32_e32 v5, vcc, 0, v5, vcc
	global_load_dwordx4 v[40:43], v[4:5], off nt
	v_add_u32_e32 v4, v3, v6
	v_add_u32_e32 v5, 0x420, v4
	s_movk_i32 s1, 0x80
	s_addc_u32 s19, s16, 0
	v_lshlrev_b32_e32 v96, 1, v2
	s_waitcnt vmcnt(0)
	ds_write2_b32 v4, v12, v13 offset1:1
	ds_write2_b32 v4, v14, v15 offset0:2 offset1:3
	ds_write2_b32 v5, v16, v17 offset1:1
	v_add_u32_e32 v5, 0x428, v4
	ds_write2_b32 v5, v18, v19 offset1:1
	v_add_u32_e32 v5, 0x840, v4
	ds_write2_b32 v5, v20, v21 offset1:1
	v_add_u32_e32 v5, 0x848, v4
	ds_write2_b32 v5, v22, v23 offset1:1
	v_add_u32_e32 v5, 0xc60, v4
	ds_write2_b32 v5, v24, v25 offset1:1
	v_add_u32_e32 v5, 0xc68, v4
	ds_write2_b32 v5, v26, v27 offset1:1
	v_add_u32_e32 v5, 0x1080, v4
	ds_write2_b32 v5, v28, v29 offset1:1
	v_add_u32_e32 v5, 0x1088, v4
	ds_write2_b32 v5, v30, v31 offset1:1
	v_add_u32_e32 v5, 0x14a0, v4
	ds_write2_b32 v5, v32, v33 offset1:1
	v_add_u32_e32 v5, 0x14a8, v4
	ds_write2_b32 v5, v34, v35 offset1:1
	v_add_u32_e32 v5, 0x18c0, v4
	ds_write2_b32 v5, v36, v37 offset1:1
	v_add_u32_e32 v5, 0x18c8, v4
	ds_write2_b32 v5, v38, v39 offset1:1
	v_add_u32_e32 v5, 0x1ce0, v4
	v_add_u32_e32 v4, 0x1ce8, v4
	ds_write2_b32 v5, v40, v41 offset1:1
	ds_write2_b32 v4, v42, v43 offset1:1
	s_waitcnt lgkmcnt(0)
	ds_read2_b32 v[214:215], v10 offset1:33
	ds_read2_b32 v[222:223], v10 offset0:66 offset1:99
	ds_read2_b32 v[224:225], v10 offset0:132 offset1:165
	ds_read2_b32 v[226:227], v10 offset0:198 offset1:231
	ds_read2_b32 v[228:229], v10 offset0:8 offset1:41
	ds_read2_b32 v[230:231], v10 offset0:74 offset1:107
	ds_read2_b32 v[232:233], v10 offset0:140 offset1:173
	ds_read2_b32 v[234:235], v10 offset0:206 offset1:239
	s_waitcnt lgkmcnt(0)
	ds_read2_b32 v[236:237], v10 offset0:16 offset1:49
	ds_read2_b32 v[238:239], v10 offset0:82 offset1:115
	ds_read2_b32 v[240:241], v10 offset0:148 offset1:181
	ds_read2_b32 v[242:243], v10 offset0:214 offset1:247
	ds_read2_b32 v[244:245], v10 offset0:24 offset1:57
	ds_read2_b32 v[246:247], v10 offset0:90 offset1:123
	ds_read2_b32 v[248:249], v10 offset0:156 offset1:189
	ds_read2_b32 v[250:251], v10 offset0:222 offset1:255
	v_cvt_pk_bf16_f32 v12, v214, v215
	v_cvt_pk_bf16_f32 v13, v222, v223
	v_cvt_pk_bf16_f32 v14, v224, v225
	v_cvt_pk_bf16_f32 v15, v226, v227
	v_and_b32_e32 v16, 0xffffff80, v11
	v_add3_u32 v16, v11, v16, s1
	v_ashrrev_i32_e32 v17, 31, v16
	v_lshl_add_u64 v[4:5], s[18:19], 0, v[96:97]
	v_lshlrev_b64 v[16:17], 12, v[16:17]
	v_lshl_add_u64 v[16:17], v[4:5], 0, v[16:17]
	global_store_dwordx4 v[16:17], v[12:15], off nt
	s_nop 1
	v_add_u32_e32 v11, s0, v7
	v_cvt_pk_bf16_f32 v12, v228, v229
	v_cvt_pk_bf16_f32 v13, v230, v231
	v_cvt_pk_bf16_f32 v14, v232, v233
	v_cvt_pk_bf16_f32 v15, v234, v235
	v_and_b32_e32 v16, 0xffffff80, v11
	v_add3_u32 v16, v11, v16, s1
	v_ashrrev_i32_e32 v17, 31, v16
	v_lshlrev_b64 v[16:17], 12, v[16:17]
	v_lshl_add_u64 v[16:17], v[4:5], 0, v[16:17]
	global_store_dwordx4 v[16:17], v[12:15], off nt
	s_nop 1
	s_waitcnt lgkmcnt(0)
	v_add_u32_e32 v11, s0, v8
	v_cvt_pk_bf16_f32 v12, v236, v237
	v_cvt_pk_bf16_f32 v13, v238, v239
	v_cvt_pk_bf16_f32 v14, v240, v241
	v_cvt_pk_bf16_f32 v15, v242, v243
	v_and_b32_e32 v16, 0xffffff80, v11
	v_add3_u32 v16, v11, v16, s1
	v_ashrrev_i32_e32 v17, 31, v16
	v_lshlrev_b64 v[16:17], 12, v[16:17]
	v_lshl_add_u64 v[16:17], v[4:5], 0, v[16:17]
	global_store_dwordx4 v[16:17], v[12:15], off nt
	s_nop 1
	v_add_u32_e32 v11, s0, v9
	v_cvt_pk_bf16_f32 v12, v244, v245
	v_cvt_pk_bf16_f32 v13, v246, v247
	v_cvt_pk_bf16_f32 v14, v248, v249
	v_cvt_pk_bf16_f32 v15, v250, v251
	v_and_b32_e32 v16, 0xffffff80, v11
	v_add3_u32 v16, v11, v16, s1
	v_ashrrev_i32_e32 v17, 31, v16
	v_lshlrev_b64 v[16:17], 12, v[16:17]
	v_lshl_add_u64 v[4:5], v[4:5], 0, v[16:17]
	global_store_dwordx4 v[4:5], v[12:15], off nt
	s_nop 1
	s_waitcnt lgkmcnt(0)

; __device__ __forceinline__ unsigned pk2(float lo, float hi) { unsigned r; asm volatile("v_cvt_pk_bf16_f32 %0, %1, %2" : "=v"(r) : "v"(lo), "v"(hi)); return r; }
; __device__ __forceinline__ void transpose_item(const float* W, int K, int N, bf16_t* WT, int rstep, int roff, float* scr, int item, int lane) {
;   const int nblk = N / 32, kb = item / nblk, nb = item % nblk, k0 = 64 * kb, n0 = 32 * nb;
;   f32x4 v[8];
; #pragma unroll
;   for (int i = 0; i < 8; ++i) v[i] = __builtin_nontemporal_load((const f32x4*)(W + (size_t)(k0 + i * 8 + (lane >> 3)) * N + n0 + (lane & 7) * 4));
; #pragma unroll
;   for (int i = 0; i < 8; ++i) { float* d = scr + (i * 8 + (lane >> 3)) * 33 + (lane & 7) * 4; d[0] = v[i].x; d[1] = v[i].y; d[2] = v[i].z; d[3] = v[i].w; }
;   __builtin_amdgcn_wave_barrier(); asm volatile("s_waitcnt lgkmcnt(0)" ::: "memory");
;   const int c = lane & 7;
; #pragma unroll
;   for (int j = 0; j < 4; ++j) { const int nl = (lane >> 3) + 8 * j, n = n0 + nl; const float* s = scr + (8 * c) * 33 + nl;
;     u32x4 o; o.x = pk2(s[0 * 33], s[1 * 33]); o.y = pk2(s[2 * 33], s[3 * 33]); o.z = pk2(s[4 * 33], s[5 * 33]); o.w = pk2(s[6 * 33], s[7 * 33]);
;     const int row = n + (n >> 7) * rstep + roff;
;     __builtin_nontemporal_store(o, (u32x4*)(WT + (size_t)row * K + k0 + 8 * c)); }
;   __builtin_amdgcn_wave_barrier(); asm volatile("s_waitcnt lgkmcnt(0)" ::: "memory");
; __device__ __forceinline__ void convert_item(const P& p, int it, float* scr, int lane) {
;     ...
;     if (which == 0) transpose_item(p.wg + (size_t)le * DM * EFF, DM, EFF, WSP(bf16_t, WS_WGU) + (size_t)le * 1024 * DM, 128, 0, scr, sub, lane);
.LBB0_247:
	s_andn2_b64 vcc, exec, s[0:1]
	s_cbranch_vccnz .LBB0_249
	s_add_u32 s16, s40, s15
	s_addc_u32 s17, s41, 0
	s_add_u32 s1, s2, s15
	s_addc_u32 s15, s3, 0
	s_lshl_b32 s0, s7, 2
	s_and_b32 s7, s0, 0x7c0
	s_and_b32 s0, s14, 0x1e0
	s_lshl_b32 s14, s0, 2
	v_add_u32_e32 v4, s7, v1
	s_add_u32 s16, s16, s14
	s_addc_u32 s17, s17, 0
	v_lshlrev_b32_e32 v96, 2, v0
	v_ashrrev_i32_e32 v5, 31, v4
	v_lshl_add_u64 v[12:13], s[16:17], 0, v[96:97]
	v_lshlrev_b64 v[4:5], 11, v[4:5]
	v_lshl_add_u64 v[4:5], v[12:13], 0, v[4:5]
	s_movk_i32 s14, 0x4000
	v_add_co_u32_e32 v16, vcc, s14, v4
	s_mov_b32 s14, 0x8000
	s_nop 0
	v_addc_co_u32_e32 v17, vcc, 0, v5, vcc
	global_load_dwordx4 v[12:15], v[4:5], off nt
	v_add_co_u32_e32 v20, vcc, s14, v4
	global_load_dwordx4 v[16:19], v[16:17], off nt
	s_nop 0
	v_addc_co_u32_e32 v21, vcc, 0, v5, vcc
	s_mov_b32 s14, 0xc000
	global_load_dwordx4 v[20:23], v[20:21], off nt
	v_add_co_u32_e32 v24, vcc, s14, v4
	s_mov_b32 s14, 0x10000
	s_nop 0
	v_addc_co_u32_e32 v25, vcc, 0, v5, vcc
	global_load_dwordx4 v[24:27], v[24:25], off nt
	v_add_co_u32_e32 v28, vcc, s14, v4
	s_mov_b32 s14, 0x14000
	s_nop 0
	v_addc_co_u32_e32 v29, vcc, 0, v5, vcc
	global_load_dwordx4 v[28:31], v[28:29], off nt
	v_add_co_u32_e32 v32, vcc, s14, v4
	v_add_u32_e32 v11, s0, v1
	s_nop 0
	v_addc_co_u32_e32 v33, vcc, 0, v5, vcc
	global_load_dwordx4 v[32:35], v[32:33], off nt
	v_add_co_u32_e32 v36, vcc, s93, v4
	s_lshl_b32 s7, s7, 1
	s_nop 0
	v_addc_co_u32_e32 v37, vcc, 0, v5, vcc
	global_load_dwordx4 v[36:39], v[36:37], off nt
	v_add_co_u32_e32 v4, vcc, s96, v4
	s_add_u32 s14, s1, s7
	s_nop 0
	v_addc_co_u32_e32 v5, vcc, 0, v5, vcc
	global_load_dwordx4 v[40:43], v[4:5], off nt
	v_add_u32_e32 v4, v3, v6
	v_add_u32_e32 v5, 0x420, v4
	s_addc_u32 s15, s15, 0
	v_lshlrev_b32_e32 v96, 1, v2
	s_waitcnt vmcnt(0)
	ds_write2_b32 v4, v12, v13 offset1:1
	ds_write2_b32 v4, v14, v15 offset0:2 offset1:3
	ds_write2_b32 v5, v16, v17 offset1:1
	v_add_u32_e32 v5, 0x428, v4
	ds_write2_b32 v5, v18, v19 offset1:1
	v_add_u32_e32 v5, 0x840, v4
	ds_write2_b32 v5, v20, v21 offset1:1
	v_add_u32_e32 v5, 0x848, v4
	ds_write2_b32 v5, v22, v23 offset1:1
	v_add_u32_e32 v5, 0xc60, v4
	ds_write2_b32 v5, v24, v25 offset1:1
	v_add_u32_e32 v5, 0xc68, v4
	ds_write2_b32 v5, v26, v27 offset1:1
	v_add_u32_e32 v5, 0x1080, v4
	ds_write2_b32 v5, v28, v29 offset1:1
	v_add_u32_e32 v5, 0x1088, v4
	ds_write2_b32 v5, v30, v31 offset1:1
	v_add_u32_e32 v5, 0x14a0, v4
	ds_write2_b32 v5, v32, v33 offset1:1
	v_add_u32_e32 v5, 0x14a8, v4
	ds_write2_b32 v5, v34, v35 offset1:1
	v_add_u32_e32 v5, 0x18c0, v4
	ds_write2_b32 v5, v36, v37 offset1:1
	v_add_u32_e32 v5, 0x18c8, v4
	ds_write2_b32 v5, v38, v39 offset1:1
	v_add_u32_e32 v5, 0x1ce0, v4
	v_add_u32_e32 v4, 0x1ce8, v4
	ds_write2_b32 v5, v40, v41 offset1:1
	ds_write2_b32 v4, v42, v43 offset1:1
	s_waitcnt lgkmcnt(0)
	ds_read2_b32 v[214:215], v10 offset1:33
	ds_read2_b32 v[222:223], v10 offset0:66 offset1:99
	ds_read2_b32 v[224:225], v10 offset0:132 offset1:165
	ds_read2_b32 v[226:227], v10 offset0:198 offset1:231
	ds_read2_b32 v[228:229], v10 offset0:8 offset1:41
	ds_read2_b32 v[230:231], v10 offset0:74 offset1:107
	ds_read2_b32 v[232:233], v10 offset0:140 offset1:173
	ds_read2_b32 v[234:235], v10 offset0:206 offset1:239
	s_waitcnt lgkmcnt(0)
	ds_read2_b32 v[236:237], v10 offset0:16 offset1:49
	ds_read2_b32 v[238:239], v10 offset0:82 offset1:115
	ds_read2_b32 v[240:241], v10 offset0:148 offset1:181
	ds_read2_b32 v[242:243], v10 offset0:214 offset1:247
	ds_read2_b32 v[244:245], v10 offset0:24 offset1:57
	ds_read2_b32 v[246:247], v10 offset0:90 offset1:123
	ds_read2_b32 v[248:249], v10 offset0:156 offset1:189
	ds_read2_b32 v[250:251], v10 offset0:222 offset1:255
	v_cvt_pk_bf16_f32 v12, v214, v215
	v_cvt_pk_bf16_f32 v13, v222, v223
	v_cvt_pk_bf16_f32 v14, v224, v225
	v_cvt_pk_bf16_f32 v15, v226, v227
	v_and_b32_e32 v16, 0xffffff80, v11
	v_add_u32_e32 v16, v16, v11
	v_ashrrev_i32_e32 v17, 31, v16
	v_lshl_add_u64 v[4:5], s[14:15], 0, v[96:97]
	v_lshlrev_b64 v[16:17], 12, v[16:17]
	v_lshl_add_u64 v[16:17], v[4:5], 0, v[16:17]
	global_store_dwordx4 v[16:17], v[12:15], off nt
	s_nop 1
	v_add_u32_e32 v11, s0, v7
	v_cvt_pk_bf16_f32 v12, v228, v229
	v_cvt_pk_bf16_f32 v13, v230, v231
	v_cvt_pk_bf16_f32 v14, v232, v233
	v_cvt_pk_bf16_f32 v15, v234, v235
	v_and_b32_e32 v16, 0xffffff80, v11
	v_add_u32_e32 v16, v16, v11
	v_ashrrev_i32_e32 v17, 31, v16
	v_lshlrev_b64 v[16:17], 12, v[16:17]
	v_lshl_add_u64 v[16:17], v[4:5], 0, v[16:17]
	global_store_dwordx4 v[16:17], v[12:15], off nt
	s_nop 1
	s_waitcnt lgkmcnt(0)
	v_add_u32_e32 v11, s0, v8
	v_cvt_pk_bf16_f32 v12, v236, v237
	v_cvt_pk_bf16_f32 v13, v238, v239
	v_cvt_pk_bf16_f32 v14, v240, v241
	v_cvt_pk_bf16_f32 v15, v242, v243
	v_and_b32_e32 v16, 0xffffff80, v11
	v_add_u32_e32 v16, v16, v11
	v_ashrrev_i32_e32 v17, 31, v16
	v_lshlrev_b64 v[16:17], 12, v[16:17]
	v_lshl_add_u64 v[16:17], v[4:5], 0, v[16:17]
	global_store_dwordx4 v[16:17], v[12:15], off nt
	s_nop 1
	v_add_u32_e32 v11, s0, v9
	v_cvt_pk_bf16_f32 v12, v244, v245
	v_cvt_pk_bf16_f32 v13, v246, v247
	v_cvt_pk_bf16_f32 v14, v248, v249
	v_cvt_pk_bf16_f32 v15, v250, v251
	v_and_b32_e32 v16, 0xffffff80, v11
	v_add_u32_e32 v16, v16, v11
	v_ashrrev_i32_e32 v17, 31, v16
	v_lshlrev_b64 v[16:17], 12, v[16:17]
	v_lshl_add_u64 v[4:5], v[4:5], 0, v[16:17]
	global_store_dwordx4 v[4:5], v[12:15], off nt
	s_nop 1
	s_waitcnt lgkmcnt(0)

; __device__ __forceinline__ unsigned pk2(float lo, float hi) { unsigned r; asm volatile("v_cvt_pk_bf16_f32 %0, %1, %2" : "=v"(r) : "v"(lo), "v"(hi)); return r; }
; __device__ __forceinline__ void transpose_item(const float* W, int K, int N, bf16_t* WT, int rstep, int roff, float* scr, int item, int lane) {
;   const int nblk = N / 32, kb = item / nblk, nb = item % nblk, k0 = 64 * kb, n0 = 32 * nb;
;   f32x4 v[8];
; #pragma unroll
;   for (int i = 0; i < 8; ++i) v[i] = __builtin_nontemporal_load((const f32x4*)(W + (size_t)(k0 + i * 8 + (lane >> 3)) * N + n0 + (lane & 7) * 4));
; #pragma unroll
;   for (int i = 0; i < 8; ++i) { float* d = scr + (i * 8 + (lane >> 3)) * 33 + (lane & 7) * 4; d[0] = v[i].x; d[1] = v[i].y; d[2] = v[i].z; d[3] = v[i].w; }
;   __builtin_amdgcn_wave_barrier(); asm volatile("s_waitcnt lgkmcnt(0)" ::: "memory");
;   const int c = lane & 7;
; #pragma unroll
;   for (int j = 0; j < 4; ++j) { const int nl = (lane >> 3) + 8 * j, n = n0 + nl; const float* s = scr + (8 * c) * 33 + nl;
;     u32x4 o; o.x = pk2(s[0 * 33], s[1 * 33]); o.y = pk2(s[2 * 33], s[3 * 33]); o.z = pk2(s[4 * 33], s[5 * 33]); o.w = pk2(s[6 * 33], s[7 * 33]);
;     const int row = n + (n >> 7) * rstep + roff;
;     __builtin_nontemporal_store(o, (u32x4*)(WT + (size_t)row * K + k0 + 8 * c)); }
;   __builtin_amdgcn_wave_barrier(); asm volatile("s_waitcnt lgkmcnt(0)" ::: "memory");
; __device__ __forceinline__ void convert_item(const P& p, int it, float* scr, int lane) {
;   if (it < IT_DENSE) {
;     const int l = it / (IT_WIN + IT_WOUT), r = it % (IT_WIN + IT_WOUT);
;     if (r < IT_WIN) transpose_item(p.w_in + (size_t)l * DM * INW, DM, INW, WSP(bf16_t, WS_WIN) + (size_t)l * INW * DM, 0, 0, scr, r, lane);
;     else transpose_item(p.w_out + (size_t)l * DM * DM, DM, DM, WSP(bf16_t, WS_WOUT) + (size_t)l * DM * DM, 0, 0, scr, r - IT_WIN, lane);
.LBB0_250:
	s_and_b64 vcc, exec, s[0:1]
	s_cbranch_vccz .LBB0_239
	s_ashr_i32 s0, s6, 31
	s_lshr_b32 s0, s0, 19
	s_add_i32 s1, s6, s0
	s_ashr_i32 s0, s1, 13
	s_and_b32 s1, s1, 0xffffe000
	s_sub_i32 s14, s6, s1
	s_ashr_i32 s1, s0, 31
	v_add_u32_e32 v11, v3, v6
	s_cmpk_gt_i32 s14, 0x17ff
	s_mov_b64 s[6:7], -1
	v_lshlrev_b32_e32 v96, 2, v0
	v_add_u32_e32 v12, 0x420, v11
	v_add_u32_e32 v13, 0x428, v11
	v_add_u32_e32 v14, 0x840, v11
	v_add_u32_e32 v15, 0x848, v11
	v_add_u32_e32 v16, 0xc60, v11
	v_add_u32_e32 v17, 0xc68, v11
	v_add_u32_e32 v18, 0x1080, v11
	v_add_u32_e32 v19, 0x1088, v11
	v_add_u32_e32 v20, 0x14a0, v11
	v_add_u32_e32 v21, 0x14a8, v11
	v_add_u32_e32 v22, 0x18c0, v11
	v_add_u32_e32 v23, 0x18c8, v11
	v_add_u32_e32 v24, 0x1ce0, v11
	v_add_u32_e32 v25, 0x1ce8, v11
	v_lshlrev_b32_e32 v4, 1, v2
	s_cbranch_scc0 .LBB0_253
	s_lshl_b64 s[6:7], s[0:1], 24
	s_add_u32 s15, s70, s6
	s_addc_u32 s16, s71, s7
	s_lshl_b64 s[6:7], s[0:1], 23
	s_add_u32 s1, s9, s6
	s_addc_u32 s17, s12, s7
	s_add_i32 s6, s14, 0xe800
	s_and_b32 s18, s6, 0xffc0
	s_lshl_b32 s6, s14, 5
	s_and_b32 s19, s6, 0x7e0
	s_lshl_b32 s6, s19, 2
	v_add_u32_e32 v26, s18, v1
	s_add_u32 s6, s15, s6
	s_addc_u32 s7, s16, 0
	v_ashrrev_i32_e32 v27, 31, v26
	v_lshl_add_u64 v[28:29], s[6:7], 0, v[96:97]
	v_lshlrev_b64 v[26:27], 13, v[26:27]
	v_lshl_add_u64 v[54:55], v[28:29], 0, v[26:27]
	s_mov_b32 s6, 0x10000
	v_add_co_u32_e32 v30, vcc, s6, v54
	s_mov_b32 s6, 0x20000
	s_nop 0
	v_addc_co_u32_e32 v31, vcc, 0, v55, vcc
	v_add_co_u32_e32 v34, vcc, s6, v54
	s_mov_b32 s6, 0x30000
	s_nop 0
	v_addc_co_u32_e32 v35, vcc, 0, v55, vcc
	v_add_co_u32_e32 v38, vcc, s6, v54
	s_mov_b32 s6, 0x40000
	s_nop 0
	v_addc_co_u32_e32 v39, vcc, 0, v55, vcc
	v_add_co_u32_e32 v42, vcc, s6, v54
	s_mov_b32 s6, 0x50000
	s_nop 0
	v_addc_co_u32_e32 v43, vcc, 0, v55, vcc
	v_add_co_u32_e32 v46, vcc, s6, v54
	global_load_dwordx4 v[26:29], v[54:55], off nt
	s_nop 0
	global_load_dwordx4 v[30:33], v[30:31], off nt
	v_addc_co_u32_e32 v47, vcc, 0, v55, vcc
	global_load_dwordx4 v[34:37], v[34:35], off nt
	s_nop 0
	global_load_dwordx4 v[38:41], v[38:39], off nt
	s_nop 0
	global_load_dwordx4 v[42:45], v[42:43], off nt
	s_nop 0
	global_load_dwordx4 v[46:49], v[46:47], off nt
	s_mov_b32 s6, 0x60000
	v_add_co_u32_e32 v50, vcc, s6, v54
	s_mov_b32 s6, 0x70000
	s_nop 0
	v_addc_co_u32_e32 v51, vcc, 0, v55, vcc
	global_load_dwordx4 v[50:53], v[50:51], off nt
	v_add_co_u32_e32 v54, vcc, s6, v54
	s_lshl_b32 s6, s18, 1
	s_nop 0
	v_addc_co_u32_e32 v55, vcc, 0, v55, vcc
	global_load_dwordx4 v[54:57], v[54:55], off nt
	s_add_u32 s6, s1, s6
	v_mov_b32_e32 v5, v97
	s_addc_u32 s7, s17, 0
	s_waitcnt vmcnt(0)
	ds_write2_b32 v11, v26, v27 offset1:1
	ds_write2_b32 v11, v28, v29 offset0:2 offset1:3
	ds_write2_b32 v12, v30, v31 offset1:1
	ds_write2_b32 v13, v32, v33 offset1:1
	ds_write2_b32 v14, v34, v35 offset1:1
	ds_write2_b32 v15, v36, v37 offset1:1
	ds_write2_b32 v16, v38, v39 offset1:1
	ds_write2_b32 v17, v40, v41 offset1:1
	ds_write2_b32 v18, v42, v43 offset1:1
	ds_write2_b32 v19, v44, v45 offset1:1
	ds_write2_b32 v20, v46, v47 offset1:1
	ds_write2_b32 v21, v48, v49 offset1:1
	ds_write2_b32 v22, v50, v51 offset1:1
	ds_write2_b32 v23, v52, v53 offset1:1
	ds_write2_b32 v24, v54, v55 offset1:1
	ds_write2_b32 v25, v56, v57 offset1:1
	s_waitcnt lgkmcnt(0)
	ds_read2_b32 v[214:215], v10 offset1:33
	ds_read2_b32 v[222:223], v10 offset0:66 offset1:99
	ds_read2_b32 v[224:225], v10 offset0:132 offset1:165
	ds_read2_b32 v[226:227], v10 offset0:198 offset1:231
	ds_read2_b32 v[228:229], v10 offset0:8 offset1:41
	ds_read2_b32 v[230:231], v10 offset0:74 offset1:107
	ds_read2_b32 v[232:233], v10 offset0:140 offset1:173
	ds_read2_b32 v[234:235], v10 offset0:206 offset1:239
	s_waitcnt lgkmcnt(0)
	ds_read2_b32 v[236:237], v10 offset0:16 offset1:49
	ds_read2_b32 v[238:239], v10 offset0:82 offset1:115
	ds_read2_b32 v[240:241], v10 offset0:148 offset1:181
	ds_read2_b32 v[242:243], v10 offset0:214 offset1:247
	ds_read2_b32 v[244:245], v10 offset0:24 offset1:57
	ds_read2_b32 v[246:247], v10 offset0:90 offset1:123
	ds_read2_b32 v[248:249], v10 offset0:156 offset1:189
	ds_read2_b32 v[250:251], v10 offset0:222 offset1:255
	v_cvt_pk_bf16_f32 v26, v214, v215
	v_add_u32_e32 v30, s19, v1
	v_cvt_pk_bf16_f32 v27, v222, v223
	v_ashrrev_i32_e32 v31, 31, v30
	v_cvt_pk_bf16_f32 v28, v224, v225
	v_lshlrev_b64 v[30:31], 12, v[30:31]
	v_lshl_add_u64 v[34:35], s[6:7], 0, v[4:5]
	v_cvt_pk_bf16_f32 v29, v226, v227
	v_lshl_add_u64 v[30:31], v[34:35], 0, v[30:31]
	global_store_dwordx4 v[30:31], v[26:29], off nt
	s_nop 1
	s_mov_b64 s[6:7], 0
	v_cvt_pk_bf16_f32 v26, v228, v229
	v_add_u32_e32 v32, s19, v7
	v_ashrrev_i32_e32 v33, 31, v32
	v_lshlrev_b64 v[32:33], 12, v[32:33]
	v_cvt_pk_bf16_f32 v27, v230, v231
	v_lshl_add_u64 v[32:33], v[34:35], 0, v[32:33]
	v_cvt_pk_bf16_f32 v28, v232, v233
	v_cvt_pk_bf16_f32 v29, v234, v235
	global_store_dwordx4 v[32:33], v[26:29], off nt
	s_nop 1
	v_add_u32_e32 v32, s19, v8
	v_ashrrev_i32_e32 v33, 31, v32
	s_waitcnt lgkmcnt(0)
	v_cvt_pk_bf16_f32 v26, v236, v237
	v_lshlrev_b64 v[32:33], 12, v[32:33]
	v_cvt_pk_bf16_f32 v27, v238, v239
	v_lshl_add_u64 v[32:33], v[34:35], 0, v[32:33]
	v_cvt_pk_bf16_f32 v28, v240, v241
	v_cvt_pk_bf16_f32 v29, v242, v243
	global_store_dwordx4 v[32:33], v[26:29], off nt
	s_nop 1
	v_add_u32_e32 v32, s19, v9
	v_ashrrev_i32_e32 v33, 31, v32
	v_cvt_pk_bf16_f32 v26, v244, v245
	v_lshlrev_b64 v[32:33], 12, v[32:33]
	v_cvt_pk_bf16_f32 v27, v246, v247
	v_lshl_add_u64 v[32:33], v[34:35], 0, v[32:33]
	v_cvt_pk_bf16_f32 v28, v248, v249
	v_cvt_pk_bf16_f32 v29, v250, v251
	global_store_dwordx4 v[32:33], v[26:29], off nt
	s_nop 1
	s_waitcnt lgkmcnt(0)
; __device__ __forceinline__ unsigned pk2(float lo, float hi) { unsigned r; asm volatile("v_cvt_pk_bf16_f32 %0, %1, %2" : "=v"(r) : "v"(lo), "v"(hi)); return r; }
; __device__ __forceinline__ void transpose_item(const float* W, int K, int N, bf16_t* WT, int rstep, int roff, float* scr, int item, int lane) {
;   const int nblk = N / 32, kb = item / nblk, nb = item % nblk, k0 = 64 * kb, n0 = 32 * nb;
;   f32x4 v[8];
; #pragma unroll
;   for (int i = 0; i < 8; ++i) v[i] = __builtin_nontemporal_load((const f32x4*)(W + (size_t)(k0 + i * 8 + (lane >> 3)) * N + n0 + (lane & 7) * 4));
; #pragma unroll
;   for (int i = 0; i < 8; ++i) { float* d = scr + (i * 8 + (lane >> 3)) * 33 + (lane & 7) * 4; d[0] = v[i].x; d[1] = v[i].y; d[2] = v[i].z; d[3] = v[i].w; }
;   __builtin_amdgcn_wave_barrier(); asm volatile("s_waitcnt lgkmcnt(0)" ::: "memory");
;   const int c = lane & 7;
; #pragma unroll
;   for (int j = 0; j < 4; ++j) { const int nl = (lane >> 3) + 8 * j, n = n0 + nl; const float* s = scr + (8 * c) * 33 + nl;
;     u32x4 o; o.x = pk2(s[0 * 33], s[1 * 33]); o.y = pk2(s[2 * 33], s[3 * 33]); o.z = pk2(s[4 * 33], s[5 * 33]); o.w = pk2(s[6 * 33], s[7 * 33]);
;     const int row = n + (n >> 7) * rstep + roff;
;     __builtin_nontemporal_store(o, (u32x4*)(WT + (size_t)row * K + k0 + 8 * c)); }
;   __builtin_amdgcn_wave_barrier(); asm volatile("s_waitcnt lgkmcnt(0)" ::: "memory");
; __device__ __forceinline__ void convert_item(const P& p, int it, float* scr, int lane) {
;     ...
;     if (r < IT_WIN) transpose_item(p.w_in + (size_t)l * DM * INW, DM, INW, WSP(bf16_t, WS_WIN) + (size_t)l * INW * DM, 0, 0, scr, r, lane);
.LBB0_253:
	s_andn2_b64 vcc, exec, s[6:7]
	s_cbranch_vccnz .LBB0_239
	s_mul_i32 s6, s0, 0x3000000
	s_mul_hi_i32 s1, s0, 0x3000000
	s_add_u32 s7, s68, s6
	s_addc_u32 s16, s69, s1
	s_mul_hi_i32 s1, s0, 0x1800000
	s_mul_i32 s0, s0, 0x1800000
	s_add_u32 s17, s24, s0
	s_mul_i32 s0, s14, 0x2aab
	s_addc_u32 s18, s30, s1
	s_lshr_b32 s1, s0, 31
	s_ashr_i32 s0, s0, 21
	s_add_i32 s0, s0, s1
	s_sext_i32_i16 s1, s0
	s_mulk_i32 s0, 0xc0
	s_sub_i32 s0, s14, s0
	s_sext_i32_i16 s0, s0
	s_lshl_b32 s0, s0, 5
	s_lshl_b32 s6, s1, 6
	s_ashr_i32 s1, s0, 31
	s_lshl_b64 s[14:15], s[0:1], 2
	s_add_u32 s14, s7, s14
	v_add_u32_e32 v5, s6, v1
	s_addc_u32 s15, s16, s15
	v_lshl_add_u64 v[54:55], s[14:15], 0, v[96:97]
	s_movk_i32 s1, 0x6000
	v_add_u32_e32 v28, 8, v5
	v_add_u32_e32 v34, 16, v5
	v_add_u32_e32 v36, 24, v5
	v_add_u32_e32 v42, 32, v5
	v_add_u32_e32 v44, 40, v5
	v_mad_i64_i32 v[26:27], s[14:15], v5, s1, v[54:55]
	v_mad_i64_i32 v[30:31], s[14:15], v28, s1, v[54:55]
	v_mad_i64_i32 v[34:35], s[14:15], v34, s1, v[54:55]
	v_mad_i64_i32 v[38:39], s[14:15], v36, s1, v[54:55]
	v_mad_i64_i32 v[42:43], s[14:15], v42, s1, v[54:55]
	v_mad_i64_i32 v[46:47], s[14:15], v44, s1, v[54:55]
	global_load_dwordx4 v[26:29], v[26:27], off nt
	s_nop 0
	global_load_dwordx4 v[30:33], v[30:31], off nt
	s_nop 0
	global_load_dwordx4 v[34:37], v[34:35], off nt
	s_nop 0
	global_load_dwordx4 v[38:41], v[38:39], off nt
	s_nop 0
	global_load_dwordx4 v[42:45], v[42:43], off nt
	s_nop 0
	global_load_dwordx4 v[46:49], v[46:47], off nt
	v_add_u32_e32 v50, 48, v5
	v_mad_i64_i32 v[50:51], s[14:15], v50, s1, v[54:55]
	global_load_dwordx4 v[50:53], v[50:51], off nt
	v_add_u32_e32 v5, 56, v5
	v_mad_i64_i32 v[54:55], s[14:15], v5, s1, v[54:55]
	global_load_dwordx4 v[54:57], v[54:55], off nt
	s_ashr_i32 s7, s6, 31
	s_lshl_b64 s[6:7], s[6:7], 1
	s_add_u32 s6, s17, s6
	v_mov_b32_e32 v5, v97
	s_addc_u32 s7, s18, s7
	v_lshl_add_u64 v[4:5], s[6:7], 0, v[4:5]
	s_movk_i32 s82, 0x6000
	s_waitcnt vmcnt(0)
	ds_write2_b32 v11, v26, v27 offset1:1
	ds_write2_b32 v11, v28, v29 offset0:2 offset1:3
	ds_write2_b32 v12, v30, v31 offset1:1
	ds_write2_b32 v13, v32, v33 offset1:1
	ds_write2_b32 v14, v34, v35 offset1:1
	ds_write2_b32 v15, v36, v37 offset1:1
	ds_write2_b32 v16, v38, v39 offset1:1
	ds_write2_b32 v17, v40, v41 offset1:1
	ds_write2_b32 v18, v42, v43 offset1:1
	ds_write2_b32 v19, v44, v45 offset1:1
	ds_write2_b32 v20, v46, v47 offset1:1
	ds_write2_b32 v21, v48, v49 offset1:1
	ds_write2_b32 v22, v50, v51 offset1:1
	ds_write2_b32 v23, v52, v53 offset1:1
	ds_write2_b32 v24, v54, v55 offset1:1
	ds_write2_b32 v25, v56, v57 offset1:1
	s_waitcnt lgkmcnt(0)
	ds_read2_b32 v[214:215], v10 offset1:33
	ds_read2_b32 v[222:223], v10 offset0:66 offset1:99
	ds_read2_b32 v[224:225], v10 offset0:132 offset1:165
	ds_read2_b32 v[226:227], v10 offset0:198 offset1:231
	ds_read2_b32 v[228:229], v10 offset0:8 offset1:41
	ds_read2_b32 v[230:231], v10 offset0:74 offset1:107
	ds_read2_b32 v[232:233], v10 offset0:140 offset1:173
	ds_read2_b32 v[234:235], v10 offset0:206 offset1:239
	s_waitcnt lgkmcnt(0)
	ds_read2_b32 v[236:237], v10 offset0:16 offset1:49
	ds_read2_b32 v[238:239], v10 offset0:82 offset1:115
	ds_read2_b32 v[240:241], v10 offset0:148 offset1:181
	ds_read2_b32 v[242:243], v10 offset0:214 offset1:247
	ds_read2_b32 v[244:245], v10 offset0:24 offset1:57
	ds_read2_b32 v[246:247], v10 offset0:90 offset1:123
	ds_read2_b32 v[248:249], v10 offset0:156 offset1:189
	ds_read2_b32 v[250:251], v10 offset0:222 offset1:255
	v_cvt_pk_bf16_f32 v12, v214, v215
	v_add_u32_e32 v16, s0, v1
	v_cvt_pk_bf16_f32 v13, v222, v223
	v_ashrrev_i32_e32 v17, 31, v16
	v_cvt_pk_bf16_f32 v14, v224, v225
	v_lshlrev_b64 v[16:17], 12, v[16:17]
	v_cvt_pk_bf16_f32 v15, v226, v227
	v_lshl_add_u64 v[16:17], v[4:5], 0, v[16:17]
	global_store_dwordx4 v[16:17], v[12:15], off nt
	s_nop 1
	s_nop 0
	v_cvt_pk_bf16_f32 v12, v228, v229
	v_add_u32_e32 v18, s0, v7
	v_ashrrev_i32_e32 v19, 31, v18
	v_lshlrev_b64 v[18:19], 12, v[18:19]
	v_cvt_pk_bf16_f32 v13, v230, v231
	v_lshl_add_u64 v[18:19], v[4:5], 0, v[18:19]
	v_cvt_pk_bf16_f32 v14, v232, v233
	v_cvt_pk_bf16_f32 v15, v234, v235
	global_store_dwordx4 v[18:19], v[12:15], off nt
	s_nop 1
	v_add_u32_e32 v18, s0, v8
	v_ashrrev_i32_e32 v19, 31, v18
	s_waitcnt lgkmcnt(0)
	v_cvt_pk_bf16_f32 v12, v236, v237
	v_lshlrev_b64 v[18:19], 12, v[18:19]
	v_cvt_pk_bf16_f32 v13, v238, v239
	v_lshl_add_u64 v[18:19], v[4:5], 0, v[18:19]
	v_cvt_pk_bf16_f32 v14, v240, v241
	v_cvt_pk_bf16_f32 v15, v242, v243
	global_store_dwordx4 v[18:19], v[12:15], off nt
	s_nop 1
	v_add_u32_e32 v18, s0, v9
	v_ashrrev_i32_e32 v19, 31, v18
	v_cvt_pk_bf16_f32 v12, v244, v245
	v_lshlrev_b64 v[18:19], 12, v[18:19]
	v_cvt_pk_bf16_f32 v13, v246, v247
	v_lshl_add_u64 v[4:5], v[4:5], 0, v[18:19]
	v_cvt_pk_bf16_f32 v14, v248, v249
	v_cvt_pk_bf16_f32 v15, v250, v251
	global_store_dwordx4 v[4:5], v[12:15], off nt
	s_nop 1
	s_waitcnt lgkmcnt(0)
	s_branch .LBB0_239

; __device__ __forceinline__ void transpose_item(const float* W, int K, int N, bf16_t* WT, int rstep, int roff, float* scr, int item, int lane) {
;   const int nblk = N / 32, kb = item / nblk, nb = item % nblk, k0 = 64 * kb, n0 = 32 * nb;
;   f32x4 v[8];
; #pragma unroll
;   for (int i = 0; i < 8; ++i) v[i] = __builtin_nontemporal_load((const f32x4*)(W + (size_t)(k0 + i * 8 + (lane >> 3)) * N + n0 + (lane & 7) * 4));
; #pragma unroll
;   for (int i = 0; i < 8; ++i) { float* d = scr + (i * 8 + (lane >> 3)) * 33 + (lane & 7) * 4; d[0] = v[i].x; d[1] = v[i].y; d[2] = v[i].z; d[3] = v[i].w; }
;   __builtin_amdgcn_wave_barrier(); asm volatile("s_waitcnt lgkmcnt(0)" ::: "memory");
;   const int c = lane & 7;
; #pragma unroll
;   for (int j = 0; j < 4; ++j) { const int nl = (lane >> 3) + 8 * j, n = n0 + nl; const float* s = scr + (8 * c) * 33 + nl;
;     u32x4 o; o.x = pk2(s[0 * 33], s[1 * 33]); o.y = pk2(s[2 * 33], s[3 * 33]); o.z = pk2(s[4 * 33], s[5 * 33]); o.w = pk2(s[6 * 33], s[7 * 33]);
;     const int row = n + (n >> 7) * rstep + roff;
;     __builtin_nontemporal_store(o, (u32x4*)(WT + (size_t)row * K + k0 + 8 * c)); }
;   __builtin_amdgcn_wave_barrier(); asm volatile("s_waitcnt lgkmcnt(0)" ::: "memory");
; __device__ __forceinline__ void convert_item(const P& p, int it, float* scr, int lane) {
;     ...
;     const int idx = it - IT_DENSE, m = idx / IT_EXP, sub = idx % IT_EXP, le = m / 3, which = m % 3;
;     if (which == 0) transpose_item(p.wg + (size_t)le * DM * EFF, DM, EFF, WSP(bf16_t, WS_WGU) + (size_t)le * 1024 * DM, 128, 0, scr, sub, lane);
;     else if (which == 1) transpose_item(p.wu + (size_t)le * DM * EFF, DM, EFF, WSP(bf16_t, WS_WGU) + (size_t)le * 1024 * DM, 128, 128, scr, sub, lane);
;     else transpose_item(p.wd + (size_t)le * EFF * DM, EFF, DM, WSP(bf16_t, WS_WD) + (size_t)le * DM * EFF, 0, 0, scr, sub, lane);
; __device__ __forceinline__ void convert_item_n(const P& p, int n, float* scr, int lane) {
;   int it;
;   if (n < CV_E0) it = n; else if (n < CV_D1) it = IT_DENSE + (n - CV_E0); else if (n < CV_E1) it = (IT_WIN + IT_WOUT) + (n - CV_D1); else { const int k = n - CV_E1;
;     if (k < NEXP * 2 * IT_EXP) { const int m = k / IT_EXP; it = IT_DENSE + ((NEXP + (m >> 1)) * 3 + (m & 1)) * IT_EXP + k % IT_EXP; }
;     else { const int k2 = k - NEXP * 2 * IT_EXP; it = IT_DENSE + ((NEXP + k2 / IT_EXP) * 3 + 2) * IT_EXP + k2 % IT_EXP; } }
.LBB0_573:
	s_add_i32 s6, s19, 0x2000
	s_cmpk_lt_i32 s19, 0x2000
	s_cselect_b32 s15, s19, s6
	s_cmpk_gt_i32 s15, 0x3fff
	s_mov_b64 s[6:7], -1
	s_cbranch_scc0 .LBB0_583
	s_add_i32 s6, s15, 0xffffc000
	s_lshr_b32 s7, s6, 9
	s_mul_i32 s6, s6, 0xaaab
	s_lshr_b32 s24, s6, 26
	s_mul_i32 s6, s7, 0xab
	s_bfe_u32 s6, s6, 0x70009
	s_mul_i32 s6, s6, 3
	s_sub_i32 s6, s7, s6
	s_and_b32 s14, s15, 0x1ff
	s_lshl_b32 s23, s24, 22
	s_lshl_b32 s22, s15, 5
	s_and_b32 s30, s6, 0xff
	s_cmp_lt_i32 s30, 1
	s_mov_b64 s[6:7], -1
	s_cbranch_scc1 .LBB0_580
	s_and_b32 s6, 0xffff, s30
	s_cmp_lg_u32 s6, 1
	s_mov_b64 s[6:7], -1
	s_cbranch_scc0 .LBB0_577
	v_readlane_b32 s6, v255, 25
	v_readlane_b32 s7, v255, 26
	s_add_u32 s31, s6, s23
	s_addc_u32 s35, s7, 0
	s_lshl_b32 s6, s24, 21
	s_add_u32 s7, s4, s6
	s_addc_u32 s24, s5, 0
	s_and_b32 s6, s22, 0x7e0
	s_and_b32 s30, s15, 0x1c0
	s_lshl_b32 s34, s6, 2
	v_add_u32_e32 v10, s30, v7
	s_add_u32 s34, s31, s34
	s_addc_u32 s35, s35, 0
	v_lshlrev_b32_e32 v96, 2, v6
	v_ashrrev_i32_e32 v11, 31, v10
	v_lshl_add_u64 v[18:19], s[34:35], 0, v[96:97]
	v_lshlrev_b64 v[10:11], 13, v[10:11]
	v_lshl_add_u64 v[10:11], v[18:19], 0, v[10:11]
	s_mov_b32 s31, 0x10000
	v_add_co_u32_e32 v22, vcc, s31, v10
	s_mov_b32 s31, 0x20000
	s_nop 0
	v_addc_co_u32_e32 v23, vcc, 0, v11, vcc
	global_load_dwordx4 v[18:21], v[10:11], off nt
	v_add_co_u32_e32 v26, vcc, s31, v10
	global_load_dwordx4 v[22:25], v[22:23], off nt
	s_nop 0
	v_addc_co_u32_e32 v27, vcc, 0, v11, vcc
	s_mov_b32 s31, 0x30000
	global_load_dwordx4 v[26:29], v[26:27], off nt
	v_add_co_u32_e32 v30, vcc, s31, v10
	s_mov_b32 s31, 0x40000
	s_nop 0
	v_addc_co_u32_e32 v31, vcc, 0, v11, vcc
	global_load_dwordx4 v[30:33], v[30:31], off nt
	v_add_co_u32_e32 v34, vcc, s31, v10
	s_mov_b32 s31, 0x50000
	s_nop 0
	v_addc_co_u32_e32 v35, vcc, 0, v11, vcc
	global_load_dwordx4 v[34:37], v[34:35], off nt
	v_add_co_u32_e32 v38, vcc, s31, v10
	s_mov_b32 s31, 0x60000
	s_nop 0
	v_addc_co_u32_e32 v39, vcc, 0, v11, vcc
	global_load_dwordx4 v[38:41], v[38:39], off nt
	v_add_co_u32_e32 v42, vcc, s31, v10
	s_mov_b32 s31, 0x70000
	s_nop 0
	v_addc_co_u32_e32 v43, vcc, 0, v11, vcc
	global_load_dwordx4 v[42:45], v[42:43], off nt
	v_add_co_u32_e32 v10, vcc, s31, v10
	s_lshl_b32 s30, s30, 1
	s_nop 0
	v_addc_co_u32_e32 v11, vcc, 0, v11, vcc
	global_load_dwordx4 v[46:49], v[10:11], off nt
	v_add_u32_e32 v10, v9, v12
	v_add_u32_e32 v11, 0x420, v10
	s_add_u32 s30, s7, s30
	s_addc_u32 s31, s24, 0
	v_lshlrev_b32_e32 v96, 1, v8
	s_waitcnt vmcnt(7)
	ds_write2_b32 v10, v18, v19 offset1:1
	ds_write2_b32 v10, v20, v21 offset0:2 offset1:3
	s_waitcnt vmcnt(6)
	ds_write2_b32 v11, v22, v23 offset1:1
	v_add_u32_e32 v11, 0x428, v10
	ds_write2_b32 v11, v24, v25 offset1:1
	v_add_u32_e32 v11, 0x840, v10
	s_waitcnt vmcnt(5)
	ds_write2_b32 v11, v26, v27 offset1:1
	v_add_u32_e32 v11, 0x848, v10
	ds_write2_b32 v11, v28, v29 offset1:1
	v_add_u32_e32 v11, 0xc60, v10
	v_add_u32_e32 v22, s6, v7
	v_ashrrev_i32_e32 v23, 31, v22
	s_waitcnt vmcnt(4)
	ds_write2_b32 v11, v30, v31 offset1:1
	v_add_u32_e32 v11, 0xc68, v10
	ds_write2_b32 v11, v32, v33 offset1:1
	v_add_u32_e32 v11, 0x1080, v10
	v_lshlrev_b64 v[22:23], 10, v[22:23]
	s_waitcnt vmcnt(3)
	ds_write2_b32 v11, v34, v35 offset1:1
	v_add_u32_e32 v11, 0x1088, v10
	ds_write2_b32 v11, v36, v37 offset1:1
	v_add_u32_e32 v11, 0x14a0, v10
	s_waitcnt vmcnt(2)
	ds_write2_b32 v11, v38, v39 offset1:1
	v_add_u32_e32 v11, 0x14a8, v10
	ds_write2_b32 v11, v40, v41 offset1:1
	v_add_u32_e32 v11, 0x18c0, v10
	s_waitcnt vmcnt(1)
	ds_write2_b32 v11, v42, v43 offset1:1
	v_add_u32_e32 v11, 0x18c8, v10
	ds_write2_b32 v11, v44, v45 offset1:1
	v_add_u32_e32 v11, 0x1ce0, v10
	v_add_u32_e32 v10, 0x1ce8, v10
	s_waitcnt vmcnt(0)
	ds_write2_b32 v11, v46, v47 offset1:1
	ds_write2_b32 v10, v48, v49 offset1:1
	s_waitcnt lgkmcnt(0)
	ds_read2_b32 v[214:215], v17 offset1:33
	ds_read2_b32 v[222:223], v17 offset0:66 offset1:99
	ds_read2_b32 v[224:225], v17 offset0:132 offset1:165
	ds_read2_b32 v[226:227], v17 offset0:198 offset1:231
	ds_read2_b32 v[228:229], v17 offset0:8 offset1:41
	ds_read2_b32 v[230:231], v17 offset0:74 offset1:107
	ds_read2_b32 v[232:233], v17 offset0:140 offset1:173
	ds_read2_b32 v[234:235], v17 offset0:206 offset1:239
	s_waitcnt lgkmcnt(0)
	ds_read2_b32 v[236:237], v17 offset0:16 offset1:49
	ds_read2_b32 v[238:239], v17 offset0:82 offset1:115
	ds_read2_b32 v[240:241], v17 offset0:148 offset1:181
	ds_read2_b32 v[242:243], v17 offset0:214 offset1:247
	ds_read2_b32 v[244:245], v17 offset0:24 offset1:57
	ds_read2_b32 v[246:247], v17 offset0:90 offset1:123
	ds_read2_b32 v[248:249], v17 offset0:156 offset1:189
	ds_read2_b32 v[250:251], v17 offset0:222 offset1:255
	v_lshl_add_u64 v[10:11], s[30:31], 0, v[96:97]
	v_cvt_pk_bf16_f32 v18, v214, v215
	v_cvt_pk_bf16_f32 v19, v222, v223
	v_lshl_add_u64 v[22:23], v[10:11], 0, v[22:23]
	v_cvt_pk_bf16_f32 v20, v224, v225
	v_cvt_pk_bf16_f32 v21, v226, v227
	global_store_dwordx4 v[22:23], v[18:21], off nt
	s_nop 1
	v_add_u32_e32 v22, s6, v13
	v_ashrrev_i32_e32 v23, 31, v22
	v_cvt_pk_bf16_f32 v18, v228, v229
	v_lshlrev_b64 v[22:23], 10, v[22:23]
	v_cvt_pk_bf16_f32 v19, v230, v231
	v_lshl_add_u64 v[22:23], v[10:11], 0, v[22:23]
	v_cvt_pk_bf16_f32 v20, v232, v233
	v_cvt_pk_bf16_f32 v21, v234, v235
	global_store_dwordx4 v[22:23], v[18:21], off nt
	s_nop 1
	v_add_u32_e32 v22, s6, v15
	s_waitcnt lgkmcnt(0)
	v_ashrrev_i32_e32 v23, 31, v22
	v_cvt_pk_bf16_f32 v18, v236, v237
	v_lshlrev_b64 v[22:23], 10, v[22:23]
	v_cvt_pk_bf16_f32 v19, v238, v239
	v_lshl_add_u64 v[22:23], v[10:11], 0, v[22:23]
	v_cvt_pk_bf16_f32 v20, v240, v241
	v_cvt_pk_bf16_f32 v21, v242, v243
	global_store_dwordx4 v[22:23], v[18:21], off nt
	s_nop 1
	v_add_u32_e32 v22, s6, v16
	v_ashrrev_i32_e32 v23, 31, v22
	v_cvt_pk_bf16_f32 v18, v244, v245
	v_lshlrev_b64 v[22:23], 10, v[22:23]
	v_cvt_pk_bf16_f32 v19, v246, v247
	v_lshl_add_u64 v[10:11], v[10:11], 0, v[22:23]
	v_cvt_pk_bf16_f32 v20, v248, v249
	v_cvt_pk_bf16_f32 v21, v250, v251
	global_store_dwordx4 v[10:11], v[18:21], off nt
	s_nop 1
	s_waitcnt lgkmcnt(0)
	s_mov_b64 s[6:7], 0
; __device__ __forceinline__ unsigned pk2(float lo, float hi) { unsigned r; asm volatile("v_cvt_pk_bf16_f32 %0, %1, %2" : "=v"(r) : "v"(lo), "v"(hi)); return r; }
; __device__ __forceinline__ void transpose_item(const float* W, int K, int N, bf16_t* WT, int rstep, int roff, float* scr, int item, int lane) {
;   const int nblk = N / 32, kb = item / nblk, nb = item % nblk, k0 = 64 * kb, n0 = 32 * nb;
;   f32x4 v[8];
; #pragma unroll
;   for (int i = 0; i < 8; ++i) v[i] = __builtin_nontemporal_load((const f32x4*)(W + (size_t)(k0 + i * 8 + (lane >> 3)) * N + n0 + (lane & 7) * 4));
; #pragma unroll
;   for (int i = 0; i < 8; ++i) { float* d = scr + (i * 8 + (lane >> 3)) * 33 + (lane & 7) * 4; d[0] = v[i].x; d[1] = v[i].y; d[2] = v[i].z; d[3] = v[i].w; }
;   __builtin_amdgcn_wave_barrier(); asm volatile("s_waitcnt lgkmcnt(0)" ::: "memory");
;   const int c = lane & 7;
; #pragma unroll
;   for (int j = 0; j < 4; ++j) { const int nl = (lane >> 3) + 8 * j, n = n0 + nl; const float* s = scr + (8 * c) * 33 + nl;
;     u32x4 o; o.x = pk2(s[0 * 33], s[1 * 33]); o.y = pk2(s[2 * 33], s[3 * 33]); o.z = pk2(s[4 * 33], s[5 * 33]); o.w = pk2(s[6 * 33], s[7 * 33]);
;     const int row = n + (n >> 7) * rstep + roff;
;     __builtin_nontemporal_store(o, (u32x4*)(WT + (size_t)row * K + k0 + 8 * c)); }
;   __builtin_amdgcn_wave_barrier(); asm volatile("s_waitcnt lgkmcnt(0)" ::: "memory");
; __device__ __forceinline__ void convert_item(const P& p, int it, float* scr, int lane) {
;     ...
;     else if (which == 1) transpose_item(p.wu + (size_t)le * DM * EFF, DM, EFF, WSP(bf16_t, WS_WGU) + (size_t)le * 1024 * DM, 128, 128, scr, sub, lane);
.LBB0_577:
	s_andn2_b64 vcc, exec, s[6:7]
	s_cbranch_vccnz .LBB0_579
	s_add_u32 s31, s70, s23
	s_addc_u32 s35, s71, 0
	s_add_u32 s7, s2, s23
	s_addc_u32 s24, s3, 0
	s_lshl_b32 s6, s14, 2
	s_and_b32 s30, s6, 0x7c0
	s_and_b32 s6, s22, 0x1e0
	s_lshl_b32 s34, s6, 2
	v_add_u32_e32 v10, s30, v7
	s_add_u32 s34, s31, s34
	s_addc_u32 s35, s35, 0
	v_lshlrev_b32_e32 v96, 2, v6
	v_ashrrev_i32_e32 v11, 31, v10
	v_lshl_add_u64 v[18:19], s[34:35], 0, v[96:97]
	v_lshlrev_b64 v[10:11], 11, v[10:11]
	v_lshl_add_u64 v[10:11], v[18:19], 0, v[10:11]
	s_movk_i32 s31, 0x4000
	v_add_co_u32_e32 v22, vcc, s31, v10
	s_mov_b32 s31, 0x8000
	s_nop 0
	v_addc_co_u32_e32 v23, vcc, 0, v11, vcc
	global_load_dwordx4 v[18:21], v[10:11], off nt
	v_add_co_u32_e32 v26, vcc, s31, v10
	global_load_dwordx4 v[22:25], v[22:23], off nt
	s_nop 0
	v_addc_co_u32_e32 v27, vcc, 0, v11, vcc
	global_load_dwordx4 v[26:29], v[26:27], off nt
	v_add_co_u32_e32 v30, vcc, s38, v10
	s_mov_b32 s31, 0x10000
	s_nop 0
	v_addc_co_u32_e32 v31, vcc, 0, v11, vcc
	global_load_dwordx4 v[30:33], v[30:31], off nt
	v_add_co_u32_e32 v34, vcc, s31, v10
	s_mov_b32 s31, 0x14000
	s_nop 0
	v_addc_co_u32_e32 v35, vcc, 0, v11, vcc
	global_load_dwordx4 v[34:37], v[34:35], off nt
	v_add_co_u32_e32 v38, vcc, s31, v10
	s_lshl_b32 s30, s30, 1
	s_nop 0
	v_addc_co_u32_e32 v39, vcc, 0, v11, vcc
	global_load_dwordx4 v[38:41], v[38:39], off nt
	v_add_co_u32_e32 v42, vcc, s93, v10
	s_add_u32 s30, s7, s30
	s_nop 0
	v_addc_co_u32_e32 v43, vcc, 0, v11, vcc
	global_load_dwordx4 v[42:45], v[42:43], off nt
	v_add_co_u32_e32 v10, vcc, s96, v10
	s_movk_i32 s7, 0x80
	s_nop 0
	v_addc_co_u32_e32 v11, vcc, 0, v11, vcc
	global_load_dwordx4 v[46:49], v[10:11], off nt
	v_add_u32_e32 v10, v9, v12
	v_add_u32_e32 v11, 0x420, v10
	s_addc_u32 s31, s24, 0
	v_lshlrev_b32_e32 v96, 1, v8
	s_waitcnt vmcnt(7)
	ds_write2_b32 v10, v18, v19 offset1:1
	ds_write2_b32 v10, v20, v21 offset0:2 offset1:3
	s_waitcnt vmcnt(6)
	ds_write2_b32 v11, v22, v23 offset1:1
	v_add_u32_e32 v11, 0x428, v10
	ds_write2_b32 v11, v24, v25 offset1:1
	v_add_u32_e32 v11, 0x840, v10
	s_waitcnt vmcnt(5)
	ds_write2_b32 v11, v26, v27 offset1:1
	v_add_u32_e32 v11, 0x848, v10
	ds_write2_b32 v11, v28, v29 offset1:1
	v_add_u32_e32 v11, 0xc60, v10
	v_add_u32_e32 v24, s6, v7
	s_waitcnt vmcnt(4)
	ds_write2_b32 v11, v30, v31 offset1:1
	v_add_u32_e32 v11, 0xc68, v10
	ds_write2_b32 v11, v32, v33 offset1:1
	v_add_u32_e32 v11, 0x1080, v10
	s_waitcnt vmcnt(3)
	ds_write2_b32 v11, v34, v35 offset1:1
	v_add_u32_e32 v11, 0x1088, v10
	ds_write2_b32 v11, v36, v37 offset1:1
	v_add_u32_e32 v11, 0x14a0, v10
	s_waitcnt vmcnt(2)
	ds_write2_b32 v11, v38, v39 offset1:1
	v_add_u32_e32 v11, 0x14a8, v10
	ds_write2_b32 v11, v40, v41 offset1:1
	v_add_u32_e32 v11, 0x18c0, v10
	s_waitcnt vmcnt(1)
	ds_write2_b32 v11, v42, v43 offset1:1
	v_add_u32_e32 v11, 0x18c8, v10
	ds_write2_b32 v11, v44, v45 offset1:1
	v_add_u32_e32 v11, 0x1ce0, v10
	v_add_u32_e32 v10, 0x1ce8, v10
	s_waitcnt vmcnt(0)
	ds_write2_b32 v11, v46, v47 offset1:1
	ds_write2_b32 v10, v48, v49 offset1:1
	s_waitcnt lgkmcnt(0)
	ds_read2_b32 v[214:215], v17 offset1:33
	ds_read2_b32 v[222:223], v17 offset0:66 offset1:99
	ds_read2_b32 v[224:225], v17 offset0:132 offset1:165
	ds_read2_b32 v[226:227], v17 offset0:198 offset1:231
	ds_read2_b32 v[228:229], v17 offset0:8 offset1:41
	ds_read2_b32 v[230:231], v17 offset0:74 offset1:107
	ds_read2_b32 v[232:233], v17 offset0:140 offset1:173
	ds_read2_b32 v[234:235], v17 offset0:206 offset1:239
	s_waitcnt lgkmcnt(0)
	ds_read2_b32 v[236:237], v17 offset0:16 offset1:49
	ds_read2_b32 v[238:239], v17 offset0:82 offset1:115
	ds_read2_b32 v[240:241], v17 offset0:148 offset1:181
	ds_read2_b32 v[242:243], v17 offset0:214 offset1:247
	ds_read2_b32 v[244:245], v17 offset0:24 offset1:57
	ds_read2_b32 v[246:247], v17 offset0:90 offset1:123
	ds_read2_b32 v[248:249], v17 offset0:156 offset1:189
	ds_read2_b32 v[250:251], v17 offset0:222 offset1:255
	v_cvt_pk_bf16_f32 v18, v214, v215
	v_cvt_pk_bf16_f32 v19, v222, v223
	v_cvt_pk_bf16_f32 v20, v224, v225
	v_cvt_pk_bf16_f32 v21, v226, v227
	v_and_b32_e32 v22, 0xffffff80, v24
	v_add3_u32 v22, v24, v22, s7
	v_ashrrev_i32_e32 v23, 31, v22
	v_lshl_add_u64 v[10:11], s[30:31], 0, v[96:97]
	v_lshlrev_b64 v[22:23], 12, v[22:23]
	v_lshl_add_u64 v[22:23], v[10:11], 0, v[22:23]
	global_store_dwordx4 v[22:23], v[18:21], off nt
	s_nop 1
	v_add_u32_e32 v24, s6, v13
	v_cvt_pk_bf16_f32 v18, v228, v229
	v_cvt_pk_bf16_f32 v19, v230, v231
	v_cvt_pk_bf16_f32 v20, v232, v233
	v_cvt_pk_bf16_f32 v21, v234, v235
	v_and_b32_e32 v22, 0xffffff80, v24
	v_add3_u32 v22, v24, v22, s7
	v_ashrrev_i32_e32 v23, 31, v22
	v_lshlrev_b64 v[22:23], 12, v[22:23]
	v_lshl_add_u64 v[22:23], v[10:11], 0, v[22:23]
	global_store_dwordx4 v[22:23], v[18:21], off nt
	s_nop 1
	s_waitcnt lgkmcnt(0)
	v_add_u32_e32 v24, s6, v15
	v_cvt_pk_bf16_f32 v18, v236, v237
	v_cvt_pk_bf16_f32 v19, v238, v239
	v_cvt_pk_bf16_f32 v20, v240, v241
	v_cvt_pk_bf16_f32 v21, v242, v243
	v_and_b32_e32 v22, 0xffffff80, v24
	v_add3_u32 v22, v24, v22, s7
	v_ashrrev_i32_e32 v23, 31, v22
	v_lshlrev_b64 v[22:23], 12, v[22:23]
	v_lshl_add_u64 v[22:23], v[10:11], 0, v[22:23]
	global_store_dwordx4 v[22:23], v[18:21], off nt
	s_nop 1
	v_add_u32_e32 v24, s6, v16
	v_cvt_pk_bf16_f32 v18, v244, v245
	v_cvt_pk_bf16_f32 v19, v246, v247
	v_cvt_pk_bf16_f32 v20, v248, v249
	v_cvt_pk_bf16_f32 v21, v250, v251
	v_and_b32_e32 v22, 0xffffff80, v24
	v_add3_u32 v22, v24, v22, s7
	v_ashrrev_i32_e32 v23, 31, v22
	v_lshlrev_b64 v[22:23], 12, v[22:23]
	v_lshl_add_u64 v[10:11], v[10:11], 0, v[22:23]
	global_store_dwordx4 v[10:11], v[18:21], off nt
	s_nop 1
	s_waitcnt lgkmcnt(0)

; __device__ __forceinline__ unsigned pk2(float lo, float hi) { unsigned r; asm volatile("v_cvt_pk_bf16_f32 %0, %1, %2" : "=v"(r) : "v"(lo), "v"(hi)); return r; }
; __device__ __forceinline__ void transpose_item(const float* W, int K, int N, bf16_t* WT, int rstep, int roff, float* scr, int item, int lane) {
;   const int nblk = N / 32, kb = item / nblk, nb = item % nblk, k0 = 64 * kb, n0 = 32 * nb;
;   f32x4 v[8];
; #pragma unroll
;   for (int i = 0; i < 8; ++i) v[i] = __builtin_nontemporal_load((const f32x4*)(W + (size_t)(k0 + i * 8 + (lane >> 3)) * N + n0 + (lane & 7) * 4));
; #pragma unroll
;   for (int i = 0; i < 8; ++i) { float* d = scr + (i * 8 + (lane >> 3)) * 33 + (lane & 7) * 4; d[0] = v[i].x; d[1] = v[i].y; d[2] = v[i].z; d[3] = v[i].w; }
;   __builtin_amdgcn_wave_barrier(); asm volatile("s_waitcnt lgkmcnt(0)" ::: "memory");
;   const int c = lane & 7;
; #pragma unroll
;   for (int j = 0; j < 4; ++j) { const int nl = (lane >> 3) + 8 * j, n = n0 + nl; const float* s = scr + (8 * c) * 33 + nl;
;     u32x4 o; o.x = pk2(s[0 * 33], s[1 * 33]); o.y = pk2(s[2 * 33], s[3 * 33]); o.z = pk2(s[4 * 33], s[5 * 33]); o.w = pk2(s[6 * 33], s[7 * 33]);
;     const int row = n + (n >> 7) * rstep + roff;
;     __builtin_nontemporal_store(o, (u32x4*)(WT + (size_t)row * K + k0 + 8 * c)); }
;   __builtin_amdgcn_wave_barrier(); asm volatile("s_waitcnt lgkmcnt(0)" ::: "memory");
; __device__ __forceinline__ void convert_item(const P& p, int it, float* scr, int lane) {
;     ...
;     if (which == 0) transpose_item(p.wg + (size_t)le * DM * EFF, DM, EFF, WSP(bf16_t, WS_WGU) + (size_t)le * 1024 * DM, 128, 0, scr, sub, lane);
.LBB0_580:
	s_andn2_b64 vcc, exec, s[6:7]
	s_cbranch_vccnz .LBB0_582
	s_add_u32 s24, s68, s23
	s_addc_u32 s31, s69, 0
	s_add_u32 s7, s2, s23
	s_addc_u32 s23, s3, 0
	s_lshl_b32 s6, s14, 2
	s_and_b32 s14, s6, 0x7c0
	s_and_b32 s6, s22, 0x1e0
	s_lshl_b32 s22, s6, 2
	v_add_u32_e32 v10, s14, v7
	s_add_u32 s30, s24, s22
	s_addc_u32 s31, s31, 0
	v_lshlrev_b32_e32 v96, 2, v6
	v_ashrrev_i32_e32 v11, 31, v10
	v_lshl_add_u64 v[18:19], s[30:31], 0, v[96:97]
	v_lshlrev_b64 v[10:11], 11, v[10:11]
	v_lshl_add_u64 v[10:11], v[18:19], 0, v[10:11]
	s_movk_i32 s22, 0x4000
	v_add_co_u32_e32 v22, vcc, s22, v10
	s_mov_b32 s22, 0x8000
	s_nop 0
	v_addc_co_u32_e32 v23, vcc, 0, v11, vcc
	global_load_dwordx4 v[18:21], v[10:11], off nt
	v_add_co_u32_e32 v26, vcc, s22, v10
	global_load_dwordx4 v[22:25], v[22:23], off nt
	s_nop 0
	v_addc_co_u32_e32 v27, vcc, 0, v11, vcc
	global_load_dwordx4 v[26:29], v[26:27], off nt
	v_add_co_u32_e32 v30, vcc, s38, v10
	s_mov_b32 s22, 0x10000
	s_nop 0
	v_addc_co_u32_e32 v31, vcc, 0, v11, vcc
	global_load_dwordx4 v[30:33], v[30:31], off nt
	v_add_co_u32_e32 v34, vcc, s22, v10
	s_mov_b32 s22, 0x14000
	s_nop 0
	v_addc_co_u32_e32 v35, vcc, 0, v11, vcc
	global_load_dwordx4 v[34:37], v[34:35], off nt
	v_add_co_u32_e32 v38, vcc, s22, v10
	s_lshl_b32 s14, s14, 1
	s_nop 0
	v_addc_co_u32_e32 v39, vcc, 0, v11, vcc
	global_load_dwordx4 v[38:41], v[38:39], off nt
	v_add_co_u32_e32 v42, vcc, s93, v10
	s_add_u32 s22, s7, s14
	s_nop 0
	v_addc_co_u32_e32 v43, vcc, 0, v11, vcc
	global_load_dwordx4 v[42:45], v[42:43], off nt
	v_add_co_u32_e32 v10, vcc, s96, v10
	s_addc_u32 s23, s23, 0
	s_nop 0
	v_addc_co_u32_e32 v11, vcc, 0, v11, vcc
	global_load_dwordx4 v[46:49], v[10:11], off nt
	v_add_u32_e32 v10, v9, v12
	v_add_u32_e32 v11, 0x420, v10
	v_lshlrev_b32_e32 v96, 1, v8
	s_waitcnt vmcnt(7)
	ds_write2_b32 v10, v18, v19 offset1:1
	ds_write2_b32 v10, v20, v21 offset0:2 offset1:3
	s_waitcnt vmcnt(6)
	ds_write2_b32 v11, v22, v23 offset1:1
	v_add_u32_e32 v11, 0x428, v10
	ds_write2_b32 v11, v24, v25 offset1:1
	v_add_u32_e32 v11, 0x840, v10
	s_waitcnt vmcnt(5)
	ds_write2_b32 v11, v26, v27 offset1:1
	v_add_u32_e32 v11, 0x848, v10
	ds_write2_b32 v11, v28, v29 offset1:1
	v_add_u32_e32 v11, 0xc60, v10
	v_add_u32_e32 v24, s6, v7
	s_waitcnt vmcnt(4)
	ds_write2_b32 v11, v30, v31 offset1:1
	v_add_u32_e32 v11, 0xc68, v10
	ds_write2_b32 v11, v32, v33 offset1:1
	v_add_u32_e32 v11, 0x1080, v10
	s_waitcnt vmcnt(3)
	ds_write2_b32 v11, v34, v35 offset1:1
	v_add_u32_e32 v11, 0x1088, v10
	ds_write2_b32 v11, v36, v37 offset1:1
	v_add_u32_e32 v11, 0x14a0, v10
	s_waitcnt vmcnt(2)
	ds_write2_b32 v11, v38, v39 offset1:1
	v_add_u32_e32 v11, 0x14a8, v10
	ds_write2_b32 v11, v40, v41 offset1:1
	v_add_u32_e32 v11, 0x18c0, v10
	s_waitcnt vmcnt(1)
	ds_write2_b32 v11, v42, v43 offset1:1
	v_add_u32_e32 v11, 0x18c8, v10
	ds_write2_b32 v11, v44, v45 offset1:1
	v_add_u32_e32 v11, 0x1ce0, v10
	v_add_u32_e32 v10, 0x1ce8, v10
	s_waitcnt vmcnt(0)
	ds_write2_b32 v11, v46, v47 offset1:1
	ds_write2_b32 v10, v48, v49 offset1:1
	s_waitcnt lgkmcnt(0)
	ds_read2_b32 v[214:215], v17 offset1:33
	ds_read2_b32 v[222:223], v17 offset0:66 offset1:99
	ds_read2_b32 v[224:225], v17 offset0:132 offset1:165
	ds_read2_b32 v[226:227], v17 offset0:198 offset1:231
	ds_read2_b32 v[228:229], v17 offset0:8 offset1:41
	ds_read2_b32 v[230:231], v17 offset0:74 offset1:107
	ds_read2_b32 v[232:233], v17 offset0:140 offset1:173
	ds_read2_b32 v[234:235], v17 offset0:206 offset1:239
	s_waitcnt lgkmcnt(0)
	ds_read2_b32 v[236:237], v17 offset0:16 offset1:49
	ds_read2_b32 v[238:239], v17 offset0:82 offset1:115
	ds_read2_b32 v[240:241], v17 offset0:148 offset1:181
	ds_read2_b32 v[242:243], v17 offset0:214 offset1:247
	ds_read2_b32 v[244:245], v17 offset0:24 offset1:57
	ds_read2_b32 v[246:247], v17 offset0:90 offset1:123
	ds_read2_b32 v[248:249], v17 offset0:156 offset1:189
	ds_read2_b32 v[250:251], v17 offset0:222 offset1:255
	v_cvt_pk_bf16_f32 v18, v214, v215
	v_cvt_pk_bf16_f32 v19, v222, v223
	v_cvt_pk_bf16_f32 v20, v224, v225
	v_cvt_pk_bf16_f32 v21, v226, v227
	v_and_b32_e32 v22, 0xffffff80, v24
	v_add_u32_e32 v22, v22, v24
	v_ashrrev_i32_e32 v23, 31, v22
	v_lshl_add_u64 v[10:11], s[22:23], 0, v[96:97]
	v_lshlrev_b64 v[22:23], 12, v[22:23]
	v_lshl_add_u64 v[22:23], v[10:11], 0, v[22:23]
	global_store_dwordx4 v[22:23], v[18:21], off nt
	s_nop 1
	v_add_u32_e32 v24, s6, v13
	v_cvt_pk_bf16_f32 v18, v228, v229
	v_cvt_pk_bf16_f32 v19, v230, v231
	v_cvt_pk_bf16_f32 v20, v232, v233
	v_cvt_pk_bf16_f32 v21, v234, v235
	v_and_b32_e32 v22, 0xffffff80, v24
	v_add_u32_e32 v22, v22, v24
	v_ashrrev_i32_e32 v23, 31, v22
	v_lshlrev_b64 v[22:23], 12, v[22:23]
	v_lshl_add_u64 v[22:23], v[10:11], 0, v[22:23]
	global_store_dwordx4 v[22:23], v[18:21], off nt
	s_nop 1
	s_waitcnt lgkmcnt(0)
	v_add_u32_e32 v24, s6, v15
	v_cvt_pk_bf16_f32 v18, v236, v237
	v_cvt_pk_bf16_f32 v19, v238, v239
	v_cvt_pk_bf16_f32 v20, v240, v241
	v_cvt_pk_bf16_f32 v21, v242, v243
	v_and_b32_e32 v22, 0xffffff80, v24
	v_add_u32_e32 v22, v22, v24
	v_ashrrev_i32_e32 v23, 31, v22
	v_lshlrev_b64 v[22:23], 12, v[22:23]
	v_lshl_add_u64 v[22:23], v[10:11], 0, v[22:23]
	global_store_dwordx4 v[22:23], v[18:21], off nt
	s_nop 1
	v_add_u32_e32 v24, s6, v16
	v_cvt_pk_bf16_f32 v18, v244, v245
	v_cvt_pk_bf16_f32 v19, v246, v247
	v_cvt_pk_bf16_f32 v20, v248, v249
	v_cvt_pk_bf16_f32 v21, v250, v251
	v_and_b32_e32 v22, 0xffffff80, v24
	v_add_u32_e32 v22, v22, v24
	v_ashrrev_i32_e32 v23, 31, v22
	v_lshlrev_b64 v[22:23], 12, v[22:23]
	v_lshl_add_u64 v[10:11], v[10:11], 0, v[22:23]
	global_store_dwordx4 v[10:11], v[18:21], off nt
	s_nop 1
	s_waitcnt lgkmcnt(0)

; __device__ __forceinline__ unsigned pk2(float lo, float hi) { unsigned r; asm volatile("v_cvt_pk_bf16_f32 %0, %1, %2" : "=v"(r) : "v"(lo), "v"(hi)); return r; }
; __device__ __forceinline__ void transpose_item(const float* W, int K, int N, bf16_t* WT, int rstep, int roff, float* scr, int item, int lane) {
;   const int nblk = N / 32, kb = item / nblk, nb = item % nblk, k0 = 64 * kb, n0 = 32 * nb;
;   f32x4 v[8];
; #pragma unroll
;   for (int i = 0; i < 8; ++i) v[i] = __builtin_nontemporal_load((const f32x4*)(W + (size_t)(k0 + i * 8 + (lane >> 3)) * N + n0 + (lane & 7) * 4));
; #pragma unroll
;   for (int i = 0; i < 8; ++i) { float* d = scr + (i * 8 + (lane >> 3)) * 33 + (lane & 7) * 4; d[0] = v[i].x; d[1] = v[i].y; d[2] = v[i].z; d[3] = v[i].w; }
;   __builtin_amdgcn_wave_barrier(); asm volatile("s_waitcnt lgkmcnt(0)" ::: "memory");
;   const int c = lane & 7;
; #pragma unroll
;   for (int j = 0; j < 4; ++j) { const int nl = (lane >> 3) + 8 * j, n = n0 + nl; const float* s = scr + (8 * c) * 33 + nl;
;     u32x4 o; o.x = pk2(s[0 * 33], s[1 * 33]); o.y = pk2(s[2 * 33], s[3 * 33]); o.z = pk2(s[4 * 33], s[5 * 33]); o.w = pk2(s[6 * 33], s[7 * 33]);
;     const int row = n + (n >> 7) * rstep + roff;
;     __builtin_nontemporal_store(o, (u32x4*)(WT + (size_t)row * K + k0 + 8 * c)); }
;   __builtin_amdgcn_wave_barrier(); asm volatile("s_waitcnt lgkmcnt(0)" ::: "memory");
; __device__ __forceinline__ void convert_item(const P& p, int it, float* scr, int lane) {
;   if (it < IT_DENSE) {
;     const int l = it / (IT_WIN + IT_WOUT), r = it % (IT_WIN + IT_WOUT);
;     if (r < IT_WIN) transpose_item(p.w_in + (size_t)l * DM * INW, DM, INW, WSP(bf16_t, WS_WIN) + (size_t)l * INW * DM, 0, 0, scr, r, lane);
;     else transpose_item(p.w_out + (size_t)l * DM * DM, DM, DM, WSP(bf16_t, WS_WOUT) + (size_t)l * DM * DM, 0, 0, scr, r - IT_WIN, lane);
.LBB0_583:
	s_and_b64 vcc, exec, s[6:7]
	s_cbranch_vccz .LBB0_572
	s_ashr_i32 s6, s15, 31
	s_lshr_b32 s6, s6, 19
	s_add_i32 s6, s15, s6
	s_ashr_i32 s14, s6, 13
	s_and_b32 s6, s6, 0xffffe000
	s_sub_i32 s22, s15, s6
	s_ashr_i32 s15, s14, 31
	v_add_u32_e32 v18, v9, v12
	s_cmpk_gt_i32 s22, 0x17ff
	s_mov_b64 s[6:7], -1
	v_lshlrev_b32_e32 v96, 2, v6
	v_add_u32_e32 v19, 0x420, v18
	v_add_u32_e32 v20, 0x428, v18
	v_add_u32_e32 v21, 0x840, v18
	v_add_u32_e32 v22, 0x848, v18
	v_add_u32_e32 v23, 0xc60, v18
	v_add_u32_e32 v24, 0xc68, v18
	v_add_u32_e32 v25, 0x1080, v18
	v_add_u32_e32 v26, 0x1088, v18
	v_add_u32_e32 v27, 0x14a0, v18
	v_add_u32_e32 v28, 0x14a8, v18
	v_add_u32_e32 v29, 0x18c0, v18
	v_add_u32_e32 v30, 0x18c8, v18
	v_add_u32_e32 v31, 0x1ce0, v18
	v_add_u32_e32 v32, 0x1ce8, v18
	v_lshlrev_b32_e32 v10, 1, v8
	s_cbranch_scc0 .LBB0_586
	s_lshl_b64 s[6:7], s[14:15], 24
	s_add_u32 s23, s62, s6
	s_addc_u32 s24, s63, s7
	s_lshl_b64 s[6:7], s[14:15], 23
	s_add_u32 s15, s9, s6
	s_addc_u32 s30, s16, s7
	s_add_i32 s6, s22, 0xe800
	s_and_b32 s31, s6, 0xffc0
	s_lshl_b32 s6, s22, 5
	s_and_b32 s34, s6, 0x7e0
	s_lshl_b32 s6, s34, 2
	v_add_u32_e32 v34, s31, v7
	s_add_u32 s6, s23, s6
	s_addc_u32 s7, s24, 0
	v_ashrrev_i32_e32 v35, 31, v34
	v_lshl_add_u64 v[36:37], s[6:7], 0, v[96:97]
	v_lshlrev_b64 v[34:35], 13, v[34:35]
	v_lshl_add_u64 v[62:63], v[36:37], 0, v[34:35]
	s_mov_b32 s6, 0x10000
	v_add_co_u32_e32 v38, vcc, s6, v62
	s_mov_b32 s6, 0x20000
	s_nop 0
	v_addc_co_u32_e32 v39, vcc, 0, v63, vcc
	v_add_co_u32_e32 v42, vcc, s6, v62
	s_mov_b32 s6, 0x30000
	s_nop 0
	v_addc_co_u32_e32 v43, vcc, 0, v63, vcc
	v_add_co_u32_e32 v46, vcc, s6, v62
	s_mov_b32 s6, 0x40000
	s_nop 0
	v_addc_co_u32_e32 v47, vcc, 0, v63, vcc
	v_add_co_u32_e32 v50, vcc, s6, v62
	s_mov_b32 s6, 0x50000
	s_nop 0
	v_addc_co_u32_e32 v51, vcc, 0, v63, vcc
	v_add_co_u32_e32 v54, vcc, s6, v62
	global_load_dwordx4 v[34:37], v[62:63], off nt
	s_nop 0
	global_load_dwordx4 v[38:41], v[38:39], off nt
	v_addc_co_u32_e32 v55, vcc, 0, v63, vcc
	global_load_dwordx4 v[42:45], v[42:43], off nt
	s_nop 0
	global_load_dwordx4 v[46:49], v[46:47], off nt
	s_nop 0
	global_load_dwordx4 v[50:53], v[50:51], off nt
	s_nop 0
	global_load_dwordx4 v[54:57], v[54:55], off nt
	s_mov_b32 s6, 0x60000
	v_add_co_u32_e32 v58, vcc, s6, v62
	s_mov_b32 s6, 0x70000
	s_nop 0
	v_addc_co_u32_e32 v59, vcc, 0, v63, vcc
	global_load_dwordx4 v[58:61], v[58:59], off nt
	v_add_co_u32_e32 v62, vcc, s6, v62
	s_lshl_b32 s6, s31, 1
	s_nop 0
	v_addc_co_u32_e32 v63, vcc, 0, v63, vcc
	global_load_dwordx4 v[62:65], v[62:63], off nt
	s_add_u32 s6, s15, s6
	v_mov_b32_e32 v11, v97
	s_addc_u32 s7, s30, 0
	s_waitcnt vmcnt(7)
	ds_write2_b32 v18, v34, v35 offset1:1
	ds_write2_b32 v18, v36, v37 offset0:2 offset1:3
	s_waitcnt vmcnt(6)
	ds_write2_b32 v19, v38, v39 offset1:1
	ds_write2_b32 v20, v40, v41 offset1:1
	s_waitcnt vmcnt(5)
	ds_write2_b32 v21, v42, v43 offset1:1
	ds_write2_b32 v22, v44, v45 offset1:1
	s_waitcnt vmcnt(4)
	ds_write2_b32 v23, v46, v47 offset1:1
	ds_write2_b32 v24, v48, v49 offset1:1
	s_waitcnt vmcnt(3)
	ds_write2_b32 v25, v50, v51 offset1:1
	ds_write2_b32 v26, v52, v53 offset1:1
	s_waitcnt vmcnt(2)
	ds_write2_b32 v27, v54, v55 offset1:1
	ds_write2_b32 v28, v56, v57 offset1:1
	s_waitcnt vmcnt(1)
	ds_write2_b32 v29, v58, v59 offset1:1
	ds_write2_b32 v30, v60, v61 offset1:1
	s_waitcnt vmcnt(0)
	ds_write2_b32 v31, v62, v63 offset1:1
	ds_write2_b32 v32, v64, v65 offset1:1
	s_waitcnt lgkmcnt(0)
	ds_read2_b32 v[214:215], v17 offset1:33
	ds_read2_b32 v[222:223], v17 offset0:66 offset1:99
	ds_read2_b32 v[224:225], v17 offset0:132 offset1:165
	ds_read2_b32 v[226:227], v17 offset0:198 offset1:231
	ds_read2_b32 v[228:229], v17 offset0:8 offset1:41
	ds_read2_b32 v[230:231], v17 offset0:74 offset1:107
	ds_read2_b32 v[232:233], v17 offset0:140 offset1:173
	ds_read2_b32 v[234:235], v17 offset0:206 offset1:239
	s_waitcnt lgkmcnt(0)
	ds_read2_b32 v[236:237], v17 offset0:16 offset1:49
	ds_read2_b32 v[238:239], v17 offset0:82 offset1:115
	ds_read2_b32 v[240:241], v17 offset0:148 offset1:181
	ds_read2_b32 v[242:243], v17 offset0:214 offset1:247
	ds_read2_b32 v[244:245], v17 offset0:24 offset1:57
	ds_read2_b32 v[246:247], v17 offset0:90 offset1:123
	ds_read2_b32 v[248:249], v17 offset0:156 offset1:189
	ds_read2_b32 v[250:251], v17 offset0:222 offset1:255
	v_cvt_pk_bf16_f32 v34, v214, v215
	v_add_u32_e32 v38, s34, v7
	v_cvt_pk_bf16_f32 v35, v222, v223
	v_ashrrev_i32_e32 v39, 31, v38
	v_cvt_pk_bf16_f32 v36, v224, v225
	v_lshlrev_b64 v[38:39], 12, v[38:39]
	v_lshl_add_u64 v[42:43], s[6:7], 0, v[10:11]
	v_cvt_pk_bf16_f32 v37, v226, v227
	v_lshl_add_u64 v[38:39], v[42:43], 0, v[38:39]
	global_store_dwordx4 v[38:39], v[34:37], off nt
	s_nop 1
	s_mov_b64 s[6:7], 0
	v_cvt_pk_bf16_f32 v34, v228, v229
	v_add_u32_e32 v40, s34, v13
	v_ashrrev_i32_e32 v41, 31, v40
	v_lshlrev_b64 v[40:41], 12, v[40:41]
	v_cvt_pk_bf16_f32 v35, v230, v231
	v_lshl_add_u64 v[40:41], v[42:43], 0, v[40:41]
	v_cvt_pk_bf16_f32 v36, v232, v233
	v_cvt_pk_bf16_f32 v37, v234, v235
	global_store_dwordx4 v[40:41], v[34:37], off nt
	s_nop 1
	v_add_u32_e32 v40, s34, v15
	v_ashrrev_i32_e32 v41, 31, v40
	s_waitcnt lgkmcnt(0)
	v_cvt_pk_bf16_f32 v34, v236, v237
	v_lshlrev_b64 v[40:41], 12, v[40:41]
	v_cvt_pk_bf16_f32 v35, v238, v239
	v_lshl_add_u64 v[40:41], v[42:43], 0, v[40:41]
	v_cvt_pk_bf16_f32 v36, v240, v241
	v_cvt_pk_bf16_f32 v37, v242, v243
	global_store_dwordx4 v[40:41], v[34:37], off nt
	s_nop 1
	v_add_u32_e32 v40, s34, v16
	v_ashrrev_i32_e32 v41, 31, v40
	v_cvt_pk_bf16_f32 v34, v244, v245
	v_lshlrev_b64 v[40:41], 12, v[40:41]
	v_cvt_pk_bf16_f32 v35, v246, v247
	v_lshl_add_u64 v[40:41], v[42:43], 0, v[40:41]
	v_cvt_pk_bf16_f32 v36, v248, v249
	v_cvt_pk_bf16_f32 v37, v250, v251
	global_store_dwordx4 v[40:41], v[34:37], off nt
	s_nop 1
	s_waitcnt lgkmcnt(0)
; __device__ __forceinline__ unsigned pk2(float lo, float hi) { unsigned r; asm volatile("v_cvt_pk_bf16_f32 %0, %1, %2" : "=v"(r) : "v"(lo), "v"(hi)); return r; }
; __device__ __forceinline__ void transpose_item(const float* W, int K, int N, bf16_t* WT, int rstep, int roff, float* scr, int item, int lane) {
;   const int nblk = N / 32, kb = item / nblk, nb = item % nblk, k0 = 64 * kb, n0 = 32 * nb;
;   f32x4 v[8];
; #pragma unroll
;   for (int i = 0; i < 8; ++i) v[i] = __builtin_nontemporal_load((const f32x4*)(W + (size_t)(k0 + i * 8 + (lane >> 3)) * N + n0 + (lane & 7) * 4));
; #pragma unroll
;   for (int i = 0; i < 8; ++i) { float* d = scr + (i * 8 + (lane >> 3)) * 33 + (lane & 7) * 4; d[0] = v[i].x; d[1] = v[i].y; d[2] = v[i].z; d[3] = v[i].w; }
;   __builtin_amdgcn_wave_barrier(); asm volatile("s_waitcnt lgkmcnt(0)" ::: "memory");
;   const int c = lane & 7;
; #pragma unroll
;   for (int j = 0; j < 4; ++j) { const int nl = (lane >> 3) + 8 * j, n = n0 + nl; const float* s = scr + (8 * c) * 33 + nl;
;     u32x4 o; o.x = pk2(s[0 * 33], s[1 * 33]); o.y = pk2(s[2 * 33], s[3 * 33]); o.z = pk2(s[4 * 33], s[5 * 33]); o.w = pk2(s[6 * 33], s[7 * 33]);
;     const int row = n + (n >> 7) * rstep + roff;
;     __builtin_nontemporal_store(o, (u32x4*)(WT + (size_t)row * K + k0 + 8 * c)); }
;   __builtin_amdgcn_wave_barrier(); asm volatile("s_waitcnt lgkmcnt(0)" ::: "memory");
; __device__ __forceinline__ void convert_item(const P& p, int it, float* scr, int lane) {
;     ...
;     if (r < IT_WIN) transpose_item(p.w_in + (size_t)l * DM * INW, DM, INW, WSP(bf16_t, WS_WIN) + (size_t)l * INW * DM, 0, 0, scr, r, lane);
.LBB0_586:
	s_andn2_b64 vcc, exec, s[6:7]
	s_cbranch_vccnz .LBB0_572
	s_mul_i32 s7, s14, 0x3000000
	s_mul_hi_i32 s6, s14, 0x3000000
	s_add_u32 s7, s60, s7
	s_addc_u32 s24, s61, s6
	s_mul_hi_i32 s6, s14, 0x1800000
	s_mul_i32 s14, s14, 0x1800000
	s_add_u32 s30, s17, s14
	s_addc_u32 s31, s18, s6
	s_mul_i32 s6, s22, 0x2aab
	s_lshr_b32 s14, s6, 31
	s_ashr_i32 s6, s6, 21
	s_add_i32 s6, s6, s14
	s_sext_i32_i16 s14, s6
	s_mulk_i32 s6, 0xc0
	s_sub_i32 s6, s22, s6
	s_sext_i32_i16 s15, s6
	s_lshl_b32 s6, s14, 6
	s_lshl_b32 s14, s15, 5
	s_ashr_i32 s15, s14, 31
	s_lshl_b64 s[22:23], s[14:15], 2
	s_add_u32 s22, s7, s22
	v_add_u32_e32 v11, s6, v7
	s_addc_u32 s23, s24, s23
	v_lshl_add_u64 v[62:63], s[22:23], 0, v[96:97]
	s_movk_i32 s7, 0x6000
	v_add_u32_e32 v33, 8, v11
	v_mad_i64_i32 v[38:39], s[22:23], v33, s7, v[62:63]
	v_add_u32_e32 v33, 16, v11
	v_mad_i64_i32 v[42:43], s[22:23], v33, s7, v[62:63]
	v_add_u32_e32 v33, 24, v11
	v_mad_i64_i32 v[46:47], s[22:23], v33, s7, v[62:63]
	v_add_u32_e32 v33, 32, v11
	v_mad_i64_i32 v[50:51], s[22:23], v33, s7, v[62:63]
	v_add_u32_e32 v33, 40, v11
	v_mad_i64_i32 v[34:35], s[22:23], v11, s7, v[62:63]
	v_mad_i64_i32 v[54:55], s[22:23], v33, s7, v[62:63]
	global_load_dwordx4 v[34:37], v[34:35], off nt
	s_nop 0
	global_load_dwordx4 v[38:41], v[38:39], off nt
	s_nop 0
	global_load_dwordx4 v[42:45], v[42:43], off nt
	s_nop 0
	global_load_dwordx4 v[46:49], v[46:47], off nt
	s_nop 0
	global_load_dwordx4 v[50:53], v[50:51], off nt
	s_nop 0
	global_load_dwordx4 v[54:57], v[54:55], off nt
	v_add_u32_e32 v33, 48, v11
	v_mad_i64_i32 v[58:59], s[22:23], v33, s7, v[62:63]
	global_load_dwordx4 v[58:61], v[58:59], off nt
	v_add_u32_e32 v11, 56, v11
	v_mad_i64_i32 v[62:63], s[22:23], v11, s7, v[62:63]
	global_load_dwordx4 v[62:65], v[62:63], off nt
	s_ashr_i32 s7, s6, 31
	s_lshl_b64 s[6:7], s[6:7], 1
	s_add_u32 s6, s30, s6
	v_mov_b32_e32 v11, v97
	s_addc_u32 s7, s31, s7
	v_lshl_add_u64 v[10:11], s[6:7], 0, v[10:11]
	s_movk_i32 s82, 0x6000
	s_waitcnt vmcnt(7)
	ds_write2_b32 v18, v34, v35 offset1:1
	ds_write2_b32 v18, v36, v37 offset0:2 offset1:3
	s_waitcnt vmcnt(6)
	ds_write2_b32 v19, v38, v39 offset1:1
	ds_write2_b32 v20, v40, v41 offset1:1
	s_waitcnt vmcnt(5)
	ds_write2_b32 v21, v42, v43 offset1:1
	ds_write2_b32 v22, v44, v45 offset1:1
	s_waitcnt vmcnt(4)
	ds_write2_b32 v23, v46, v47 offset1:1
	ds_write2_b32 v24, v48, v49 offset1:1
	s_waitcnt vmcnt(3)
	ds_write2_b32 v25, v50, v51 offset1:1
	ds_write2_b32 v26, v52, v53 offset1:1
	s_waitcnt vmcnt(2)
	ds_write2_b32 v27, v54, v55 offset1:1
	ds_write2_b32 v28, v56, v57 offset1:1
	s_waitcnt vmcnt(1)
	ds_write2_b32 v29, v58, v59 offset1:1
	ds_write2_b32 v30, v60, v61 offset1:1
	s_waitcnt vmcnt(0)
	ds_write2_b32 v31, v62, v63 offset1:1
	ds_write2_b32 v32, v64, v65 offset1:1
	s_waitcnt lgkmcnt(0)
	ds_read2_b32 v[214:215], v17 offset1:33
	ds_read2_b32 v[222:223], v17 offset0:66 offset1:99
	ds_read2_b32 v[224:225], v17 offset0:132 offset1:165
	ds_read2_b32 v[226:227], v17 offset0:198 offset1:231
	ds_read2_b32 v[228:229], v17 offset0:8 offset1:41
	ds_read2_b32 v[230:231], v17 offset0:74 offset1:107
	ds_read2_b32 v[232:233], v17 offset0:140 offset1:173
	ds_read2_b32 v[234:235], v17 offset0:206 offset1:239
	s_waitcnt lgkmcnt(0)
	ds_read2_b32 v[236:237], v17 offset0:16 offset1:49
	ds_read2_b32 v[238:239], v17 offset0:82 offset1:115
	ds_read2_b32 v[240:241], v17 offset0:148 offset1:181
	ds_read2_b32 v[242:243], v17 offset0:214 offset1:247
	ds_read2_b32 v[244:245], v17 offset0:24 offset1:57
	ds_read2_b32 v[246:247], v17 offset0:90 offset1:123
	ds_read2_b32 v[248:249], v17 offset0:156 offset1:189
	ds_read2_b32 v[250:251], v17 offset0:222 offset1:255
	v_cvt_pk_bf16_f32 v18, v214, v215
	v_add_u32_e32 v22, s14, v7
	v_cvt_pk_bf16_f32 v19, v222, v223
	v_ashrrev_i32_e32 v23, 31, v22
	v_cvt_pk_bf16_f32 v20, v224, v225
	v_lshlrev_b64 v[22:23], 12, v[22:23]
	v_cvt_pk_bf16_f32 v21, v226, v227
	v_lshl_add_u64 v[22:23], v[10:11], 0, v[22:23]
	global_store_dwordx4 v[22:23], v[18:21], off nt
	s_nop 1
	s_nop 0
	v_cvt_pk_bf16_f32 v18, v228, v229
	v_add_u32_e32 v24, s14, v13
	v_ashrrev_i32_e32 v25, 31, v24
	v_lshlrev_b64 v[24:25], 12, v[24:25]
	v_cvt_pk_bf16_f32 v19, v230, v231
	v_lshl_add_u64 v[24:25], v[10:11], 0, v[24:25]
	v_cvt_pk_bf16_f32 v20, v232, v233
	v_cvt_pk_bf16_f32 v21, v234, v235
	global_store_dwordx4 v[24:25], v[18:21], off nt
	s_nop 1
	v_add_u32_e32 v24, s14, v15
	v_ashrrev_i32_e32 v25, 31, v24
	s_waitcnt lgkmcnt(0)
	v_cvt_pk_bf16_f32 v18, v236, v237
	v_lshlrev_b64 v[24:25], 12, v[24:25]
	v_cvt_pk_bf16_f32 v19, v238, v239
	v_lshl_add_u64 v[24:25], v[10:11], 0, v[24:25]
	v_cvt_pk_bf16_f32 v20, v240, v241
	v_cvt_pk_bf16_f32 v21, v242, v243
	global_store_dwordx4 v[24:25], v[18:21], off nt
	s_nop 1
	v_add_u32_e32 v24, s14, v16
	v_ashrrev_i32_e32 v25, 31, v24
	v_cvt_pk_bf16_f32 v18, v244, v245
	v_lshlrev_b64 v[24:25], 12, v[24:25]
	v_cvt_pk_bf16_f32 v19, v246, v247
	v_lshl_add_u64 v[10:11], v[10:11], 0, v[24:25]
	v_cvt_pk_bf16_f32 v20, v248, v249
	v_cvt_pk_bf16_f32 v21, v250, v251
	global_store_dwordx4 v[10:11], v[18:21], off nt
	s_nop 1
	s_waitcnt lgkmcnt(0)
	s_branch .LBB0_572

; __device__ __forceinline__ unsigned pk2(float lo, float hi) { unsigned r; asm volatile("v_cvt_pk_bf16_f32 %0, %1, %2" : "=v"(r) : "v"(lo), "v"(hi)); return r; }
; __device__ __forceinline__ void transpose_item(const float* W, int K, int N, bf16_t* WT, int rstep, int roff, float* scr, int item, int lane) {
;   const int nblk = N / 32, kb = item / nblk, nb = item % nblk, k0 = 64 * kb, n0 = 32 * nb;
;   f32x4 v[8];
; #pragma unroll
;   for (int i = 0; i < 8; ++i) v[i] = __builtin_nontemporal_load((const f32x4*)(W + (size_t)(k0 + i * 8 + (lane >> 3)) * N + n0 + (lane & 7) * 4));
; #pragma unroll
;   for (int i = 0; i < 8; ++i) { float* d = scr + (i * 8 + (lane >> 3)) * 33 + (lane & 7) * 4; d[0] = v[i].x; d[1] = v[i].y; d[2] = v[i].z; d[3] = v[i].w; }
;   __builtin_amdgcn_wave_barrier(); asm volatile("s_waitcnt lgkmcnt(0)" ::: "memory");
;   const int c = lane & 7;
; #pragma unroll
;   for (int j = 0; j < 4; ++j) { const int nl = (lane >> 3) + 8 * j, n = n0 + nl; const float* s = scr + (8 * c) * 33 + nl;
;     u32x4 o; o.x = pk2(s[0 * 33], s[1 * 33]); o.y = pk2(s[2 * 33], s[3 * 33]); o.z = pk2(s[4 * 33], s[5 * 33]); o.w = pk2(s[6 * 33], s[7 * 33]);
;     const int row = n + (n >> 7) * rstep + roff;
;     __builtin_nontemporal_store(o, (u32x4*)(WT + (size_t)row * K + k0 + 8 * c)); }
;   __builtin_amdgcn_wave_barrier(); asm volatile("s_waitcnt lgkmcnt(0)" ::: "memory");
; __device__ __forceinline__ void convert_item(const P& p, int it, float* scr, int lane) {
;     ...
;     const int idx = it - IT_DENSE, m = idx / IT_EXP, sub = idx % IT_EXP, le = m / 3, which = m % 3;
;     if (which == 0) transpose_item(p.wg + (size_t)le * DM * EFF, DM, EFF, WSP(bf16_t, WS_WGU) + (size_t)le * 1024 * DM, 128, 0, scr, sub, lane);
;     else if (which == 1) transpose_item(p.wu + (size_t)le * DM * EFF, DM, EFF, WSP(bf16_t, WS_WGU) + (size_t)le * 1024 * DM, 128, 128, scr, sub, lane);
;     else transpose_item(p.wd + (size_t)le * EFF * DM, EFF, DM, WSP(bf16_t, WS_WD) + (size_t)le * DM * EFF, 0, 0, scr, sub, lane);
.LBB0_698:
	s_cmpk_gt_i32 s13, 0x3fff
	s_mov_b64 s[6:7], -1
	s_cbranch_scc0 .LBB0_708
	s_add_i32 s6, s13, 0xffffc000
	s_lshr_b32 s7, s6, 9
	s_mul_i32 s6, s6, 0xaaab
	s_lshr_b32 s22, s6, 26
	s_mul_i32 s6, s7, 0xab
	s_bfe_u32 s6, s6, 0x70009
	s_mul_i32 s6, s6, 3
	s_sub_i32 s6, s7, s6
	s_and_b32 s12, s13, 0x1ff
	s_lshl_b32 s21, s22, 22
	s_lshl_b32 s20, s13, 5
	s_and_b32 s23, s6, 0xff
	s_cmp_lt_i32 s23, 1
	s_mov_b64 s[6:7], -1
	s_cbranch_scc1 .LBB0_705
	s_and_b32 s6, 0xffff, s23
	s_cmp_lg_u32 s6, 1
	s_mov_b64 s[6:7], -1
	s_cbranch_scc0 .LBB0_702
	s_add_u32 s24, s0, s21
	s_addc_u32 s31, s1, 0
	s_lshl_b32 s6, s22, 21
	s_add_u32 s7, s9, s6
	s_addc_u32 s22, s16, 0
	s_and_b32 s6, s20, 0x7e0
	s_and_b32 s23, s13, 0x1c0
	s_lshl_b32 s30, s6, 2
	v_add_u32_e32 v4, s23, v1
	s_add_u32 s30, s24, s30
	s_addc_u32 s31, s31, 0
	v_lshlrev_b32_e32 v96, 2, v0
	v_ashrrev_i32_e32 v5, 31, v4
	v_lshl_add_u64 v[12:13], s[30:31], 0, v[96:97]
	v_lshlrev_b64 v[4:5], 13, v[4:5]
	v_lshl_add_u64 v[4:5], v[12:13], 0, v[4:5]
	s_mov_b32 s24, 0x10000
	v_add_co_u32_e32 v16, vcc, s24, v4
	s_mov_b32 s24, 0x20000
	s_nop 0
	v_addc_co_u32_e32 v17, vcc, 0, v5, vcc
	global_load_dwordx4 v[12:15], v[4:5], off nt
	v_add_co_u32_e32 v20, vcc, s24, v4
	global_load_dwordx4 v[16:19], v[16:17], off nt
	s_nop 0
	v_addc_co_u32_e32 v21, vcc, 0, v5, vcc
	s_mov_b32 s24, 0x30000
	global_load_dwordx4 v[20:23], v[20:21], off nt
	v_add_co_u32_e32 v24, vcc, s24, v4
	s_mov_b32 s24, 0x40000
	s_nop 0
	v_addc_co_u32_e32 v25, vcc, 0, v5, vcc
	global_load_dwordx4 v[24:27], v[24:25], off nt
	v_add_co_u32_e32 v28, vcc, s24, v4
	s_mov_b32 s24, 0x50000
	s_nop 0
	v_addc_co_u32_e32 v29, vcc, 0, v5, vcc
	global_load_dwordx4 v[28:31], v[28:29], off nt
	v_add_co_u32_e32 v32, vcc, s24, v4
	s_mov_b32 s24, 0x60000
	s_nop 0
	v_addc_co_u32_e32 v33, vcc, 0, v5, vcc
	global_load_dwordx4 v[32:35], v[32:33], off nt
	v_add_co_u32_e32 v36, vcc, s24, v4
	s_mov_b32 s24, 0x70000
	s_nop 0
	v_addc_co_u32_e32 v37, vcc, 0, v5, vcc
	global_load_dwordx4 v[36:39], v[36:37], off nt
	v_add_co_u32_e32 v4, vcc, s24, v4
	s_lshl_b32 s23, s23, 1
	s_nop 0
	v_addc_co_u32_e32 v5, vcc, 0, v5, vcc
	global_load_dwordx4 v[40:43], v[4:5], off nt
	v_add_u32_e32 v4, v3, v6
	v_add_u32_e32 v5, 0x420, v4
	s_add_u32 s30, s7, s23
	s_addc_u32 s31, s22, 0
	v_lshlrev_b32_e32 v96, 1, v2
	s_waitcnt vmcnt(0)
	ds_write2_b32 v4, v12, v13 offset1:1
	ds_write2_b32 v4, v14, v15 offset0:2 offset1:3
	ds_write2_b32 v5, v16, v17 offset1:1
	v_add_u32_e32 v5, 0x428, v4
	ds_write2_b32 v5, v18, v19 offset1:1
	v_add_u32_e32 v5, 0x840, v4
	ds_write2_b32 v5, v20, v21 offset1:1
	v_add_u32_e32 v5, 0x848, v4
	ds_write2_b32 v5, v22, v23 offset1:1
	v_add_u32_e32 v5, 0xc60, v4
	v_add_u32_e32 v16, s6, v1
	v_ashrrev_i32_e32 v17, 31, v16
	ds_write2_b32 v5, v24, v25 offset1:1
	v_add_u32_e32 v5, 0xc68, v4
	ds_write2_b32 v5, v26, v27 offset1:1
	v_add_u32_e32 v5, 0x1080, v4
	v_lshlrev_b64 v[16:17], 10, v[16:17]
	ds_write2_b32 v5, v28, v29 offset1:1
	v_add_u32_e32 v5, 0x1088, v4
	ds_write2_b32 v5, v30, v31 offset1:1
	v_add_u32_e32 v5, 0x14a0, v4
	ds_write2_b32 v5, v32, v33 offset1:1
	v_add_u32_e32 v5, 0x14a8, v4
	ds_write2_b32 v5, v34, v35 offset1:1
	v_add_u32_e32 v5, 0x18c0, v4
	ds_write2_b32 v5, v36, v37 offset1:1
	v_add_u32_e32 v5, 0x18c8, v4
	ds_write2_b32 v5, v38, v39 offset1:1
	v_add_u32_e32 v5, 0x1ce0, v4
	v_add_u32_e32 v4, 0x1ce8, v4
	ds_write2_b32 v5, v40, v41 offset1:1
	ds_write2_b32 v4, v42, v43 offset1:1
	s_waitcnt lgkmcnt(0)
	ds_read2_b32 v[214:215], v10 offset1:33
	ds_read2_b32 v[222:223], v10 offset0:66 offset1:99
	ds_read2_b32 v[224:225], v10 offset0:132 offset1:165
	ds_read2_b32 v[226:227], v10 offset0:198 offset1:231
	ds_read2_b32 v[228:229], v10 offset0:8 offset1:41
	ds_read2_b32 v[230:231], v10 offset0:74 offset1:107
	ds_read2_b32 v[232:233], v10 offset0:140 offset1:173
	ds_read2_b32 v[234:235], v10 offset0:206 offset1:239
	s_waitcnt lgkmcnt(0)
	ds_read2_b32 v[236:237], v10 offset0:16 offset1:49
	ds_read2_b32 v[238:239], v10 offset0:82 offset1:115
	ds_read2_b32 v[240:241], v10 offset0:148 offset1:181
	ds_read2_b32 v[242:243], v10 offset0:214 offset1:247
	ds_read2_b32 v[244:245], v10 offset0:24 offset1:57
	ds_read2_b32 v[246:247], v10 offset0:90 offset1:123
	ds_read2_b32 v[248:249], v10 offset0:156 offset1:189
	ds_read2_b32 v[250:251], v10 offset0:222 offset1:255
	v_lshl_add_u64 v[4:5], s[30:31], 0, v[96:97]
	v_cvt_pk_bf16_f32 v12, v214, v215
	v_cvt_pk_bf16_f32 v13, v222, v223
	v_lshl_add_u64 v[16:17], v[4:5], 0, v[16:17]
	v_cvt_pk_bf16_f32 v14, v224, v225
	v_cvt_pk_bf16_f32 v15, v226, v227
	global_store_dwordx4 v[16:17], v[12:15], off nt
	s_nop 1
	v_add_u32_e32 v16, s6, v7
	v_ashrrev_i32_e32 v17, 31, v16
	v_cvt_pk_bf16_f32 v12, v228, v229
	v_lshlrev_b64 v[16:17], 10, v[16:17]
	v_cvt_pk_bf16_f32 v13, v230, v231
	v_lshl_add_u64 v[16:17], v[4:5], 0, v[16:17]
	v_cvt_pk_bf16_f32 v14, v232, v233
	v_cvt_pk_bf16_f32 v15, v234, v235
	global_store_dwordx4 v[16:17], v[12:15], off nt
	s_nop 1
	v_add_u32_e32 v16, s6, v8
	s_waitcnt lgkmcnt(0)
	v_ashrrev_i32_e32 v17, 31, v16
	v_cvt_pk_bf16_f32 v12, v236, v237
	v_lshlrev_b64 v[16:17], 10, v[16:17]
	v_cvt_pk_bf16_f32 v13, v238, v239
	v_lshl_add_u64 v[16:17], v[4:5], 0, v[16:17]
	v_cvt_pk_bf16_f32 v14, v240, v241
	v_cvt_pk_bf16_f32 v15, v242, v243
	global_store_dwordx4 v[16:17], v[12:15], off nt
	s_nop 1
	v_add_u32_e32 v16, s6, v9
	v_ashrrev_i32_e32 v17, 31, v16
	v_cvt_pk_bf16_f32 v12, v244, v245
	v_lshlrev_b64 v[16:17], 10, v[16:17]
	v_cvt_pk_bf16_f32 v13, v246, v247
	v_lshl_add_u64 v[4:5], v[4:5], 0, v[16:17]
	v_cvt_pk_bf16_f32 v14, v248, v249
	v_cvt_pk_bf16_f32 v15, v250, v251
	global_store_dwordx4 v[4:5], v[12:15], off nt
	s_nop 1
	s_waitcnt lgkmcnt(0)
	s_mov_b64 s[6:7], 0
; __device__ __forceinline__ unsigned pk2(float lo, float hi) { unsigned r; asm volatile("v_cvt_pk_bf16_f32 %0, %1, %2" : "=v"(r) : "v"(lo), "v"(hi)); return r; }
; __device__ __forceinline__ void transpose_item(const float* W, int K, int N, bf16_t* WT, int rstep, int roff, float* scr, int item, int lane) {
;   const int nblk = N / 32, kb = item / nblk, nb = item % nblk, k0 = 64 * kb, n0 = 32 * nb;
;   f32x4 v[8];
; #pragma unroll
;   for (int i = 0; i < 8; ++i) v[i] = __builtin_nontemporal_load((const f32x4*)(W + (size_t)(k0 + i * 8 + (lane >> 3)) * N + n0 + (lane & 7) * 4));
; #pragma unroll
;   for (int i = 0; i < 8; ++i) { float* d = scr + (i * 8 + (lane >> 3)) * 33 + (lane & 7) * 4; d[0] = v[i].x; d[1] = v[i].y; d[2] = v[i].z; d[3] = v[i].w; }
;   __builtin_amdgcn_wave_barrier(); asm volatile("s_waitcnt lgkmcnt(0)" ::: "memory");
;   const int c = lane & 7;
; #pragma unroll
;   for (int j = 0; j < 4; ++j) { const int nl = (lane >> 3) + 8 * j, n = n0 + nl; const float* s = scr + (8 * c) * 33 + nl;
;     u32x4 o; o.x = pk2(s[0 * 33], s[1 * 33]); o.y = pk2(s[2 * 33], s[3 * 33]); o.z = pk2(s[4 * 33], s[5 * 33]); o.w = pk2(s[6 * 33], s[7 * 33]);
;     const int row = n + (n >> 7) * rstep + roff;
;     __builtin_nontemporal_store(o, (u32x4*)(WT + (size_t)row * K + k0 + 8 * c)); }
;   __builtin_amdgcn_wave_barrier(); asm volatile("s_waitcnt lgkmcnt(0)" ::: "memory");
; __device__ __forceinline__ void convert_item(const P& p, int it, float* scr, int lane) {
;     ...
;     else if (which == 1) transpose_item(p.wu + (size_t)le * DM * EFF, DM, EFF, WSP(bf16_t, WS_WGU) + (size_t)le * 1024 * DM, 128, 128, scr, sub, lane);
.LBB0_702:
	s_andn2_b64 vcc, exec, s[6:7]
	s_cbranch_vccnz .LBB0_704
	s_add_u32 s24, s54, s21
	s_addc_u32 s31, s55, 0
	s_add_u32 s7, s2, s21
	s_addc_u32 s22, s3, 0
	s_lshl_b32 s6, s12, 2
	s_and_b32 s23, s6, 0x7c0
	s_and_b32 s6, s20, 0x1e0
	s_lshl_b32 s30, s6, 2
	v_add_u32_e32 v4, s23, v1
	s_add_u32 s30, s24, s30
	s_addc_u32 s31, s31, 0
	v_lshlrev_b32_e32 v96, 2, v0
	v_ashrrev_i32_e32 v5, 31, v4
	v_lshl_add_u64 v[12:13], s[30:31], 0, v[96:97]
	v_lshlrev_b64 v[4:5], 11, v[4:5]
	v_lshl_add_u64 v[4:5], v[12:13], 0, v[4:5]
	s_movk_i32 s24, 0x4000
	v_add_co_u32_e32 v16, vcc, s24, v4
	s_mov_b32 s24, 0x8000
	s_nop 0
	v_addc_co_u32_e32 v17, vcc, 0, v5, vcc
	global_load_dwordx4 v[12:15], v[4:5], off nt
	v_add_co_u32_e32 v20, vcc, s24, v4
	global_load_dwordx4 v[16:19], v[16:17], off nt
	s_nop 0
	v_addc_co_u32_e32 v21, vcc, 0, v5, vcc
	s_mov_b32 s24, 0xc000
	global_load_dwordx4 v[20:23], v[20:21], off nt
	v_add_co_u32_e32 v24, vcc, s24, v4
	s_mov_b32 s24, 0x10000
	s_nop 0
	v_addc_co_u32_e32 v25, vcc, 0, v5, vcc
	global_load_dwordx4 v[24:27], v[24:25], off nt
	v_add_co_u32_e32 v28, vcc, s24, v4
	s_mov_b32 s24, 0x14000
	s_nop 0
	v_addc_co_u32_e32 v29, vcc, 0, v5, vcc
	global_load_dwordx4 v[28:31], v[28:29], off nt
	v_add_co_u32_e32 v32, vcc, s24, v4
	s_lshl_b32 s23, s23, 1
	s_nop 0
	v_addc_co_u32_e32 v33, vcc, 0, v5, vcc
	global_load_dwordx4 v[32:35], v[32:33], off nt
	v_add_co_u32_e32 v36, vcc, s93, v4
	v_add_u32_e32 v11, s6, v1
	s_nop 0
	v_addc_co_u32_e32 v37, vcc, 0, v5, vcc
	global_load_dwordx4 v[36:39], v[36:37], off nt
	v_add_co_u32_e32 v4, vcc, s96, v4
	s_add_u32 s30, s7, s23
	s_nop 0
	v_addc_co_u32_e32 v5, vcc, 0, v5, vcc
	global_load_dwordx4 v[40:43], v[4:5], off nt
	v_add_u32_e32 v4, v3, v6
	v_add_u32_e32 v5, 0x420, v4
	s_movk_i32 s7, 0x80
	s_addc_u32 s31, s22, 0
	v_lshlrev_b32_e32 v96, 1, v2
	s_waitcnt vmcnt(0)
	ds_write2_b32 v4, v12, v13 offset1:1
	ds_write2_b32 v4, v14, v15 offset0:2 offset1:3
	ds_write2_b32 v5, v16, v17 offset1:1
	v_add_u32_e32 v5, 0x428, v4
	ds_write2_b32 v5, v18, v19 offset1:1
	v_add_u32_e32 v5, 0x840, v4
	ds_write2_b32 v5, v20, v21 offset1:1
	v_add_u32_e32 v5, 0x848, v4
	ds_write2_b32 v5, v22, v23 offset1:1
	v_add_u32_e32 v5, 0xc60, v4
	ds_write2_b32 v5, v24, v25 offset1:1
	v_add_u32_e32 v5, 0xc68, v4
	ds_write2_b32 v5, v26, v27 offset1:1
	v_add_u32_e32 v5, 0x1080, v4
	ds_write2_b32 v5, v28, v29 offset1:1
	v_add_u32_e32 v5, 0x1088, v4
	ds_write2_b32 v5, v30, v31 offset1:1
	v_add_u32_e32 v5, 0x14a0, v4
	ds_write2_b32 v5, v32, v33 offset1:1
	v_add_u32_e32 v5, 0x14a8, v4
	ds_write2_b32 v5, v34, v35 offset1:1
	v_add_u32_e32 v5, 0x18c0, v4
	ds_write2_b32 v5, v36, v37 offset1:1
	v_add_u32_e32 v5, 0x18c8, v4
	ds_write2_b32 v5, v38, v39 offset1:1
	v_add_u32_e32 v5, 0x1ce0, v4
	v_add_u32_e32 v4, 0x1ce8, v4
	ds_write2_b32 v5, v40, v41 offset1:1
	ds_write2_b32 v4, v42, v43 offset1:1
	s_waitcnt lgkmcnt(0)
	ds_read2_b32 v[214:215], v10 offset1:33
	ds_read2_b32 v[222:223], v10 offset0:66 offset1:99
	ds_read2_b32 v[224:225], v10 offset0:132 offset1:165
	ds_read2_b32 v[226:227], v10 offset0:198 offset1:231
	ds_read2_b32 v[228:229], v10 offset0:8 offset1:41
	ds_read2_b32 v[230:231], v10 offset0:74 offset1:107
	ds_read2_b32 v[232:233], v10 offset0:140 offset1:173
	ds_read2_b32 v[234:235], v10 offset0:206 offset1:239
	s_waitcnt lgkmcnt(0)
	ds_read2_b32 v[236:237], v10 offset0:16 offset1:49
	ds_read2_b32 v[238:239], v10 offset0:82 offset1:115
	ds_read2_b32 v[240:241], v10 offset0:148 offset1:181
	ds_read2_b32 v[242:243], v10 offset0:214 offset1:247
	ds_read2_b32 v[244:245], v10 offset0:24 offset1:57
	ds_read2_b32 v[246:247], v10 offset0:90 offset1:123
	ds_read2_b32 v[248:249], v10 offset0:156 offset1:189
	ds_read2_b32 v[250:251], v10 offset0:222 offset1:255
	v_cvt_pk_bf16_f32 v12, v214, v215
	v_cvt_pk_bf16_f32 v13, v222, v223
	v_cvt_pk_bf16_f32 v14, v224, v225
	v_cvt_pk_bf16_f32 v15, v226, v227
	v_and_b32_e32 v16, 0xffffff80, v11
	v_add3_u32 v16, v11, v16, s7
	v_ashrrev_i32_e32 v17, 31, v16
	v_lshl_add_u64 v[4:5], s[30:31], 0, v[96:97]
	v_lshlrev_b64 v[16:17], 12, v[16:17]
	v_lshl_add_u64 v[16:17], v[4:5], 0, v[16:17]
	global_store_dwordx4 v[16:17], v[12:15], off nt
	s_nop 1
	v_add_u32_e32 v11, s6, v7
	v_cvt_pk_bf16_f32 v12, v228, v229
	v_cvt_pk_bf16_f32 v13, v230, v231
	v_cvt_pk_bf16_f32 v14, v232, v233
	v_cvt_pk_bf16_f32 v15, v234, v235
	v_and_b32_e32 v16, 0xffffff80, v11
	v_add3_u32 v16, v11, v16, s7
	v_ashrrev_i32_e32 v17, 31, v16
	v_lshlrev_b64 v[16:17], 12, v[16:17]
	v_lshl_add_u64 v[16:17], v[4:5], 0, v[16:17]
	global_store_dwordx4 v[16:17], v[12:15], off nt
	s_nop 1
	s_waitcnt lgkmcnt(0)
	v_add_u32_e32 v11, s6, v8
	v_cvt_pk_bf16_f32 v12, v236, v237
	v_cvt_pk_bf16_f32 v13, v238, v239
	v_cvt_pk_bf16_f32 v14, v240, v241
	v_cvt_pk_bf16_f32 v15, v242, v243
	v_and_b32_e32 v16, 0xffffff80, v11
	v_add3_u32 v16, v11, v16, s7
	v_ashrrev_i32_e32 v17, 31, v16
	v_lshlrev_b64 v[16:17], 12, v[16:17]
	v_lshl_add_u64 v[16:17], v[4:5], 0, v[16:17]
	global_store_dwordx4 v[16:17], v[12:15], off nt
	s_nop 1
	v_add_u32_e32 v11, s6, v9
	v_cvt_pk_bf16_f32 v12, v244, v245
	v_cvt_pk_bf16_f32 v13, v246, v247
	v_cvt_pk_bf16_f32 v14, v248, v249
	v_cvt_pk_bf16_f32 v15, v250, v251
	v_and_b32_e32 v16, 0xffffff80, v11
	v_add3_u32 v16, v11, v16, s7
	v_ashrrev_i32_e32 v17, 31, v16
	v_lshlrev_b64 v[16:17], 12, v[16:17]
	v_lshl_add_u64 v[4:5], v[4:5], 0, v[16:17]
	global_store_dwordx4 v[4:5], v[12:15], off nt
	s_nop 1
	s_waitcnt lgkmcnt(0)

; __device__ __forceinline__ unsigned pk2(float lo, float hi) { unsigned r; asm volatile("v_cvt_pk_bf16_f32 %0, %1, %2" : "=v"(r) : "v"(lo), "v"(hi)); return r; }
; __device__ __forceinline__ void transpose_item(const float* W, int K, int N, bf16_t* WT, int rstep, int roff, float* scr, int item, int lane) {
;   const int nblk = N / 32, kb = item / nblk, nb = item % nblk, k0 = 64 * kb, n0 = 32 * nb;
;   f32x4 v[8];
; #pragma unroll
;   for (int i = 0; i < 8; ++i) v[i] = __builtin_nontemporal_load((const f32x4*)(W + (size_t)(k0 + i * 8 + (lane >> 3)) * N + n0 + (lane & 7) * 4));
; #pragma unroll
;   for (int i = 0; i < 8; ++i) { float* d = scr + (i * 8 + (lane >> 3)) * 33 + (lane & 7) * 4; d[0] = v[i].x; d[1] = v[i].y; d[2] = v[i].z; d[3] = v[i].w; }
;   __builtin_amdgcn_wave_barrier(); asm volatile("s_waitcnt lgkmcnt(0)" ::: "memory");
;   const int c = lane & 7;
; #pragma unroll
;   for (int j = 0; j < 4; ++j) { const int nl = (lane >> 3) + 8 * j, n = n0 + nl; const float* s = scr + (8 * c) * 33 + nl;
;     u32x4 o; o.x = pk2(s[0 * 33], s[1 * 33]); o.y = pk2(s[2 * 33], s[3 * 33]); o.z = pk2(s[4 * 33], s[5 * 33]); o.w = pk2(s[6 * 33], s[7 * 33]);
;     const int row = n + (n >> 7) * rstep + roff;
;     __builtin_nontemporal_store(o, (u32x4*)(WT + (size_t)row * K + k0 + 8 * c)); }
;   __builtin_amdgcn_wave_barrier(); asm volatile("s_waitcnt lgkmcnt(0)" ::: "memory");
; __device__ __forceinline__ void convert_item(const P& p, int it, float* scr, int lane) {
;     ...
;     if (which == 0) transpose_item(p.wg + (size_t)le * DM * EFF, DM, EFF, WSP(bf16_t, WS_WGU) + (size_t)le * 1024 * DM, 128, 0, scr, sub, lane);
.LBB0_705:
	s_andn2_b64 vcc, exec, s[6:7]
	s_cbranch_vccnz .LBB0_707
	s_add_u32 s22, s52, s21
	s_addc_u32 s23, s53, 0
	s_add_u32 s7, s2, s21
	s_addc_u32 s21, s3, 0
	s_lshl_b32 s6, s12, 2
	s_and_b32 s12, s6, 0x7c0
	s_and_b32 s6, s20, 0x1e0
	s_lshl_b32 s20, s6, 2
	v_add_u32_e32 v4, s12, v1
	s_add_u32 s22, s22, s20
	s_addc_u32 s23, s23, 0
	v_lshlrev_b32_e32 v96, 2, v0
	v_ashrrev_i32_e32 v5, 31, v4
	v_lshl_add_u64 v[12:13], s[22:23], 0, v[96:97]
	v_lshlrev_b64 v[4:5], 11, v[4:5]
	v_lshl_add_u64 v[4:5], v[12:13], 0, v[4:5]
	s_movk_i32 s20, 0x4000
	v_add_co_u32_e32 v16, vcc, s20, v4
	s_mov_b32 s20, 0x8000
	s_nop 0
	v_addc_co_u32_e32 v17, vcc, 0, v5, vcc
	global_load_dwordx4 v[12:15], v[4:5], off nt
	v_add_co_u32_e32 v20, vcc, s20, v4
	global_load_dwordx4 v[16:19], v[16:17], off nt
	s_nop 0
	v_addc_co_u32_e32 v21, vcc, 0, v5, vcc
	s_mov_b32 s20, 0xc000
	global_load_dwordx4 v[20:23], v[20:21], off nt
	v_add_co_u32_e32 v24, vcc, s20, v4
	s_mov_b32 s20, 0x10000
	s_nop 0
	v_addc_co_u32_e32 v25, vcc, 0, v5, vcc
	global_load_dwordx4 v[24:27], v[24:25], off nt
	v_add_co_u32_e32 v28, vcc, s20, v4
	s_mov_b32 s20, 0x14000
	s_nop 0
	v_addc_co_u32_e32 v29, vcc, 0, v5, vcc
	global_load_dwordx4 v[28:31], v[28:29], off nt
	v_add_co_u32_e32 v32, vcc, s20, v4
	v_add_u32_e32 v11, s6, v1
	s_nop 0
	v_addc_co_u32_e32 v33, vcc, 0, v5, vcc
	global_load_dwordx4 v[32:35], v[32:33], off nt
	v_add_co_u32_e32 v36, vcc, s93, v4
	s_lshl_b32 s12, s12, 1
	s_nop 0
	v_addc_co_u32_e32 v37, vcc, 0, v5, vcc
	global_load_dwordx4 v[36:39], v[36:37], off nt
	v_add_co_u32_e32 v4, vcc, s96, v4
	s_add_u32 s20, s7, s12
	s_nop 0
	v_addc_co_u32_e32 v5, vcc, 0, v5, vcc
	global_load_dwordx4 v[40:43], v[4:5], off nt
	v_add_u32_e32 v4, v3, v6
	v_add_u32_e32 v5, 0x420, v4
	s_addc_u32 s21, s21, 0
	v_lshlrev_b32_e32 v96, 1, v2
	s_waitcnt vmcnt(0)
	ds_write2_b32 v4, v12, v13 offset1:1
	ds_write2_b32 v4, v14, v15 offset0:2 offset1:3
	ds_write2_b32 v5, v16, v17 offset1:1
	v_add_u32_e32 v5, 0x428, v4
	ds_write2_b32 v5, v18, v19 offset1:1
	v_add_u32_e32 v5, 0x840, v4
	ds_write2_b32 v5, v20, v21 offset1:1
	v_add_u32_e32 v5, 0x848, v4
	ds_write2_b32 v5, v22, v23 offset1:1
	v_add_u32_e32 v5, 0xc60, v4
	ds_write2_b32 v5, v24, v25 offset1:1
	v_add_u32_e32 v5, 0xc68, v4
	ds_write2_b32 v5, v26, v27 offset1:1
	v_add_u32_e32 v5, 0x1080, v4
	ds_write2_b32 v5, v28, v29 offset1:1
	v_add_u32_e32 v5, 0x1088, v4
	ds_write2_b32 v5, v30, v31 offset1:1
	v_add_u32_e32 v5, 0x14a0, v4
	ds_write2_b32 v5, v32, v33 offset1:1
	v_add_u32_e32 v5, 0x14a8, v4
	ds_write2_b32 v5, v34, v35 offset1:1
	v_add_u32_e32 v5, 0x18c0, v4
	ds_write2_b32 v5, v36, v37 offset1:1
	v_add_u32_e32 v5, 0x18c8, v4
	ds_write2_b32 v5, v38, v39 offset1:1
	v_add_u32_e32 v5, 0x1ce0, v4
	v_add_u32_e32 v4, 0x1ce8, v4
	ds_write2_b32 v5, v40, v41 offset1:1
	ds_write2_b32 v4, v42, v43 offset1:1
	s_waitcnt lgkmcnt(0)
	ds_read2_b32 v[214:215], v10 offset1:33
	ds_read2_b32 v[222:223], v10 offset0:66 offset1:99
	ds_read2_b32 v[224:225], v10 offset0:132 offset1:165
	ds_read2_b32 v[226:227], v10 offset0:198 offset1:231
	ds_read2_b32 v[228:229], v10 offset0:8 offset1:41
	ds_read2_b32 v[230:231], v10 offset0:74 offset1:107
	ds_read2_b32 v[232:233], v10 offset0:140 offset1:173
	ds_read2_b32 v[234:235], v10 offset0:206 offset1:239
	s_waitcnt lgkmcnt(0)
	ds_read2_b32 v[236:237], v10 offset0:16 offset1:49
	ds_read2_b32 v[238:239], v10 offset0:82 offset1:115
	ds_read2_b32 v[240:241], v10 offset0:148 offset1:181
	ds_read2_b32 v[242:243], v10 offset0:214 offset1:247
	ds_read2_b32 v[244:245], v10 offset0:24 offset1:57
	ds_read2_b32 v[246:247], v10 offset0:90 offset1:123
	ds_read2_b32 v[248:249], v10 offset0:156 offset1:189
	ds_read2_b32 v[250:251], v10 offset0:222 offset1:255
	v_cvt_pk_bf16_f32 v12, v214, v215
	v_cvt_pk_bf16_f32 v13, v222, v223
	v_cvt_pk_bf16_f32 v14, v224, v225
	v_cvt_pk_bf16_f32 v15, v226, v227
	v_and_b32_e32 v16, 0xffffff80, v11
	v_add_u32_e32 v16, v16, v11
	v_ashrrev_i32_e32 v17, 31, v16
	v_lshl_add_u64 v[4:5], s[20:21], 0, v[96:97]
	v_lshlrev_b64 v[16:17], 12, v[16:17]
	v_lshl_add_u64 v[16:17], v[4:5], 0, v[16:17]
	global_store_dwordx4 v[16:17], v[12:15], off nt
	s_nop 1
	v_add_u32_e32 v11, s6, v7
	v_cvt_pk_bf16_f32 v12, v228, v229
	v_cvt_pk_bf16_f32 v13, v230, v231
	v_cvt_pk_bf16_f32 v14, v232, v233
	v_cvt_pk_bf16_f32 v15, v234, v235
	v_and_b32_e32 v16, 0xffffff80, v11
	v_add_u32_e32 v16, v16, v11
	v_ashrrev_i32_e32 v17, 31, v16
	v_lshlrev_b64 v[16:17], 12, v[16:17]
	v_lshl_add_u64 v[16:17], v[4:5], 0, v[16:17]
	global_store_dwordx4 v[16:17], v[12:15], off nt
	s_nop 1
	s_waitcnt lgkmcnt(0)
	v_add_u32_e32 v11, s6, v8
	v_cvt_pk_bf16_f32 v12, v236, v237
	v_cvt_pk_bf16_f32 v13, v238, v239
	v_cvt_pk_bf16_f32 v14, v240, v241
	v_cvt_pk_bf16_f32 v15, v242, v243
	v_and_b32_e32 v16, 0xffffff80, v11
	v_add_u32_e32 v16, v16, v11
	v_ashrrev_i32_e32 v17, 31, v16
	v_lshlrev_b64 v[16:17], 12, v[16:17]
	v_lshl_add_u64 v[16:17], v[4:5], 0, v[16:17]
	global_store_dwordx4 v[16:17], v[12:15], off nt
	s_nop 1
	v_add_u32_e32 v11, s6, v9
	v_cvt_pk_bf16_f32 v12, v244, v245
	v_cvt_pk_bf16_f32 v13, v246, v247
	v_cvt_pk_bf16_f32 v14, v248, v249
	v_cvt_pk_bf16_f32 v15, v250, v251
	v_and_b32_e32 v16, 0xffffff80, v11
	v_add_u32_e32 v16, v16, v11
	v_ashrrev_i32_e32 v17, 31, v16
	v_lshlrev_b64 v[16:17], 12, v[16:17]
	v_lshl_add_u64 v[4:5], v[4:5], 0, v[16:17]
	global_store_dwordx4 v[4:5], v[12:15], off nt
	s_nop 1
	s_waitcnt lgkmcnt(0)

; __device__ __forceinline__ unsigned pk2(float lo, float hi) { unsigned r; asm volatile("v_cvt_pk_bf16_f32 %0, %1, %2" : "=v"(r) : "v"(lo), "v"(hi)); return r; }
; __device__ __forceinline__ void transpose_item(const float* W, int K, int N, bf16_t* WT, int rstep, int roff, float* scr, int item, int lane) {
;   const int nblk = N / 32, kb = item / nblk, nb = item % nblk, k0 = 64 * kb, n0 = 32 * nb;
;   f32x4 v[8];
; #pragma unroll
;   for (int i = 0; i < 8; ++i) v[i] = __builtin_nontemporal_load((const f32x4*)(W + (size_t)(k0 + i * 8 + (lane >> 3)) * N + n0 + (lane & 7) * 4));
; #pragma unroll
;   for (int i = 0; i < 8; ++i) { float* d = scr + (i * 8 + (lane >> 3)) * 33 + (lane & 7) * 4; d[0] = v[i].x; d[1] = v[i].y; d[2] = v[i].z; d[3] = v[i].w; }
;   __builtin_amdgcn_wave_barrier(); asm volatile("s_waitcnt lgkmcnt(0)" ::: "memory");
;   const int c = lane & 7;
; #pragma unroll
;   for (int j = 0; j < 4; ++j) { const int nl = (lane >> 3) + 8 * j, n = n0 + nl; const float* s = scr + (8 * c) * 33 + nl;
;     u32x4 o; o.x = pk2(s[0 * 33], s[1 * 33]); o.y = pk2(s[2 * 33], s[3 * 33]); o.z = pk2(s[4 * 33], s[5 * 33]); o.w = pk2(s[6 * 33], s[7 * 33]);
;     const int row = n + (n >> 7) * rstep + roff;
;     __builtin_nontemporal_store(o, (u32x4*)(WT + (size_t)row * K + k0 + 8 * c)); }
;   __builtin_amdgcn_wave_barrier(); asm volatile("s_waitcnt lgkmcnt(0)" ::: "memory");
; __device__ __forceinline__ void convert_item(const P& p, int it, float* scr, int lane) {
;   if (it < IT_DENSE) {
;     const int l = it / (IT_WIN + IT_WOUT), r = it % (IT_WIN + IT_WOUT);
;     if (r < IT_WIN) transpose_item(p.w_in + (size_t)l * DM * INW, DM, INW, WSP(bf16_t, WS_WIN) + (size_t)l * INW * DM, 0, 0, scr, r, lane);
;     else transpose_item(p.w_out + (size_t)l * DM * DM, DM, DM, WSP(bf16_t, WS_WOUT) + (size_t)l * DM * DM, 0, 0, scr, r - IT_WIN, lane);
.LBB0_708:
	s_and_b64 vcc, exec, s[6:7]
	s_cbranch_vccz .LBB0_688
	s_ashr_i32 s6, s13, 31
	s_lshr_b32 s6, s6, 19
	s_add_i32 s6, s13, s6
	s_ashr_i32 s12, s6, 13
	s_and_b32 s6, s6, 0xffffe000
	s_sub_i32 s20, s13, s6
	s_ashr_i32 s13, s12, 31
	v_add_u32_e32 v11, v3, v6
	s_cmpk_gt_i32 s20, 0x17ff
	s_mov_b64 s[6:7], -1
	v_lshlrev_b32_e32 v96, 2, v0
	v_add_u32_e32 v12, 0x420, v11
	v_add_u32_e32 v13, 0x428, v11
	v_add_u32_e32 v14, 0x840, v11
	v_add_u32_e32 v15, 0x848, v11
	v_add_u32_e32 v16, 0xc60, v11
	v_add_u32_e32 v17, 0xc68, v11
	v_add_u32_e32 v18, 0x1080, v11
	v_add_u32_e32 v19, 0x1088, v11
	v_add_u32_e32 v20, 0x14a0, v11
	v_add_u32_e32 v21, 0x14a8, v11
	v_add_u32_e32 v22, 0x18c0, v11
	v_add_u32_e32 v23, 0x18c8, v11
	v_add_u32_e32 v24, 0x1ce0, v11
	v_add_u32_e32 v25, 0x1ce8, v11
	v_lshlrev_b32_e32 v4, 1, v2
	s_cbranch_scc0 .LBB0_711
	s_lshl_b64 s[6:7], s[12:13], 24
	s_add_u32 s21, s50, s6
	s_addc_u32 s22, s51, s7
	s_lshl_b64 s[6:7], s[12:13], 23
	s_add_u32 s13, s4, s6
	s_addc_u32 s23, s5, s7
	s_add_i32 s6, s20, 0xe800
	s_and_b32 s24, s6, 0xffc0
	s_lshl_b32 s6, s20, 5
	s_and_b32 s30, s6, 0x7e0
	s_lshl_b32 s6, s30, 2
	v_add_u32_e32 v26, s24, v1
	s_add_u32 s6, s21, s6
	s_addc_u32 s7, s22, 0
	v_ashrrev_i32_e32 v27, 31, v26
	v_lshl_add_u64 v[28:29], s[6:7], 0, v[96:97]
	v_lshlrev_b64 v[26:27], 13, v[26:27]
	v_lshl_add_u64 v[54:55], v[28:29], 0, v[26:27]
	s_mov_b32 s6, 0x10000
	v_add_co_u32_e32 v30, vcc, s6, v54
	s_mov_b32 s6, 0x20000
	s_nop 0
	v_addc_co_u32_e32 v31, vcc, 0, v55, vcc
	v_add_co_u32_e32 v34, vcc, s6, v54
	s_mov_b32 s6, 0x30000
	s_nop 0
	v_addc_co_u32_e32 v35, vcc, 0, v55, vcc
	v_add_co_u32_e32 v38, vcc, s6, v54
	s_mov_b32 s6, 0x40000
	s_nop 0
	v_addc_co_u32_e32 v39, vcc, 0, v55, vcc
	v_add_co_u32_e32 v42, vcc, s6, v54
	s_mov_b32 s6, 0x50000
	s_nop 0
	v_addc_co_u32_e32 v43, vcc, 0, v55, vcc
	v_add_co_u32_e32 v46, vcc, s6, v54
	global_load_dwordx4 v[26:29], v[54:55], off nt
	s_nop 0
	global_load_dwordx4 v[30:33], v[30:31], off nt
	v_addc_co_u32_e32 v47, vcc, 0, v55, vcc
	global_load_dwordx4 v[34:37], v[34:35], off nt
	s_nop 0
	global_load_dwordx4 v[38:41], v[38:39], off nt
	s_nop 0
	global_load_dwordx4 v[42:45], v[42:43], off nt
	s_nop 0
	global_load_dwordx4 v[46:49], v[46:47], off nt
	s_mov_b32 s6, 0x60000
	v_add_co_u32_e32 v50, vcc, s6, v54
	s_mov_b32 s6, 0x70000
	s_nop 0
	v_addc_co_u32_e32 v51, vcc, 0, v55, vcc
	global_load_dwordx4 v[50:53], v[50:51], off nt
	v_add_co_u32_e32 v54, vcc, s6, v54
	s_lshl_b32 s6, s24, 1
	s_nop 0
	v_addc_co_u32_e32 v55, vcc, 0, v55, vcc
	global_load_dwordx4 v[54:57], v[54:55], off nt
	s_add_u32 s6, s13, s6
	v_mov_b32_e32 v5, v97
	s_addc_u32 s7, s23, 0
	s_waitcnt vmcnt(0)
	ds_write2_b32 v11, v26, v27 offset1:1
	ds_write2_b32 v11, v28, v29 offset0:2 offset1:3
	ds_write2_b32 v12, v30, v31 offset1:1
	ds_write2_b32 v13, v32, v33 offset1:1
	ds_write2_b32 v14, v34, v35 offset1:1
	ds_write2_b32 v15, v36, v37 offset1:1
	ds_write2_b32 v16, v38, v39 offset1:1
	ds_write2_b32 v17, v40, v41 offset1:1
	ds_write2_b32 v18, v42, v43 offset1:1
	ds_write2_b32 v19, v44, v45 offset1:1
	ds_write2_b32 v20, v46, v47 offset1:1
	ds_write2_b32 v21, v48, v49 offset1:1
	ds_write2_b32 v22, v50, v51 offset1:1
	ds_write2_b32 v23, v52, v53 offset1:1
	ds_write2_b32 v24, v54, v55 offset1:1
	ds_write2_b32 v25, v56, v57 offset1:1
	s_waitcnt lgkmcnt(0)
	ds_read2_b32 v[214:215], v10 offset1:33
	ds_read2_b32 v[222:223], v10 offset0:66 offset1:99
	ds_read2_b32 v[224:225], v10 offset0:132 offset1:165
	ds_read2_b32 v[226:227], v10 offset0:198 offset1:231
	ds_read2_b32 v[228:229], v10 offset0:8 offset1:41
	ds_read2_b32 v[230:231], v10 offset0:74 offset1:107
	ds_read2_b32 v[232:233], v10 offset0:140 offset1:173
	ds_read2_b32 v[234:235], v10 offset0:206 offset1:239
	s_waitcnt lgkmcnt(0)
	ds_read2_b32 v[236:237], v10 offset0:16 offset1:49
	ds_read2_b32 v[238:239], v10 offset0:82 offset1:115
	ds_read2_b32 v[240:241], v10 offset0:148 offset1:181
	ds_read2_b32 v[242:243], v10 offset0:214 offset1:247
	ds_read2_b32 v[244:245], v10 offset0:24 offset1:57
	ds_read2_b32 v[246:247], v10 offset0:90 offset1:123
	ds_read2_b32 v[248:249], v10 offset0:156 offset1:189
	ds_read2_b32 v[250:251], v10 offset0:222 offset1:255
	v_cvt_pk_bf16_f32 v26, v214, v215
	v_add_u32_e32 v30, s30, v1
	v_cvt_pk_bf16_f32 v27, v222, v223
	v_ashrrev_i32_e32 v31, 31, v30
	v_cvt_pk_bf16_f32 v28, v224, v225
	v_lshlrev_b64 v[30:31], 12, v[30:31]
	v_lshl_add_u64 v[34:35], s[6:7], 0, v[4:5]
	v_cvt_pk_bf16_f32 v29, v226, v227
	v_lshl_add_u64 v[30:31], v[34:35], 0, v[30:31]
	global_store_dwordx4 v[30:31], v[26:29], off nt
	s_nop 1
	s_mov_b64 s[6:7], 0
	v_cvt_pk_bf16_f32 v26, v228, v229
	v_add_u32_e32 v32, s30, v7
	v_ashrrev_i32_e32 v33, 31, v32
	v_lshlrev_b64 v[32:33], 12, v[32:33]
	v_cvt_pk_bf16_f32 v27, v230, v231
	v_lshl_add_u64 v[32:33], v[34:35], 0, v[32:33]
	v_cvt_pk_bf16_f32 v28, v232, v233
	v_cvt_pk_bf16_f32 v29, v234, v235
	global_store_dwordx4 v[32:33], v[26:29], off nt
	s_nop 1
	v_add_u32_e32 v32, s30, v8
	v_ashrrev_i32_e32 v33, 31, v32
	s_waitcnt lgkmcnt(0)
	v_cvt_pk_bf16_f32 v26, v236, v237
	v_lshlrev_b64 v[32:33], 12, v[32:33]
	v_cvt_pk_bf16_f32 v27, v238, v239
	v_lshl_add_u64 v[32:33], v[34:35], 0, v[32:33]
	v_cvt_pk_bf16_f32 v28, v240, v241
	v_cvt_pk_bf16_f32 v29, v242, v243
	global_store_dwordx4 v[32:33], v[26:29], off nt
	s_nop 1
	v_add_u32_e32 v32, s30, v9
	v_ashrrev_i32_e32 v33, 31, v32
	v_cvt_pk_bf16_f32 v26, v244, v245
	v_lshlrev_b64 v[32:33], 12, v[32:33]
	v_cvt_pk_bf16_f32 v27, v246, v247
	v_lshl_add_u64 v[32:33], v[34:35], 0, v[32:33]
	v_cvt_pk_bf16_f32 v28, v248, v249
	v_cvt_pk_bf16_f32 v29, v250, v251
	global_store_dwordx4 v[32:33], v[26:29], off nt
	s_nop 1
	s_waitcnt lgkmcnt(0)
; __device__ __forceinline__ unsigned pk2(float lo, float hi) { unsigned r; asm volatile("v_cvt_pk_bf16_f32 %0, %1, %2" : "=v"(r) : "v"(lo), "v"(hi)); return r; }
; __device__ __forceinline__ void transpose_item(const float* W, int K, int N, bf16_t* WT, int rstep, int roff, float* scr, int item, int lane) {
;   const int nblk = N / 32, kb = item / nblk, nb = item % nblk, k0 = 64 * kb, n0 = 32 * nb;
;   f32x4 v[8];
; #pragma unroll
;   for (int i = 0; i < 8; ++i) v[i] = __builtin_nontemporal_load((const f32x4*)(W + (size_t)(k0 + i * 8 + (lane >> 3)) * N + n0 + (lane & 7) * 4));
; #pragma unroll
;   for (int i = 0; i < 8; ++i) { float* d = scr + (i * 8 + (lane >> 3)) * 33 + (lane & 7) * 4; d[0] = v[i].x; d[1] = v[i].y; d[2] = v[i].z; d[3] = v[i].w; }
;   __builtin_amdgcn_wave_barrier(); asm volatile("s_waitcnt lgkmcnt(0)" ::: "memory");
;   const int c = lane & 7;
; #pragma unroll
;   for (int j = 0; j < 4; ++j) { const int nl = (lane >> 3) + 8 * j, n = n0 + nl; const float* s = scr + (8 * c) * 33 + nl;
;     u32x4 o; o.x = pk2(s[0 * 33], s[1 * 33]); o.y = pk2(s[2 * 33], s[3 * 33]); o.z = pk2(s[4 * 33], s[5 * 33]); o.w = pk2(s[6 * 33], s[7 * 33]);
;     const int row = n + (n >> 7) * rstep + roff;
;     __builtin_nontemporal_store(o, (u32x4*)(WT + (size_t)row * K + k0 + 8 * c)); }
;   __builtin_amdgcn_wave_barrier(); asm volatile("s_waitcnt lgkmcnt(0)" ::: "memory");
; __device__ __forceinline__ void convert_item(const P& p, int it, float* scr, int lane) {
;     ...
;     if (r < IT_WIN) transpose_item(p.w_in + (size_t)l * DM * INW, DM, INW, WSP(bf16_t, WS_WIN) + (size_t)l * INW * DM, 0, 0, scr, r, lane);
.LBB0_711:
	s_andn2_b64 vcc, exec, s[6:7]
	s_cbranch_vccnz .LBB0_688
	s_mul_i32 s7, s12, 0x3000000
	s_mul_hi_i32 s6, s12, 0x3000000
	s_add_u32 s7, s48, s7
	s_addc_u32 s22, s49, s6
	s_mul_hi_i32 s6, s12, 0x1800000
	s_mul_i32 s12, s12, 0x1800000
	s_add_u32 s23, s14, s12
	s_addc_u32 s24, s15, s6
	s_mul_i32 s6, s20, 0x2aab
	s_lshr_b32 s12, s6, 31
	s_ashr_i32 s6, s6, 21
	s_add_i32 s6, s6, s12
	s_sext_i32_i16 s12, s6
	s_mulk_i32 s6, 0xc0
	s_sub_i32 s6, s20, s6
	s_sext_i32_i16 s13, s6
	s_lshl_b32 s6, s12, 6
	s_lshl_b32 s12, s13, 5
	s_ashr_i32 s13, s12, 31
	s_lshl_b64 s[20:21], s[12:13], 2
	s_add_u32 s20, s7, s20
	v_add_u32_e32 v5, s6, v1
	s_addc_u32 s21, s22, s21
	v_lshl_add_u64 v[54:55], s[20:21], 0, v[96:97]
	s_movk_i32 s7, 0x6000
	v_add_u32_e32 v28, 8, v5
	v_add_u32_e32 v34, 16, v5
	v_add_u32_e32 v36, 24, v5
	v_add_u32_e32 v42, 32, v5
	v_add_u32_e32 v44, 40, v5
	v_mad_i64_i32 v[26:27], s[20:21], v5, s7, v[54:55]
	v_mad_i64_i32 v[30:31], s[20:21], v28, s7, v[54:55]
	v_mad_i64_i32 v[34:35], s[20:21], v34, s7, v[54:55]
	v_mad_i64_i32 v[38:39], s[20:21], v36, s7, v[54:55]
	v_mad_i64_i32 v[42:43], s[20:21], v42, s7, v[54:55]
	v_mad_i64_i32 v[46:47], s[20:21], v44, s7, v[54:55]
	global_load_dwordx4 v[26:29], v[26:27], off nt
	s_nop 0
	global_load_dwordx4 v[30:33], v[30:31], off nt
	s_nop 0
	global_load_dwordx4 v[34:37], v[34:35], off nt
	s_nop 0
	global_load_dwordx4 v[38:41], v[38:39], off nt
	s_nop 0
	global_load_dwordx4 v[42:45], v[42:43], off nt
	s_nop 0
	global_load_dwordx4 v[46:49], v[46:47], off nt
	v_add_u32_e32 v50, 48, v5
	v_mad_i64_i32 v[50:51], s[20:21], v50, s7, v[54:55]
	global_load_dwordx4 v[50:53], v[50:51], off nt
	v_add_u32_e32 v5, 56, v5
	v_mad_i64_i32 v[54:55], s[20:21], v5, s7, v[54:55]
	global_load_dwordx4 v[54:57], v[54:55], off nt
	s_ashr_i32 s7, s6, 31
	s_lshl_b64 s[6:7], s[6:7], 1
	s_add_u32 s6, s23, s6
	v_mov_b32_e32 v5, v97
	s_addc_u32 s7, s24, s7
	v_lshl_add_u64 v[4:5], s[6:7], 0, v[4:5]
	s_movk_i32 s82, 0x6000
	s_waitcnt vmcnt(0)
	ds_write2_b32 v11, v26, v27 offset1:1
	ds_write2_b32 v11, v28, v29 offset0:2 offset1:3
	ds_write2_b32 v12, v30, v31 offset1:1
	ds_write2_b32 v13, v32, v33 offset1:1
	ds_write2_b32 v14, v34, v35 offset1:1
	ds_write2_b32 v15, v36, v37 offset1:1
	ds_write2_b32 v16, v38, v39 offset1:1
	ds_write2_b32 v17, v40, v41 offset1:1
	ds_write2_b32 v18, v42, v43 offset1:1
	ds_write2_b32 v19, v44, v45 offset1:1
	ds_write2_b32 v20, v46, v47 offset1:1
	ds_write2_b32 v21, v48, v49 offset1:1
	ds_write2_b32 v22, v50, v51 offset1:1
	ds_write2_b32 v23, v52, v53 offset1:1
	ds_write2_b32 v24, v54, v55 offset1:1
	ds_write2_b32 v25, v56, v57 offset1:1
	s_waitcnt lgkmcnt(0)
	ds_read2_b32 v[214:215], v10 offset1:33
	ds_read2_b32 v[222:223], v10 offset0:66 offset1:99
	ds_read2_b32 v[224:225], v10 offset0:132 offset1:165
	ds_read2_b32 v[226:227], v10 offset0:198 offset1:231
	ds_read2_b32 v[228:229], v10 offset0:8 offset1:41
	ds_read2_b32 v[230:231], v10 offset0:74 offset1:107
	ds_read2_b32 v[232:233], v10 offset0:140 offset1:173
	ds_read2_b32 v[234:235], v10 offset0:206 offset1:239
	s_waitcnt lgkmcnt(0)
	ds_read2_b32 v[236:237], v10 offset0:16 offset1:49
	ds_read2_b32 v[238:239], v10 offset0:82 offset1:115
	ds_read2_b32 v[240:241], v10 offset0:148 offset1:181
	ds_read2_b32 v[242:243], v10 offset0:214 offset1:247
	ds_read2_b32 v[244:245], v10 offset0:24 offset1:57
	ds_read2_b32 v[246:247], v10 offset0:90 offset1:123
	ds_read2_b32 v[248:249], v10 offset0:156 offset1:189
	ds_read2_b32 v[250:251], v10 offset0:222 offset1:255
	v_cvt_pk_bf16_f32 v12, v214, v215
	v_add_u32_e32 v16, s12, v1
	v_cvt_pk_bf16_f32 v13, v222, v223
	v_ashrrev_i32_e32 v17, 31, v16
	v_cvt_pk_bf16_f32 v14, v224, v225
	v_lshlrev_b64 v[16:17], 12, v[16:17]
	v_cvt_pk_bf16_f32 v15, v226, v227
	v_lshl_add_u64 v[16:17], v[4:5], 0, v[16:17]
	global_store_dwordx4 v[16:17], v[12:15], off nt
	s_nop 1
	s_nop 0
	v_cvt_pk_bf16_f32 v12, v228, v229
	v_add_u32_e32 v18, s12, v7
	v_ashrrev_i32_e32 v19, 31, v18
	v_lshlrev_b64 v[18:19], 12, v[18:19]
	v_cvt_pk_bf16_f32 v13, v230, v231
	v_lshl_add_u64 v[18:19], v[4:5], 0, v[18:19]
	v_cvt_pk_bf16_f32 v14, v232, v233
	v_cvt_pk_bf16_f32 v15, v234, v235
	global_store_dwordx4 v[18:19], v[12:15], off nt
	s_nop 1
	v_add_u32_e32 v18, s12, v8
	v_ashrrev_i32_e32 v19, 31, v18
	s_waitcnt lgkmcnt(0)
	v_cvt_pk_bf16_f32 v12, v236, v237
	v_lshlrev_b64 v[18:19], 12, v[18:19]
	v_cvt_pk_bf16_f32 v13, v238, v239
	v_lshl_add_u64 v[18:19], v[4:5], 0, v[18:19]
	v_cvt_pk_bf16_f32 v14, v240, v241
	v_cvt_pk_bf16_f32 v15, v242, v243
	global_store_dwordx4 v[18:19], v[12:15], off nt
	s_nop 1
	v_add_u32_e32 v18, s12, v9
	v_ashrrev_i32_e32 v19, 31, v18
	v_cvt_pk_bf16_f32 v12, v244, v245
	v_lshlrev_b64 v[18:19], 12, v[18:19]
	v_cvt_pk_bf16_f32 v13, v246, v247
	v_lshl_add_u64 v[4:5], v[4:5], 0, v[18:19]
	v_cvt_pk_bf16_f32 v14, v248, v249
	v_cvt_pk_bf16_f32 v15, v250, v251
	global_store_dwordx4 v[4:5], v[12:15], off nt
	s_nop 1
	s_waitcnt lgkmcnt(0)
	s_branch .LBB0_688

; __device__ __forceinline__ unsigned pk2(float lo, float hi) { unsigned r; asm volatile("v_cvt_pk_bf16_f32 %0, %1, %2" : "=v"(r) : "v"(lo), "v"(hi)); return r; }
; __device__ __forceinline__ void transpose_item(const float* W, int K, int N, bf16_t* WT, int rstep, int roff, float* scr, int item, int lane) {
;   const int nblk = N / 32, kb = item / nblk, nb = item % nblk, k0 = 64 * kb, n0 = 32 * nb;
;   f32x4 v[8];
; #pragma unroll
;   for (int i = 0; i < 8; ++i) v[i] = __builtin_nontemporal_load((const f32x4*)(W + (size_t)(k0 + i * 8 + (lane >> 3)) * N + n0 + (lane & 7) * 4));
; #pragma unroll
;   for (int i = 0; i < 8; ++i) { float* d = scr + (i * 8 + (lane >> 3)) * 33 + (lane & 7) * 4; d[0] = v[i].x; d[1] = v[i].y; d[2] = v[i].z; d[3] = v[i].w; }
;   __builtin_amdgcn_wave_barrier(); asm volatile("s_waitcnt lgkmcnt(0)" ::: "memory");
;   const int c = lane & 7;
; #pragma unroll
;   for (int j = 0; j < 4; ++j) { const int nl = (lane >> 3) + 8 * j, n = n0 + nl; const float* s = scr + (8 * c) * 33 + nl;
;     u32x4 o; o.x = pk2(s[0 * 33], s[1 * 33]); o.y = pk2(s[2 * 33], s[3 * 33]); o.z = pk2(s[4 * 33], s[5 * 33]); o.w = pk2(s[6 * 33], s[7 * 33]);
;     const int row = n + (n >> 7) * rstep + roff;
;     __builtin_nontemporal_store(o, (u32x4*)(WT + (size_t)row * K + k0 + 8 * c)); }
;   __builtin_amdgcn_wave_barrier(); asm volatile("s_waitcnt lgkmcnt(0)" ::: "memory");
; __device__ __forceinline__ void convert_item(const P& p, int it, float* scr, int lane) {
;     ...
;     const int idx = it - IT_DENSE, m = idx / IT_EXP, sub = idx % IT_EXP, le = m / 3, which = m % 3;
;     if (which == 0) transpose_item(p.wg + (size_t)le * DM * EFF, DM, EFF, WSP(bf16_t, WS_WGU) + (size_t)le * 1024 * DM, 128, 0, scr, sub, lane);
;     else if (which == 1) transpose_item(p.wu + (size_t)le * DM * EFF, DM, EFF, WSP(bf16_t, WS_WGU) + (size_t)le * 1024 * DM, 128, 128, scr, sub, lane);
;     else transpose_item(p.wd + (size_t)le * EFF * DM, EFF, DM, WSP(bf16_t, WS_WD) + (size_t)le * DM * EFF, 0, 0, scr, sub, lane);
.LBB0_1002:
	s_cmpk_gt_i32 s21, 0x3fff
	s_mov_b64 s[6:7], -1
	s_cbranch_scc0 .LBB0_1012
	s_add_i32 s6, s21, 0xffffc000
	s_lshr_b32 s7, s6, 9
	s_mul_hi_u32 s6, s6, 0xaaaaaaab
	s_lshr_b32 s64, s6, 10
	s_mul_hi_u32 s6, s7, 0x55555556
	s_mul_i32 s6, s6, 3
	s_and_b32 s22, s21, 0x1ff
	s_sub_i32 s24, s7, s6
	s_lshl_b64 s[14:15], s[64:65], 22
	s_lshl_b32 s23, s21, 5
	s_cmp_lt_i32 s24, 1
	s_mov_b64 s[6:7], -1
	s_cbranch_scc1 .LBB0_1009
	s_cmp_lg_u32 s24, 1
	s_cbranch_scc0 .LBB0_1006
	s_add_u32 s34, s0, s14
	s_addc_u32 s35, s1, s15
	s_lshl_b64 s[30:31], s[64:65], 21
	s_add_u32 s7, s9, s30
	s_addc_u32 s24, s16, s31
	s_and_b32 s6, s23, 0x7e0
	s_and_b32 s30, s21, 0x1c0
	s_lshl_b32 s31, s6, 2
	v_add_u32_e32 v4, s30, v1
	s_add_u32 s34, s34, s31
	s_addc_u32 s35, s35, 0
	v_lshlrev_b32_e32 v96, 2, v0
	v_ashrrev_i32_e32 v5, 31, v4
	v_lshl_add_u64 v[12:13], s[34:35], 0, v[96:97]
	v_lshlrev_b64 v[4:5], 13, v[4:5]
	v_lshl_add_u64 v[4:5], v[12:13], 0, v[4:5]
	s_mov_b32 s31, 0x10000
	v_add_co_u32_e32 v16, vcc, s31, v4
	s_mov_b32 s31, 0x20000
	s_nop 0
	v_addc_co_u32_e32 v17, vcc, 0, v5, vcc
	global_load_dwordx4 v[12:15], v[4:5], off nt
	global_load_dwordx4 v[20:23], v[16:17], off nt
	v_add_co_u32_e32 v16, vcc, s31, v4
	s_mov_b32 s31, 0x30000
	s_nop 0
	v_addc_co_u32_e32 v17, vcc, 0, v5, vcc
	global_load_dwordx4 v[24:27], v[16:17], off nt
	v_add_co_u32_e32 v16, vcc, s31, v4
	s_mov_b32 s31, 0x40000
	s_nop 0
	v_addc_co_u32_e32 v17, vcc, 0, v5, vcc
	global_load_dwordx4 v[28:31], v[16:17], off nt
	v_add_co_u32_e32 v16, vcc, s31, v4
	s_mov_b32 s31, 0x50000
	s_nop 0
	v_addc_co_u32_e32 v17, vcc, 0, v5, vcc
	global_load_dwordx4 v[32:35], v[16:17], off nt
	v_add_co_u32_e32 v16, vcc, s31, v4
	s_mov_b32 s31, 0x60000
	s_nop 0
	v_addc_co_u32_e32 v17, vcc, 0, v5, vcc
	global_load_dwordx4 v[36:39], v[16:17], off nt
	v_add_co_u32_e32 v16, vcc, s31, v4
	s_mov_b32 s31, 0x70000
	s_nop 0
	v_addc_co_u32_e32 v17, vcc, 0, v5, vcc
	global_load_dwordx4 v[40:43], v[16:17], off nt
	v_add_co_u32_e32 v4, vcc, s31, v4
	s_lshl_b32 s30, s30, 1
	s_nop 0
	v_addc_co_u32_e32 v5, vcc, 0, v5, vcc
	global_load_dwordx4 v[44:47], v[4:5], off nt
	v_add_u32_e32 v4, v3, v6
	v_add_u32_e32 v5, 0x420, v4
	s_add_u32 s30, s7, s30
	v_add_u32_e32 v16, s6, v1
	s_addc_u32 s31, s24, 0
	v_lshlrev_b32_e32 v96, 1, v2
	v_ashrrev_i32_e32 v17, 31, v16
	v_lshlrev_b64 v[16:17], 10, v[16:17]
	s_waitcnt vmcnt(7)
	ds_write2_b32 v4, v12, v13 offset1:1
	ds_write2_b32 v4, v14, v15 offset0:2 offset1:3
	s_waitcnt vmcnt(6)
	ds_write2_b32 v5, v20, v21 offset1:1
	v_add_u32_e32 v5, 0x428, v4
	ds_write2_b32 v5, v22, v23 offset1:1
	v_add_u32_e32 v5, 0x840, v4
	s_waitcnt vmcnt(5)
	ds_write2_b32 v5, v24, v25 offset1:1
	v_add_u32_e32 v5, 0x848, v4
	ds_write2_b32 v5, v26, v27 offset1:1
	v_add_u32_e32 v5, 0xc60, v4
	s_waitcnt vmcnt(4)
	ds_write2_b32 v5, v28, v29 offset1:1
	v_add_u32_e32 v5, 0xc68, v4
	ds_write2_b32 v5, v30, v31 offset1:1
	v_add_u32_e32 v5, 0x1080, v4
	s_waitcnt vmcnt(3)
	ds_write2_b32 v5, v32, v33 offset1:1
	v_add_u32_e32 v5, 0x1088, v4
	ds_write2_b32 v5, v34, v35 offset1:1
	v_add_u32_e32 v5, 0x14a0, v4
	s_waitcnt vmcnt(2)
	ds_write2_b32 v5, v36, v37 offset1:1
	v_add_u32_e32 v5, 0x14a8, v4
	ds_write2_b32 v5, v38, v39 offset1:1
	v_add_u32_e32 v5, 0x18c0, v4
	s_waitcnt vmcnt(1)
	ds_write2_b32 v5, v40, v41 offset1:1
	v_add_u32_e32 v5, 0x18c8, v4
	ds_write2_b32 v5, v42, v43 offset1:1
	v_add_u32_e32 v5, 0x1ce0, v4
	v_add_u32_e32 v4, 0x1ce8, v4
	s_waitcnt vmcnt(0)
	ds_write2_b32 v5, v44, v45 offset1:1
	ds_write2_b32 v4, v46, v47 offset1:1
	s_waitcnt lgkmcnt(0)
	ds_read2_b32 v[214:215], v10 offset1:33
	ds_read2_b32 v[222:223], v10 offset0:66 offset1:99
	ds_read2_b32 v[224:225], v10 offset0:132 offset1:165
	ds_read2_b32 v[226:227], v10 offset0:198 offset1:231
	ds_read2_b32 v[228:229], v10 offset0:8 offset1:41
	ds_read2_b32 v[230:231], v10 offset0:74 offset1:107
	ds_read2_b32 v[232:233], v10 offset0:140 offset1:173
	ds_read2_b32 v[234:235], v10 offset0:206 offset1:239
	s_waitcnt lgkmcnt(0)
	ds_read2_b32 v[236:237], v10 offset0:16 offset1:49
	ds_read2_b32 v[238:239], v10 offset0:82 offset1:115
	ds_read2_b32 v[240:241], v10 offset0:148 offset1:181
	ds_read2_b32 v[242:243], v10 offset0:214 offset1:247
	ds_read2_b32 v[244:245], v10 offset0:24 offset1:57
	ds_read2_b32 v[246:247], v10 offset0:90 offset1:123
	ds_read2_b32 v[248:249], v10 offset0:156 offset1:189
	ds_read2_b32 v[250:251], v10 offset0:222 offset1:255
	v_lshl_add_u64 v[4:5], s[30:31], 0, v[96:97]
	v_cvt_pk_bf16_f32 v12, v214, v215
	v_cvt_pk_bf16_f32 v13, v222, v223
	v_lshl_add_u64 v[16:17], v[4:5], 0, v[16:17]
	v_cvt_pk_bf16_f32 v14, v224, v225
	v_cvt_pk_bf16_f32 v15, v226, v227
	global_store_dwordx4 v[16:17], v[12:15], off nt
	s_nop 1
	v_add_u32_e32 v16, s6, v7
	v_ashrrev_i32_e32 v17, 31, v16
	v_cvt_pk_bf16_f32 v12, v228, v229
	v_lshlrev_b64 v[16:17], 10, v[16:17]
	v_cvt_pk_bf16_f32 v13, v230, v231
	v_lshl_add_u64 v[16:17], v[4:5], 0, v[16:17]
	v_cvt_pk_bf16_f32 v14, v232, v233
	v_cvt_pk_bf16_f32 v15, v234, v235
	global_store_dwordx4 v[16:17], v[12:15], off nt
	s_nop 1
	v_add_u32_e32 v16, s6, v8
	s_waitcnt lgkmcnt(0)
	v_ashrrev_i32_e32 v17, 31, v16
	v_cvt_pk_bf16_f32 v12, v236, v237
	v_lshlrev_b64 v[16:17], 10, v[16:17]
	v_cvt_pk_bf16_f32 v13, v238, v239
	v_lshl_add_u64 v[16:17], v[4:5], 0, v[16:17]
	v_cvt_pk_bf16_f32 v14, v240, v241
	v_cvt_pk_bf16_f32 v15, v242, v243
	global_store_dwordx4 v[16:17], v[12:15], off nt
	s_nop 1
	v_add_u32_e32 v16, s6, v9
	v_ashrrev_i32_e32 v17, 31, v16
	v_cvt_pk_bf16_f32 v12, v244, v245
	v_lshlrev_b64 v[16:17], 10, v[16:17]
	v_cvt_pk_bf16_f32 v13, v246, v247
	v_lshl_add_u64 v[4:5], v[4:5], 0, v[16:17]
	v_cvt_pk_bf16_f32 v14, v248, v249
	v_cvt_pk_bf16_f32 v15, v250, v251
	global_store_dwordx4 v[4:5], v[12:15], off nt
	s_nop 1
	s_waitcnt lgkmcnt(0)
	s_mov_b64 s[6:7], 0
; __device__ __forceinline__ unsigned pk2(float lo, float hi) { unsigned r; asm volatile("v_cvt_pk_bf16_f32 %0, %1, %2" : "=v"(r) : "v"(lo), "v"(hi)); return r; }
; __device__ __forceinline__ void transpose_item(const float* W, int K, int N, bf16_t* WT, int rstep, int roff, float* scr, int item, int lane) {
;   const int nblk = N / 32, kb = item / nblk, nb = item % nblk, k0 = 64 * kb, n0 = 32 * nb;
;   f32x4 v[8];
; #pragma unroll
;   for (int i = 0; i < 8; ++i) v[i] = __builtin_nontemporal_load((const f32x4*)(W + (size_t)(k0 + i * 8 + (lane >> 3)) * N + n0 + (lane & 7) * 4));
; #pragma unroll
;   for (int i = 0; i < 8; ++i) { float* d = scr + (i * 8 + (lane >> 3)) * 33 + (lane & 7) * 4; d[0] = v[i].x; d[1] = v[i].y; d[2] = v[i].z; d[3] = v[i].w; }
;   __builtin_amdgcn_wave_barrier(); asm volatile("s_waitcnt lgkmcnt(0)" ::: "memory");
;   const int c = lane & 7;
; #pragma unroll
;   for (int j = 0; j < 4; ++j) { const int nl = (lane >> 3) + 8 * j, n = n0 + nl; const float* s = scr + (8 * c) * 33 + nl;
;     u32x4 o; o.x = pk2(s[0 * 33], s[1 * 33]); o.y = pk2(s[2 * 33], s[3 * 33]); o.z = pk2(s[4 * 33], s[5 * 33]); o.w = pk2(s[6 * 33], s[7 * 33]);
;     const int row = n + (n >> 7) * rstep + roff;
;     __builtin_nontemporal_store(o, (u32x4*)(WT + (size_t)row * K + k0 + 8 * c)); }
;   __builtin_amdgcn_wave_barrier(); asm volatile("s_waitcnt lgkmcnt(0)" ::: "memory");
; __device__ __forceinline__ void convert_item(const P& p, int it, float* scr, int lane) {
;     ...
;     else if (which == 1) transpose_item(p.wu + (size_t)le * DM * EFF, DM, EFF, WSP(bf16_t, WS_WGU) + (size_t)le * 1024 * DM, 128, 128, scr, sub, lane);
.LBB0_1006:
	s_andn2_b64 vcc, exec, s[6:7]
	s_cbranch_vccnz .LBB0_1008
	s_add_u32 s31, s62, s14
	s_addc_u32 s35, s63, s15
	s_add_u32 s7, s4, s14
	s_addc_u32 s24, s5, s15
	s_lshl_b32 s6, s22, 2
	s_and_b32 s30, s6, 0x7c0
	s_and_b32 s6, s23, 0x1e0
	s_lshl_b32 s34, s6, 2
	v_add_u32_e32 v4, s30, v1
	s_add_u32 s34, s31, s34
	s_addc_u32 s35, s35, 0
	v_lshlrev_b32_e32 v96, 2, v0
	v_ashrrev_i32_e32 v5, 31, v4
	v_lshl_add_u64 v[12:13], s[34:35], 0, v[96:97]
	v_lshlrev_b64 v[4:5], 11, v[4:5]
	v_lshl_add_u64 v[4:5], v[12:13], 0, v[4:5]
	s_movk_i32 s31, 0x4000
	v_add_co_u32_e32 v16, vcc, s31, v4
	s_mov_b32 s31, 0x8000
	s_nop 0
	v_addc_co_u32_e32 v17, vcc, 0, v5, vcc
	global_load_dwordx4 v[12:15], v[4:5], off nt
	global_load_dwordx4 v[20:23], v[16:17], off nt
	v_add_co_u32_e32 v16, vcc, s31, v4
	s_mov_b32 s31, 0xc000
	s_nop 0
	v_addc_co_u32_e32 v17, vcc, 0, v5, vcc
	global_load_dwordx4 v[24:27], v[16:17], off nt
	v_add_co_u32_e32 v16, vcc, s31, v4
	s_mov_b32 s31, 0x10000
	s_nop 0
	v_addc_co_u32_e32 v17, vcc, 0, v5, vcc
	global_load_dwordx4 v[28:31], v[16:17], off nt
	v_add_co_u32_e32 v16, vcc, s31, v4
	s_mov_b32 s31, 0x14000
	s_nop 0
	v_addc_co_u32_e32 v17, vcc, 0, v5, vcc
	global_load_dwordx4 v[32:35], v[16:17], off nt
	v_add_co_u32_e32 v16, vcc, s31, v4
	s_lshl_b32 s30, s30, 1
	s_nop 0
	v_addc_co_u32_e32 v17, vcc, 0, v5, vcc
	global_load_dwordx4 v[36:39], v[16:17], off nt
	v_add_co_u32_e32 v16, vcc, s93, v4
	v_add_u32_e32 v11, s6, v1
	s_nop 0
	v_addc_co_u32_e32 v17, vcc, 0, v5, vcc
	global_load_dwordx4 v[40:43], v[16:17], off nt
	v_add_co_u32_e32 v4, vcc, s96, v4
	s_add_u32 s30, s7, s30
	s_nop 0
	v_addc_co_u32_e32 v5, vcc, 0, v5, vcc
	global_load_dwordx4 v[44:47], v[4:5], off nt
	v_add_u32_e32 v4, v3, v6
	v_add_u32_e32 v5, 0x420, v4
	s_movk_i32 s7, 0x80
	s_addc_u32 s31, s24, 0
	v_lshlrev_b32_e32 v96, 1, v2
	s_waitcnt vmcnt(7)
	ds_write2_b32 v4, v12, v13 offset1:1
	ds_write2_b32 v4, v14, v15 offset0:2 offset1:3
	s_waitcnt vmcnt(6)
	ds_write2_b32 v5, v20, v21 offset1:1
	v_add_u32_e32 v5, 0x428, v4
	ds_write2_b32 v5, v22, v23 offset1:1
	v_add_u32_e32 v5, 0x840, v4
	s_waitcnt vmcnt(5)
	ds_write2_b32 v5, v24, v25 offset1:1
	v_add_u32_e32 v5, 0x848, v4
	ds_write2_b32 v5, v26, v27 offset1:1
	v_add_u32_e32 v5, 0xc60, v4
	s_waitcnt vmcnt(4)
	ds_write2_b32 v5, v28, v29 offset1:1
	v_add_u32_e32 v5, 0xc68, v4
	ds_write2_b32 v5, v30, v31 offset1:1
	v_add_u32_e32 v5, 0x1080, v4
	s_waitcnt vmcnt(3)
	ds_write2_b32 v5, v32, v33 offset1:1
	v_add_u32_e32 v5, 0x1088, v4
	ds_write2_b32 v5, v34, v35 offset1:1
	v_add_u32_e32 v5, 0x14a0, v4
	s_waitcnt vmcnt(2)
	ds_write2_b32 v5, v36, v37 offset1:1
	v_add_u32_e32 v5, 0x14a8, v4
	ds_write2_b32 v5, v38, v39 offset1:1
	v_add_u32_e32 v5, 0x18c0, v4
	s_waitcnt vmcnt(1)
	ds_write2_b32 v5, v40, v41 offset1:1
	v_add_u32_e32 v5, 0x18c8, v4
	ds_write2_b32 v5, v42, v43 offset1:1
	v_add_u32_e32 v5, 0x1ce0, v4
	v_add_u32_e32 v4, 0x1ce8, v4
	s_waitcnt vmcnt(0)
	ds_write2_b32 v5, v44, v45 offset1:1
	ds_write2_b32 v4, v46, v47 offset1:1
	s_waitcnt lgkmcnt(0)
	ds_read2_b32 v[214:215], v10 offset1:33
	ds_read2_b32 v[222:223], v10 offset0:66 offset1:99
	ds_read2_b32 v[224:225], v10 offset0:132 offset1:165
	ds_read2_b32 v[226:227], v10 offset0:198 offset1:231
	ds_read2_b32 v[228:229], v10 offset0:8 offset1:41
	ds_read2_b32 v[230:231], v10 offset0:74 offset1:107
	ds_read2_b32 v[232:233], v10 offset0:140 offset1:173
	ds_read2_b32 v[234:235], v10 offset0:206 offset1:239
	s_waitcnt lgkmcnt(0)
	ds_read2_b32 v[236:237], v10 offset0:16 offset1:49
	ds_read2_b32 v[238:239], v10 offset0:82 offset1:115
	ds_read2_b32 v[240:241], v10 offset0:148 offset1:181
	ds_read2_b32 v[242:243], v10 offset0:214 offset1:247
	ds_read2_b32 v[244:245], v10 offset0:24 offset1:57
	ds_read2_b32 v[246:247], v10 offset0:90 offset1:123
	ds_read2_b32 v[248:249], v10 offset0:156 offset1:189
	ds_read2_b32 v[250:251], v10 offset0:222 offset1:255
	v_cvt_pk_bf16_f32 v12, v214, v215
	v_cvt_pk_bf16_f32 v13, v222, v223
	v_cvt_pk_bf16_f32 v14, v224, v225
	v_cvt_pk_bf16_f32 v15, v226, v227
	v_and_b32_e32 v16, 0xffffff80, v11
	v_add3_u32 v16, v11, v16, s7
	v_ashrrev_i32_e32 v17, 31, v16
	v_lshl_add_u64 v[4:5], s[30:31], 0, v[96:97]
	v_lshlrev_b64 v[16:17], 12, v[16:17]
	v_lshl_add_u64 v[16:17], v[4:5], 0, v[16:17]
	global_store_dwordx4 v[16:17], v[12:15], off nt
	s_nop 1
	v_add_u32_e32 v11, s6, v7
	v_cvt_pk_bf16_f32 v12, v228, v229
	v_cvt_pk_bf16_f32 v13, v230, v231
	v_cvt_pk_bf16_f32 v14, v232, v233
	v_cvt_pk_bf16_f32 v15, v234, v235
	v_and_b32_e32 v16, 0xffffff80, v11
	v_add3_u32 v16, v11, v16, s7
	v_ashrrev_i32_e32 v17, 31, v16
	v_lshlrev_b64 v[16:17], 12, v[16:17]
	v_lshl_add_u64 v[16:17], v[4:5], 0, v[16:17]
	global_store_dwordx4 v[16:17], v[12:15], off nt
	s_nop 1
	s_waitcnt lgkmcnt(0)
	v_add_u32_e32 v11, s6, v8
	v_cvt_pk_bf16_f32 v12, v236, v237
	v_cvt_pk_bf16_f32 v13, v238, v239
	v_cvt_pk_bf16_f32 v14, v240, v241
	v_cvt_pk_bf16_f32 v15, v242, v243
	v_and_b32_e32 v16, 0xffffff80, v11
	v_add3_u32 v16, v11, v16, s7
	v_ashrrev_i32_e32 v17, 31, v16
	v_lshlrev_b64 v[16:17], 12, v[16:17]
	v_lshl_add_u64 v[16:17], v[4:5], 0, v[16:17]
	global_store_dwordx4 v[16:17], v[12:15], off nt
	s_nop 1
	v_add_u32_e32 v11, s6, v9
	v_cvt_pk_bf16_f32 v12, v244, v245
	v_cvt_pk_bf16_f32 v13, v246, v247
	v_cvt_pk_bf16_f32 v14, v248, v249
	v_cvt_pk_bf16_f32 v15, v250, v251
	v_and_b32_e32 v16, 0xffffff80, v11
	v_add3_u32 v16, v11, v16, s7
	v_ashrrev_i32_e32 v17, 31, v16
	v_lshlrev_b64 v[16:17], 12, v[16:17]
	v_lshl_add_u64 v[4:5], v[4:5], 0, v[16:17]
	global_store_dwordx4 v[4:5], v[12:15], off nt
	s_nop 1
	s_waitcnt lgkmcnt(0)

; __device__ __forceinline__ unsigned pk2(float lo, float hi) { unsigned r; asm volatile("v_cvt_pk_bf16_f32 %0, %1, %2" : "=v"(r) : "v"(lo), "v"(hi)); return r; }
; __device__ __forceinline__ void transpose_item(const float* W, int K, int N, bf16_t* WT, int rstep, int roff, float* scr, int item, int lane) {
;   const int nblk = N / 32, kb = item / nblk, nb = item % nblk, k0 = 64 * kb, n0 = 32 * nb;
;   f32x4 v[8];
; #pragma unroll
;   for (int i = 0; i < 8; ++i) v[i] = __builtin_nontemporal_load((const f32x4*)(W + (size_t)(k0 + i * 8 + (lane >> 3)) * N + n0 + (lane & 7) * 4));
; #pragma unroll
;   for (int i = 0; i < 8; ++i) { float* d = scr + (i * 8 + (lane >> 3)) * 33 + (lane & 7) * 4; d[0] = v[i].x; d[1] = v[i].y; d[2] = v[i].z; d[3] = v[i].w; }
;   __builtin_amdgcn_wave_barrier(); asm volatile("s_waitcnt lgkmcnt(0)" ::: "memory");
;   const int c = lane & 7;
; #pragma unroll
;   for (int j = 0; j < 4; ++j) { const int nl = (lane >> 3) + 8 * j, n = n0 + nl; const float* s = scr + (8 * c) * 33 + nl;
;     u32x4 o; o.x = pk2(s[0 * 33], s[1 * 33]); o.y = pk2(s[2 * 33], s[3 * 33]); o.z = pk2(s[4 * 33], s[5 * 33]); o.w = pk2(s[6 * 33], s[7 * 33]);
;     const int row = n + (n >> 7) * rstep + roff;
;     __builtin_nontemporal_store(o, (u32x4*)(WT + (size_t)row * K + k0 + 8 * c)); }
;   __builtin_amdgcn_wave_barrier(); asm volatile("s_waitcnt lgkmcnt(0)" ::: "memory");
; __device__ __forceinline__ void convert_item(const P& p, int it, float* scr, int lane) {
;     ...
;     if (which == 0) transpose_item(p.wg + (size_t)le * DM * EFF, DM, EFF, WSP(bf16_t, WS_WGU) + (size_t)le * 1024 * DM, 128, 0, scr, sub, lane);
.LBB0_1009:
	s_andn2_b64 vcc, exec, s[6:7]
	s_cbranch_vccnz .LBB0_1011
	s_add_u32 s24, s60, s14
	s_addc_u32 s30, s61, s15
	s_add_u32 s7, s4, s14
	s_addc_u32 s14, s5, s15
	s_lshl_b32 s6, s22, 2
	s_and_b32 s15, s6, 0x7c0
	s_and_b32 s6, s23, 0x1e0
	s_lshl_b32 s22, s6, 2
	v_add_u32_e32 v4, s15, v1
	s_add_u32 s22, s24, s22
	s_addc_u32 s23, s30, 0
	v_lshlrev_b32_e32 v96, 2, v0
	v_ashrrev_i32_e32 v5, 31, v4
	v_lshl_add_u64 v[12:13], s[22:23], 0, v[96:97]
	v_lshlrev_b64 v[4:5], 11, v[4:5]
	v_lshl_add_u64 v[4:5], v[12:13], 0, v[4:5]
	s_movk_i32 s22, 0x4000
	v_add_co_u32_e32 v16, vcc, s22, v4
	s_mov_b32 s22, 0x8000
	s_nop 0
	v_addc_co_u32_e32 v17, vcc, 0, v5, vcc
	global_load_dwordx4 v[12:15], v[4:5], off nt
	global_load_dwordx4 v[20:23], v[16:17], off nt
	v_add_co_u32_e32 v16, vcc, s22, v4
	s_mov_b32 s22, 0xc000
	s_nop 0
	v_addc_co_u32_e32 v17, vcc, 0, v5, vcc
	global_load_dwordx4 v[24:27], v[16:17], off nt
	v_add_co_u32_e32 v16, vcc, s22, v4
	s_mov_b32 s22, 0x10000
	s_nop 0
	v_addc_co_u32_e32 v17, vcc, 0, v5, vcc
	global_load_dwordx4 v[28:31], v[16:17], off nt
	v_add_co_u32_e32 v16, vcc, s22, v4
	s_mov_b32 s22, 0x14000
	s_nop 0
	v_addc_co_u32_e32 v17, vcc, 0, v5, vcc
	global_load_dwordx4 v[32:35], v[16:17], off nt
	v_add_co_u32_e32 v16, vcc, s22, v4
	v_add_u32_e32 v11, s6, v1
	s_nop 0
	v_addc_co_u32_e32 v17, vcc, 0, v5, vcc
	global_load_dwordx4 v[36:39], v[16:17], off nt
	v_add_co_u32_e32 v16, vcc, s93, v4
	s_lshl_b32 s15, s15, 1
	s_nop 0
	v_addc_co_u32_e32 v17, vcc, 0, v5, vcc
	global_load_dwordx4 v[40:43], v[16:17], off nt
	v_add_co_u32_e32 v4, vcc, s96, v4
	s_add_u32 s22, s7, s15
	s_nop 0
	v_addc_co_u32_e32 v5, vcc, 0, v5, vcc
	global_load_dwordx4 v[44:47], v[4:5], off nt
	v_add_u32_e32 v4, v3, v6
	v_add_u32_e32 v5, 0x420, v4
	s_addc_u32 s23, s14, 0
	v_lshlrev_b32_e32 v96, 1, v2
	s_waitcnt vmcnt(7)
	ds_write2_b32 v4, v12, v13 offset1:1
	ds_write2_b32 v4, v14, v15 offset0:2 offset1:3
	s_waitcnt vmcnt(6)
	ds_write2_b32 v5, v20, v21 offset1:1
	v_add_u32_e32 v5, 0x428, v4
	ds_write2_b32 v5, v22, v23 offset1:1
	v_add_u32_e32 v5, 0x840, v4
	s_waitcnt vmcnt(5)
	ds_write2_b32 v5, v24, v25 offset1:1
	v_add_u32_e32 v5, 0x848, v4
	ds_write2_b32 v5, v26, v27 offset1:1
	v_add_u32_e32 v5, 0xc60, v4
	s_waitcnt vmcnt(4)
	ds_write2_b32 v5, v28, v29 offset1:1
	v_add_u32_e32 v5, 0xc68, v4
	ds_write2_b32 v5, v30, v31 offset1:1
	v_add_u32_e32 v5, 0x1080, v4
	s_waitcnt vmcnt(3)
	ds_write2_b32 v5, v32, v33 offset1:1
	v_add_u32_e32 v5, 0x1088, v4
	ds_write2_b32 v5, v34, v35 offset1:1
	v_add_u32_e32 v5, 0x14a0, v4
	s_waitcnt vmcnt(2)
	ds_write2_b32 v5, v36, v37 offset1:1
	v_add_u32_e32 v5, 0x14a8, v4
	ds_write2_b32 v5, v38, v39 offset1:1
	v_add_u32_e32 v5, 0x18c0, v4
	s_waitcnt vmcnt(1)
	ds_write2_b32 v5, v40, v41 offset1:1
	v_add_u32_e32 v5, 0x18c8, v4
	ds_write2_b32 v5, v42, v43 offset1:1
	v_add_u32_e32 v5, 0x1ce0, v4
	v_add_u32_e32 v4, 0x1ce8, v4
	s_waitcnt vmcnt(0)
	ds_write2_b32 v5, v44, v45 offset1:1
	ds_write2_b32 v4, v46, v47 offset1:1
	s_waitcnt lgkmcnt(0)
	ds_read2_b32 v[214:215], v10 offset1:33
	ds_read2_b32 v[222:223], v10 offset0:66 offset1:99
	ds_read2_b32 v[224:225], v10 offset0:132 offset1:165
	ds_read2_b32 v[226:227], v10 offset0:198 offset1:231
	ds_read2_b32 v[228:229], v10 offset0:8 offset1:41
	ds_read2_b32 v[230:231], v10 offset0:74 offset1:107
	ds_read2_b32 v[232:233], v10 offset0:140 offset1:173
	ds_read2_b32 v[234:235], v10 offset0:206 offset1:239
	s_waitcnt lgkmcnt(0)
	ds_read2_b32 v[236:237], v10 offset0:16 offset1:49
	ds_read2_b32 v[238:239], v10 offset0:82 offset1:115
	ds_read2_b32 v[240:241], v10 offset0:148 offset1:181
	ds_read2_b32 v[242:243], v10 offset0:214 offset1:247
	ds_read2_b32 v[244:245], v10 offset0:24 offset1:57
	ds_read2_b32 v[246:247], v10 offset0:90 offset1:123
	ds_read2_b32 v[248:249], v10 offset0:156 offset1:189
	ds_read2_b32 v[250:251], v10 offset0:222 offset1:255
	v_cvt_pk_bf16_f32 v12, v214, v215
	v_cvt_pk_bf16_f32 v13, v222, v223
	v_cvt_pk_bf16_f32 v14, v224, v225
	v_cvt_pk_bf16_f32 v15, v226, v227
	v_and_b32_e32 v16, 0xffffff80, v11
	v_add_u32_e32 v16, v16, v11
	v_ashrrev_i32_e32 v17, 31, v16
	v_lshl_add_u64 v[4:5], s[22:23], 0, v[96:97]
	v_lshlrev_b64 v[16:17], 12, v[16:17]
	v_lshl_add_u64 v[16:17], v[4:5], 0, v[16:17]
	global_store_dwordx4 v[16:17], v[12:15], off nt
	s_nop 1
	v_add_u32_e32 v11, s6, v7
	v_cvt_pk_bf16_f32 v12, v228, v229
	v_cvt_pk_bf16_f32 v13, v230, v231
	v_cvt_pk_bf16_f32 v14, v232, v233
	v_cvt_pk_bf16_f32 v15, v234, v235
	v_and_b32_e32 v16, 0xffffff80, v11
	v_add_u32_e32 v16, v16, v11
	v_ashrrev_i32_e32 v17, 31, v16
	v_lshlrev_b64 v[16:17], 12, v[16:17]
	v_lshl_add_u64 v[16:17], v[4:5], 0, v[16:17]
	global_store_dwordx4 v[16:17], v[12:15], off nt
	s_nop 1
	s_waitcnt lgkmcnt(0)
	v_add_u32_e32 v11, s6, v8
	v_cvt_pk_bf16_f32 v12, v236, v237
	v_cvt_pk_bf16_f32 v13, v238, v239
	v_cvt_pk_bf16_f32 v14, v240, v241
	v_cvt_pk_bf16_f32 v15, v242, v243
	v_and_b32_e32 v16, 0xffffff80, v11
	v_add_u32_e32 v16, v16, v11
	v_ashrrev_i32_e32 v17, 31, v16
	v_lshlrev_b64 v[16:17], 12, v[16:17]
	v_lshl_add_u64 v[16:17], v[4:5], 0, v[16:17]
	global_store_dwordx4 v[16:17], v[12:15], off nt
	s_nop 1
	v_add_u32_e32 v11, s6, v9
	v_cvt_pk_bf16_f32 v12, v244, v245
	v_cvt_pk_bf16_f32 v13, v246, v247
	v_cvt_pk_bf16_f32 v14, v248, v249
	v_cvt_pk_bf16_f32 v15, v250, v251
	v_and_b32_e32 v16, 0xffffff80, v11
	v_add_u32_e32 v16, v16, v11
	v_ashrrev_i32_e32 v17, 31, v16
	v_lshlrev_b64 v[16:17], 12, v[16:17]
	v_lshl_add_u64 v[4:5], v[4:5], 0, v[16:17]
	global_store_dwordx4 v[4:5], v[12:15], off nt
	s_nop 1
	s_waitcnt lgkmcnt(0)

; __device__ __forceinline__ unsigned pk2(float lo, float hi) { unsigned r; asm volatile("v_cvt_pk_bf16_f32 %0, %1, %2" : "=v"(r) : "v"(lo), "v"(hi)); return r; }
; __device__ __forceinline__ void transpose_item(const float* W, int K, int N, bf16_t* WT, int rstep, int roff, float* scr, int item, int lane) {
;   const int nblk = N / 32, kb = item / nblk, nb = item % nblk, k0 = 64 * kb, n0 = 32 * nb;
;   f32x4 v[8];
; #pragma unroll
;   for (int i = 0; i < 8; ++i) v[i] = __builtin_nontemporal_load((const f32x4*)(W + (size_t)(k0 + i * 8 + (lane >> 3)) * N + n0 + (lane & 7) * 4));
; #pragma unroll
;   for (int i = 0; i < 8; ++i) { float* d = scr + (i * 8 + (lane >> 3)) * 33 + (lane & 7) * 4; d[0] = v[i].x; d[1] = v[i].y; d[2] = v[i].z; d[3] = v[i].w; }
;   __builtin_amdgcn_wave_barrier(); asm volatile("s_waitcnt lgkmcnt(0)" ::: "memory");
;   const int c = lane & 7;
; #pragma unroll
;   for (int j = 0; j < 4; ++j) { const int nl = (lane >> 3) + 8 * j, n = n0 + nl; const float* s = scr + (8 * c) * 33 + nl;
;     u32x4 o; o.x = pk2(s[0 * 33], s[1 * 33]); o.y = pk2(s[2 * 33], s[3 * 33]); o.z = pk2(s[4 * 33], s[5 * 33]); o.w = pk2(s[6 * 33], s[7 * 33]);
;     const int row = n + (n >> 7) * rstep + roff;
;     __builtin_nontemporal_store(o, (u32x4*)(WT + (size_t)row * K + k0 + 8 * c)); }
;   __builtin_amdgcn_wave_barrier(); asm volatile("s_waitcnt lgkmcnt(0)" ::: "memory");
; __device__ __forceinline__ void convert_item(const P& p, int it, float* scr, int lane) {
;   if (it < IT_DENSE) {
;     const int l = it / (IT_WIN + IT_WOUT), r = it % (IT_WIN + IT_WOUT);
;     if (r < IT_WIN) transpose_item(p.w_in + (size_t)l * DM * INW, DM, INW, WSP(bf16_t, WS_WIN) + (size_t)l * INW * DM, 0, 0, scr, r, lane);
;     else transpose_item(p.w_out + (size_t)l * DM * DM, DM, DM, WSP(bf16_t, WS_WOUT) + (size_t)l * DM * DM, 0, 0, scr, r - IT_WIN, lane);
.LBB0_1012:
	s_and_b64 vcc, exec, s[6:7]
	s_cbranch_vccz .LBB0_988
	s_ashr_i32 s6, s21, 31
	s_lshr_b32 s6, s6, 19
	s_add_i32 s6, s21, s6
	s_ashr_i32 s14, s6, 13
	s_and_b32 s6, s6, 0xffffe000
	s_sub_i32 s21, s21, s6
	s_ashr_i32 s15, s14, 31
	v_add_u32_e32 v11, v3, v6
	s_cmpk_gt_i32 s21, 0x17ff
	s_mov_b64 s[6:7], -1
	v_lshlrev_b32_e32 v96, 2, v0
	v_add_u32_e32 v12, 0x420, v11
	v_add_u32_e32 v13, 0x428, v11
	v_add_u32_e32 v14, 0x840, v11
	v_add_u32_e32 v15, 0x848, v11
	v_add_u32_e32 v16, 0xc60, v11
	v_add_u32_e32 v17, 0xc68, v11
	v_add_u32_e32 v19, 0x1080, v11
	v_add_u32_e32 v20, 0x1088, v11
	v_add_u32_e32 v21, 0x14a0, v11
	v_add_u32_e32 v22, 0x14a8, v11
	v_add_u32_e32 v23, 0x18c0, v11
	v_add_u32_e32 v24, 0x18c8, v11
	v_add_u32_e32 v25, 0x1ce0, v11
	v_add_u32_e32 v26, 0x1ce8, v11
	v_lshlrev_b32_e32 v4, 1, v2
	s_cbranch_scc0 .LBB0_1015
	s_lshl_b64 s[6:7], s[14:15], 24
	s_add_u32 s22, s58, s6
	s_addc_u32 s23, s59, s7
	s_lshl_b64 s[6:7], s[14:15], 23
	s_add_u32 s15, s17, s6
	s_addc_u32 s24, s18, s7
	s_add_i32 s6, s21, 0xe800
	s_and_b32 s30, s6, 0xffc0
	s_lshl_b32 s6, s21, 5
	s_and_b32 s31, s6, 0x7e0
	s_lshl_b32 s6, s31, 2
	v_add_u32_e32 v28, s30, v1
	s_add_u32 s6, s22, s6
	s_addc_u32 s7, s23, 0
	v_ashrrev_i32_e32 v29, 31, v28
	v_lshl_add_u64 v[30:31], s[6:7], 0, v[96:97]
	v_lshlrev_b64 v[28:29], 13, v[28:29]
	v_lshl_add_u64 v[56:57], v[30:31], 0, v[28:29]
	s_mov_b32 s6, 0x10000
	v_add_co_u32_e32 v32, vcc, s6, v56
	s_mov_b32 s6, 0x20000
	s_nop 0
	v_addc_co_u32_e32 v33, vcc, 0, v57, vcc
	v_add_co_u32_e32 v36, vcc, s6, v56
	s_mov_b32 s6, 0x30000
	s_nop 0
	v_addc_co_u32_e32 v37, vcc, 0, v57, vcc
	v_add_co_u32_e32 v40, vcc, s6, v56
	s_mov_b32 s6, 0x40000
	s_nop 0
	v_addc_co_u32_e32 v41, vcc, 0, v57, vcc
	v_add_co_u32_e32 v44, vcc, s6, v56
	s_mov_b32 s6, 0x50000
	s_nop 0
	v_addc_co_u32_e32 v45, vcc, 0, v57, vcc
	v_add_co_u32_e32 v48, vcc, s6, v56
	global_load_dwordx4 v[28:31], v[56:57], off nt
	s_nop 0
	global_load_dwordx4 v[32:35], v[32:33], off nt
	v_addc_co_u32_e32 v49, vcc, 0, v57, vcc
	global_load_dwordx4 v[36:39], v[36:37], off nt
	s_nop 0
	global_load_dwordx4 v[40:43], v[40:41], off nt
	s_nop 0
	global_load_dwordx4 v[44:47], v[44:45], off nt
	s_nop 0
	global_load_dwordx4 v[48:51], v[48:49], off nt
	s_mov_b32 s6, 0x60000
	v_add_co_u32_e32 v52, vcc, s6, v56
	s_mov_b32 s6, 0x70000
	s_nop 0
	v_addc_co_u32_e32 v53, vcc, 0, v57, vcc
	global_load_dwordx4 v[52:55], v[52:53], off nt
	v_add_co_u32_e32 v56, vcc, s6, v56
	s_lshl_b32 s6, s30, 1
	s_nop 0
	v_addc_co_u32_e32 v57, vcc, 0, v57, vcc
	global_load_dwordx4 v[56:59], v[56:57], off nt
	s_add_u32 s6, s15, s6
	v_mov_b32_e32 v5, v97
	s_addc_u32 s7, s24, 0
	s_waitcnt vmcnt(7)
	ds_write2_b32 v11, v28, v29 offset1:1
	ds_write2_b32 v11, v30, v31 offset0:2 offset1:3
	s_waitcnt vmcnt(6)
	ds_write2_b32 v12, v32, v33 offset1:1
	ds_write2_b32 v13, v34, v35 offset1:1
	s_waitcnt vmcnt(5)
	ds_write2_b32 v14, v36, v37 offset1:1
	ds_write2_b32 v15, v38, v39 offset1:1
	s_waitcnt vmcnt(4)
	ds_write2_b32 v16, v40, v41 offset1:1
	ds_write2_b32 v17, v42, v43 offset1:1
	s_waitcnt vmcnt(3)
	ds_write2_b32 v19, v44, v45 offset1:1
	ds_write2_b32 v20, v46, v47 offset1:1
	s_waitcnt vmcnt(2)
	ds_write2_b32 v21, v48, v49 offset1:1
	ds_write2_b32 v22, v50, v51 offset1:1
	s_waitcnt vmcnt(1)
	ds_write2_b32 v23, v52, v53 offset1:1
	ds_write2_b32 v24, v54, v55 offset1:1
	s_waitcnt vmcnt(0)
	ds_write2_b32 v25, v56, v57 offset1:1
	ds_write2_b32 v26, v58, v59 offset1:1
	s_waitcnt lgkmcnt(0)
	ds_read2_b32 v[214:215], v10 offset1:33
	ds_read2_b32 v[222:223], v10 offset0:66 offset1:99
	ds_read2_b32 v[224:225], v10 offset0:132 offset1:165
	ds_read2_b32 v[226:227], v10 offset0:198 offset1:231
	ds_read2_b32 v[228:229], v10 offset0:8 offset1:41
	ds_read2_b32 v[230:231], v10 offset0:74 offset1:107
	ds_read2_b32 v[232:233], v10 offset0:140 offset1:173
	ds_read2_b32 v[234:235], v10 offset0:206 offset1:239
	s_waitcnt lgkmcnt(0)
	ds_read2_b32 v[236:237], v10 offset0:16 offset1:49
	ds_read2_b32 v[238:239], v10 offset0:82 offset1:115
	ds_read2_b32 v[240:241], v10 offset0:148 offset1:181
	ds_read2_b32 v[242:243], v10 offset0:214 offset1:247
	ds_read2_b32 v[244:245], v10 offset0:24 offset1:57
	ds_read2_b32 v[246:247], v10 offset0:90 offset1:123
	ds_read2_b32 v[248:249], v10 offset0:156 offset1:189
	ds_read2_b32 v[250:251], v10 offset0:222 offset1:255
	v_cvt_pk_bf16_f32 v28, v214, v215
	v_add_u32_e32 v32, s31, v1
	v_cvt_pk_bf16_f32 v29, v222, v223
	v_ashrrev_i32_e32 v33, 31, v32
	v_cvt_pk_bf16_f32 v30, v224, v225
	v_lshlrev_b64 v[32:33], 12, v[32:33]
	v_lshl_add_u64 v[36:37], s[6:7], 0, v[4:5]
	v_cvt_pk_bf16_f32 v31, v226, v227
	v_lshl_add_u64 v[32:33], v[36:37], 0, v[32:33]
	global_store_dwordx4 v[32:33], v[28:31], off nt
	s_nop 1
	s_mov_b64 s[6:7], 0
	v_cvt_pk_bf16_f32 v28, v228, v229
	v_add_u32_e32 v34, s31, v7
	v_ashrrev_i32_e32 v35, 31, v34
	v_lshlrev_b64 v[34:35], 12, v[34:35]
	v_cvt_pk_bf16_f32 v29, v230, v231
	v_lshl_add_u64 v[34:35], v[36:37], 0, v[34:35]
	v_cvt_pk_bf16_f32 v30, v232, v233
	v_cvt_pk_bf16_f32 v31, v234, v235
	global_store_dwordx4 v[34:35], v[28:31], off nt
	s_nop 1
	v_add_u32_e32 v34, s31, v8
	v_ashrrev_i32_e32 v35, 31, v34
	s_waitcnt lgkmcnt(0)
	v_cvt_pk_bf16_f32 v28, v236, v237
	v_lshlrev_b64 v[34:35], 12, v[34:35]
	v_cvt_pk_bf16_f32 v29, v238, v239
	v_lshl_add_u64 v[34:35], v[36:37], 0, v[34:35]
	v_cvt_pk_bf16_f32 v30, v240, v241
	v_cvt_pk_bf16_f32 v31, v242, v243
	global_store_dwordx4 v[34:35], v[28:31], off nt
	s_nop 1
	v_add_u32_e32 v34, s31, v9
	v_ashrrev_i32_e32 v35, 31, v34
	v_cvt_pk_bf16_f32 v28, v244, v245
	v_lshlrev_b64 v[34:35], 12, v[34:35]
	v_cvt_pk_bf16_f32 v29, v246, v247
	v_lshl_add_u64 v[34:35], v[36:37], 0, v[34:35]
	v_cvt_pk_bf16_f32 v30, v248, v249
	v_cvt_pk_bf16_f32 v31, v250, v251
	global_store_dwordx4 v[34:35], v[28:31], off nt
	s_nop 1
	s_waitcnt lgkmcnt(0)
; __device__ __forceinline__ unsigned pk2(float lo, float hi) { unsigned r; asm volatile("v_cvt_pk_bf16_f32 %0, %1, %2" : "=v"(r) : "v"(lo), "v"(hi)); return r; }
; __device__ __forceinline__ void transpose_item(const float* W, int K, int N, bf16_t* WT, int rstep, int roff, float* scr, int item, int lane) {
;   const int nblk = N / 32, kb = item / nblk, nb = item % nblk, k0 = 64 * kb, n0 = 32 * nb;
;   f32x4 v[8];
; #pragma unroll
;   for (int i = 0; i < 8; ++i) v[i] = __builtin_nontemporal_load((const f32x4*)(W + (size_t)(k0 + i * 8 + (lane >> 3)) * N + n0 + (lane & 7) * 4));
; #pragma unroll
;   for (int i = 0; i < 8; ++i) { float* d = scr + (i * 8 + (lane >> 3)) * 33 + (lane & 7) * 4; d[0] = v[i].x; d[1] = v[i].y; d[2] = v[i].z; d[3] = v[i].w; }
;   __builtin_amdgcn_wave_barrier(); asm volatile("s_waitcnt lgkmcnt(0)" ::: "memory");
;   const int c = lane & 7;
; #pragma unroll
;   for (int j = 0; j < 4; ++j) { const int nl = (lane >> 3) + 8 * j, n = n0 + nl; const float* s = scr + (8 * c) * 33 + nl;
;     u32x4 o; o.x = pk2(s[0 * 33], s[1 * 33]); o.y = pk2(s[2 * 33], s[3 * 33]); o.z = pk2(s[4 * 33], s[5 * 33]); o.w = pk2(s[6 * 33], s[7 * 33]);
;     const int row = n + (n >> 7) * rstep + roff;
;     __builtin_nontemporal_store(o, (u32x4*)(WT + (size_t)row * K + k0 + 8 * c)); }
;   __builtin_amdgcn_wave_barrier(); asm volatile("s_waitcnt lgkmcnt(0)" ::: "memory");
; }
; __device__ __forceinline__ void convert_item(const P& p, int it, float* scr, int lane) {
;     ...
;     if (r < IT_WIN) transpose_item(p.w_in + (size_t)l * DM * INW, DM, INW, WSP(bf16_t, WS_WIN) + (size_t)l * INW * DM, 0, 0, scr, r, lane);
.LBB0_1015:
	s_andn2_b64 vcc, exec, s[6:7]
	s_cbranch_vccnz .LBB0_988
	s_mul_i32 s7, s14, 0x3000000
	s_mul_hi_i32 s6, s14, 0x3000000
	s_add_u32 s7, s56, s7
	s_addc_u32 s24, s57, s6
	s_mul_hi_i32 s6, s14, 0x1800000
	s_mul_i32 s14, s14, 0x1800000
	s_add_u32 s30, s19, s14
	s_addc_u32 s31, s20, s6
	s_mul_i32 s6, s21, 0x2aab
	s_lshr_b32 s14, s6, 31
	s_ashr_i32 s6, s6, 21
	s_add_i32 s6, s6, s14
	s_sext_i32_i16 s14, s6
	s_mulk_i32 s6, 0xc0
	s_sub_i32 s6, s21, s6
	s_sext_i32_i16 s15, s6
	s_lshl_b32 s6, s14, 6
	s_lshl_b32 s14, s15, 5
	s_ashr_i32 s15, s14, 31
	s_lshl_b64 s[22:23], s[14:15], 2
	s_add_u32 s22, s7, s22
	v_add_u32_e32 v5, s6, v1
	s_addc_u32 s23, s24, s23
	v_lshl_add_u64 v[56:57], s[22:23], 0, v[96:97]
	s_movk_i32 s7, 0x6000
	v_add_u32_e32 v27, 8, v5
	v_mad_i64_i32 v[32:33], s[22:23], v27, s7, v[56:57]
	v_add_u32_e32 v27, 16, v5
	v_mad_i64_i32 v[36:37], s[22:23], v27, s7, v[56:57]
	v_add_u32_e32 v27, 24, v5
	v_mad_i64_i32 v[40:41], s[22:23], v27, s7, v[56:57]
	v_add_u32_e32 v27, 32, v5
	v_mad_i64_i32 v[44:45], s[22:23], v27, s7, v[56:57]
	v_add_u32_e32 v27, 40, v5
	v_mad_i64_i32 v[28:29], s[22:23], v5, s7, v[56:57]
	v_mad_i64_i32 v[48:49], s[22:23], v27, s7, v[56:57]
	global_load_dwordx4 v[28:31], v[28:29], off nt
	s_nop 0
	global_load_dwordx4 v[32:35], v[32:33], off nt
	s_nop 0
	global_load_dwordx4 v[36:39], v[36:37], off nt
	s_nop 0
	global_load_dwordx4 v[40:43], v[40:41], off nt
	s_nop 0
	global_load_dwordx4 v[44:47], v[44:45], off nt
	s_nop 0
	global_load_dwordx4 v[48:51], v[48:49], off nt
	v_add_u32_e32 v27, 48, v5
	v_mad_i64_i32 v[52:53], s[22:23], v27, s7, v[56:57]
	global_load_dwordx4 v[52:55], v[52:53], off nt
	v_add_u32_e32 v5, 56, v5
	v_mad_i64_i32 v[56:57], s[22:23], v5, s7, v[56:57]
	global_load_dwordx4 v[56:59], v[56:57], off nt
	s_ashr_i32 s7, s6, 31
	s_lshl_b64 s[6:7], s[6:7], 1
	s_add_u32 s6, s30, s6
	v_mov_b32_e32 v5, v97
	s_addc_u32 s7, s31, s7
	v_lshl_add_u64 v[4:5], s[6:7], 0, v[4:5]
	s_movk_i32 s82, 0x6000
	s_waitcnt vmcnt(7)
	ds_write2_b32 v11, v28, v29 offset1:1
	ds_write2_b32 v11, v30, v31 offset0:2 offset1:3
	s_waitcnt vmcnt(6)
	ds_write2_b32 v12, v32, v33 offset1:1
	ds_write2_b32 v13, v34, v35 offset1:1
	s_waitcnt vmcnt(5)
	ds_write2_b32 v14, v36, v37 offset1:1
	ds_write2_b32 v15, v38, v39 offset1:1
	s_waitcnt vmcnt(4)
	ds_write2_b32 v16, v40, v41 offset1:1
	ds_write2_b32 v17, v42, v43 offset1:1
	s_waitcnt vmcnt(3)
	ds_write2_b32 v19, v44, v45 offset1:1
	ds_write2_b32 v20, v46, v47 offset1:1
	s_waitcnt vmcnt(2)
	ds_write2_b32 v21, v48, v49 offset1:1
	ds_write2_b32 v22, v50, v51 offset1:1
	s_waitcnt vmcnt(1)
	ds_write2_b32 v23, v52, v53 offset1:1
	ds_write2_b32 v24, v54, v55 offset1:1
	s_waitcnt vmcnt(0)
	ds_write2_b32 v25, v56, v57 offset1:1
	ds_write2_b32 v26, v58, v59 offset1:1
	s_waitcnt lgkmcnt(0)
	ds_read2_b32 v[214:215], v10 offset1:33
	ds_read2_b32 v[222:223], v10 offset0:66 offset1:99
	ds_read2_b32 v[224:225], v10 offset0:132 offset1:165
	ds_read2_b32 v[226:227], v10 offset0:198 offset1:231
	ds_read2_b32 v[228:229], v10 offset0:8 offset1:41
	ds_read2_b32 v[230:231], v10 offset0:74 offset1:107
	ds_read2_b32 v[232:233], v10 offset0:140 offset1:173
	ds_read2_b32 v[234:235], v10 offset0:206 offset1:239
	s_waitcnt lgkmcnt(0)
	ds_read2_b32 v[236:237], v10 offset0:16 offset1:49
	ds_read2_b32 v[238:239], v10 offset0:82 offset1:115
	ds_read2_b32 v[240:241], v10 offset0:148 offset1:181
	ds_read2_b32 v[242:243], v10 offset0:214 offset1:247
	ds_read2_b32 v[244:245], v10 offset0:24 offset1:57
	ds_read2_b32 v[246:247], v10 offset0:90 offset1:123
	ds_read2_b32 v[248:249], v10 offset0:156 offset1:189
	ds_read2_b32 v[250:251], v10 offset0:222 offset1:255
	v_cvt_pk_bf16_f32 v12, v214, v215
	v_add_u32_e32 v16, s14, v1
	v_cvt_pk_bf16_f32 v13, v222, v223
	v_ashrrev_i32_e32 v17, 31, v16
	v_cvt_pk_bf16_f32 v14, v224, v225
	v_lshlrev_b64 v[16:17], 12, v[16:17]
	v_cvt_pk_bf16_f32 v15, v226, v227
	v_lshl_add_u64 v[16:17], v[4:5], 0, v[16:17]
	global_store_dwordx4 v[16:17], v[12:15], off nt
	s_nop 1
	s_nop 0
	v_cvt_pk_bf16_f32 v12, v228, v229
	v_add_u32_e32 v20, s14, v7
	v_ashrrev_i32_e32 v21, 31, v20
	v_lshlrev_b64 v[20:21], 12, v[20:21]
	v_cvt_pk_bf16_f32 v13, v230, v231
	v_lshl_add_u64 v[20:21], v[4:5], 0, v[20:21]
	v_cvt_pk_bf16_f32 v14, v232, v233
	v_cvt_pk_bf16_f32 v15, v234, v235
	global_store_dwordx4 v[20:21], v[12:15], off nt
	s_nop 1
	v_add_u32_e32 v20, s14, v8
	v_ashrrev_i32_e32 v21, 31, v20
	s_waitcnt lgkmcnt(0)
	v_cvt_pk_bf16_f32 v12, v236, v237
	v_lshlrev_b64 v[20:21], 12, v[20:21]
	v_cvt_pk_bf16_f32 v13, v238, v239
	v_lshl_add_u64 v[20:21], v[4:5], 0, v[20:21]
	v_cvt_pk_bf16_f32 v14, v240, v241
	v_cvt_pk_bf16_f32 v15, v242, v243
	global_store_dwordx4 v[20:21], v[12:15], off nt
	s_nop 1
	v_add_u32_e32 v20, s14, v9
	v_ashrrev_i32_e32 v21, 31, v20
	v_cvt_pk_bf16_f32 v12, v244, v245
	v_lshlrev_b64 v[20:21], 12, v[20:21]
	v_cvt_pk_bf16_f32 v13, v246, v247
	v_lshl_add_u64 v[4:5], v[4:5], 0, v[20:21]
	v_cvt_pk_bf16_f32 v14, v248, v249
	v_cvt_pk_bf16_f32 v15, v250, v251
	global_store_dwordx4 v[4:5], v[12:15], off nt
	s_nop 1
	s_waitcnt lgkmcnt(0)
	s_branch .LBB0_988

; __device__ __forceinline__ void transpose_item(const float* W, int K, int N, bf16_t* WT, int rstep, int roff, float* scr, int item, int lane) {
;   const int nblk = N / 32, kb = item / nblk, nb = item % nblk, k0 = 64 * kb, n0 = 32 * nb;
;   f32x4 v[8];
; #pragma unroll
;   for (int i = 0; i < 8; ++i) v[i] = __builtin_nontemporal_load((const f32x4*)(W + (size_t)(k0 + i * 8 + (lane >> 3)) * N + n0 + (lane & 7) * 4));
; #pragma unroll
;   for (int i = 0; i < 8; ++i) { float* d = scr + (i * 8 + (lane >> 3)) * 33 + (lane & 7) * 4; d[0] = v[i].x; d[1] = v[i].y; d[2] = v[i].z; d[3] = v[i].w; }
;   __builtin_amdgcn_wave_barrier(); asm volatile("s_waitcnt lgkmcnt(0)" ::: "memory");
;   const int c = lane & 7;
; #pragma unroll
;   for (int j = 0; j < 4; ++j) { const int nl = (lane >> 3) + 8 * j, n = n0 + nl; const float* s = scr + (8 * c) * 33 + nl;
;     u32x4 o; o.x = pk2(s[0 * 33], s[1 * 33]); o.y = pk2(s[2 * 33], s[3 * 33]); o.z = pk2(s[4 * 33], s[5 * 33]); o.w = pk2(s[6 * 33], s[7 * 33]);
;     const int row = n + (n >> 7) * rstep + roff;
;     __builtin_nontemporal_store(o, (u32x4*)(WT + (size_t)row * K + k0 + 8 * c)); }
;   __builtin_amdgcn_wave_barrier(); asm volatile("s_waitcnt lgkmcnt(0)" ::: "memory");
; }
; __device__ __forceinline__ void convert_item(const P& p, int it, float* scr, int lane) {
;   if (it < IT_DENSE) {
;     const int l = it / (IT_WIN + IT_WOUT), r = it % (IT_WIN + IT_WOUT);
;     if (r < IT_WIN) transpose_item(p.w_in + (size_t)l * DM * INW, DM, INW, WSP(bf16_t, WS_WIN) + (size_t)l * INW * DM, 0, 0, scr, r, lane);
;     else transpose_item(p.w_out + (size_t)l * DM * DM, DM, DM, WSP(bf16_t, WS_WOUT) + (size_t)l * DM * DM, 0, 0, scr, r - IT_WIN, lane);
;   } else {
;     const int idx = it - IT_DENSE, m = idx / IT_EXP, sub = idx % IT_EXP, le = m / 3, which = m % 3;
;     if (which == 0) transpose_item(p.wg + (size_t)le * DM * EFF, DM, EFF, WSP(bf16_t, WS_WGU) + (size_t)le * 1024 * DM, 128, 0, scr, sub, lane);
;     else if (which == 1) transpose_item(p.wu + (size_t)le * DM * EFF, DM, EFF, WSP(bf16_t, WS_WGU) + (size_t)le * 1024 * DM, 128, 128, scr, sub, lane);
;     else transpose_item(p.wd + (size_t)le * EFF * DM, EFF, DM, WSP(bf16_t, WS_WD) + (size_t)le * DM * EFF, 0, 0, scr, sub, lane);
.LBB0_1031:
	s_cmpk_gt_i32 s15, 0x3fff
	s_mov_b64 s[6:7], -1
	s_cbranch_scc0 .LBB0_1041
	s_add_i32 s6, s15, 0xffffc000
	s_lshr_b32 s7, s6, 9
	s_mul_i32 s6, s6, 0xaaab
	s_lshr_b32 s23, s6, 26
	s_mul_i32 s6, s7, 0xab
	s_bfe_u32 s6, s6, 0x70009
	s_mul_i32 s6, s6, 3
	s_sub_i32 s6, s7, s6
	s_and_b32 s14, s15, 0x1ff
	s_lshl_b32 s22, s23, 22
	s_lshl_b32 s21, s15, 5
	s_and_b32 s24, s6, 0xff
	s_cmp_lt_i32 s24, 1
	s_mov_b64 s[6:7], -1
	s_cbranch_scc1 .LBB0_1038
	s_and_b32 s6, 0xffff, s24
	s_cmp_lg_u32 s6, 1
	s_mov_b64 s[6:7], -1
	s_cbranch_scc0 .LBB0_1035
	s_add_u32 s30, s0, s22
	s_addc_u32 s31, s1, 0
	s_lshl_b32 s6, s23, 21
	s_add_u32 s7, s4, s6
	s_addc_u32 s23, s5, 0
	s_and_b32 s6, s21, 0x7e0
	s_and_b32 s24, s15, 0x1c0
	s_lshl_b32 s34, s6, 2
	v_add_u32_e32 v4, s24, v1
	s_add_u32 s30, s30, s34
	s_addc_u32 s31, s31, 0
	v_lshlrev_b32_e32 v96, 2, v0
	v_ashrrev_i32_e32 v5, 31, v4
	v_lshl_add_u64 v[12:13], s[30:31], 0, v[96:97]
	v_lshlrev_b64 v[4:5], 13, v[4:5]
	v_lshl_add_u64 v[4:5], v[12:13], 0, v[4:5]
	s_mov_b32 s30, 0x10000
	v_add_co_u32_e32 v16, vcc, s30, v4
	s_mov_b32 s30, 0x20000
	s_nop 0
	v_addc_co_u32_e32 v17, vcc, 0, v5, vcc
	global_load_dwordx4 v[12:15], v[4:5], off nt
	v_add_co_u32_e32 v20, vcc, s30, v4
	global_load_dwordx4 v[16:19], v[16:17], off nt
	s_nop 0
	v_addc_co_u32_e32 v21, vcc, 0, v5, vcc
	s_mov_b32 s30, 0x30000
	global_load_dwordx4 v[20:23], v[20:21], off nt
	v_add_co_u32_e32 v24, vcc, s30, v4
	s_mov_b32 s30, 0x40000
	s_nop 0
	v_addc_co_u32_e32 v25, vcc, 0, v5, vcc
	global_load_dwordx4 v[24:27], v[24:25], off nt
	v_add_co_u32_e32 v28, vcc, s30, v4
	s_mov_b32 s30, 0x50000
	s_nop 0
	v_addc_co_u32_e32 v29, vcc, 0, v5, vcc
	global_load_dwordx4 v[28:31], v[28:29], off nt
	v_add_co_u32_e32 v32, vcc, s30, v4
	s_mov_b32 s30, 0x60000
	s_nop 0
	v_addc_co_u32_e32 v33, vcc, 0, v5, vcc
	global_load_dwordx4 v[32:35], v[32:33], off nt
	v_add_co_u32_e32 v36, vcc, s30, v4
	s_mov_b32 s30, 0x70000
	s_nop 0
	v_addc_co_u32_e32 v37, vcc, 0, v5, vcc
	global_load_dwordx4 v[36:39], v[36:37], off nt
	v_add_co_u32_e32 v4, vcc, s30, v4
	s_lshl_b32 s24, s24, 1
	s_nop 0
	v_addc_co_u32_e32 v5, vcc, 0, v5, vcc
	global_load_dwordx4 v[40:43], v[4:5], off nt
	v_add_u32_e32 v4, v10, v3
	v_add_u32_e32 v5, 0x420, v4
	s_add_u32 s30, s7, s24
	s_addc_u32 s31, s23, 0
	v_lshlrev_b32_e32 v96, 1, v2
	s_waitcnt vmcnt(7)
	ds_write2_b32 v4, v12, v13 offset1:1
	ds_write2_b32 v4, v14, v15 offset0:2 offset1:3
	s_waitcnt vmcnt(6)
	ds_write2_b32 v5, v16, v17 offset1:1
	v_add_u32_e32 v5, 0x428, v4
	ds_write2_b32 v5, v18, v19 offset1:1
	v_add_u32_e32 v5, 0x840, v4
	s_waitcnt vmcnt(5)
	ds_write2_b32 v5, v20, v21 offset1:1
	v_add_u32_e32 v5, 0x848, v4
	ds_write2_b32 v5, v22, v23 offset1:1
	v_add_u32_e32 v5, 0xc60, v4
	v_add_u32_e32 v16, s6, v1
	v_ashrrev_i32_e32 v17, 31, v16
	s_waitcnt vmcnt(4)
	ds_write2_b32 v5, v24, v25 offset1:1
	v_add_u32_e32 v5, 0xc68, v4
	ds_write2_b32 v5, v26, v27 offset1:1
	v_add_u32_e32 v5, 0x1080, v4
	v_lshlrev_b64 v[16:17], 10, v[16:17]
	s_waitcnt vmcnt(3)
	ds_write2_b32 v5, v28, v29 offset1:1
	v_add_u32_e32 v5, 0x1088, v4
	ds_write2_b32 v5, v30, v31 offset1:1
	v_add_u32_e32 v5, 0x14a0, v4
	s_waitcnt vmcnt(2)
	ds_write2_b32 v5, v32, v33 offset1:1
	v_add_u32_e32 v5, 0x14a8, v4
	ds_write2_b32 v5, v34, v35 offset1:1
	v_add_u32_e32 v5, 0x18c0, v4
	s_waitcnt vmcnt(1)
	ds_write2_b32 v5, v36, v37 offset1:1
	v_add_u32_e32 v5, 0x18c8, v4
	ds_write2_b32 v5, v38, v39 offset1:1
	v_add_u32_e32 v5, 0x1ce0, v4
	v_add_u32_e32 v4, 0x1ce8, v4
	s_waitcnt vmcnt(0)
	ds_write2_b32 v5, v40, v41 offset1:1
	ds_write2_b32 v4, v42, v43 offset1:1
	s_waitcnt lgkmcnt(0)
	ds_read2_b32 v[214:215], v11 offset1:33
	ds_read2_b32 v[222:223], v11 offset0:66 offset1:99
	ds_read2_b32 v[224:225], v11 offset0:132 offset1:165
	ds_read2_b32 v[226:227], v11 offset0:198 offset1:231
	ds_read2_b32 v[228:229], v11 offset0:8 offset1:41
	ds_read2_b32 v[230:231], v11 offset0:74 offset1:107
	ds_read2_b32 v[232:233], v11 offset0:140 offset1:173
	ds_read2_b32 v[234:235], v11 offset0:206 offset1:239
	s_waitcnt lgkmcnt(0)
	ds_read2_b32 v[236:237], v11 offset0:16 offset1:49
	ds_read2_b32 v[238:239], v11 offset0:82 offset1:115
	ds_read2_b32 v[240:241], v11 offset0:148 offset1:181
	ds_read2_b32 v[242:243], v11 offset0:214 offset1:247
	ds_read2_b32 v[244:245], v11 offset0:24 offset1:57
	ds_read2_b32 v[246:247], v11 offset0:90 offset1:123
	ds_read2_b32 v[248:249], v11 offset0:156 offset1:189
	ds_read2_b32 v[250:251], v11 offset0:222 offset1:255
	v_lshl_add_u64 v[4:5], s[30:31], 0, v[96:97]
	v_cvt_pk_bf16_f32 v12, v214, v215
	v_cvt_pk_bf16_f32 v13, v222, v223
	v_lshl_add_u64 v[16:17], v[4:5], 0, v[16:17]
	v_cvt_pk_bf16_f32 v14, v224, v225
	v_cvt_pk_bf16_f32 v15, v226, v227
	global_store_dwordx4 v[16:17], v[12:15], off nt
	s_nop 1
	v_add_u32_e32 v16, s6, v6
	v_ashrrev_i32_e32 v17, 31, v16
	v_cvt_pk_bf16_f32 v12, v228, v229
	v_lshlrev_b64 v[16:17], 10, v[16:17]
	v_cvt_pk_bf16_f32 v13, v230, v231
	v_lshl_add_u64 v[16:17], v[4:5], 0, v[16:17]
	v_cvt_pk_bf16_f32 v14, v232, v233
	v_cvt_pk_bf16_f32 v15, v234, v235
	global_store_dwordx4 v[16:17], v[12:15], off nt
	s_nop 1
	v_add_u32_e32 v16, s6, v7
	s_waitcnt lgkmcnt(0)
	v_ashrrev_i32_e32 v17, 31, v16
	v_cvt_pk_bf16_f32 v12, v236, v237
	v_lshlrev_b64 v[16:17], 10, v[16:17]
	v_cvt_pk_bf16_f32 v13, v238, v239
	v_lshl_add_u64 v[16:17], v[4:5], 0, v[16:17]
	v_cvt_pk_bf16_f32 v14, v240, v241
	v_cvt_pk_bf16_f32 v15, v242, v243
	global_store_dwordx4 v[16:17], v[12:15], off nt
	s_nop 1
	v_add_u32_e32 v16, s6, v8
	v_ashrrev_i32_e32 v17, 31, v16
	v_cvt_pk_bf16_f32 v12, v244, v245
	v_lshlrev_b64 v[16:17], 10, v[16:17]
	v_cvt_pk_bf16_f32 v13, v246, v247
	v_lshl_add_u64 v[4:5], v[4:5], 0, v[16:17]
	v_cvt_pk_bf16_f32 v14, v248, v249
	v_cvt_pk_bf16_f32 v15, v250, v251
	global_store_dwordx4 v[4:5], v[12:15], off nt
	s_nop 1
	s_waitcnt lgkmcnt(0)
	s_mov_b64 s[6:7], 0
; __device__ __forceinline__ unsigned pk2(float lo, float hi) { unsigned r; asm volatile("v_cvt_pk_bf16_f32 %0, %1, %2" : "=v"(r) : "v"(lo), "v"(hi)); return r; }
; __device__ __forceinline__ void transpose_item(const float* W, int K, int N, bf16_t* WT, int rstep, int roff, float* scr, int item, int lane) {
;   const int nblk = N / 32, kb = item / nblk, nb = item % nblk, k0 = 64 * kb, n0 = 32 * nb;
;   f32x4 v[8];
; #pragma unroll
;   for (int i = 0; i < 8; ++i) v[i] = __builtin_nontemporal_load((const f32x4*)(W + (size_t)(k0 + i * 8 + (lane >> 3)) * N + n0 + (lane & 7) * 4));
; #pragma unroll
;   for (int i = 0; i < 8; ++i) { float* d = scr + (i * 8 + (lane >> 3)) * 33 + (lane & 7) * 4; d[0] = v[i].x; d[1] = v[i].y; d[2] = v[i].z; d[3] = v[i].w; }
;   __builtin_amdgcn_wave_barrier(); asm volatile("s_waitcnt lgkmcnt(0)" ::: "memory");
;   const int c = lane & 7;
; #pragma unroll
;   for (int j = 0; j < 4; ++j) { const int nl = (lane >> 3) + 8 * j, n = n0 + nl; const float* s = scr + (8 * c) * 33 + nl;
;     u32x4 o; o.x = pk2(s[0 * 33], s[1 * 33]); o.y = pk2(s[2 * 33], s[3 * 33]); o.z = pk2(s[4 * 33], s[5 * 33]); o.w = pk2(s[6 * 33], s[7 * 33]);
;     const int row = n + (n >> 7) * rstep + roff;
;     __builtin_nontemporal_store(o, (u32x4*)(WT + (size_t)row * K + k0 + 8 * c)); }
;   __builtin_amdgcn_wave_barrier(); asm volatile("s_waitcnt lgkmcnt(0)" ::: "memory");
; }
; __device__ __forceinline__ void convert_item(const P& p, int it, float* scr, int lane) {
;     ...
;     else if (which == 1) transpose_item(p.wu + (size_t)le * DM * EFF, DM, EFF, WSP(bf16_t, WS_WGU) + (size_t)le * 1024 * DM, 128, 128, scr, sub, lane);
.LBB0_1035:
	s_andn2_b64 vcc, exec, s[6:7]
	s_cbranch_vccnz .LBB0_1037
	s_add_u32 s30, s62, s22
	s_addc_u32 s31, s63, 0
	s_add_u32 s7, s2, s22
	s_addc_u32 s23, s3, 0
	s_lshl_b32 s6, s14, 2
	s_and_b32 s24, s6, 0x7c0
	s_and_b32 s6, s21, 0x1e0
	s_lshl_b32 s34, s6, 2
	v_add_u32_e32 v4, s24, v1
	s_add_u32 s30, s30, s34
	s_addc_u32 s31, s31, 0
	v_lshlrev_b32_e32 v96, 2, v0
	v_ashrrev_i32_e32 v5, 31, v4
	v_lshl_add_u64 v[12:13], s[30:31], 0, v[96:97]
	v_lshlrev_b64 v[4:5], 11, v[4:5]
	v_lshl_add_u64 v[4:5], v[12:13], 0, v[4:5]
	s_movk_i32 s30, 0x4000
	v_add_co_u32_e32 v16, vcc, s30, v4
	s_mov_b32 s30, 0x8000
	s_nop 0
	v_addc_co_u32_e32 v17, vcc, 0, v5, vcc
	global_load_dwordx4 v[12:15], v[4:5], off nt
	v_add_co_u32_e32 v20, vcc, s30, v4
	global_load_dwordx4 v[16:19], v[16:17], off nt
	s_nop 0
	v_addc_co_u32_e32 v21, vcc, 0, v5, vcc
	s_mov_b32 s30, 0xc000
	global_load_dwordx4 v[20:23], v[20:21], off nt
	v_add_co_u32_e32 v24, vcc, s30, v4
	s_mov_b32 s30, 0x10000
	s_nop 0
	v_addc_co_u32_e32 v25, vcc, 0, v5, vcc
	global_load_dwordx4 v[24:27], v[24:25], off nt
	v_add_co_u32_e32 v28, vcc, s30, v4
	s_mov_b32 s30, 0x14000
	s_nop 0
	v_addc_co_u32_e32 v29, vcc, 0, v5, vcc
	global_load_dwordx4 v[28:31], v[28:29], off nt
	v_add_co_u32_e32 v32, vcc, s30, v4
	s_lshl_b32 s24, s24, 1
	s_nop 0
	v_addc_co_u32_e32 v33, vcc, 0, v5, vcc
	global_load_dwordx4 v[32:35], v[32:33], off nt
	v_add_co_u32_e32 v36, vcc, s93, v4
	s_add_u32 s30, s7, s24
	s_nop 0
	v_addc_co_u32_e32 v37, vcc, 0, v5, vcc
	global_load_dwordx4 v[36:39], v[36:37], off nt
	v_add_co_u32_e32 v4, vcc, s96, v4
	s_movk_i32 s7, 0x80
	s_nop 0
	v_addc_co_u32_e32 v5, vcc, 0, v5, vcc
	global_load_dwordx4 v[40:43], v[4:5], off nt
	v_add_u32_e32 v4, v10, v3
	v_add_u32_e32 v5, 0x420, v4
	s_addc_u32 s31, s23, 0
	v_lshlrev_b32_e32 v96, 1, v2
	s_waitcnt vmcnt(7)
	ds_write2_b32 v4, v12, v13 offset1:1
	ds_write2_b32 v4, v14, v15 offset0:2 offset1:3
	s_waitcnt vmcnt(6)
	ds_write2_b32 v5, v16, v17 offset1:1
	v_add_u32_e32 v5, 0x428, v4
	ds_write2_b32 v5, v18, v19 offset1:1
	v_add_u32_e32 v5, 0x840, v4
	s_waitcnt vmcnt(5)
	ds_write2_b32 v5, v20, v21 offset1:1
	v_add_u32_e32 v5, 0x848, v4
	ds_write2_b32 v5, v22, v23 offset1:1
	v_add_u32_e32 v5, 0xc60, v4
	v_add_u32_e32 v18, s6, v1
	s_waitcnt vmcnt(4)
	ds_write2_b32 v5, v24, v25 offset1:1
	v_add_u32_e32 v5, 0xc68, v4
	ds_write2_b32 v5, v26, v27 offset1:1
	v_add_u32_e32 v5, 0x1080, v4
	s_waitcnt vmcnt(3)
	ds_write2_b32 v5, v28, v29 offset1:1
	v_add_u32_e32 v5, 0x1088, v4
	ds_write2_b32 v5, v30, v31 offset1:1
	v_add_u32_e32 v5, 0x14a0, v4
	s_waitcnt vmcnt(2)
	ds_write2_b32 v5, v32, v33 offset1:1
	v_add_u32_e32 v5, 0x14a8, v4
	ds_write2_b32 v5, v34, v35 offset1:1
	v_add_u32_e32 v5, 0x18c0, v4
	s_waitcnt vmcnt(1)
	ds_write2_b32 v5, v36, v37 offset1:1
	v_add_u32_e32 v5, 0x18c8, v4
	ds_write2_b32 v5, v38, v39 offset1:1
	v_add_u32_e32 v5, 0x1ce0, v4
	v_add_u32_e32 v4, 0x1ce8, v4
	s_waitcnt vmcnt(0)
	ds_write2_b32 v5, v40, v41 offset1:1
	ds_write2_b32 v4, v42, v43 offset1:1
	s_waitcnt lgkmcnt(0)
	ds_read2_b32 v[214:215], v11 offset1:33
	ds_read2_b32 v[222:223], v11 offset0:66 offset1:99
	ds_read2_b32 v[224:225], v11 offset0:132 offset1:165
	ds_read2_b32 v[226:227], v11 offset0:198 offset1:231
	ds_read2_b32 v[228:229], v11 offset0:8 offset1:41
	ds_read2_b32 v[230:231], v11 offset0:74 offset1:107
	ds_read2_b32 v[232:233], v11 offset0:140 offset1:173
	ds_read2_b32 v[234:235], v11 offset0:206 offset1:239
	s_waitcnt lgkmcnt(0)
	ds_read2_b32 v[236:237], v11 offset0:16 offset1:49
	ds_read2_b32 v[238:239], v11 offset0:82 offset1:115
	ds_read2_b32 v[240:241], v11 offset0:148 offset1:181
	ds_read2_b32 v[242:243], v11 offset0:214 offset1:247
	ds_read2_b32 v[244:245], v11 offset0:24 offset1:57
	ds_read2_b32 v[246:247], v11 offset0:90 offset1:123
	ds_read2_b32 v[248:249], v11 offset0:156 offset1:189
	ds_read2_b32 v[250:251], v11 offset0:222 offset1:255
	v_cvt_pk_bf16_f32 v12, v214, v215
	v_cvt_pk_bf16_f32 v13, v222, v223
	v_cvt_pk_bf16_f32 v14, v224, v225
	v_cvt_pk_bf16_f32 v15, v226, v227
	v_and_b32_e32 v16, 0xffffff80, v18
	v_add3_u32 v16, v18, v16, s7
	v_ashrrev_i32_e32 v17, 31, v16
	v_lshl_add_u64 v[4:5], s[30:31], 0, v[96:97]
	v_lshlrev_b64 v[16:17], 12, v[16:17]
	v_lshl_add_u64 v[16:17], v[4:5], 0, v[16:17]
	global_store_dwordx4 v[16:17], v[12:15], off nt
	s_nop 1
	v_add_u32_e32 v18, s6, v6
	v_cvt_pk_bf16_f32 v12, v228, v229
	v_cvt_pk_bf16_f32 v13, v230, v231
	v_cvt_pk_bf16_f32 v14, v232, v233
	v_cvt_pk_bf16_f32 v15, v234, v235
	v_and_b32_e32 v16, 0xffffff80, v18
	v_add3_u32 v16, v18, v16, s7
	v_ashrrev_i32_e32 v17, 31, v16
	v_lshlrev_b64 v[16:17], 12, v[16:17]
	v_lshl_add_u64 v[16:17], v[4:5], 0, v[16:17]
	global_store_dwordx4 v[16:17], v[12:15], off nt
	s_nop 1
	s_waitcnt lgkmcnt(0)
	v_add_u32_e32 v18, s6, v7
	v_cvt_pk_bf16_f32 v12, v236, v237
	v_cvt_pk_bf16_f32 v13, v238, v239
	v_cvt_pk_bf16_f32 v14, v240, v241
	v_cvt_pk_bf16_f32 v15, v242, v243
	v_and_b32_e32 v16, 0xffffff80, v18
	v_add3_u32 v16, v18, v16, s7
	v_ashrrev_i32_e32 v17, 31, v16
	v_lshlrev_b64 v[16:17], 12, v[16:17]
	v_lshl_add_u64 v[16:17], v[4:5], 0, v[16:17]
	global_store_dwordx4 v[16:17], v[12:15], off nt
	s_nop 1
	v_add_u32_e32 v18, s6, v8
	v_cvt_pk_bf16_f32 v12, v244, v245
	v_cvt_pk_bf16_f32 v13, v246, v247
	v_cvt_pk_bf16_f32 v14, v248, v249
	v_cvt_pk_bf16_f32 v15, v250, v251
	v_and_b32_e32 v16, 0xffffff80, v18
	v_add3_u32 v16, v18, v16, s7
	v_ashrrev_i32_e32 v17, 31, v16
	v_lshlrev_b64 v[16:17], 12, v[16:17]
	v_lshl_add_u64 v[4:5], v[4:5], 0, v[16:17]
	global_store_dwordx4 v[4:5], v[12:15], off nt
	s_nop 1
	s_waitcnt lgkmcnt(0)

; __device__ __forceinline__ unsigned pk2(float lo, float hi) { unsigned r; asm volatile("v_cvt_pk_bf16_f32 %0, %1, %2" : "=v"(r) : "v"(lo), "v"(hi)); return r; }
; __device__ __forceinline__ void transpose_item(const float* W, int K, int N, bf16_t* WT, int rstep, int roff, float* scr, int item, int lane) {
;   const int nblk = N / 32, kb = item / nblk, nb = item % nblk, k0 = 64 * kb, n0 = 32 * nb;
;   f32x4 v[8];
; #pragma unroll
;   for (int i = 0; i < 8; ++i) v[i] = __builtin_nontemporal_load((const f32x4*)(W + (size_t)(k0 + i * 8 + (lane >> 3)) * N + n0 + (lane & 7) * 4));
; #pragma unroll
;   for (int i = 0; i < 8; ++i) { float* d = scr + (i * 8 + (lane >> 3)) * 33 + (lane & 7) * 4; d[0] = v[i].x; d[1] = v[i].y; d[2] = v[i].z; d[3] = v[i].w; }
;   __builtin_amdgcn_wave_barrier(); asm volatile("s_waitcnt lgkmcnt(0)" ::: "memory");
;   const int c = lane & 7;
; #pragma unroll
;   for (int j = 0; j < 4; ++j) { const int nl = (lane >> 3) + 8 * j, n = n0 + nl; const float* s = scr + (8 * c) * 33 + nl;
;     u32x4 o; o.x = pk2(s[0 * 33], s[1 * 33]); o.y = pk2(s[2 * 33], s[3 * 33]); o.z = pk2(s[4 * 33], s[5 * 33]); o.w = pk2(s[6 * 33], s[7 * 33]);
;     const int row = n + (n >> 7) * rstep + roff;
;     __builtin_nontemporal_store(o, (u32x4*)(WT + (size_t)row * K + k0 + 8 * c)); }
;   __builtin_amdgcn_wave_barrier(); asm volatile("s_waitcnt lgkmcnt(0)" ::: "memory");
; }
; __device__ __forceinline__ void convert_item(const P& p, int it, float* scr, int lane) {
;     ...
;     if (which == 0) transpose_item(p.wg + (size_t)le * DM * EFF, DM, EFF, WSP(bf16_t, WS_WGU) + (size_t)le * 1024 * DM, 128, 0, scr, sub, lane);
.LBB0_1038:
	s_andn2_b64 vcc, exec, s[6:7]
	s_cbranch_vccnz .LBB0_1040
	s_add_u32 s23, s60, s22
	s_addc_u32 s24, s61, 0
	s_add_u32 s7, s2, s22
	s_addc_u32 s22, s3, 0
	s_lshl_b32 s6, s14, 2
	s_and_b32 s14, s6, 0x7c0
	s_and_b32 s6, s21, 0x1e0
	s_lshl_b32 s21, s6, 2
	v_add_u32_e32 v4, s14, v1
	s_add_u32 s30, s23, s21
	s_addc_u32 s31, s24, 0
	v_lshlrev_b32_e32 v96, 2, v0
	v_ashrrev_i32_e32 v5, 31, v4
	v_lshl_add_u64 v[12:13], s[30:31], 0, v[96:97]
	v_lshlrev_b64 v[4:5], 11, v[4:5]
	v_lshl_add_u64 v[4:5], v[12:13], 0, v[4:5]
	s_movk_i32 s21, 0x4000
	v_add_co_u32_e32 v16, vcc, s21, v4
	s_mov_b32 s21, 0x8000
	s_nop 0
	v_addc_co_u32_e32 v17, vcc, 0, v5, vcc
	global_load_dwordx4 v[12:15], v[4:5], off nt
	v_add_co_u32_e32 v20, vcc, s21, v4
	global_load_dwordx4 v[16:19], v[16:17], off nt
	s_nop 0
	v_addc_co_u32_e32 v21, vcc, 0, v5, vcc
	s_mov_b32 s21, 0xc000
	global_load_dwordx4 v[20:23], v[20:21], off nt
	v_add_co_u32_e32 v24, vcc, s21, v4
	s_mov_b32 s21, 0x10000
	s_nop 0
	v_addc_co_u32_e32 v25, vcc, 0, v5, vcc
	global_load_dwordx4 v[24:27], v[24:25], off nt
	v_add_co_u32_e32 v28, vcc, s21, v4
	s_mov_b32 s21, 0x14000
	s_nop 0
	v_addc_co_u32_e32 v29, vcc, 0, v5, vcc
	global_load_dwordx4 v[28:31], v[28:29], off nt
	v_add_co_u32_e32 v32, vcc, s21, v4
	s_lshl_b32 s14, s14, 1
	s_nop 0
	v_addc_co_u32_e32 v33, vcc, 0, v5, vcc
	global_load_dwordx4 v[32:35], v[32:33], off nt
	v_add_co_u32_e32 v36, vcc, s93, v4
	s_add_u32 s30, s7, s14
	s_nop 0
	v_addc_co_u32_e32 v37, vcc, 0, v5, vcc
	global_load_dwordx4 v[36:39], v[36:37], off nt
	v_add_co_u32_e32 v4, vcc, s96, v4
	s_addc_u32 s31, s22, 0
	s_nop 0
	v_addc_co_u32_e32 v5, vcc, 0, v5, vcc
	global_load_dwordx4 v[40:43], v[4:5], off nt
	v_add_u32_e32 v4, v10, v3
	v_add_u32_e32 v5, 0x420, v4
	v_lshlrev_b32_e32 v96, 1, v2
	s_waitcnt vmcnt(7)
	ds_write2_b32 v4, v12, v13 offset1:1
	ds_write2_b32 v4, v14, v15 offset0:2 offset1:3
	s_waitcnt vmcnt(6)
	ds_write2_b32 v5, v16, v17 offset1:1
	v_add_u32_e32 v5, 0x428, v4
	ds_write2_b32 v5, v18, v19 offset1:1
	v_add_u32_e32 v5, 0x840, v4
	s_waitcnt vmcnt(5)
	ds_write2_b32 v5, v20, v21 offset1:1
	v_add_u32_e32 v5, 0x848, v4
	ds_write2_b32 v5, v22, v23 offset1:1
	v_add_u32_e32 v5, 0xc60, v4
	v_add_u32_e32 v18, s6, v1
	s_waitcnt vmcnt(4)
	ds_write2_b32 v5, v24, v25 offset1:1
	v_add_u32_e32 v5, 0xc68, v4
	ds_write2_b32 v5, v26, v27 offset1:1
	v_add_u32_e32 v5, 0x1080, v4
	s_waitcnt vmcnt(3)
	ds_write2_b32 v5, v28, v29 offset1:1
	v_add_u32_e32 v5, 0x1088, v4
	ds_write2_b32 v5, v30, v31 offset1:1
	v_add_u32_e32 v5, 0x14a0, v4
	s_waitcnt vmcnt(2)
	ds_write2_b32 v5, v32, v33 offset1:1
	v_add_u32_e32 v5, 0x14a8, v4
	ds_write2_b32 v5, v34, v35 offset1:1
	v_add_u32_e32 v5, 0x18c0, v4
	s_waitcnt vmcnt(1)
	ds_write2_b32 v5, v36, v37 offset1:1
	v_add_u32_e32 v5, 0x18c8, v4
	ds_write2_b32 v5, v38, v39 offset1:1
	v_add_u32_e32 v5, 0x1ce0, v4
	v_add_u32_e32 v4, 0x1ce8, v4
	s_waitcnt vmcnt(0)
	ds_write2_b32 v5, v40, v41 offset1:1
	ds_write2_b32 v4, v42, v43 offset1:1
	s_waitcnt lgkmcnt(0)
	ds_read2_b32 v[214:215], v11 offset1:33
	ds_read2_b32 v[222:223], v11 offset0:66 offset1:99
	ds_read2_b32 v[224:225], v11 offset0:132 offset1:165
	ds_read2_b32 v[226:227], v11 offset0:198 offset1:231
	ds_read2_b32 v[228:229], v11 offset0:8 offset1:41
	ds_read2_b32 v[230:231], v11 offset0:74 offset1:107
	ds_read2_b32 v[232:233], v11 offset0:140 offset1:173
	ds_read2_b32 v[234:235], v11 offset0:206 offset1:239
	s_waitcnt lgkmcnt(0)
	ds_read2_b32 v[236:237], v11 offset0:16 offset1:49
	ds_read2_b32 v[238:239], v11 offset0:82 offset1:115
	ds_read2_b32 v[240:241], v11 offset0:148 offset1:181
	ds_read2_b32 v[242:243], v11 offset0:214 offset1:247
	ds_read2_b32 v[244:245], v11 offset0:24 offset1:57
	ds_read2_b32 v[246:247], v11 offset0:90 offset1:123
	ds_read2_b32 v[248:249], v11 offset0:156 offset1:189
	ds_read2_b32 v[250:251], v11 offset0:222 offset1:255
	v_cvt_pk_bf16_f32 v12, v214, v215
	v_cvt_pk_bf16_f32 v13, v222, v223
	v_cvt_pk_bf16_f32 v14, v224, v225
	v_cvt_pk_bf16_f32 v15, v226, v227
	v_and_b32_e32 v16, 0xffffff80, v18
	v_add_u32_e32 v16, v16, v18
	v_ashrrev_i32_e32 v17, 31, v16
	v_lshl_add_u64 v[4:5], s[30:31], 0, v[96:97]
	v_lshlrev_b64 v[16:17], 12, v[16:17]
	v_lshl_add_u64 v[16:17], v[4:5], 0, v[16:17]
	global_store_dwordx4 v[16:17], v[12:15], off nt
	s_nop 1
	v_add_u32_e32 v18, s6, v6
	v_cvt_pk_bf16_f32 v12, v228, v229
	v_cvt_pk_bf16_f32 v13, v230, v231
	v_cvt_pk_bf16_f32 v14, v232, v233
	v_cvt_pk_bf16_f32 v15, v234, v235
	v_and_b32_e32 v16, 0xffffff80, v18
	v_add_u32_e32 v16, v16, v18
	v_ashrrev_i32_e32 v17, 31, v16
	v_lshlrev_b64 v[16:17], 12, v[16:17]
	v_lshl_add_u64 v[16:17], v[4:5], 0, v[16:17]
	global_store_dwordx4 v[16:17], v[12:15], off nt
	s_nop 1
	s_waitcnt lgkmcnt(0)
	v_add_u32_e32 v18, s6, v7
	v_cvt_pk_bf16_f32 v12, v236, v237
	v_cvt_pk_bf16_f32 v13, v238, v239
	v_cvt_pk_bf16_f32 v14, v240, v241
	v_cvt_pk_bf16_f32 v15, v242, v243
	v_and_b32_e32 v16, 0xffffff80, v18
	v_add_u32_e32 v16, v16, v18
	v_ashrrev_i32_e32 v17, 31, v16
	v_lshlrev_b64 v[16:17], 12, v[16:17]
	v_lshl_add_u64 v[16:17], v[4:5], 0, v[16:17]
	global_store_dwordx4 v[16:17], v[12:15], off nt
	s_nop 1
	v_add_u32_e32 v18, s6, v8
	v_cvt_pk_bf16_f32 v12, v244, v245
	v_cvt_pk_bf16_f32 v13, v246, v247
	v_cvt_pk_bf16_f32 v14, v248, v249
	v_cvt_pk_bf16_f32 v15, v250, v251
	v_and_b32_e32 v16, 0xffffff80, v18
	v_add_u32_e32 v16, v16, v18
	v_ashrrev_i32_e32 v17, 31, v16
	v_lshlrev_b64 v[16:17], 12, v[16:17]
	v_lshl_add_u64 v[4:5], v[4:5], 0, v[16:17]
	global_store_dwordx4 v[4:5], v[12:15], off nt
	s_nop 1
	s_waitcnt lgkmcnt(0)

; __device__ __forceinline__ unsigned pk2(float lo, float hi) { unsigned r; asm volatile("v_cvt_pk_bf16_f32 %0, %1, %2" : "=v"(r) : "v"(lo), "v"(hi)); return r; }
; __device__ __forceinline__ void transpose_item(const float* W, int K, int N, bf16_t* WT, int rstep, int roff, float* scr, int item, int lane) {
;   const int nblk = N / 32, kb = item / nblk, nb = item % nblk, k0 = 64 * kb, n0 = 32 * nb;
;   f32x4 v[8];
; #pragma unroll
;   for (int i = 0; i < 8; ++i) v[i] = __builtin_nontemporal_load((const f32x4*)(W + (size_t)(k0 + i * 8 + (lane >> 3)) * N + n0 + (lane & 7) * 4));
; #pragma unroll
;   for (int i = 0; i < 8; ++i) { float* d = scr + (i * 8 + (lane >> 3)) * 33 + (lane & 7) * 4; d[0] = v[i].x; d[1] = v[i].y; d[2] = v[i].z; d[3] = v[i].w; }
;   __builtin_amdgcn_wave_barrier(); asm volatile("s_waitcnt lgkmcnt(0)" ::: "memory");
;   const int c = lane & 7;
; #pragma unroll
;   for (int j = 0; j < 4; ++j) { const int nl = (lane >> 3) + 8 * j, n = n0 + nl; const float* s = scr + (8 * c) * 33 + nl;
;     u32x4 o; o.x = pk2(s[0 * 33], s[1 * 33]); o.y = pk2(s[2 * 33], s[3 * 33]); o.z = pk2(s[4 * 33], s[5 * 33]); o.w = pk2(s[6 * 33], s[7 * 33]);
;     const int row = n + (n >> 7) * rstep + roff;
;     __builtin_nontemporal_store(o, (u32x4*)(WT + (size_t)row * K + k0 + 8 * c)); }
;   __builtin_amdgcn_wave_barrier(); asm volatile("s_waitcnt lgkmcnt(0)" ::: "memory");
; }
; __device__ __forceinline__ void convert_item(const P& p, int it, float* scr, int lane) {
;   if (it < IT_DENSE) {
;     const int l = it / (IT_WIN + IT_WOUT), r = it % (IT_WIN + IT_WOUT);
;     if (r < IT_WIN) transpose_item(p.w_in + (size_t)l * DM * INW, DM, INW, WSP(bf16_t, WS_WIN) + (size_t)l * INW * DM, 0, 0, scr, r, lane);
;     else transpose_item(p.w_out + (size_t)l * DM * DM, DM, DM, WSP(bf16_t, WS_WOUT) + (size_t)l * DM * DM, 0, 0, scr, r - IT_WIN, lane);
.LBB0_1041:
	s_and_b64 vcc, exec, s[6:7]
	s_cbranch_vccz .LBB0_1021
	s_ashr_i32 s6, s15, 31
	s_lshr_b32 s6, s6, 19
	s_add_i32 s6, s15, s6
	s_ashr_i32 s14, s6, 13
	s_and_b32 s6, s6, 0xffffe000
	s_sub_i32 s21, s15, s6
	s_ashr_i32 s15, s14, 31
	v_add_u32_e32 v12, v10, v3
	s_cmpk_gt_i32 s21, 0x17ff
	s_mov_b64 s[6:7], -1
	v_lshlrev_b32_e32 v96, 2, v0
	v_add_u32_e32 v13, 0x420, v12
	v_add_u32_e32 v14, 0x428, v12
	v_add_u32_e32 v15, 0x840, v12
	v_add_u32_e32 v16, 0x848, v12
	v_add_u32_e32 v17, 0xc60, v12
	v_add_u32_e32 v18, 0xc68, v12
	v_add_u32_e32 v19, 0x1080, v12
	v_add_u32_e32 v20, 0x1088, v12
	v_add_u32_e32 v21, 0x14a0, v12
	v_add_u32_e32 v22, 0x14a8, v12
	v_add_u32_e32 v23, 0x18c0, v12
	v_add_u32_e32 v24, 0x18c8, v12
	v_add_u32_e32 v25, 0x1ce0, v12
	v_add_u32_e32 v26, 0x1ce8, v12
	v_lshlrev_b32_e32 v4, 1, v2
	s_cbranch_scc0 .LBB0_1044
	s_lshl_b64 s[6:7], s[14:15], 24
	s_add_u32 s22, s58, s6
	s_addc_u32 s23, s59, s7
	s_lshl_b64 s[6:7], s[14:15], 23
	s_add_u32 s15, s9, s6
	s_addc_u32 s24, s16, s7
	s_add_i32 s6, s21, 0xe800
	s_and_b32 s30, s6, 0xffc0
	s_lshl_b32 s6, s21, 5
	s_and_b32 s31, s6, 0x7e0
	s_lshl_b32 s6, s31, 2
	v_add_u32_e32 v28, s30, v1
	s_add_u32 s6, s22, s6
	s_addc_u32 s7, s23, 0
	v_ashrrev_i32_e32 v29, 31, v28
	v_lshl_add_u64 v[30:31], s[6:7], 0, v[96:97]
	v_lshlrev_b64 v[28:29], 13, v[28:29]
	v_lshl_add_u64 v[56:57], v[30:31], 0, v[28:29]
	s_mov_b32 s6, 0x10000
	v_add_co_u32_e32 v32, vcc, s6, v56
	s_mov_b32 s6, 0x20000
	s_nop 0
	v_addc_co_u32_e32 v33, vcc, 0, v57, vcc
	v_add_co_u32_e32 v36, vcc, s6, v56
	s_mov_b32 s6, 0x30000
	s_nop 0
	v_addc_co_u32_e32 v37, vcc, 0, v57, vcc
	v_add_co_u32_e32 v40, vcc, s6, v56
	s_mov_b32 s6, 0x40000
	s_nop 0
	v_addc_co_u32_e32 v41, vcc, 0, v57, vcc
	v_add_co_u32_e32 v44, vcc, s6, v56
	s_mov_b32 s6, 0x50000
	s_nop 0
	v_addc_co_u32_e32 v45, vcc, 0, v57, vcc
	v_add_co_u32_e32 v48, vcc, s6, v56
	global_load_dwordx4 v[28:31], v[56:57], off nt
	s_nop 0
	global_load_dwordx4 v[32:35], v[32:33], off nt
	v_addc_co_u32_e32 v49, vcc, 0, v57, vcc
	global_load_dwordx4 v[36:39], v[36:37], off nt
	s_nop 0
	global_load_dwordx4 v[40:43], v[40:41], off nt
	s_nop 0
	global_load_dwordx4 v[44:47], v[44:45], off nt
	s_nop 0
	global_load_dwordx4 v[48:51], v[48:49], off nt
	s_mov_b32 s6, 0x60000
	v_add_co_u32_e32 v52, vcc, s6, v56
	s_mov_b32 s6, 0x70000
	s_nop 0
	v_addc_co_u32_e32 v53, vcc, 0, v57, vcc
	global_load_dwordx4 v[52:55], v[52:53], off nt
	v_add_co_u32_e32 v56, vcc, s6, v56
	s_lshl_b32 s6, s30, 1
	s_nop 0
	v_addc_co_u32_e32 v57, vcc, 0, v57, vcc
	global_load_dwordx4 v[56:59], v[56:57], off nt
	s_add_u32 s6, s15, s6
	v_mov_b32_e32 v5, v97
	s_addc_u32 s7, s24, 0
	s_waitcnt vmcnt(7)
	ds_write2_b32 v12, v28, v29 offset1:1
	ds_write2_b32 v12, v30, v31 offset0:2 offset1:3
	s_waitcnt vmcnt(6)
	ds_write2_b32 v13, v32, v33 offset1:1
	ds_write2_b32 v14, v34, v35 offset1:1
	s_waitcnt vmcnt(5)
	ds_write2_b32 v15, v36, v37 offset1:1
	ds_write2_b32 v16, v38, v39 offset1:1
	s_waitcnt vmcnt(4)
	ds_write2_b32 v17, v40, v41 offset1:1
	ds_write2_b32 v18, v42, v43 offset1:1
	s_waitcnt vmcnt(3)
	ds_write2_b32 v19, v44, v45 offset1:1
	ds_write2_b32 v20, v46, v47 offset1:1
	s_waitcnt vmcnt(2)
	ds_write2_b32 v21, v48, v49 offset1:1
	ds_write2_b32 v22, v50, v51 offset1:1
	s_waitcnt vmcnt(1)
	ds_write2_b32 v23, v52, v53 offset1:1
	ds_write2_b32 v24, v54, v55 offset1:1
	s_waitcnt vmcnt(0)
	ds_write2_b32 v25, v56, v57 offset1:1
	ds_write2_b32 v26, v58, v59 offset1:1
	s_waitcnt lgkmcnt(0)
	ds_read2_b32 v[214:215], v11 offset1:33
	ds_read2_b32 v[222:223], v11 offset0:66 offset1:99
	ds_read2_b32 v[224:225], v11 offset0:132 offset1:165
	ds_read2_b32 v[226:227], v11 offset0:198 offset1:231
	ds_read2_b32 v[228:229], v11 offset0:8 offset1:41
	ds_read2_b32 v[230:231], v11 offset0:74 offset1:107
	ds_read2_b32 v[232:233], v11 offset0:140 offset1:173
	ds_read2_b32 v[234:235], v11 offset0:206 offset1:239
	s_waitcnt lgkmcnt(0)
	ds_read2_b32 v[236:237], v11 offset0:16 offset1:49
	ds_read2_b32 v[238:239], v11 offset0:82 offset1:115
	ds_read2_b32 v[240:241], v11 offset0:148 offset1:181
	ds_read2_b32 v[242:243], v11 offset0:214 offset1:247
	ds_read2_b32 v[244:245], v11 offset0:24 offset1:57
	ds_read2_b32 v[246:247], v11 offset0:90 offset1:123
	ds_read2_b32 v[248:249], v11 offset0:156 offset1:189
	ds_read2_b32 v[250:251], v11 offset0:222 offset1:255
	v_cvt_pk_bf16_f32 v28, v214, v215
	v_add_u32_e32 v32, s31, v1
	v_cvt_pk_bf16_f32 v29, v222, v223
	v_ashrrev_i32_e32 v33, 31, v32
	v_cvt_pk_bf16_f32 v30, v224, v225
	v_lshlrev_b64 v[32:33], 12, v[32:33]
	v_lshl_add_u64 v[36:37], s[6:7], 0, v[4:5]
	v_cvt_pk_bf16_f32 v31, v226, v227
	v_lshl_add_u64 v[32:33], v[36:37], 0, v[32:33]
	global_store_dwordx4 v[32:33], v[28:31], off nt
	s_nop 1
	s_mov_b64 s[6:7], 0
	v_cvt_pk_bf16_f32 v28, v228, v229
	v_add_u32_e32 v34, s31, v6
	v_ashrrev_i32_e32 v35, 31, v34
	v_lshlrev_b64 v[34:35], 12, v[34:35]
	v_cvt_pk_bf16_f32 v29, v230, v231
	v_lshl_add_u64 v[34:35], v[36:37], 0, v[34:35]
	v_cvt_pk_bf16_f32 v30, v232, v233
	v_cvt_pk_bf16_f32 v31, v234, v235
	global_store_dwordx4 v[34:35], v[28:31], off nt
	s_nop 1
	v_add_u32_e32 v34, s31, v7
	v_ashrrev_i32_e32 v35, 31, v34
	s_waitcnt lgkmcnt(0)
	v_cvt_pk_bf16_f32 v28, v236, v237
	v_lshlrev_b64 v[34:35], 12, v[34:35]
	v_cvt_pk_bf16_f32 v29, v238, v239
	v_lshl_add_u64 v[34:35], v[36:37], 0, v[34:35]
	v_cvt_pk_bf16_f32 v30, v240, v241
	v_cvt_pk_bf16_f32 v31, v242, v243
	global_store_dwordx4 v[34:35], v[28:31], off nt
	s_nop 1
	v_add_u32_e32 v34, s31, v8
	v_ashrrev_i32_e32 v35, 31, v34
	v_cvt_pk_bf16_f32 v28, v244, v245
	v_lshlrev_b64 v[34:35], 12, v[34:35]
	v_cvt_pk_bf16_f32 v29, v246, v247
	v_lshl_add_u64 v[34:35], v[36:37], 0, v[34:35]
	v_cvt_pk_bf16_f32 v30, v248, v249
	v_cvt_pk_bf16_f32 v31, v250, v251
	global_store_dwordx4 v[34:35], v[28:31], off nt
	s_nop 1
	s_waitcnt lgkmcnt(0)
; __device__ __forceinline__ unsigned pk2(float lo, float hi) { unsigned r; asm volatile("v_cvt_pk_bf16_f32 %0, %1, %2" : "=v"(r) : "v"(lo), "v"(hi)); return r; }
; __device__ __forceinline__ void transpose_item(const float* W, int K, int N, bf16_t* WT, int rstep, int roff, float* scr, int item, int lane) {
;   const int nblk = N / 32, kb = item / nblk, nb = item % nblk, k0 = 64 * kb, n0 = 32 * nb;
;   f32x4 v[8];
; #pragma unroll
;   for (int i = 0; i < 8; ++i) v[i] = __builtin_nontemporal_load((const f32x4*)(W + (size_t)(k0 + i * 8 + (lane >> 3)) * N + n0 + (lane & 7) * 4));
; #pragma unroll
;   for (int i = 0; i < 8; ++i) { float* d = scr + (i * 8 + (lane >> 3)) * 33 + (lane & 7) * 4; d[0] = v[i].x; d[1] = v[i].y; d[2] = v[i].z; d[3] = v[i].w; }
;   __builtin_amdgcn_wave_barrier(); asm volatile("s_waitcnt lgkmcnt(0)" ::: "memory");
;   const int c = lane & 7;
; #pragma unroll
;   for (int j = 0; j < 4; ++j) { const int nl = (lane >> 3) + 8 * j, n = n0 + nl; const float* s = scr + (8 * c) * 33 + nl;
;     u32x4 o; o.x = pk2(s[0 * 33], s[1 * 33]); o.y = pk2(s[2 * 33], s[3 * 33]); o.z = pk2(s[4 * 33], s[5 * 33]); o.w = pk2(s[6 * 33], s[7 * 33]);
;     const int row = n + (n >> 7) * rstep + roff;
;     __builtin_nontemporal_store(o, (u32x4*)(WT + (size_t)row * K + k0 + 8 * c)); }
;   __builtin_amdgcn_wave_barrier(); asm volatile("s_waitcnt lgkmcnt(0)" ::: "memory");
; }
; __device__ __forceinline__ void convert_item(const P& p, int it, float* scr, int lane) {
;     ...
;     if (r < IT_WIN) transpose_item(p.w_in + (size_t)l * DM * INW, DM, INW, WSP(bf16_t, WS_WIN) + (size_t)l * INW * DM, 0, 0, scr, r, lane);
.LBB0_1044:
	s_andn2_b64 vcc, exec, s[6:7]
	s_cbranch_vccnz .LBB0_1021
	s_mul_i32 s7, s14, 0x3000000
	s_mul_hi_i32 s6, s14, 0x3000000
	s_add_u32 s7, s56, s7
	s_addc_u32 s24, s57, s6
	s_mul_hi_i32 s6, s14, 0x1800000
	s_mul_i32 s14, s14, 0x1800000
	s_add_u32 s30, s17, s14
	s_addc_u32 s31, s18, s6
	s_mul_i32 s6, s21, 0x2aab
	s_lshr_b32 s14, s6, 31
	s_ashr_i32 s6, s6, 21
	s_add_i32 s6, s6, s14
	s_sext_i32_i16 s14, s6
	s_mulk_i32 s6, 0xc0
	s_sub_i32 s6, s21, s6
	s_sext_i32_i16 s15, s6
	s_lshl_b32 s6, s14, 6
	s_lshl_b32 s14, s15, 5
	s_ashr_i32 s15, s14, 31
	s_lshl_b64 s[22:23], s[14:15], 2
	s_add_u32 s22, s7, s22
	v_add_u32_e32 v5, s6, v1
	s_addc_u32 s23, s24, s23
	v_lshl_add_u64 v[56:57], s[22:23], 0, v[96:97]
	s_movk_i32 s7, 0x6000
	v_add_u32_e32 v27, 8, v5
	v_mad_i64_i32 v[32:33], s[22:23], v27, s7, v[56:57]
	v_add_u32_e32 v27, 16, v5
	v_mad_i64_i32 v[36:37], s[22:23], v27, s7, v[56:57]
	v_add_u32_e32 v27, 24, v5
	v_mad_i64_i32 v[40:41], s[22:23], v27, s7, v[56:57]
	v_add_u32_e32 v27, 32, v5
	v_mad_i64_i32 v[44:45], s[22:23], v27, s7, v[56:57]
	v_add_u32_e32 v27, 40, v5
	v_mad_i64_i32 v[28:29], s[22:23], v5, s7, v[56:57]
	v_mad_i64_i32 v[48:49], s[22:23], v27, s7, v[56:57]
	global_load_dwordx4 v[28:31], v[28:29], off nt
	s_nop 0
	global_load_dwordx4 v[32:35], v[32:33], off nt
	s_nop 0
	global_load_dwordx4 v[36:39], v[36:37], off nt
	s_nop 0
	global_load_dwordx4 v[40:43], v[40:41], off nt
	s_nop 0
	global_load_dwordx4 v[44:47], v[44:45], off nt
	s_nop 0
	global_load_dwordx4 v[48:51], v[48:49], off nt
	v_add_u32_e32 v27, 48, v5
	v_mad_i64_i32 v[52:53], s[22:23], v27, s7, v[56:57]
	global_load_dwordx4 v[52:55], v[52:53], off nt
	v_add_u32_e32 v5, 56, v5
	v_mad_i64_i32 v[56:57], s[22:23], v5, s7, v[56:57]
	global_load_dwordx4 v[56:59], v[56:57], off nt
	s_ashr_i32 s7, s6, 31
	s_lshl_b64 s[6:7], s[6:7], 1
	s_add_u32 s6, s30, s6
	v_mov_b32_e32 v5, v97
	s_addc_u32 s7, s31, s7
	v_lshl_add_u64 v[4:5], s[6:7], 0, v[4:5]
	s_movk_i32 s82, 0x6000
	s_waitcnt vmcnt(7)
	ds_write2_b32 v12, v28, v29 offset1:1
	ds_write2_b32 v12, v30, v31 offset0:2 offset1:3
	s_waitcnt vmcnt(6)
	ds_write2_b32 v13, v32, v33 offset1:1
	ds_write2_b32 v14, v34, v35 offset1:1
	s_waitcnt vmcnt(5)
	ds_write2_b32 v15, v36, v37 offset1:1
	ds_write2_b32 v16, v38, v39 offset1:1
	s_waitcnt vmcnt(4)
	ds_write2_b32 v17, v40, v41 offset1:1
	ds_write2_b32 v18, v42, v43 offset1:1
	s_waitcnt vmcnt(3)
	ds_write2_b32 v19, v44, v45 offset1:1
	ds_write2_b32 v20, v46, v47 offset1:1
	s_waitcnt vmcnt(2)
	ds_write2_b32 v21, v48, v49 offset1:1
	ds_write2_b32 v22, v50, v51 offset1:1
	s_waitcnt vmcnt(1)
	ds_write2_b32 v23, v52, v53 offset1:1
	ds_write2_b32 v24, v54, v55 offset1:1
	s_waitcnt vmcnt(0)
	ds_write2_b32 v25, v56, v57 offset1:1
	ds_write2_b32 v26, v58, v59 offset1:1
	s_waitcnt lgkmcnt(0)
	ds_read2_b32 v[214:215], v11 offset1:33
	ds_read2_b32 v[222:223], v11 offset0:66 offset1:99
	ds_read2_b32 v[224:225], v11 offset0:132 offset1:165
	ds_read2_b32 v[226:227], v11 offset0:198 offset1:231
	ds_read2_b32 v[228:229], v11 offset0:8 offset1:41
	ds_read2_b32 v[230:231], v11 offset0:74 offset1:107
	ds_read2_b32 v[232:233], v11 offset0:140 offset1:173
	ds_read2_b32 v[234:235], v11 offset0:206 offset1:239
	s_waitcnt lgkmcnt(0)
	ds_read2_b32 v[236:237], v11 offset0:16 offset1:49
	ds_read2_b32 v[238:239], v11 offset0:82 offset1:115
	ds_read2_b32 v[240:241], v11 offset0:148 offset1:181
	ds_read2_b32 v[242:243], v11 offset0:214 offset1:247
	ds_read2_b32 v[244:245], v11 offset0:24 offset1:57
	ds_read2_b32 v[246:247], v11 offset0:90 offset1:123
	ds_read2_b32 v[248:249], v11 offset0:156 offset1:189
	ds_read2_b32 v[250:251], v11 offset0:222 offset1:255
	v_cvt_pk_bf16_f32 v12, v214, v215
	v_add_u32_e32 v16, s14, v1
	v_cvt_pk_bf16_f32 v13, v222, v223
	v_ashrrev_i32_e32 v17, 31, v16
	v_cvt_pk_bf16_f32 v14, v224, v225
	v_lshlrev_b64 v[16:17], 12, v[16:17]
	v_cvt_pk_bf16_f32 v15, v226, v227
	v_lshl_add_u64 v[16:17], v[4:5], 0, v[16:17]
	global_store_dwordx4 v[16:17], v[12:15], off nt
	s_nop 1
	s_nop 0
	v_cvt_pk_bf16_f32 v12, v228, v229
	v_add_u32_e32 v18, s14, v6
	v_ashrrev_i32_e32 v19, 31, v18
	v_lshlrev_b64 v[18:19], 12, v[18:19]
	v_cvt_pk_bf16_f32 v13, v230, v231
	v_lshl_add_u64 v[18:19], v[4:5], 0, v[18:19]
	v_cvt_pk_bf16_f32 v14, v232, v233
	v_cvt_pk_bf16_f32 v15, v234, v235
	global_store_dwordx4 v[18:19], v[12:15], off nt
	s_nop 1
	v_add_u32_e32 v18, s14, v7
	v_ashrrev_i32_e32 v19, 31, v18
	s_waitcnt lgkmcnt(0)
	v_cvt_pk_bf16_f32 v12, v236, v237
	v_lshlrev_b64 v[18:19], 12, v[18:19]
	v_cvt_pk_bf16_f32 v13, v238, v239
	v_lshl_add_u64 v[18:19], v[4:5], 0, v[18:19]
	v_cvt_pk_bf16_f32 v14, v240, v241
	v_cvt_pk_bf16_f32 v15, v242, v243
	global_store_dwordx4 v[18:19], v[12:15], off nt
	s_nop 1
	v_add_u32_e32 v18, s14, v8
	v_ashrrev_i32_e32 v19, 31, v18
	v_cvt_pk_bf16_f32 v12, v244, v245
	v_lshlrev_b64 v[18:19], 12, v[18:19]
	v_cvt_pk_bf16_f32 v13, v246, v247
	v_lshl_add_u64 v[4:5], v[4:5], 0, v[18:19]
	v_cvt_pk_bf16_f32 v14, v248, v249
	v_cvt_pk_bf16_f32 v15, v250, v251
	global_store_dwordx4 v[4:5], v[12:15], off nt
	s_nop 1
	s_waitcnt lgkmcnt(0)
	s_branch .LBB0_1021

; __device__ __forceinline__ void transpose_item(const float* W, int K, int N, bf16_t* WT, int rstep, int roff, float* scr, int item, int lane) {
;   const int nblk = N / 32, kb = item / nblk, nb = item % nblk, k0 = 64 * kb, n0 = 32 * nb;
;   f32x4 v[8];
; #pragma unroll
;   for (int i = 0; i < 8; ++i) v[i] = __builtin_nontemporal_load((const f32x4*)(W + (size_t)(k0 + i * 8 + (lane >> 3)) * N + n0 + (lane & 7) * 4));
; #pragma unroll
;   for (int i = 0; i < 8; ++i) { float* d = scr + (i * 8 + (lane >> 3)) * 33 + (lane & 7) * 4; d[0] = v[i].x; d[1] = v[i].y; d[2] = v[i].z; d[3] = v[i].w; }
;   __builtin_amdgcn_wave_barrier(); asm volatile("s_waitcnt lgkmcnt(0)" ::: "memory");
;   const int c = lane & 7;
; #pragma unroll
; __device__ __forceinline__ void convert_item(const P& p, int it, float* scr, int lane) {
;   if (it < IT_DENSE) {
;     const int l = it / (IT_WIN + IT_WOUT), r = it % (IT_WIN + IT_WOUT);
;     if (r < IT_WIN) transpose_item(p.w_in + (size_t)l * DM * INW, DM, INW, WSP(bf16_t, WS_WIN) + (size_t)l * INW * DM, 0, 0, scr, r, lane);
;     else transpose_item(p.w_out + (size_t)l * DM * DM, DM, DM, WSP(bf16_t, WS_WOUT) + (size_t)l * DM * DM, 0, 0, scr, r - IT_WIN, lane);
;   } else {
;     const int idx = it - IT_DENSE, m = idx / IT_EXP, sub = idx % IT_EXP, le = m / 3, which = m % 3;
;     if (which == 0) transpose_item(p.wg + (size_t)le * DM * EFF, DM, EFF, WSP(bf16_t, WS_WGU) + (size_t)le * 1024 * DM, 128, 0, scr, sub, lane);
;     else if (which == 1) transpose_item(p.wu + (size_t)le * DM * EFF, DM, EFF, WSP(bf16_t, WS_WGU) + (size_t)le * 1024 * DM, 128, 128, scr, sub, lane);
;     else transpose_item(p.wd + (size_t)le * EFF * DM, EFF, DM, WSP(bf16_t, WS_WD) + (size_t)le * DM * EFF, 0, 0, scr, sub, lane);
; __device__ __forceinline__ void convert_item_n(const P& p, int n, float* scr, int lane) {
;   int it;
;   if (n < CV_E0) it = n; else if (n < CV_D1) it = IT_DENSE + (n - CV_E0); else if (n < CV_E1) it = (IT_WIN + IT_WOUT) + (n - CV_D1); else { const int k = n - CV_E1;
;     if (k < NEXP * 2 * IT_EXP) { const int m = k / IT_EXP; it = IT_DENSE + ((NEXP + (m >> 1)) * 3 + (m & 1)) * IT_EXP + k % IT_EXP; }
;     else { const int k2 = k - NEXP * 2 * IT_EXP; it = IT_DENSE + ((NEXP + k2 / IT_EXP) * 3 + 2) * IT_EXP + k2 % IT_EXP; } }
;   convert_item(p, it, scr, lane);
.LBB0_1049:
	s_add_i32 s6, s17, 0x2000
	s_cmpk_lt_i32 s17, 0x2000
	s_cselect_b32 s13, s17, s6
	s_cmpk_gt_i32 s13, 0x3fff
	s_mov_b64 s[6:7], -1
	s_cbranch_scc0 .LBB0_1059
	s_add_i32 s6, s13, 0xffffc000
	s_lshr_b32 s7, s6, 9
	s_mul_i32 s6, s6, 0xaaab
	s_lshr_b32 s20, s6, 26
	s_mul_i32 s6, s7, 0xab
	s_bfe_u32 s6, s6, 0x70009
	s_mul_i32 s6, s6, 3
	s_sub_i32 s6, s7, s6
	s_and_b32 s12, s13, 0x1ff
	s_lshl_b32 s19, s20, 22
	s_lshl_b32 s18, s13, 5
	s_and_b32 s21, s6, 0xff
	s_cmp_lt_i32 s21, 1
	s_mov_b64 s[6:7], -1
	s_cbranch_scc1 .LBB0_1056
	s_and_b32 s6, 0xffff, s21
	s_cmp_lg_u32 s6, 1
	s_mov_b64 s[6:7], -1
	s_cbranch_scc0 .LBB0_1053
	s_add_u32 s22, s0, s19
	s_addc_u32 s23, s1, 0
	s_lshl_b32 s6, s20, 21
	s_add_u32 s7, s4, s6
	s_addc_u32 s20, s5, 0
	s_and_b32 s6, s18, 0x7e0
	s_and_b32 s21, s13, 0x1c0
	s_lshl_b32 s24, s6, 2
	v_add_u32_e32 v4, s21, v1
	s_add_u32 s22, s22, s24
	s_addc_u32 s23, s23, 0
	v_lshlrev_b32_e32 v96, 2, v0
	v_ashrrev_i32_e32 v5, 31, v4
	v_lshl_add_u64 v[12:13], s[22:23], 0, v[96:97]
	v_lshlrev_b64 v[4:5], 13, v[4:5]
	v_lshl_add_u64 v[4:5], v[12:13], 0, v[4:5]
	s_mov_b32 s22, 0x10000
	v_add_co_u32_e32 v16, vcc, s22, v4
	s_mov_b32 s22, 0x20000
	s_nop 0
	v_addc_co_u32_e32 v17, vcc, 0, v5, vcc
	global_load_dwordx4 v[12:15], v[4:5], off nt
	v_add_co_u32_e32 v20, vcc, s22, v4
	global_load_dwordx4 v[16:19], v[16:17], off nt
	s_nop 0
	v_addc_co_u32_e32 v21, vcc, 0, v5, vcc
	s_mov_b32 s22, 0x30000
	global_load_dwordx4 v[20:23], v[20:21], off nt
	v_add_co_u32_e32 v24, vcc, s22, v4
	s_mov_b32 s22, 0x40000
	s_nop 0
	v_addc_co_u32_e32 v25, vcc, 0, v5, vcc
	global_load_dwordx4 v[24:27], v[24:25], off nt
	v_add_co_u32_e32 v28, vcc, s22, v4
	s_mov_b32 s22, 0x50000
	s_nop 0
	v_addc_co_u32_e32 v29, vcc, 0, v5, vcc
	global_load_dwordx4 v[28:31], v[28:29], off nt
	v_add_co_u32_e32 v32, vcc, s22, v4
	s_mov_b32 s22, 0x60000
	s_nop 0
	v_addc_co_u32_e32 v33, vcc, 0, v5, vcc
	global_load_dwordx4 v[32:35], v[32:33], off nt
	v_add_co_u32_e32 v36, vcc, s22, v4
	s_mov_b32 s22, 0x70000
	s_nop 0
	v_addc_co_u32_e32 v37, vcc, 0, v5, vcc
	global_load_dwordx4 v[36:39], v[36:37], off nt
	v_add_co_u32_e32 v4, vcc, s22, v4
	s_lshl_b32 s21, s21, 1
	s_nop 0
	v_addc_co_u32_e32 v5, vcc, 0, v5, vcc
	global_load_dwordx4 v[40:43], v[4:5], off nt
	v_add_u32_e32 v4, v10, v3
	v_add_u32_e32 v5, 0x420, v4
	s_add_u32 s22, s7, s21
	s_addc_u32 s23, s20, 0
	v_lshlrev_b32_e32 v96, 1, v2
	s_waitcnt vmcnt(7)
	ds_write2_b32 v4, v12, v13 offset1:1
	ds_write2_b32 v4, v14, v15 offset0:2 offset1:3
	s_waitcnt vmcnt(6)
	ds_write2_b32 v5, v16, v17 offset1:1
	v_add_u32_e32 v5, 0x428, v4
	ds_write2_b32 v5, v18, v19 offset1:1
	v_add_u32_e32 v5, 0x840, v4
	s_waitcnt vmcnt(5)
	ds_write2_b32 v5, v20, v21 offset1:1
	v_add_u32_e32 v5, 0x848, v4
	ds_write2_b32 v5, v22, v23 offset1:1
	v_add_u32_e32 v5, 0xc60, v4
	v_add_u32_e32 v16, s6, v1
	v_ashrrev_i32_e32 v17, 31, v16
	s_waitcnt vmcnt(4)
	ds_write2_b32 v5, v24, v25 offset1:1
	v_add_u32_e32 v5, 0xc68, v4
	ds_write2_b32 v5, v26, v27 offset1:1
	v_add_u32_e32 v5, 0x1080, v4
	v_lshlrev_b64 v[16:17], 10, v[16:17]
	s_waitcnt vmcnt(3)
	ds_write2_b32 v5, v28, v29 offset1:1
	v_add_u32_e32 v5, 0x1088, v4
	ds_write2_b32 v5, v30, v31 offset1:1
	v_add_u32_e32 v5, 0x14a0, v4
	s_waitcnt vmcnt(2)
	ds_write2_b32 v5, v32, v33 offset1:1
	v_add_u32_e32 v5, 0x14a8, v4
	ds_write2_b32 v5, v34, v35 offset1:1
	v_add_u32_e32 v5, 0x18c0, v4
	s_waitcnt vmcnt(1)
	ds_write2_b32 v5, v36, v37 offset1:1
	v_add_u32_e32 v5, 0x18c8, v4
	ds_write2_b32 v5, v38, v39 offset1:1
	v_add_u32_e32 v5, 0x1ce0, v4
	v_add_u32_e32 v4, 0x1ce8, v4
	s_waitcnt vmcnt(0)
	ds_write2_b32 v5, v40, v41 offset1:1
	ds_write2_b32 v4, v42, v43 offset1:1
	s_waitcnt lgkmcnt(0)
	ds_read2_b32 v[214:215], v9 offset1:33
	ds_read2_b32 v[222:223], v9 offset0:66 offset1:99
	ds_read2_b32 v[224:225], v9 offset0:132 offset1:165
	ds_read2_b32 v[226:227], v9 offset0:198 offset1:231
	ds_read2_b32 v[228:229], v9 offset0:8 offset1:41
	ds_read2_b32 v[230:231], v9 offset0:74 offset1:107
	ds_read2_b32 v[232:233], v9 offset0:140 offset1:173
	ds_read2_b32 v[234:235], v9 offset0:206 offset1:239
	s_waitcnt lgkmcnt(0)
	ds_read2_b32 v[236:237], v9 offset0:16 offset1:49
	ds_read2_b32 v[238:239], v9 offset0:82 offset1:115
	ds_read2_b32 v[240:241], v9 offset0:148 offset1:181
	ds_read2_b32 v[242:243], v9 offset0:214 offset1:247
	ds_read2_b32 v[244:245], v9 offset0:24 offset1:57
	ds_read2_b32 v[246:247], v9 offset0:90 offset1:123
	ds_read2_b32 v[248:249], v9 offset0:156 offset1:189
	ds_read2_b32 v[250:251], v9 offset0:222 offset1:255
	v_lshl_add_u64 v[4:5], s[22:23], 0, v[96:97]
	v_cvt_pk_bf16_f32 v12, v214, v215
	v_cvt_pk_bf16_f32 v13, v222, v223
	v_lshl_add_u64 v[16:17], v[4:5], 0, v[16:17]
	v_cvt_pk_bf16_f32 v14, v224, v225
	v_cvt_pk_bf16_f32 v15, v226, v227
	global_store_dwordx4 v[16:17], v[12:15], off nt
	s_nop 1
	v_add_u32_e32 v16, s6, v6
	v_ashrrev_i32_e32 v17, 31, v16
	v_cvt_pk_bf16_f32 v12, v228, v229
	v_lshlrev_b64 v[16:17], 10, v[16:17]
	v_cvt_pk_bf16_f32 v13, v230, v231
	v_lshl_add_u64 v[16:17], v[4:5], 0, v[16:17]
	v_cvt_pk_bf16_f32 v14, v232, v233
	v_cvt_pk_bf16_f32 v15, v234, v235
	global_store_dwordx4 v[16:17], v[12:15], off nt
	s_nop 1
	v_add_u32_e32 v16, s6, v7
	s_waitcnt lgkmcnt(0)
	v_ashrrev_i32_e32 v17, 31, v16
	v_cvt_pk_bf16_f32 v12, v236, v237
	v_lshlrev_b64 v[16:17], 10, v[16:17]
	v_cvt_pk_bf16_f32 v13, v238, v239
	v_lshl_add_u64 v[16:17], v[4:5], 0, v[16:17]
	v_cvt_pk_bf16_f32 v14, v240, v241
	v_cvt_pk_bf16_f32 v15, v242, v243
	global_store_dwordx4 v[16:17], v[12:15], off nt
	s_nop 1
	v_add_u32_e32 v16, s6, v8
	v_ashrrev_i32_e32 v17, 31, v16
	v_cvt_pk_bf16_f32 v12, v244, v245
	v_lshlrev_b64 v[16:17], 10, v[16:17]
	v_cvt_pk_bf16_f32 v13, v246, v247
	v_lshl_add_u64 v[4:5], v[4:5], 0, v[16:17]
	v_cvt_pk_bf16_f32 v14, v248, v249
	v_cvt_pk_bf16_f32 v15, v250, v251
	global_store_dwordx4 v[4:5], v[12:15], off nt
	s_nop 1
	s_waitcnt lgkmcnt(0)
	s_mov_b64 s[6:7], 0
; __device__ __forceinline__ unsigned pk2(float lo, float hi) { unsigned r; asm volatile("v_cvt_pk_bf16_f32 %0, %1, %2" : "=v"(r) : "v"(lo), "v"(hi)); return r; }
; __device__ __forceinline__ void transpose_item(const float* W, int K, int N, bf16_t* WT, int rstep, int roff, float* scr, int item, int lane) {
;   const int nblk = N / 32, kb = item / nblk, nb = item % nblk, k0 = 64 * kb, n0 = 32 * nb;
;   f32x4 v[8];
; #pragma unroll
;   for (int i = 0; i < 8; ++i) v[i] = __builtin_nontemporal_load((const f32x4*)(W + (size_t)(k0 + i * 8 + (lane >> 3)) * N + n0 + (lane & 7) * 4));
; #pragma unroll
;   for (int i = 0; i < 8; ++i) { float* d = scr + (i * 8 + (lane >> 3)) * 33 + (lane & 7) * 4; d[0] = v[i].x; d[1] = v[i].y; d[2] = v[i].z; d[3] = v[i].w; }
;   __builtin_amdgcn_wave_barrier(); asm volatile("s_waitcnt lgkmcnt(0)" ::: "memory");
;   const int c = lane & 7;
; #pragma unroll
;   for (int j = 0; j < 4; ++j) { const int nl = (lane >> 3) + 8 * j, n = n0 + nl; const float* s = scr + (8 * c) * 33 + nl;
;     u32x4 o; o.x = pk2(s[0 * 33], s[1 * 33]); o.y = pk2(s[2 * 33], s[3 * 33]); o.z = pk2(s[4 * 33], s[5 * 33]); o.w = pk2(s[6 * 33], s[7 * 33]);
;     const int row = n + (n >> 7) * rstep + roff;
;     __builtin_nontemporal_store(o, (u32x4*)(WT + (size_t)row * K + k0 + 8 * c)); }
;   __builtin_amdgcn_wave_barrier(); asm volatile("s_waitcnt lgkmcnt(0)" ::: "memory");
; }
; __device__ __forceinline__ void convert_item(const P& p, int it, float* scr, int lane) {
;     ...
;     else if (which == 1) transpose_item(p.wu + (size_t)le * DM * EFF, DM, EFF, WSP(bf16_t, WS_WGU) + (size_t)le * 1024 * DM, 128, 128, scr, sub, lane);
.LBB0_1053:
	s_andn2_b64 vcc, exec, s[6:7]
	s_cbranch_vccnz .LBB0_1055
	s_add_u32 s22, s62, s19
	s_addc_u32 s23, s63, 0
	s_add_u32 s7, s2, s19
	s_addc_u32 s20, s3, 0
	s_lshl_b32 s6, s12, 2
	s_and_b32 s21, s6, 0x7c0
	s_and_b32 s6, s18, 0x1e0
	s_lshl_b32 s24, s6, 2
	v_add_u32_e32 v4, s21, v1
	s_add_u32 s22, s22, s24
	s_addc_u32 s23, s23, 0
	v_lshlrev_b32_e32 v96, 2, v0
	v_ashrrev_i32_e32 v5, 31, v4
	v_lshl_add_u64 v[12:13], s[22:23], 0, v[96:97]
	v_lshlrev_b64 v[4:5], 11, v[4:5]
	v_lshl_add_u64 v[4:5], v[12:13], 0, v[4:5]
	s_movk_i32 s22, 0x4000
	v_add_co_u32_e32 v16, vcc, s22, v4
	s_mov_b32 s22, 0x8000
	s_nop 0
	v_addc_co_u32_e32 v17, vcc, 0, v5, vcc
	global_load_dwordx4 v[12:15], v[4:5], off nt
	v_add_co_u32_e32 v20, vcc, s22, v4
	global_load_dwordx4 v[16:19], v[16:17], off nt
	s_nop 0
	v_addc_co_u32_e32 v21, vcc, 0, v5, vcc
	s_mov_b32 s22, 0xc000
	global_load_dwordx4 v[20:23], v[20:21], off nt
	v_add_co_u32_e32 v24, vcc, s22, v4
	s_mov_b32 s22, 0x10000
	s_nop 0
	v_addc_co_u32_e32 v25, vcc, 0, v5, vcc
	global_load_dwordx4 v[24:27], v[24:25], off nt
	v_add_co_u32_e32 v28, vcc, s22, v4
	s_mov_b32 s22, 0x14000
	s_nop 0
	v_addc_co_u32_e32 v29, vcc, 0, v5, vcc
	global_load_dwordx4 v[28:31], v[28:29], off nt
	v_add_co_u32_e32 v32, vcc, s22, v4
	s_lshl_b32 s21, s21, 1
	s_nop 0
	v_addc_co_u32_e32 v33, vcc, 0, v5, vcc
	global_load_dwordx4 v[32:35], v[32:33], off nt
	v_add_co_u32_e32 v36, vcc, s93, v4
	v_add_u32_e32 v11, s6, v1
	s_nop 0
	v_addc_co_u32_e32 v37, vcc, 0, v5, vcc
	global_load_dwordx4 v[36:39], v[36:37], off nt
	v_add_co_u32_e32 v4, vcc, s96, v4
	s_add_u32 s22, s7, s21
	s_nop 0
	v_addc_co_u32_e32 v5, vcc, 0, v5, vcc
	global_load_dwordx4 v[40:43], v[4:5], off nt
	v_add_u32_e32 v4, v10, v3
	v_add_u32_e32 v5, 0x420, v4
	s_movk_i32 s7, 0x80
	s_addc_u32 s23, s20, 0
	v_lshlrev_b32_e32 v96, 1, v2
	s_waitcnt vmcnt(7)
	ds_write2_b32 v4, v12, v13 offset1:1
	ds_write2_b32 v4, v14, v15 offset0:2 offset1:3
	s_waitcnt vmcnt(6)
	ds_write2_b32 v5, v16, v17 offset1:1
	v_add_u32_e32 v5, 0x428, v4
	ds_write2_b32 v5, v18, v19 offset1:1
	v_add_u32_e32 v5, 0x840, v4
	s_waitcnt vmcnt(5)
	ds_write2_b32 v5, v20, v21 offset1:1
	v_add_u32_e32 v5, 0x848, v4
	ds_write2_b32 v5, v22, v23 offset1:1
	v_add_u32_e32 v5, 0xc60, v4
	s_waitcnt vmcnt(4)
	ds_write2_b32 v5, v24, v25 offset1:1
	v_add_u32_e32 v5, 0xc68, v4
	ds_write2_b32 v5, v26, v27 offset1:1
	v_add_u32_e32 v5, 0x1080, v4
	s_waitcnt vmcnt(3)
	ds_write2_b32 v5, v28, v29 offset1:1
	v_add_u32_e32 v5, 0x1088, v4
	ds_write2_b32 v5, v30, v31 offset1:1
	v_add_u32_e32 v5, 0x14a0, v4
	s_waitcnt vmcnt(2)
	ds_write2_b32 v5, v32, v33 offset1:1
	v_add_u32_e32 v5, 0x14a8, v4
	ds_write2_b32 v5, v34, v35 offset1:1
	v_add_u32_e32 v5, 0x18c0, v4
	s_waitcnt vmcnt(1)
	ds_write2_b32 v5, v36, v37 offset1:1
	v_add_u32_e32 v5, 0x18c8, v4
	ds_write2_b32 v5, v38, v39 offset1:1
	v_add_u32_e32 v5, 0x1ce0, v4
	v_add_u32_e32 v4, 0x1ce8, v4
	s_waitcnt vmcnt(0)
	ds_write2_b32 v5, v40, v41 offset1:1
	ds_write2_b32 v4, v42, v43 offset1:1
	s_waitcnt lgkmcnt(0)
	ds_read2_b32 v[214:215], v9 offset1:33
	ds_read2_b32 v[222:223], v9 offset0:66 offset1:99
	ds_read2_b32 v[224:225], v9 offset0:132 offset1:165
	ds_read2_b32 v[226:227], v9 offset0:198 offset1:231
	ds_read2_b32 v[228:229], v9 offset0:8 offset1:41
	ds_read2_b32 v[230:231], v9 offset0:74 offset1:107
	ds_read2_b32 v[232:233], v9 offset0:140 offset1:173
	ds_read2_b32 v[234:235], v9 offset0:206 offset1:239
	s_waitcnt lgkmcnt(0)
	ds_read2_b32 v[236:237], v9 offset0:16 offset1:49
	ds_read2_b32 v[238:239], v9 offset0:82 offset1:115
	ds_read2_b32 v[240:241], v9 offset0:148 offset1:181
	ds_read2_b32 v[242:243], v9 offset0:214 offset1:247
	ds_read2_b32 v[244:245], v9 offset0:24 offset1:57
	ds_read2_b32 v[246:247], v9 offset0:90 offset1:123
	ds_read2_b32 v[248:249], v9 offset0:156 offset1:189
	ds_read2_b32 v[250:251], v9 offset0:222 offset1:255
	v_cvt_pk_bf16_f32 v12, v214, v215
	v_cvt_pk_bf16_f32 v13, v222, v223
	v_cvt_pk_bf16_f32 v14, v224, v225
	v_cvt_pk_bf16_f32 v15, v226, v227
	v_and_b32_e32 v16, 0xffffff80, v11
	v_add3_u32 v16, v11, v16, s7
	v_ashrrev_i32_e32 v17, 31, v16
	v_lshl_add_u64 v[4:5], s[22:23], 0, v[96:97]
	v_lshlrev_b64 v[16:17], 12, v[16:17]
	v_lshl_add_u64 v[16:17], v[4:5], 0, v[16:17]
	global_store_dwordx4 v[16:17], v[12:15], off nt
	s_nop 1
	v_add_u32_e32 v11, s6, v6
	v_cvt_pk_bf16_f32 v12, v228, v229
	v_cvt_pk_bf16_f32 v13, v230, v231
	v_cvt_pk_bf16_f32 v14, v232, v233
	v_cvt_pk_bf16_f32 v15, v234, v235
	v_and_b32_e32 v16, 0xffffff80, v11
	v_add3_u32 v16, v11, v16, s7
	v_ashrrev_i32_e32 v17, 31, v16
	v_lshlrev_b64 v[16:17], 12, v[16:17]
	v_lshl_add_u64 v[16:17], v[4:5], 0, v[16:17]
	global_store_dwordx4 v[16:17], v[12:15], off nt
	s_nop 1
	s_waitcnt lgkmcnt(0)
	v_add_u32_e32 v11, s6, v7
	v_cvt_pk_bf16_f32 v12, v236, v237
	v_cvt_pk_bf16_f32 v13, v238, v239
	v_cvt_pk_bf16_f32 v14, v240, v241
	v_cvt_pk_bf16_f32 v15, v242, v243
	v_and_b32_e32 v16, 0xffffff80, v11
	v_add3_u32 v16, v11, v16, s7
	v_ashrrev_i32_e32 v17, 31, v16
	v_lshlrev_b64 v[16:17], 12, v[16:17]
	v_lshl_add_u64 v[16:17], v[4:5], 0, v[16:17]
	global_store_dwordx4 v[16:17], v[12:15], off nt
	s_nop 1
	v_add_u32_e32 v11, s6, v8
	v_cvt_pk_bf16_f32 v12, v244, v245
	v_cvt_pk_bf16_f32 v13, v246, v247
	v_cvt_pk_bf16_f32 v14, v248, v249
	v_cvt_pk_bf16_f32 v15, v250, v251
	v_and_b32_e32 v16, 0xffffff80, v11
	v_add3_u32 v16, v11, v16, s7
	v_ashrrev_i32_e32 v17, 31, v16
	v_lshlrev_b64 v[16:17], 12, v[16:17]
	v_lshl_add_u64 v[4:5], v[4:5], 0, v[16:17]
	global_store_dwordx4 v[4:5], v[12:15], off nt
	s_nop 1
	s_waitcnt lgkmcnt(0)

; __device__ __forceinline__ unsigned pk2(float lo, float hi) { unsigned r; asm volatile("v_cvt_pk_bf16_f32 %0, %1, %2" : "=v"(r) : "v"(lo), "v"(hi)); return r; }
; __device__ __forceinline__ void transpose_item(const float* W, int K, int N, bf16_t* WT, int rstep, int roff, float* scr, int item, int lane) {
;   const int nblk = N / 32, kb = item / nblk, nb = item % nblk, k0 = 64 * kb, n0 = 32 * nb;
;   f32x4 v[8];
; #pragma unroll
;   for (int i = 0; i < 8; ++i) v[i] = __builtin_nontemporal_load((const f32x4*)(W + (size_t)(k0 + i * 8 + (lane >> 3)) * N + n0 + (lane & 7) * 4));
; #pragma unroll
;   for (int i = 0; i < 8; ++i) { float* d = scr + (i * 8 + (lane >> 3)) * 33 + (lane & 7) * 4; d[0] = v[i].x; d[1] = v[i].y; d[2] = v[i].z; d[3] = v[i].w; }
;   __builtin_amdgcn_wave_barrier(); asm volatile("s_waitcnt lgkmcnt(0)" ::: "memory");
;   const int c = lane & 7;
; #pragma unroll
;   for (int j = 0; j < 4; ++j) { const int nl = (lane >> 3) + 8 * j, n = n0 + nl; const float* s = scr + (8 * c) * 33 + nl;
;     u32x4 o; o.x = pk2(s[0 * 33], s[1 * 33]); o.y = pk2(s[2 * 33], s[3 * 33]); o.z = pk2(s[4 * 33], s[5 * 33]); o.w = pk2(s[6 * 33], s[7 * 33]);
;     const int row = n + (n >> 7) * rstep + roff;
;     __builtin_nontemporal_store(o, (u32x4*)(WT + (size_t)row * K + k0 + 8 * c)); }
;   __builtin_amdgcn_wave_barrier(); asm volatile("s_waitcnt lgkmcnt(0)" ::: "memory");
; }
; __device__ __forceinline__ void convert_item(const P& p, int it, float* scr, int lane) {
;     ...
;     if (which == 0) transpose_item(p.wg + (size_t)le * DM * EFF, DM, EFF, WSP(bf16_t, WS_WGU) + (size_t)le * 1024 * DM, 128, 0, scr, sub, lane);
.LBB0_1056:
	s_andn2_b64 vcc, exec, s[6:7]
	s_cbranch_vccnz .LBB0_1058
	s_add_u32 s20, s60, s19
	s_addc_u32 s21, s61, 0
	s_add_u32 s7, s2, s19
	s_addc_u32 s19, s3, 0
	s_lshl_b32 s6, s12, 2
	s_and_b32 s12, s6, 0x7c0
	s_and_b32 s6, s18, 0x1e0
	s_lshl_b32 s18, s6, 2
	v_add_u32_e32 v4, s12, v1
	s_add_u32 s20, s20, s18
	s_addc_u32 s21, s21, 0
	v_lshlrev_b32_e32 v96, 2, v0
	v_ashrrev_i32_e32 v5, 31, v4
	v_lshl_add_u64 v[12:13], s[20:21], 0, v[96:97]
	v_lshlrev_b64 v[4:5], 11, v[4:5]
	v_lshl_add_u64 v[4:5], v[12:13], 0, v[4:5]
	s_movk_i32 s18, 0x4000
	v_add_co_u32_e32 v16, vcc, s18, v4
	s_mov_b32 s18, 0x8000
	s_nop 0
	v_addc_co_u32_e32 v17, vcc, 0, v5, vcc
	global_load_dwordx4 v[12:15], v[4:5], off nt
	v_add_co_u32_e32 v20, vcc, s18, v4
	global_load_dwordx4 v[16:19], v[16:17], off nt
	s_nop 0
	v_addc_co_u32_e32 v21, vcc, 0, v5, vcc
	s_mov_b32 s18, 0xc000
	global_load_dwordx4 v[20:23], v[20:21], off nt
	v_add_co_u32_e32 v24, vcc, s18, v4
	s_mov_b32 s18, 0x10000
	s_nop 0
	v_addc_co_u32_e32 v25, vcc, 0, v5, vcc
	global_load_dwordx4 v[24:27], v[24:25], off nt
	v_add_co_u32_e32 v28, vcc, s18, v4
	s_mov_b32 s18, 0x14000
	s_nop 0
	v_addc_co_u32_e32 v29, vcc, 0, v5, vcc
	global_load_dwordx4 v[28:31], v[28:29], off nt
	v_add_co_u32_e32 v32, vcc, s18, v4
	v_add_u32_e32 v11, s6, v1
	s_nop 0
	v_addc_co_u32_e32 v33, vcc, 0, v5, vcc
	global_load_dwordx4 v[32:35], v[32:33], off nt
	v_add_co_u32_e32 v36, vcc, s93, v4
	s_lshl_b32 s12, s12, 1
	s_nop 0
	v_addc_co_u32_e32 v37, vcc, 0, v5, vcc
	global_load_dwordx4 v[36:39], v[36:37], off nt
	v_add_co_u32_e32 v4, vcc, s96, v4
	s_add_u32 s18, s7, s12
	s_nop 0
	v_addc_co_u32_e32 v5, vcc, 0, v5, vcc
	global_load_dwordx4 v[40:43], v[4:5], off nt
	v_add_u32_e32 v4, v10, v3
	v_add_u32_e32 v5, 0x420, v4
	s_addc_u32 s19, s19, 0
	v_lshlrev_b32_e32 v96, 1, v2
	s_waitcnt vmcnt(7)
	ds_write2_b32 v4, v12, v13 offset1:1
	ds_write2_b32 v4, v14, v15 offset0:2 offset1:3
	s_waitcnt vmcnt(6)
	ds_write2_b32 v5, v16, v17 offset1:1
	v_add_u32_e32 v5, 0x428, v4
	ds_write2_b32 v5, v18, v19 offset1:1
	v_add_u32_e32 v5, 0x840, v4
	s_waitcnt vmcnt(5)
	ds_write2_b32 v5, v20, v21 offset1:1
	v_add_u32_e32 v5, 0x848, v4
	ds_write2_b32 v5, v22, v23 offset1:1
	v_add_u32_e32 v5, 0xc60, v4
	s_waitcnt vmcnt(4)
	ds_write2_b32 v5, v24, v25 offset1:1
	v_add_u32_e32 v5, 0xc68, v4
	ds_write2_b32 v5, v26, v27 offset1:1
	v_add_u32_e32 v5, 0x1080, v4
	s_waitcnt vmcnt(3)
	ds_write2_b32 v5, v28, v29 offset1:1
	v_add_u32_e32 v5, 0x1088, v4
	ds_write2_b32 v5, v30, v31 offset1:1
	v_add_u32_e32 v5, 0x14a0, v4
	s_waitcnt vmcnt(2)
	ds_write2_b32 v5, v32, v33 offset1:1
	v_add_u32_e32 v5, 0x14a8, v4
	ds_write2_b32 v5, v34, v35 offset1:1
	v_add_u32_e32 v5, 0x18c0, v4
	s_waitcnt vmcnt(1)
	ds_write2_b32 v5, v36, v37 offset1:1
	v_add_u32_e32 v5, 0x18c8, v4
	ds_write2_b32 v5, v38, v39 offset1:1
	v_add_u32_e32 v5, 0x1ce0, v4
	v_add_u32_e32 v4, 0x1ce8, v4
	s_waitcnt vmcnt(0)
	ds_write2_b32 v5, v40, v41 offset1:1
	ds_write2_b32 v4, v42, v43 offset1:1
	s_waitcnt lgkmcnt(0)
	ds_read2_b32 v[214:215], v9 offset1:33
	ds_read2_b32 v[222:223], v9 offset0:66 offset1:99
	ds_read2_b32 v[224:225], v9 offset0:132 offset1:165
	ds_read2_b32 v[226:227], v9 offset0:198 offset1:231
	ds_read2_b32 v[228:229], v9 offset0:8 offset1:41
	ds_read2_b32 v[230:231], v9 offset0:74 offset1:107
	ds_read2_b32 v[232:233], v9 offset0:140 offset1:173
	ds_read2_b32 v[234:235], v9 offset0:206 offset1:239
	s_waitcnt lgkmcnt(0)
	ds_read2_b32 v[236:237], v9 offset0:16 offset1:49
	ds_read2_b32 v[238:239], v9 offset0:82 offset1:115
	ds_read2_b32 v[240:241], v9 offset0:148 offset1:181
	ds_read2_b32 v[242:243], v9 offset0:214 offset1:247
	ds_read2_b32 v[244:245], v9 offset0:24 offset1:57
	ds_read2_b32 v[246:247], v9 offset0:90 offset1:123
	ds_read2_b32 v[248:249], v9 offset0:156 offset1:189
	ds_read2_b32 v[250:251], v9 offset0:222 offset1:255
	v_cvt_pk_bf16_f32 v12, v214, v215
	v_cvt_pk_bf16_f32 v13, v222, v223
	v_cvt_pk_bf16_f32 v14, v224, v225
	v_cvt_pk_bf16_f32 v15, v226, v227
	v_and_b32_e32 v16, 0xffffff80, v11
	v_add_u32_e32 v16, v16, v11
	v_ashrrev_i32_e32 v17, 31, v16
	v_lshl_add_u64 v[4:5], s[18:19], 0, v[96:97]
	v_lshlrev_b64 v[16:17], 12, v[16:17]
	v_lshl_add_u64 v[16:17], v[4:5], 0, v[16:17]
	global_store_dwordx4 v[16:17], v[12:15], off nt
	s_nop 1
	v_add_u32_e32 v11, s6, v6
	v_cvt_pk_bf16_f32 v12, v228, v229
	v_cvt_pk_bf16_f32 v13, v230, v231
	v_cvt_pk_bf16_f32 v14, v232, v233
	v_cvt_pk_bf16_f32 v15, v234, v235
	v_and_b32_e32 v16, 0xffffff80, v11
	v_add_u32_e32 v16, v16, v11
	v_ashrrev_i32_e32 v17, 31, v16
	v_lshlrev_b64 v[16:17], 12, v[16:17]
	v_lshl_add_u64 v[16:17], v[4:5], 0, v[16:17]
	global_store_dwordx4 v[16:17], v[12:15], off nt
	s_nop 1
	s_waitcnt lgkmcnt(0)
	v_add_u32_e32 v11, s6, v7
	v_cvt_pk_bf16_f32 v12, v236, v237
	v_cvt_pk_bf16_f32 v13, v238, v239
	v_cvt_pk_bf16_f32 v14, v240, v241
	v_cvt_pk_bf16_f32 v15, v242, v243
	v_and_b32_e32 v16, 0xffffff80, v11
	v_add_u32_e32 v16, v16, v11
	v_ashrrev_i32_e32 v17, 31, v16
	v_lshlrev_b64 v[16:17], 12, v[16:17]
	v_lshl_add_u64 v[16:17], v[4:5], 0, v[16:17]
	global_store_dwordx4 v[16:17], v[12:15], off nt
	s_nop 1
	v_add_u32_e32 v11, s6, v8
	v_cvt_pk_bf16_f32 v12, v244, v245
	v_cvt_pk_bf16_f32 v13, v246, v247
	v_cvt_pk_bf16_f32 v14, v248, v249
	v_cvt_pk_bf16_f32 v15, v250, v251
	v_and_b32_e32 v16, 0xffffff80, v11
	v_add_u32_e32 v16, v16, v11
	v_ashrrev_i32_e32 v17, 31, v16
	v_lshlrev_b64 v[16:17], 12, v[16:17]
	v_lshl_add_u64 v[4:5], v[4:5], 0, v[16:17]
	global_store_dwordx4 v[4:5], v[12:15], off nt
	s_nop 1
	s_waitcnt lgkmcnt(0)

; __device__ __forceinline__ unsigned pk2(float lo, float hi) { unsigned r; asm volatile("v_cvt_pk_bf16_f32 %0, %1, %2" : "=v"(r) : "v"(lo), "v"(hi)); return r; }
; __device__ __forceinline__ void transpose_item(const float* W, int K, int N, bf16_t* WT, int rstep, int roff, float* scr, int item, int lane) {
;   const int nblk = N / 32, kb = item / nblk, nb = item % nblk, k0 = 64 * kb, n0 = 32 * nb;
;   f32x4 v[8];
; #pragma unroll
;   for (int i = 0; i < 8; ++i) v[i] = __builtin_nontemporal_load((const f32x4*)(W + (size_t)(k0 + i * 8 + (lane >> 3)) * N + n0 + (lane & 7) * 4));
; #pragma unroll
;   for (int i = 0; i < 8; ++i) { float* d = scr + (i * 8 + (lane >> 3)) * 33 + (lane & 7) * 4; d[0] = v[i].x; d[1] = v[i].y; d[2] = v[i].z; d[3] = v[i].w; }
;   __builtin_amdgcn_wave_barrier(); asm volatile("s_waitcnt lgkmcnt(0)" ::: "memory");
;   const int c = lane & 7;
; #pragma unroll
;   for (int j = 0; j < 4; ++j) { const int nl = (lane >> 3) + 8 * j, n = n0 + nl; const float* s = scr + (8 * c) * 33 + nl;
;     u32x4 o; o.x = pk2(s[0 * 33], s[1 * 33]); o.y = pk2(s[2 * 33], s[3 * 33]); o.z = pk2(s[4 * 33], s[5 * 33]); o.w = pk2(s[6 * 33], s[7 * 33]);
;     const int row = n + (n >> 7) * rstep + roff;
;     __builtin_nontemporal_store(o, (u32x4*)(WT + (size_t)row * K + k0 + 8 * c)); }
;   __builtin_amdgcn_wave_barrier(); asm volatile("s_waitcnt lgkmcnt(0)" ::: "memory");
; }
; __device__ __forceinline__ void convert_item(const P& p, int it, float* scr, int lane) {
;   if (it < IT_DENSE) {
;     const int l = it / (IT_WIN + IT_WOUT), r = it % (IT_WIN + IT_WOUT);
;     if (r < IT_WIN) transpose_item(p.w_in + (size_t)l * DM * INW, DM, INW, WSP(bf16_t, WS_WIN) + (size_t)l * INW * DM, 0, 0, scr, r, lane);
;     else transpose_item(p.w_out + (size_t)l * DM * DM, DM, DM, WSP(bf16_t, WS_WOUT) + (size_t)l * DM * DM, 0, 0, scr, r - IT_WIN, lane);
.LBB0_1059:
	s_and_b64 vcc, exec, s[6:7]
	s_cbranch_vccz .LBB0_1048
	s_ashr_i32 s6, s13, 31
	s_lshr_b32 s6, s6, 19
	s_add_i32 s6, s13, s6
	s_ashr_i32 s12, s6, 13
	s_and_b32 s6, s6, 0xffffe000
	s_sub_i32 s18, s13, s6
	s_ashr_i32 s13, s12, 31
	v_add_u32_e32 v11, v10, v3
	s_cmpk_gt_i32 s18, 0x17ff
	s_mov_b64 s[6:7], -1
	v_lshlrev_b32_e32 v96, 2, v0
	v_add_u32_e32 v12, 0x420, v11
	v_add_u32_e32 v13, 0x428, v11
	v_add_u32_e32 v14, 0x840, v11
	v_add_u32_e32 v15, 0x848, v11
	v_add_u32_e32 v16, 0xc60, v11
	v_add_u32_e32 v17, 0xc68, v11
	v_add_u32_e32 v18, 0x1080, v11
	v_add_u32_e32 v19, 0x1088, v11
	v_add_u32_e32 v20, 0x14a0, v11
	v_add_u32_e32 v21, 0x14a8, v11
	v_add_u32_e32 v22, 0x18c0, v11
	v_add_u32_e32 v23, 0x18c8, v11
	v_add_u32_e32 v24, 0x1ce0, v11
	v_add_u32_e32 v25, 0x1ce8, v11
	v_lshlrev_b32_e32 v4, 1, v2
	s_cbranch_scc0 .LBB0_1062
	s_lshl_b64 s[6:7], s[12:13], 24
	s_add_u32 s19, s58, s6
	s_addc_u32 s20, s59, s7
	s_lshl_b64 s[6:7], s[12:13], 23
	s_add_u32 s13, s9, s6
	s_addc_u32 s21, s14, s7
	s_add_i32 s6, s18, 0xe800
	s_and_b32 s22, s6, 0xffc0
	s_lshl_b32 s6, s18, 5
	s_and_b32 s23, s6, 0x7e0
	s_lshl_b32 s6, s23, 2
	v_add_u32_e32 v26, s22, v1
	s_add_u32 s6, s19, s6
	s_addc_u32 s7, s20, 0
	v_ashrrev_i32_e32 v27, 31, v26
	v_lshl_add_u64 v[28:29], s[6:7], 0, v[96:97]
	v_lshlrev_b64 v[26:27], 13, v[26:27]
	v_lshl_add_u64 v[54:55], v[28:29], 0, v[26:27]
	s_mov_b32 s6, 0x10000
	v_add_co_u32_e32 v30, vcc, s6, v54
	s_mov_b32 s6, 0x20000
	s_nop 0
	v_addc_co_u32_e32 v31, vcc, 0, v55, vcc
	v_add_co_u32_e32 v34, vcc, s6, v54
	s_mov_b32 s6, 0x30000
	s_nop 0
	v_addc_co_u32_e32 v35, vcc, 0, v55, vcc
	v_add_co_u32_e32 v38, vcc, s6, v54
	s_mov_b32 s6, 0x40000
	s_nop 0
	v_addc_co_u32_e32 v39, vcc, 0, v55, vcc
	v_add_co_u32_e32 v42, vcc, s6, v54
	s_mov_b32 s6, 0x50000
	s_nop 0
	v_addc_co_u32_e32 v43, vcc, 0, v55, vcc
	v_add_co_u32_e32 v46, vcc, s6, v54
	global_load_dwordx4 v[26:29], v[54:55], off nt
	s_nop 0
	global_load_dwordx4 v[30:33], v[30:31], off nt
	v_addc_co_u32_e32 v47, vcc, 0, v55, vcc
	global_load_dwordx4 v[34:37], v[34:35], off nt
	s_nop 0
	global_load_dwordx4 v[38:41], v[38:39], off nt
	s_nop 0
	global_load_dwordx4 v[42:45], v[42:43], off nt
	s_nop 0
	global_load_dwordx4 v[46:49], v[46:47], off nt
	s_mov_b32 s6, 0x60000
	v_add_co_u32_e32 v50, vcc, s6, v54
	s_mov_b32 s6, 0x70000
	s_nop 0
	v_addc_co_u32_e32 v51, vcc, 0, v55, vcc
	global_load_dwordx4 v[50:53], v[50:51], off nt
	v_add_co_u32_e32 v54, vcc, s6, v54
	s_lshl_b32 s6, s22, 1
	s_nop 0
	v_addc_co_u32_e32 v55, vcc, 0, v55, vcc
	global_load_dwordx4 v[54:57], v[54:55], off nt
	s_add_u32 s6, s13, s6
	v_mov_b32_e32 v5, v97
	s_addc_u32 s7, s21, 0
	s_waitcnt vmcnt(7)
	ds_write2_b32 v11, v26, v27 offset1:1
	ds_write2_b32 v11, v28, v29 offset0:2 offset1:3
	s_waitcnt vmcnt(6)
	ds_write2_b32 v12, v30, v31 offset1:1
	ds_write2_b32 v13, v32, v33 offset1:1
	s_waitcnt vmcnt(5)
	ds_write2_b32 v14, v34, v35 offset1:1
	ds_write2_b32 v15, v36, v37 offset1:1
	s_waitcnt vmcnt(4)
	ds_write2_b32 v16, v38, v39 offset1:1
	ds_write2_b32 v17, v40, v41 offset1:1
	s_waitcnt vmcnt(3)
	ds_write2_b32 v18, v42, v43 offset1:1
	ds_write2_b32 v19, v44, v45 offset1:1
	s_waitcnt vmcnt(2)
	ds_write2_b32 v20, v46, v47 offset1:1
	ds_write2_b32 v21, v48, v49 offset1:1
	s_waitcnt vmcnt(1)
	ds_write2_b32 v22, v50, v51 offset1:1
	ds_write2_b32 v23, v52, v53 offset1:1
	s_waitcnt vmcnt(0)
	ds_write2_b32 v24, v54, v55 offset1:1
	ds_write2_b32 v25, v56, v57 offset1:1
	s_waitcnt lgkmcnt(0)
	ds_read2_b32 v[214:215], v9 offset1:33
	ds_read2_b32 v[222:223], v9 offset0:66 offset1:99
	ds_read2_b32 v[224:225], v9 offset0:132 offset1:165
	ds_read2_b32 v[226:227], v9 offset0:198 offset1:231
	ds_read2_b32 v[228:229], v9 offset0:8 offset1:41
	ds_read2_b32 v[230:231], v9 offset0:74 offset1:107
	ds_read2_b32 v[232:233], v9 offset0:140 offset1:173
	ds_read2_b32 v[234:235], v9 offset0:206 offset1:239
	s_waitcnt lgkmcnt(0)
	ds_read2_b32 v[236:237], v9 offset0:16 offset1:49
	ds_read2_b32 v[238:239], v9 offset0:82 offset1:115
	ds_read2_b32 v[240:241], v9 offset0:148 offset1:181
	ds_read2_b32 v[242:243], v9 offset0:214 offset1:247
	ds_read2_b32 v[244:245], v9 offset0:24 offset1:57
	ds_read2_b32 v[246:247], v9 offset0:90 offset1:123
	ds_read2_b32 v[248:249], v9 offset0:156 offset1:189
	ds_read2_b32 v[250:251], v9 offset0:222 offset1:255
	v_cvt_pk_bf16_f32 v26, v214, v215
	v_add_u32_e32 v30, s23, v1
	v_cvt_pk_bf16_f32 v27, v222, v223
	v_ashrrev_i32_e32 v31, 31, v30
	v_cvt_pk_bf16_f32 v28, v224, v225
	v_lshlrev_b64 v[30:31], 12, v[30:31]
	v_lshl_add_u64 v[34:35], s[6:7], 0, v[4:5]
	v_cvt_pk_bf16_f32 v29, v226, v227
	v_lshl_add_u64 v[30:31], v[34:35], 0, v[30:31]
	global_store_dwordx4 v[30:31], v[26:29], off nt
	s_nop 1
	s_mov_b64 s[6:7], 0
	v_cvt_pk_bf16_f32 v26, v228, v229
	v_add_u32_e32 v32, s23, v6
	v_ashrrev_i32_e32 v33, 31, v32
	v_lshlrev_b64 v[32:33], 12, v[32:33]
	v_cvt_pk_bf16_f32 v27, v230, v231
	v_lshl_add_u64 v[32:33], v[34:35], 0, v[32:33]
	v_cvt_pk_bf16_f32 v28, v232, v233
	v_cvt_pk_bf16_f32 v29, v234, v235
	global_store_dwordx4 v[32:33], v[26:29], off nt
	s_nop 1
	v_add_u32_e32 v32, s23, v7
	v_ashrrev_i32_e32 v33, 31, v32
	s_waitcnt lgkmcnt(0)
	v_cvt_pk_bf16_f32 v26, v236, v237
	v_lshlrev_b64 v[32:33], 12, v[32:33]
	v_cvt_pk_bf16_f32 v27, v238, v239
	v_lshl_add_u64 v[32:33], v[34:35], 0, v[32:33]
	v_cvt_pk_bf16_f32 v28, v240, v241
	v_cvt_pk_bf16_f32 v29, v242, v243
	global_store_dwordx4 v[32:33], v[26:29], off nt
	s_nop 1
	v_add_u32_e32 v32, s23, v8
	v_ashrrev_i32_e32 v33, 31, v32
	v_cvt_pk_bf16_f32 v26, v244, v245
	v_lshlrev_b64 v[32:33], 12, v[32:33]
	v_cvt_pk_bf16_f32 v27, v246, v247
	v_lshl_add_u64 v[32:33], v[34:35], 0, v[32:33]
	v_cvt_pk_bf16_f32 v28, v248, v249
	v_cvt_pk_bf16_f32 v29, v250, v251
	global_store_dwordx4 v[32:33], v[26:29], off nt
	s_nop 1
	s_waitcnt lgkmcnt(0)
; __device__ __forceinline__ unsigned pk2(float lo, float hi) { unsigned r; asm volatile("v_cvt_pk_bf16_f32 %0, %1, %2" : "=v"(r) : "v"(lo), "v"(hi)); return r; }
; __device__ __forceinline__ void transpose_item(const float* W, int K, int N, bf16_t* WT, int rstep, int roff, float* scr, int item, int lane) {
;   const int nblk = N / 32, kb = item / nblk, nb = item % nblk, k0 = 64 * kb, n0 = 32 * nb;
;   f32x4 v[8];
; #pragma unroll
;   for (int i = 0; i < 8; ++i) v[i] = __builtin_nontemporal_load((const f32x4*)(W + (size_t)(k0 + i * 8 + (lane >> 3)) * N + n0 + (lane & 7) * 4));
; #pragma unroll
;   for (int i = 0; i < 8; ++i) { float* d = scr + (i * 8 + (lane >> 3)) * 33 + (lane & 7) * 4; d[0] = v[i].x; d[1] = v[i].y; d[2] = v[i].z; d[3] = v[i].w; }
;   __builtin_amdgcn_wave_barrier(); asm volatile("s_waitcnt lgkmcnt(0)" ::: "memory");
;   const int c = lane & 7;
; #pragma unroll
;   for (int j = 0; j < 4; ++j) { const int nl = (lane >> 3) + 8 * j, n = n0 + nl; const float* s = scr + (8 * c) * 33 + nl;
;     u32x4 o; o.x = pk2(s[0 * 33], s[1 * 33]); o.y = pk2(s[2 * 33], s[3 * 33]); o.z = pk2(s[4 * 33], s[5 * 33]); o.w = pk2(s[6 * 33], s[7 * 33]);
;     const int row = n + (n >> 7) * rstep + roff;
;     __builtin_nontemporal_store(o, (u32x4*)(WT + (size_t)row * K + k0 + 8 * c)); }
;   __builtin_amdgcn_wave_barrier(); asm volatile("s_waitcnt lgkmcnt(0)" ::: "memory");
; }
; __device__ __forceinline__ void convert_item(const P& p, int it, float* scr, int lane) {
;     ...
;     if (r < IT_WIN) transpose_item(p.w_in + (size_t)l * DM * INW, DM, INW, WSP(bf16_t, WS_WIN) + (size_t)l * INW * DM, 0, 0, scr, r, lane);
.LBB0_1062:
	s_andn2_b64 vcc, exec, s[6:7]
	s_cbranch_vccnz .LBB0_1048
	s_mul_i32 s7, s12, 0x3000000
	s_mul_hi_i32 s6, s12, 0x3000000
	s_add_u32 s7, s56, s7
	s_addc_u32 s20, s57, s6
	s_mul_hi_i32 s6, s12, 0x1800000
	s_mul_i32 s12, s12, 0x1800000
	s_add_u32 s21, s15, s12
	s_addc_u32 s22, s16, s6
	s_mul_i32 s6, s18, 0x2aab
	s_lshr_b32 s12, s6, 31
	s_ashr_i32 s6, s6, 21
	s_add_i32 s6, s6, s12
	s_sext_i32_i16 s12, s6
	s_mulk_i32 s6, 0xc0
	s_sub_i32 s6, s18, s6
	s_sext_i32_i16 s13, s6
	s_lshl_b32 s6, s12, 6
	s_lshl_b32 s12, s13, 5
	s_ashr_i32 s13, s12, 31
	s_lshl_b64 s[18:19], s[12:13], 2
	s_add_u32 s18, s7, s18
	v_add_u32_e32 v5, s6, v1
	s_addc_u32 s19, s20, s19
	v_lshl_add_u64 v[54:55], s[18:19], 0, v[96:97]
	s_movk_i32 s7, 0x6000
	v_add_u32_e32 v28, 8, v5
	v_add_u32_e32 v34, 16, v5
	v_add_u32_e32 v36, 24, v5
	v_add_u32_e32 v42, 32, v5
	v_add_u32_e32 v44, 40, v5
	v_mad_i64_i32 v[26:27], s[18:19], v5, s7, v[54:55]
	v_mad_i64_i32 v[30:31], s[18:19], v28, s7, v[54:55]
	v_mad_i64_i32 v[34:35], s[18:19], v34, s7, v[54:55]
	v_mad_i64_i32 v[38:39], s[18:19], v36, s7, v[54:55]
	v_mad_i64_i32 v[42:43], s[18:19], v42, s7, v[54:55]
	v_mad_i64_i32 v[46:47], s[18:19], v44, s7, v[54:55]
	global_load_dwordx4 v[26:29], v[26:27], off nt
	s_nop 0
	global_load_dwordx4 v[30:33], v[30:31], off nt
	s_nop 0
	global_load_dwordx4 v[34:37], v[34:35], off nt
	s_nop 0
	global_load_dwordx4 v[38:41], v[38:39], off nt
	s_nop 0
	global_load_dwordx4 v[42:45], v[42:43], off nt
	s_nop 0
	global_load_dwordx4 v[46:49], v[46:47], off nt
	v_add_u32_e32 v50, 48, v5
	v_mad_i64_i32 v[50:51], s[18:19], v50, s7, v[54:55]
	global_load_dwordx4 v[50:53], v[50:51], off nt
	v_add_u32_e32 v5, 56, v5
	v_mad_i64_i32 v[54:55], s[18:19], v5, s7, v[54:55]
	global_load_dwordx4 v[54:57], v[54:55], off nt
	s_ashr_i32 s7, s6, 31
	s_lshl_b64 s[6:7], s[6:7], 1
	s_add_u32 s6, s21, s6
	v_mov_b32_e32 v5, v97
	s_addc_u32 s7, s22, s7
	v_lshl_add_u64 v[4:5], s[6:7], 0, v[4:5]
	s_movk_i32 s82, 0x6000
	s_waitcnt vmcnt(7)
	ds_write2_b32 v11, v26, v27 offset1:1
	ds_write2_b32 v11, v28, v29 offset0:2 offset1:3
	s_waitcnt vmcnt(6)
	ds_write2_b32 v12, v30, v31 offset1:1
	ds_write2_b32 v13, v32, v33 offset1:1
	s_waitcnt vmcnt(5)
	ds_write2_b32 v14, v34, v35 offset1:1
	ds_write2_b32 v15, v36, v37 offset1:1
	s_waitcnt vmcnt(4)
	ds_write2_b32 v16, v38, v39 offset1:1
	ds_write2_b32 v17, v40, v41 offset1:1
	s_waitcnt vmcnt(3)
	ds_write2_b32 v18, v42, v43 offset1:1
	ds_write2_b32 v19, v44, v45 offset1:1
	s_waitcnt vmcnt(2)
	ds_write2_b32 v20, v46, v47 offset1:1
	ds_write2_b32 v21, v48, v49 offset1:1
	s_waitcnt vmcnt(1)
	ds_write2_b32 v22, v50, v51 offset1:1
	ds_write2_b32 v23, v52, v53 offset1:1
	s_waitcnt vmcnt(0)
	ds_write2_b32 v24, v54, v55 offset1:1
	ds_write2_b32 v25, v56, v57 offset1:1
	s_waitcnt lgkmcnt(0)
	ds_read2_b32 v[214:215], v9 offset1:33
	ds_read2_b32 v[222:223], v9 offset0:66 offset1:99
	ds_read2_b32 v[224:225], v9 offset0:132 offset1:165
	ds_read2_b32 v[226:227], v9 offset0:198 offset1:231
	ds_read2_b32 v[228:229], v9 offset0:8 offset1:41
	ds_read2_b32 v[230:231], v9 offset0:74 offset1:107
	ds_read2_b32 v[232:233], v9 offset0:140 offset1:173
	ds_read2_b32 v[234:235], v9 offset0:206 offset1:239
	s_waitcnt lgkmcnt(0)
	ds_read2_b32 v[236:237], v9 offset0:16 offset1:49
	ds_read2_b32 v[238:239], v9 offset0:82 offset1:115
	ds_read2_b32 v[240:241], v9 offset0:148 offset1:181
	ds_read2_b32 v[242:243], v9 offset0:214 offset1:247
	ds_read2_b32 v[244:245], v9 offset0:24 offset1:57
	ds_read2_b32 v[246:247], v9 offset0:90 offset1:123
	ds_read2_b32 v[248:249], v9 offset0:156 offset1:189
	ds_read2_b32 v[250:251], v9 offset0:222 offset1:255
	v_cvt_pk_bf16_f32 v12, v214, v215
	v_add_u32_e32 v16, s12, v1
	v_cvt_pk_bf16_f32 v13, v222, v223
	v_ashrrev_i32_e32 v17, 31, v16
	v_cvt_pk_bf16_f32 v14, v224, v225
	v_lshlrev_b64 v[16:17], 12, v[16:17]
	v_cvt_pk_bf16_f32 v15, v226, v227
	v_lshl_add_u64 v[16:17], v[4:5], 0, v[16:17]
	global_store_dwordx4 v[16:17], v[12:15], off nt
	s_nop 1
	s_nop 0
	v_cvt_pk_bf16_f32 v12, v228, v229
	v_add_u32_e32 v18, s12, v6
	v_ashrrev_i32_e32 v19, 31, v18
	v_lshlrev_b64 v[18:19], 12, v[18:19]
	v_cvt_pk_bf16_f32 v13, v230, v231
	v_lshl_add_u64 v[18:19], v[4:5], 0, v[18:19]
	v_cvt_pk_bf16_f32 v14, v232, v233
	v_cvt_pk_bf16_f32 v15, v234, v235
	global_store_dwordx4 v[18:19], v[12:15], off nt
	s_nop 1
	v_add_u32_e32 v18, s12, v7
	v_ashrrev_i32_e32 v19, 31, v18
	s_waitcnt lgkmcnt(0)
	v_cvt_pk_bf16_f32 v12, v236, v237
	v_lshlrev_b64 v[18:19], 12, v[18:19]
	v_cvt_pk_bf16_f32 v13, v238, v239
	v_lshl_add_u64 v[18:19], v[4:5], 0, v[18:19]
	v_cvt_pk_bf16_f32 v14, v240, v241
	v_cvt_pk_bf16_f32 v15, v242, v243
	global_store_dwordx4 v[18:19], v[12:15], off nt
	s_nop 1
	v_add_u32_e32 v18, s12, v8
	v_ashrrev_i32_e32 v19, 31, v18
	v_cvt_pk_bf16_f32 v12, v244, v245
	v_lshlrev_b64 v[18:19], 12, v[18:19]
	v_cvt_pk_bf16_f32 v13, v246, v247
	v_lshl_add_u64 v[4:5], v[4:5], 0, v[18:19]
	v_cvt_pk_bf16_f32 v14, v248, v249
	v_cvt_pk_bf16_f32 v15, v250, v251
	global_store_dwordx4 v[4:5], v[12:15], off nt
	s_nop 1
	s_waitcnt lgkmcnt(0)
	s_branch .LBB0_1048

; __device__ __forceinline__ void transpose_item(const float* W, int K, int N, bf16_t* WT, int rstep, int roff, float* scr, int item, int lane) {
;   const int nblk = N / 32, kb = item / nblk, nb = item % nblk, k0 = 64 * kb, n0 = 32 * nb;
;   f32x4 v[8];
; #pragma unroll
;   for (int i = 0; i < 8; ++i) v[i] = __builtin_nontemporal_load((const f32x4*)(W + (size_t)(k0 + i * 8 + (lane >> 3)) * N + n0 + (lane & 7) * 4));
; #pragma unroll
;   for (int i = 0; i < 8; ++i) { float* d = scr + (i * 8 + (lane >> 3)) * 33 + (lane & 7) * 4; d[0] = v[i].x; d[1] = v[i].y; d[2] = v[i].z; d[3] = v[i].w; }
;   __builtin_amdgcn_wave_barrier(); asm volatile("s_waitcnt lgkmcnt(0)" ::: "memory");
;   const int c = lane & 7;
; #pragma unroll
;   for (int j = 0; j < 4; ++j) { const int nl = (lane >> 3) + 8 * j, n = n0 + nl; const float* s = scr + (8 * c) * 33 + nl;
;     u32x4 o; o.x = pk2(s[0 * 33], s[1 * 33]); o.y = pk2(s[2 * 33], s[3 * 33]); o.z = pk2(s[4 * 33], s[5 * 33]); o.w = pk2(s[6 * 33], s[7 * 33]);
;     const int row = n + (n >> 7) * rstep + roff;
;     __builtin_nontemporal_store(o, (u32x4*)(WT + (size_t)row * K + k0 + 8 * c)); }
;   __builtin_amdgcn_wave_barrier(); asm volatile("s_waitcnt lgkmcnt(0)" ::: "memory");
; }
; __device__ __forceinline__ void convert_item(const P& p, int it, float* scr, int lane) {
;   if (it < IT_DENSE) {
;     const int l = it / (IT_WIN + IT_WOUT), r = it % (IT_WIN + IT_WOUT);
;     if (r < IT_WIN) transpose_item(p.w_in + (size_t)l * DM * INW, DM, INW, WSP(bf16_t, WS_WIN) + (size_t)l * INW * DM, 0, 0, scr, r, lane);
;     else transpose_item(p.w_out + (size_t)l * DM * DM, DM, DM, WSP(bf16_t, WS_WOUT) + (size_t)l * DM * DM, 0, 0, scr, r - IT_WIN, lane);
;   } else {
;     const int idx = it - IT_DENSE, m = idx / IT_EXP, sub = idx % IT_EXP, le = m / 3, which = m % 3;
;     if (which == 0) transpose_item(p.wg + (size_t)le * DM * EFF, DM, EFF, WSP(bf16_t, WS_WGU) + (size_t)le * 1024 * DM, 128, 0, scr, sub, lane);
;     else if (which == 1) transpose_item(p.wu + (size_t)le * DM * EFF, DM, EFF, WSP(bf16_t, WS_WGU) + (size_t)le * 1024 * DM, 128, 128, scr, sub, lane);
;     else transpose_item(p.wd + (size_t)le * EFF * DM, EFF, DM, WSP(bf16_t, WS_WD) + (size_t)le * DM * EFF, 0, 0, scr, sub, lane);
.LBB0_1175:
	s_cmpk_gt_i32 s22, 0x3fff
	s_mov_b64 s[6:7], -1
	s_cbranch_scc0 .LBB0_1185
	s_add_i32 s6, s22, 0xffffc000
	s_lshr_b32 s7, s6, 9
	s_mul_hi_u32 s6, s6, 0xaaaaaaab
	s_lshr_b32 s64, s6, 10
	s_mul_i32 s6, s7, 0xab
	s_bfe_u32 s6, s6, 0x70009
	s_mul_i32 s6, s6, 3
	s_sub_i32 s6, s7, s6
	s_and_b32 s23, s22, 0x1ff
	s_lshl_b64 s[14:15], s[64:65], 22
	s_lshl_b32 s24, s22, 5
	s_and_b32 s30, s6, 0xff
	s_cmp_lt_i32 s30, 1
	s_mov_b64 s[6:7], -1
	s_cbranch_scc1 .LBB0_1182
	s_and_b32 s6, 0xffff, s30
	s_cmp_lg_u32 s6, 1
	s_mov_b64 s[6:7], -1
	s_cbranch_scc0 .LBB0_1179
	s_waitcnt lgkmcnt(0)
	s_add_u32 s34, s0, s14
	s_addc_u32 s35, s1, s15
	s_lshl_b64 s[30:31], s[64:65], 21
	s_add_u32 s7, s3, s30
	s_addc_u32 s30, s5, s31
	s_and_b32 s6, s24, 0x7e0
	s_and_b32 s31, s22, 0x1c0
	s_lshl_b32 s38, s6, 2
	v_add_u32_e32 v4, s31, v1
	s_add_u32 s34, s34, s38
	s_addc_u32 s35, s35, 0
	v_lshlrev_b32_e32 v96, 2, v0
	v_ashrrev_i32_e32 v5, 31, v4
	v_lshl_add_u64 v[12:13], s[34:35], 0, v[96:97]
	v_lshlrev_b64 v[4:5], 13, v[4:5]
	v_lshl_add_u64 v[4:5], v[12:13], 0, v[4:5]
	s_mov_b32 s34, 0x10000
	v_add_co_u32_e32 v16, vcc, s34, v4
	s_mov_b32 s34, 0x20000
	s_nop 0
	v_addc_co_u32_e32 v17, vcc, 0, v5, vcc
	global_load_dwordx4 v[12:15], v[4:5], off nt
	v_add_co_u32_e32 v20, vcc, s34, v4
	global_load_dwordx4 v[16:19], v[16:17], off nt
	s_nop 0
	v_addc_co_u32_e32 v21, vcc, 0, v5, vcc
	s_mov_b32 s34, 0x30000
	global_load_dwordx4 v[20:23], v[20:21], off nt
	v_add_co_u32_e32 v24, vcc, s34, v4
	s_mov_b32 s34, 0x40000
	s_nop 0
	v_addc_co_u32_e32 v25, vcc, 0, v5, vcc
	global_load_dwordx4 v[24:27], v[24:25], off nt
	v_add_co_u32_e32 v28, vcc, s34, v4
	s_mov_b32 s34, 0x50000
	s_nop 0
	v_addc_co_u32_e32 v29, vcc, 0, v5, vcc
	global_load_dwordx4 v[28:31], v[28:29], off nt
	v_add_co_u32_e32 v32, vcc, s34, v4
	s_mov_b32 s34, 0x60000
	s_nop 0
	v_addc_co_u32_e32 v33, vcc, 0, v5, vcc
	global_load_dwordx4 v[32:35], v[32:33], off nt
	v_add_co_u32_e32 v36, vcc, s34, v4
	s_mov_b32 s34, 0x70000
	s_nop 0
	v_addc_co_u32_e32 v37, vcc, 0, v5, vcc
	global_load_dwordx4 v[36:39], v[36:37], off nt
	v_add_co_u32_e32 v4, vcc, s34, v4
	s_lshl_b32 s31, s31, 1
	s_nop 0
	v_addc_co_u32_e32 v5, vcc, 0, v5, vcc
	global_load_dwordx4 v[40:43], v[4:5], off nt
	v_add_u32_e32 v4, v3, v6
	v_add_u32_e32 v5, 0x420, v4
	s_add_u32 s34, s7, s31
	s_addc_u32 s35, s30, 0
	v_lshlrev_b32_e32 v96, 1, v2
	s_waitcnt vmcnt(0)
	ds_write2_b32 v4, v12, v13 offset1:1
	ds_write2_b32 v4, v14, v15 offset0:2 offset1:3
	ds_write2_b32 v5, v16, v17 offset1:1
	v_add_u32_e32 v5, 0x428, v4
	ds_write2_b32 v5, v18, v19 offset1:1
	v_add_u32_e32 v5, 0x840, v4
	ds_write2_b32 v5, v20, v21 offset1:1
	v_add_u32_e32 v5, 0x848, v4
	ds_write2_b32 v5, v22, v23 offset1:1
	v_add_u32_e32 v5, 0xc60, v4
	v_add_u32_e32 v16, s6, v1
	v_ashrrev_i32_e32 v17, 31, v16
	ds_write2_b32 v5, v24, v25 offset1:1
	v_add_u32_e32 v5, 0xc68, v4
	ds_write2_b32 v5, v26, v27 offset1:1
	v_add_u32_e32 v5, 0x1080, v4
	v_lshlrev_b64 v[16:17], 10, v[16:17]
	ds_write2_b32 v5, v28, v29 offset1:1
	v_add_u32_e32 v5, 0x1088, v4
	ds_write2_b32 v5, v30, v31 offset1:1
	v_add_u32_e32 v5, 0x14a0, v4
	ds_write2_b32 v5, v32, v33 offset1:1
	v_add_u32_e32 v5, 0x14a8, v4
	ds_write2_b32 v5, v34, v35 offset1:1
	v_add_u32_e32 v5, 0x18c0, v4
	ds_write2_b32 v5, v36, v37 offset1:1
	v_add_u32_e32 v5, 0x18c8, v4
	ds_write2_b32 v5, v38, v39 offset1:1
	v_add_u32_e32 v5, 0x1ce0, v4
	v_add_u32_e32 v4, 0x1ce8, v4
	ds_write2_b32 v5, v40, v41 offset1:1
	ds_write2_b32 v4, v42, v43 offset1:1
	s_waitcnt lgkmcnt(0)
	ds_read2_b32 v[214:215], v10 offset1:33
	ds_read2_b32 v[222:223], v10 offset0:66 offset1:99
	ds_read2_b32 v[224:225], v10 offset0:132 offset1:165
	ds_read2_b32 v[226:227], v10 offset0:198 offset1:231
	ds_read2_b32 v[228:229], v10 offset0:8 offset1:41
	ds_read2_b32 v[230:231], v10 offset0:74 offset1:107
	ds_read2_b32 v[232:233], v10 offset0:140 offset1:173
	ds_read2_b32 v[234:235], v10 offset0:206 offset1:239
	s_waitcnt lgkmcnt(0)
	ds_read2_b32 v[236:237], v10 offset0:16 offset1:49
	ds_read2_b32 v[238:239], v10 offset0:82 offset1:115
	ds_read2_b32 v[240:241], v10 offset0:148 offset1:181
	ds_read2_b32 v[242:243], v10 offset0:214 offset1:247
	ds_read2_b32 v[244:245], v10 offset0:24 offset1:57
	ds_read2_b32 v[246:247], v10 offset0:90 offset1:123
	ds_read2_b32 v[248:249], v10 offset0:156 offset1:189
	ds_read2_b32 v[250:251], v10 offset0:222 offset1:255
	v_lshl_add_u64 v[4:5], s[34:35], 0, v[96:97]
	v_cvt_pk_bf16_f32 v12, v214, v215
	v_cvt_pk_bf16_f32 v13, v222, v223
	v_lshl_add_u64 v[16:17], v[4:5], 0, v[16:17]
	v_cvt_pk_bf16_f32 v14, v224, v225
	v_cvt_pk_bf16_f32 v15, v226, v227
	global_store_dwordx4 v[16:17], v[12:15], off nt
	s_nop 1
	v_add_u32_e32 v16, s6, v7
	v_ashrrev_i32_e32 v17, 31, v16
	v_cvt_pk_bf16_f32 v12, v228, v229
	v_lshlrev_b64 v[16:17], 10, v[16:17]
	v_cvt_pk_bf16_f32 v13, v230, v231
	v_lshl_add_u64 v[16:17], v[4:5], 0, v[16:17]
	v_cvt_pk_bf16_f32 v14, v232, v233
	v_cvt_pk_bf16_f32 v15, v234, v235
	global_store_dwordx4 v[16:17], v[12:15], off nt
	s_nop 1
	v_add_u32_e32 v16, s6, v8
	s_waitcnt lgkmcnt(0)
	v_ashrrev_i32_e32 v17, 31, v16
	v_cvt_pk_bf16_f32 v12, v236, v237
	v_lshlrev_b64 v[16:17], 10, v[16:17]
	v_cvt_pk_bf16_f32 v13, v238, v239
	v_lshl_add_u64 v[16:17], v[4:5], 0, v[16:17]
	v_cvt_pk_bf16_f32 v14, v240, v241
	v_cvt_pk_bf16_f32 v15, v242, v243
	global_store_dwordx4 v[16:17], v[12:15], off nt
	s_nop 1
	v_add_u32_e32 v16, s6, v9
	v_ashrrev_i32_e32 v17, 31, v16
	v_cvt_pk_bf16_f32 v12, v244, v245
	v_lshlrev_b64 v[16:17], 10, v[16:17]
	v_cvt_pk_bf16_f32 v13, v246, v247
	v_lshl_add_u64 v[4:5], v[4:5], 0, v[16:17]
	v_cvt_pk_bf16_f32 v14, v248, v249
	v_cvt_pk_bf16_f32 v15, v250, v251
	global_store_dwordx4 v[4:5], v[12:15], off nt
	s_nop 1
	s_waitcnt lgkmcnt(0)
	s_mov_b64 s[6:7], 0
; __device__ __forceinline__ unsigned pk2(float lo, float hi) { unsigned r; asm volatile("v_cvt_pk_bf16_f32 %0, %1, %2" : "=v"(r) : "v"(lo), "v"(hi)); return r; }
; __device__ __forceinline__ void transpose_item(const float* W, int K, int N, bf16_t* WT, int rstep, int roff, float* scr, int item, int lane) {
;   const int nblk = N / 32, kb = item / nblk, nb = item % nblk, k0 = 64 * kb, n0 = 32 * nb;
;   f32x4 v[8];
; #pragma unroll
;   for (int i = 0; i < 8; ++i) v[i] = __builtin_nontemporal_load((const f32x4*)(W + (size_t)(k0 + i * 8 + (lane >> 3)) * N + n0 + (lane & 7) * 4));
; #pragma unroll
;   for (int i = 0; i < 8; ++i) { float* d = scr + (i * 8 + (lane >> 3)) * 33 + (lane & 7) * 4; d[0] = v[i].x; d[1] = v[i].y; d[2] = v[i].z; d[3] = v[i].w; }
;   __builtin_amdgcn_wave_barrier(); asm volatile("s_waitcnt lgkmcnt(0)" ::: "memory");
;   const int c = lane & 7;
; #pragma unroll
;   for (int j = 0; j < 4; ++j) { const int nl = (lane >> 3) + 8 * j, n = n0 + nl; const float* s = scr + (8 * c) * 33 + nl;
;     u32x4 o; o.x = pk2(s[0 * 33], s[1 * 33]); o.y = pk2(s[2 * 33], s[3 * 33]); o.z = pk2(s[4 * 33], s[5 * 33]); o.w = pk2(s[6 * 33], s[7 * 33]);
;     const int row = n + (n >> 7) * rstep + roff;
;     __builtin_nontemporal_store(o, (u32x4*)(WT + (size_t)row * K + k0 + 8 * c)); }
;   __builtin_amdgcn_wave_barrier(); asm volatile("s_waitcnt lgkmcnt(0)" ::: "memory");
; }
; __device__ __forceinline__ void convert_item(const P& p, int it, float* scr, int lane) {
;     ...
;     else if (which == 1) transpose_item(p.wu + (size_t)le * DM * EFF, DM, EFF, WSP(bf16_t, WS_WGU) + (size_t)le * 1024 * DM, 128, 128, scr, sub, lane);
.LBB0_1179:
	s_andn2_b64 vcc, exec, s[6:7]
	s_cbranch_vccnz .LBB0_1181
	s_waitcnt lgkmcnt(0)
	s_add_u32 s34, s50, s14
	s_addc_u32 s35, s51, s15
	s_add_u32 s7, s70, s14
	s_addc_u32 s30, s71, s15
	s_lshl_b32 s6, s23, 2
	s_and_b32 s31, s6, 0x7c0
	s_and_b32 s6, s24, 0x1e0
	s_lshl_b32 s38, s6, 2
	v_add_u32_e32 v4, s31, v1
	s_add_u32 s34, s34, s38
	s_addc_u32 s35, s35, 0
	v_lshlrev_b32_e32 v96, 2, v0
	v_ashrrev_i32_e32 v5, 31, v4
	v_lshl_add_u64 v[12:13], s[34:35], 0, v[96:97]
	v_lshlrev_b64 v[4:5], 11, v[4:5]
	v_lshl_add_u64 v[4:5], v[12:13], 0, v[4:5]
	s_movk_i32 s34, 0x4000
	v_add_co_u32_e32 v16, vcc, s34, v4
	s_mov_b32 s34, 0x8000
	s_nop 0
	v_addc_co_u32_e32 v17, vcc, 0, v5, vcc
	global_load_dwordx4 v[12:15], v[4:5], off nt
	v_add_co_u32_e32 v20, vcc, s34, v4
	global_load_dwordx4 v[16:19], v[16:17], off nt
	s_nop 0
	v_addc_co_u32_e32 v21, vcc, 0, v5, vcc
	s_mov_b32 s34, 0xc000
	global_load_dwordx4 v[20:23], v[20:21], off nt
	v_add_co_u32_e32 v24, vcc, s34, v4
	s_mov_b32 s34, 0x10000
	s_nop 0
	v_addc_co_u32_e32 v25, vcc, 0, v5, vcc
	global_load_dwordx4 v[24:27], v[24:25], off nt
	v_add_co_u32_e32 v28, vcc, s34, v4
	s_mov_b32 s34, 0x14000
	s_nop 0
	v_addc_co_u32_e32 v29, vcc, 0, v5, vcc
	global_load_dwordx4 v[28:31], v[28:29], off nt
	v_add_co_u32_e32 v32, vcc, s34, v4
	s_lshl_b32 s31, s31, 1
	s_nop 0
	v_addc_co_u32_e32 v33, vcc, 0, v5, vcc
	global_load_dwordx4 v[32:35], v[32:33], off nt
	v_add_co_u32_e32 v36, vcc, s93, v4
	v_add_u32_e32 v11, s6, v1
	s_nop 0
	v_addc_co_u32_e32 v37, vcc, 0, v5, vcc
	global_load_dwordx4 v[36:39], v[36:37], off nt
	v_add_co_u32_e32 v4, vcc, s96, v4
	s_add_u32 s34, s7, s31
	s_nop 0
	v_addc_co_u32_e32 v5, vcc, 0, v5, vcc
	global_load_dwordx4 v[40:43], v[4:5], off nt
	v_add_u32_e32 v4, v3, v6
	v_add_u32_e32 v5, 0x420, v4
	s_movk_i32 s7, 0x80
	s_addc_u32 s35, s30, 0
	v_lshlrev_b32_e32 v96, 1, v2
	s_waitcnt vmcnt(0)
	ds_write2_b32 v4, v12, v13 offset1:1
	ds_write2_b32 v4, v14, v15 offset0:2 offset1:3
	ds_write2_b32 v5, v16, v17 offset1:1
	v_add_u32_e32 v5, 0x428, v4
	ds_write2_b32 v5, v18, v19 offset1:1
	v_add_u32_e32 v5, 0x840, v4
	ds_write2_b32 v5, v20, v21 offset1:1
	v_add_u32_e32 v5, 0x848, v4
	ds_write2_b32 v5, v22, v23 offset1:1
	v_add_u32_e32 v5, 0xc60, v4
	ds_write2_b32 v5, v24, v25 offset1:1
	v_add_u32_e32 v5, 0xc68, v4
	ds_write2_b32 v5, v26, v27 offset1:1
	v_add_u32_e32 v5, 0x1080, v4
	ds_write2_b32 v5, v28, v29 offset1:1
	v_add_u32_e32 v5, 0x1088, v4
	ds_write2_b32 v5, v30, v31 offset1:1
	v_add_u32_e32 v5, 0x14a0, v4
	ds_write2_b32 v5, v32, v33 offset1:1
	v_add_u32_e32 v5, 0x14a8, v4
	ds_write2_b32 v5, v34, v35 offset1:1
	v_add_u32_e32 v5, 0x18c0, v4
	ds_write2_b32 v5, v36, v37 offset1:1
	v_add_u32_e32 v5, 0x18c8, v4
	ds_write2_b32 v5, v38, v39 offset1:1
	v_add_u32_e32 v5, 0x1ce0, v4
	v_add_u32_e32 v4, 0x1ce8, v4
	ds_write2_b32 v5, v40, v41 offset1:1
	ds_write2_b32 v4, v42, v43 offset1:1
	s_waitcnt lgkmcnt(0)
	ds_read2_b32 v[214:215], v10 offset1:33
	ds_read2_b32 v[222:223], v10 offset0:66 offset1:99
	ds_read2_b32 v[224:225], v10 offset0:132 offset1:165
	ds_read2_b32 v[226:227], v10 offset0:198 offset1:231
	ds_read2_b32 v[228:229], v10 offset0:8 offset1:41
	ds_read2_b32 v[230:231], v10 offset0:74 offset1:107
	ds_read2_b32 v[232:233], v10 offset0:140 offset1:173
	ds_read2_b32 v[234:235], v10 offset0:206 offset1:239
	s_waitcnt lgkmcnt(0)
	ds_read2_b32 v[236:237], v10 offset0:16 offset1:49
	ds_read2_b32 v[238:239], v10 offset0:82 offset1:115
	ds_read2_b32 v[240:241], v10 offset0:148 offset1:181
	ds_read2_b32 v[242:243], v10 offset0:214 offset1:247
	ds_read2_b32 v[244:245], v10 offset0:24 offset1:57
	ds_read2_b32 v[246:247], v10 offset0:90 offset1:123
	ds_read2_b32 v[248:249], v10 offset0:156 offset1:189
	ds_read2_b32 v[250:251], v10 offset0:222 offset1:255
	v_cvt_pk_bf16_f32 v12, v214, v215
	v_cvt_pk_bf16_f32 v13, v222, v223
	v_cvt_pk_bf16_f32 v14, v224, v225
	v_cvt_pk_bf16_f32 v15, v226, v227
	v_and_b32_e32 v16, 0xffffff80, v11
	v_add3_u32 v16, v11, v16, s7
	v_ashrrev_i32_e32 v17, 31, v16
	v_lshl_add_u64 v[4:5], s[34:35], 0, v[96:97]
	v_lshlrev_b64 v[16:17], 12, v[16:17]
	v_lshl_add_u64 v[16:17], v[4:5], 0, v[16:17]
	global_store_dwordx4 v[16:17], v[12:15], off nt
	s_nop 1
	v_add_u32_e32 v11, s6, v7
	v_cvt_pk_bf16_f32 v12, v228, v229
	v_cvt_pk_bf16_f32 v13, v230, v231
	v_cvt_pk_bf16_f32 v14, v232, v233
	v_cvt_pk_bf16_f32 v15, v234, v235
	v_and_b32_e32 v16, 0xffffff80, v11
	v_add3_u32 v16, v11, v16, s7
	v_ashrrev_i32_e32 v17, 31, v16
	v_lshlrev_b64 v[16:17], 12, v[16:17]
	v_lshl_add_u64 v[16:17], v[4:5], 0, v[16:17]
	global_store_dwordx4 v[16:17], v[12:15], off nt
	s_nop 1
	s_waitcnt lgkmcnt(0)
	v_add_u32_e32 v11, s6, v8
	v_cvt_pk_bf16_f32 v12, v236, v237
	v_cvt_pk_bf16_f32 v13, v238, v239
	v_cvt_pk_bf16_f32 v14, v240, v241
	v_cvt_pk_bf16_f32 v15, v242, v243
	v_and_b32_e32 v16, 0xffffff80, v11
	v_add3_u32 v16, v11, v16, s7
	v_ashrrev_i32_e32 v17, 31, v16
	v_lshlrev_b64 v[16:17], 12, v[16:17]
	v_lshl_add_u64 v[16:17], v[4:5], 0, v[16:17]
	global_store_dwordx4 v[16:17], v[12:15], off nt
	s_nop 1
	v_add_u32_e32 v11, s6, v9
	v_cvt_pk_bf16_f32 v12, v244, v245
	v_cvt_pk_bf16_f32 v13, v246, v247
	v_cvt_pk_bf16_f32 v14, v248, v249
	v_cvt_pk_bf16_f32 v15, v250, v251
	v_and_b32_e32 v16, 0xffffff80, v11
	v_add3_u32 v16, v11, v16, s7
	v_ashrrev_i32_e32 v17, 31, v16
	v_lshlrev_b64 v[16:17], 12, v[16:17]
	v_lshl_add_u64 v[4:5], v[4:5], 0, v[16:17]
	global_store_dwordx4 v[4:5], v[12:15], off nt
	s_nop 1
	s_waitcnt lgkmcnt(0)

; __device__ __forceinline__ unsigned pk2(float lo, float hi) { unsigned r; asm volatile("v_cvt_pk_bf16_f32 %0, %1, %2" : "=v"(r) : "v"(lo), "v"(hi)); return r; }
; __device__ __forceinline__ void transpose_item(const float* W, int K, int N, bf16_t* WT, int rstep, int roff, float* scr, int item, int lane) {
;   const int nblk = N / 32, kb = item / nblk, nb = item % nblk, k0 = 64 * kb, n0 = 32 * nb;
;   f32x4 v[8];
; #pragma unroll
;   for (int i = 0; i < 8; ++i) v[i] = __builtin_nontemporal_load((const f32x4*)(W + (size_t)(k0 + i * 8 + (lane >> 3)) * N + n0 + (lane & 7) * 4));
; #pragma unroll
;   for (int i = 0; i < 8; ++i) { float* d = scr + (i * 8 + (lane >> 3)) * 33 + (lane & 7) * 4; d[0] = v[i].x; d[1] = v[i].y; d[2] = v[i].z; d[3] = v[i].w; }
;   __builtin_amdgcn_wave_barrier(); asm volatile("s_waitcnt lgkmcnt(0)" ::: "memory");
;   const int c = lane & 7;
; #pragma unroll
;   for (int j = 0; j < 4; ++j) { const int nl = (lane >> 3) + 8 * j, n = n0 + nl; const float* s = scr + (8 * c) * 33 + nl;
;     u32x4 o; o.x = pk2(s[0 * 33], s[1 * 33]); o.y = pk2(s[2 * 33], s[3 * 33]); o.z = pk2(s[4 * 33], s[5 * 33]); o.w = pk2(s[6 * 33], s[7 * 33]);
;     const int row = n + (n >> 7) * rstep + roff;
;     __builtin_nontemporal_store(o, (u32x4*)(WT + (size_t)row * K + k0 + 8 * c)); }
;   __builtin_amdgcn_wave_barrier(); asm volatile("s_waitcnt lgkmcnt(0)" ::: "memory");
; }
; __device__ __forceinline__ void convert_item(const P& p, int it, float* scr, int lane) {
;     ...
;     if (which == 0) transpose_item(p.wg + (size_t)le * DM * EFF, DM, EFF, WSP(bf16_t, WS_WGU) + (size_t)le * 1024 * DM, 128, 0, scr, sub, lane);
.LBB0_1182:
	s_andn2_b64 vcc, exec, s[6:7]
	s_cbranch_vccnz .LBB0_1184
	s_waitcnt lgkmcnt(0)
	s_add_u32 s30, s48, s14
	s_addc_u32 s31, s49, s15
	s_add_u32 s7, s70, s14
	s_addc_u32 s14, s71, s15
	s_lshl_b32 s6, s23, 2
	s_and_b32 s15, s6, 0x7c0
	s_and_b32 s6, s24, 0x1e0
	s_lshl_b32 s23, s6, 2
	v_add_u32_e32 v4, s15, v1
	s_add_u32 s30, s30, s23
	s_addc_u32 s31, s31, 0
	v_lshlrev_b32_e32 v96, 2, v0
	v_ashrrev_i32_e32 v5, 31, v4
	v_lshl_add_u64 v[12:13], s[30:31], 0, v[96:97]
	v_lshlrev_b64 v[4:5], 11, v[4:5]
	v_lshl_add_u64 v[4:5], v[12:13], 0, v[4:5]
	s_movk_i32 s23, 0x4000
	v_add_co_u32_e32 v16, vcc, s23, v4
	s_mov_b32 s23, 0x8000
	s_nop 0
	v_addc_co_u32_e32 v17, vcc, 0, v5, vcc
	global_load_dwordx4 v[12:15], v[4:5], off nt
	v_add_co_u32_e32 v20, vcc, s23, v4
	global_load_dwordx4 v[16:19], v[16:17], off nt
	s_nop 0
	v_addc_co_u32_e32 v21, vcc, 0, v5, vcc
	s_mov_b32 s23, 0xc000
	global_load_dwordx4 v[20:23], v[20:21], off nt
	v_add_co_u32_e32 v24, vcc, s23, v4
	s_mov_b32 s23, 0x10000
	s_nop 0
	v_addc_co_u32_e32 v25, vcc, 0, v5, vcc
	global_load_dwordx4 v[24:27], v[24:25], off nt
	v_add_co_u32_e32 v28, vcc, s23, v4
	s_mov_b32 s23, 0x14000
	s_nop 0
	v_addc_co_u32_e32 v29, vcc, 0, v5, vcc
	global_load_dwordx4 v[28:31], v[28:29], off nt
	v_add_co_u32_e32 v32, vcc, s23, v4
	v_add_u32_e32 v11, s6, v1
	s_nop 0
	v_addc_co_u32_e32 v33, vcc, 0, v5, vcc
	global_load_dwordx4 v[32:35], v[32:33], off nt
	v_add_co_u32_e32 v36, vcc, s93, v4
	s_lshl_b32 s15, s15, 1
	s_nop 0
	v_addc_co_u32_e32 v37, vcc, 0, v5, vcc
	global_load_dwordx4 v[36:39], v[36:37], off nt
	v_add_co_u32_e32 v4, vcc, s96, v4
	s_add_u32 s30, s7, s15
	s_nop 0
	v_addc_co_u32_e32 v5, vcc, 0, v5, vcc
	global_load_dwordx4 v[40:43], v[4:5], off nt
	v_add_u32_e32 v4, v3, v6
	v_add_u32_e32 v5, 0x420, v4
	s_addc_u32 s31, s14, 0
	v_lshlrev_b32_e32 v96, 1, v2
	s_waitcnt vmcnt(0)
	ds_write2_b32 v4, v12, v13 offset1:1
	ds_write2_b32 v4, v14, v15 offset0:2 offset1:3
	ds_write2_b32 v5, v16, v17 offset1:1
	v_add_u32_e32 v5, 0x428, v4
	ds_write2_b32 v5, v18, v19 offset1:1
	v_add_u32_e32 v5, 0x840, v4
	ds_write2_b32 v5, v20, v21 offset1:1
	v_add_u32_e32 v5, 0x848, v4
	ds_write2_b32 v5, v22, v23 offset1:1
	v_add_u32_e32 v5, 0xc60, v4
	ds_write2_b32 v5, v24, v25 offset1:1
	v_add_u32_e32 v5, 0xc68, v4
	ds_write2_b32 v5, v26, v27 offset1:1
	v_add_u32_e32 v5, 0x1080, v4
	ds_write2_b32 v5, v28, v29 offset1:1
	v_add_u32_e32 v5, 0x1088, v4
	ds_write2_b32 v5, v30, v31 offset1:1
	v_add_u32_e32 v5, 0x14a0, v4
	ds_write2_b32 v5, v32, v33 offset1:1
	v_add_u32_e32 v5, 0x14a8, v4
	ds_write2_b32 v5, v34, v35 offset1:1
	v_add_u32_e32 v5, 0x18c0, v4
	ds_write2_b32 v5, v36, v37 offset1:1
	v_add_u32_e32 v5, 0x18c8, v4
	ds_write2_b32 v5, v38, v39 offset1:1
	v_add_u32_e32 v5, 0x1ce0, v4
	v_add_u32_e32 v4, 0x1ce8, v4
	ds_write2_b32 v5, v40, v41 offset1:1
	ds_write2_b32 v4, v42, v43 offset1:1
	s_waitcnt lgkmcnt(0)
	ds_read2_b32 v[214:215], v10 offset1:33
	ds_read2_b32 v[222:223], v10 offset0:66 offset1:99
	ds_read2_b32 v[224:225], v10 offset0:132 offset1:165
	ds_read2_b32 v[226:227], v10 offset0:198 offset1:231
	ds_read2_b32 v[228:229], v10 offset0:8 offset1:41
	ds_read2_b32 v[230:231], v10 offset0:74 offset1:107
	ds_read2_b32 v[232:233], v10 offset0:140 offset1:173
	ds_read2_b32 v[234:235], v10 offset0:206 offset1:239
	s_waitcnt lgkmcnt(0)
	ds_read2_b32 v[236:237], v10 offset0:16 offset1:49
	ds_read2_b32 v[238:239], v10 offset0:82 offset1:115
	ds_read2_b32 v[240:241], v10 offset0:148 offset1:181
	ds_read2_b32 v[242:243], v10 offset0:214 offset1:247
	ds_read2_b32 v[244:245], v10 offset0:24 offset1:57
	ds_read2_b32 v[246:247], v10 offset0:90 offset1:123
	ds_read2_b32 v[248:249], v10 offset0:156 offset1:189
	ds_read2_b32 v[250:251], v10 offset0:222 offset1:255
	v_cvt_pk_bf16_f32 v12, v214, v215
	v_cvt_pk_bf16_f32 v13, v222, v223
	v_cvt_pk_bf16_f32 v14, v224, v225
	v_cvt_pk_bf16_f32 v15, v226, v227
	v_and_b32_e32 v16, 0xffffff80, v11
	v_add_u32_e32 v16, v16, v11
	v_ashrrev_i32_e32 v17, 31, v16
	v_lshl_add_u64 v[4:5], s[30:31], 0, v[96:97]
	v_lshlrev_b64 v[16:17], 12, v[16:17]
	v_lshl_add_u64 v[16:17], v[4:5], 0, v[16:17]
	global_store_dwordx4 v[16:17], v[12:15], off nt
	s_nop 1
	v_add_u32_e32 v11, s6, v7
	v_cvt_pk_bf16_f32 v12, v228, v229
	v_cvt_pk_bf16_f32 v13, v230, v231
	v_cvt_pk_bf16_f32 v14, v232, v233
	v_cvt_pk_bf16_f32 v15, v234, v235
	v_and_b32_e32 v16, 0xffffff80, v11
	v_add_u32_e32 v16, v16, v11
	v_ashrrev_i32_e32 v17, 31, v16
	v_lshlrev_b64 v[16:17], 12, v[16:17]
	v_lshl_add_u64 v[16:17], v[4:5], 0, v[16:17]
	global_store_dwordx4 v[16:17], v[12:15], off nt
	s_nop 1
	s_waitcnt lgkmcnt(0)
	v_add_u32_e32 v11, s6, v8
	v_cvt_pk_bf16_f32 v12, v236, v237
	v_cvt_pk_bf16_f32 v13, v238, v239
	v_cvt_pk_bf16_f32 v14, v240, v241
	v_cvt_pk_bf16_f32 v15, v242, v243
	v_and_b32_e32 v16, 0xffffff80, v11
	v_add_u32_e32 v16, v16, v11
	v_ashrrev_i32_e32 v17, 31, v16
	v_lshlrev_b64 v[16:17], 12, v[16:17]
	v_lshl_add_u64 v[16:17], v[4:5], 0, v[16:17]
	global_store_dwordx4 v[16:17], v[12:15], off nt
	s_nop 1
	v_add_u32_e32 v11, s6, v9
	v_cvt_pk_bf16_f32 v12, v244, v245
	v_cvt_pk_bf16_f32 v13, v246, v247
	v_cvt_pk_bf16_f32 v14, v248, v249
	v_cvt_pk_bf16_f32 v15, v250, v251
	v_and_b32_e32 v16, 0xffffff80, v11
	v_add_u32_e32 v16, v16, v11
	v_ashrrev_i32_e32 v17, 31, v16
	v_lshlrev_b64 v[16:17], 12, v[16:17]
	v_lshl_add_u64 v[4:5], v[4:5], 0, v[16:17]
	global_store_dwordx4 v[4:5], v[12:15], off nt
	s_nop 1
	s_waitcnt lgkmcnt(0)

; __device__ __forceinline__ unsigned pk2(float lo, float hi) { unsigned r; asm volatile("v_cvt_pk_bf16_f32 %0, %1, %2" : "=v"(r) : "v"(lo), "v"(hi)); return r; }
; __device__ __forceinline__ void transpose_item(const float* W, int K, int N, bf16_t* WT, int rstep, int roff, float* scr, int item, int lane) {
;   const int nblk = N / 32, kb = item / nblk, nb = item % nblk, k0 = 64 * kb, n0 = 32 * nb;
;   f32x4 v[8];
; #pragma unroll
;   for (int i = 0; i < 8; ++i) v[i] = __builtin_nontemporal_load((const f32x4*)(W + (size_t)(k0 + i * 8 + (lane >> 3)) * N + n0 + (lane & 7) * 4));
; #pragma unroll
;   for (int i = 0; i < 8; ++i) { float* d = scr + (i * 8 + (lane >> 3)) * 33 + (lane & 7) * 4; d[0] = v[i].x; d[1] = v[i].y; d[2] = v[i].z; d[3] = v[i].w; }
;   __builtin_amdgcn_wave_barrier(); asm volatile("s_waitcnt lgkmcnt(0)" ::: "memory");
;   const int c = lane & 7;
; #pragma unroll
;   for (int j = 0; j < 4; ++j) { const int nl = (lane >> 3) + 8 * j, n = n0 + nl; const float* s = scr + (8 * c) * 33 + nl;
;     u32x4 o; o.x = pk2(s[0 * 33], s[1 * 33]); o.y = pk2(s[2 * 33], s[3 * 33]); o.z = pk2(s[4 * 33], s[5 * 33]); o.w = pk2(s[6 * 33], s[7 * 33]);
;     const int row = n + (n >> 7) * rstep + roff;
;     __builtin_nontemporal_store(o, (u32x4*)(WT + (size_t)row * K + k0 + 8 * c)); }
;   __builtin_amdgcn_wave_barrier(); asm volatile("s_waitcnt lgkmcnt(0)" ::: "memory");
; }
; __device__ __forceinline__ void convert_item(const P& p, int it, float* scr, int lane) {
;   if (it < IT_DENSE) {
;     const int l = it / (IT_WIN + IT_WOUT), r = it % (IT_WIN + IT_WOUT);
;     if (r < IT_WIN) transpose_item(p.w_in + (size_t)l * DM * INW, DM, INW, WSP(bf16_t, WS_WIN) + (size_t)l * INW * DM, 0, 0, scr, r, lane);
;     else transpose_item(p.w_out + (size_t)l * DM * DM, DM, DM, WSP(bf16_t, WS_WOUT) + (size_t)l * DM * DM, 0, 0, scr, r - IT_WIN, lane);
.LBB0_1185:
	s_and_b64 vcc, exec, s[6:7]
	s_cbranch_vccz .LBB0_1161
	s_ashr_i32 s6, s22, 31
	s_lshr_b32 s6, s6, 19
	s_add_i32 s6, s22, s6
	s_ashr_i32 s14, s6, 13
	s_and_b32 s6, s6, 0xffffe000
	s_sub_i32 s22, s22, s6
	s_ashr_i32 s15, s14, 31
	v_add_u32_e32 v11, v3, v6
	s_cmpk_gt_i32 s22, 0x17ff
	s_mov_b64 s[6:7], -1
	v_lshlrev_b32_e32 v96, 2, v0
	v_add_u32_e32 v12, 0x420, v11
	v_add_u32_e32 v13, 0x428, v11
	v_add_u32_e32 v14, 0x840, v11
	v_add_u32_e32 v15, 0x848, v11
	v_add_u32_e32 v16, 0xc60, v11
	v_add_u32_e32 v17, 0xc68, v11
	v_add_u32_e32 v18, 0x1080, v11
	v_add_u32_e32 v19, 0x1088, v11
	v_add_u32_e32 v20, 0x14a0, v11
	v_add_u32_e32 v21, 0x14a8, v11
	v_add_u32_e32 v22, 0x18c0, v11
	v_add_u32_e32 v23, 0x18c8, v11
	v_add_u32_e32 v24, 0x1ce0, v11
	v_add_u32_e32 v25, 0x1ce8, v11
	v_lshlrev_b32_e32 v4, 1, v2
	s_cbranch_scc0 .LBB0_1188
	s_lshl_b64 s[6:7], s[14:15], 24
	s_waitcnt lgkmcnt(0)
	s_add_u32 s23, s46, s6
	s_addc_u32 s24, s47, s7
	s_lshl_b64 s[6:7], s[14:15], 23
	s_add_u32 s15, s9, s6
	s_addc_u32 s30, s16, s7
	s_add_i32 s6, s22, 0xe800
	s_and_b32 s31, s6, 0xffc0
	s_lshl_b32 s6, s22, 5
	s_and_b32 s34, s6, 0x7e0
	s_lshl_b32 s6, s34, 2
	v_add_u32_e32 v26, s31, v1
	s_add_u32 s6, s23, s6
	s_addc_u32 s7, s24, 0
	v_ashrrev_i32_e32 v27, 31, v26
	v_lshl_add_u64 v[28:29], s[6:7], 0, v[96:97]
	v_lshlrev_b64 v[26:27], 13, v[26:27]
	v_lshl_add_u64 v[54:55], v[28:29], 0, v[26:27]
	s_mov_b32 s6, 0x10000
	v_add_co_u32_e32 v30, vcc, s6, v54
	s_mov_b32 s6, 0x20000
	s_nop 0
	v_addc_co_u32_e32 v31, vcc, 0, v55, vcc
	v_add_co_u32_e32 v34, vcc, s6, v54
	s_mov_b32 s6, 0x30000
	s_nop 0
	v_addc_co_u32_e32 v35, vcc, 0, v55, vcc
	v_add_co_u32_e32 v38, vcc, s6, v54
	s_mov_b32 s6, 0x40000
	s_nop 0
	v_addc_co_u32_e32 v39, vcc, 0, v55, vcc
	v_add_co_u32_e32 v42, vcc, s6, v54
	s_mov_b32 s6, 0x50000
	s_nop 0
	v_addc_co_u32_e32 v43, vcc, 0, v55, vcc
	v_add_co_u32_e32 v46, vcc, s6, v54
	global_load_dwordx4 v[26:29], v[54:55], off nt
	s_nop 0
	global_load_dwordx4 v[30:33], v[30:31], off nt
	v_addc_co_u32_e32 v47, vcc, 0, v55, vcc
	global_load_dwordx4 v[34:37], v[34:35], off nt
	s_nop 0
	global_load_dwordx4 v[38:41], v[38:39], off nt
	s_nop 0
	global_load_dwordx4 v[42:45], v[42:43], off nt
	s_nop 0
	global_load_dwordx4 v[46:49], v[46:47], off nt
	s_mov_b32 s6, 0x60000
	v_add_co_u32_e32 v50, vcc, s6, v54
	s_mov_b32 s6, 0x70000
	s_nop 0
	v_addc_co_u32_e32 v51, vcc, 0, v55, vcc
	global_load_dwordx4 v[50:53], v[50:51], off nt
	v_add_co_u32_e32 v54, vcc, s6, v54
	s_lshl_b32 s6, s31, 1
	s_nop 0
	v_addc_co_u32_e32 v55, vcc, 0, v55, vcc
	global_load_dwordx4 v[54:57], v[54:55], off nt
	s_add_u32 s6, s15, s6
	v_mov_b32_e32 v5, v97
	s_addc_u32 s7, s30, 0
	s_waitcnt vmcnt(0)
	ds_write2_b32 v11, v26, v27 offset1:1
	ds_write2_b32 v11, v28, v29 offset0:2 offset1:3
	ds_write2_b32 v12, v30, v31 offset1:1
	ds_write2_b32 v13, v32, v33 offset1:1
	ds_write2_b32 v14, v34, v35 offset1:1
	ds_write2_b32 v15, v36, v37 offset1:1
	ds_write2_b32 v16, v38, v39 offset1:1
	ds_write2_b32 v17, v40, v41 offset1:1
	ds_write2_b32 v18, v42, v43 offset1:1
	ds_write2_b32 v19, v44, v45 offset1:1
	ds_write2_b32 v20, v46, v47 offset1:1
	ds_write2_b32 v21, v48, v49 offset1:1
	ds_write2_b32 v22, v50, v51 offset1:1
	ds_write2_b32 v23, v52, v53 offset1:1
	ds_write2_b32 v24, v54, v55 offset1:1
	ds_write2_b32 v25, v56, v57 offset1:1
	s_waitcnt lgkmcnt(0)
	ds_read2_b32 v[214:215], v10 offset1:33
	ds_read2_b32 v[222:223], v10 offset0:66 offset1:99
	ds_read2_b32 v[224:225], v10 offset0:132 offset1:165
	ds_read2_b32 v[226:227], v10 offset0:198 offset1:231
	ds_read2_b32 v[228:229], v10 offset0:8 offset1:41
	ds_read2_b32 v[230:231], v10 offset0:74 offset1:107
	ds_read2_b32 v[232:233], v10 offset0:140 offset1:173
	ds_read2_b32 v[234:235], v10 offset0:206 offset1:239
	s_waitcnt lgkmcnt(0)
	ds_read2_b32 v[236:237], v10 offset0:16 offset1:49
	ds_read2_b32 v[238:239], v10 offset0:82 offset1:115
	ds_read2_b32 v[240:241], v10 offset0:148 offset1:181
	ds_read2_b32 v[242:243], v10 offset0:214 offset1:247
	ds_read2_b32 v[244:245], v10 offset0:24 offset1:57
	ds_read2_b32 v[246:247], v10 offset0:90 offset1:123
	ds_read2_b32 v[248:249], v10 offset0:156 offset1:189
	ds_read2_b32 v[250:251], v10 offset0:222 offset1:255
	v_cvt_pk_bf16_f32 v26, v214, v215
	v_add_u32_e32 v30, s34, v1
	v_cvt_pk_bf16_f32 v27, v222, v223
	v_ashrrev_i32_e32 v31, 31, v30
	v_cvt_pk_bf16_f32 v28, v224, v225
	v_lshlrev_b64 v[30:31], 12, v[30:31]
	v_lshl_add_u64 v[34:35], s[6:7], 0, v[4:5]
	v_cvt_pk_bf16_f32 v29, v226, v227
	v_lshl_add_u64 v[30:31], v[34:35], 0, v[30:31]
	global_store_dwordx4 v[30:31], v[26:29], off nt
	s_nop 1
	s_mov_b64 s[6:7], 0
	v_cvt_pk_bf16_f32 v26, v228, v229
	v_add_u32_e32 v32, s34, v7
	v_ashrrev_i32_e32 v33, 31, v32
	v_lshlrev_b64 v[32:33], 12, v[32:33]
	v_cvt_pk_bf16_f32 v27, v230, v231
	v_lshl_add_u64 v[32:33], v[34:35], 0, v[32:33]
	v_cvt_pk_bf16_f32 v28, v232, v233
	v_cvt_pk_bf16_f32 v29, v234, v235
	global_store_dwordx4 v[32:33], v[26:29], off nt
	s_nop 1
	v_add_u32_e32 v32, s34, v8
	v_ashrrev_i32_e32 v33, 31, v32
	s_waitcnt lgkmcnt(0)
	v_cvt_pk_bf16_f32 v26, v236, v237
	v_lshlrev_b64 v[32:33], 12, v[32:33]
	v_cvt_pk_bf16_f32 v27, v238, v239
	v_lshl_add_u64 v[32:33], v[34:35], 0, v[32:33]
	v_cvt_pk_bf16_f32 v28, v240, v241
	v_cvt_pk_bf16_f32 v29, v242, v243
	global_store_dwordx4 v[32:33], v[26:29], off nt
	s_nop 1
	v_add_u32_e32 v32, s34, v9
	v_ashrrev_i32_e32 v33, 31, v32
	v_cvt_pk_bf16_f32 v26, v244, v245
	v_lshlrev_b64 v[32:33], 12, v[32:33]
	v_cvt_pk_bf16_f32 v27, v246, v247
	v_lshl_add_u64 v[32:33], v[34:35], 0, v[32:33]
	v_cvt_pk_bf16_f32 v28, v248, v249
	v_cvt_pk_bf16_f32 v29, v250, v251
	global_store_dwordx4 v[32:33], v[26:29], off nt
	s_nop 1
	s_waitcnt lgkmcnt(0)
; __device__ __forceinline__ unsigned pk2(float lo, float hi) { unsigned r; asm volatile("v_cvt_pk_bf16_f32 %0, %1, %2" : "=v"(r) : "v"(lo), "v"(hi)); return r; }
; __device__ __forceinline__ void transpose_item(const float* W, int K, int N, bf16_t* WT, int rstep, int roff, float* scr, int item, int lane) {
;   const int nblk = N / 32, kb = item / nblk, nb = item % nblk, k0 = 64 * kb, n0 = 32 * nb;
;   f32x4 v[8];
; #pragma unroll
;   for (int i = 0; i < 8; ++i) v[i] = __builtin_nontemporal_load((const f32x4*)(W + (size_t)(k0 + i * 8 + (lane >> 3)) * N + n0 + (lane & 7) * 4));
; #pragma unroll
;   for (int i = 0; i < 8; ++i) { float* d = scr + (i * 8 + (lane >> 3)) * 33 + (lane & 7) * 4; d[0] = v[i].x; d[1] = v[i].y; d[2] = v[i].z; d[3] = v[i].w; }
;   __builtin_amdgcn_wave_barrier(); asm volatile("s_waitcnt lgkmcnt(0)" ::: "memory");
;   const int c = lane & 7;
; #pragma unroll
;   for (int j = 0; j < 4; ++j) { const int nl = (lane >> 3) + 8 * j, n = n0 + nl; const float* s = scr + (8 * c) * 33 + nl;
;     u32x4 o; o.x = pk2(s[0 * 33], s[1 * 33]); o.y = pk2(s[2 * 33], s[3 * 33]); o.z = pk2(s[4 * 33], s[5 * 33]); o.w = pk2(s[6 * 33], s[7 * 33]);
;     const int row = n + (n >> 7) * rstep + roff;
;     __builtin_nontemporal_store(o, (u32x4*)(WT + (size_t)row * K + k0 + 8 * c)); }
;   __builtin_amdgcn_wave_barrier(); asm volatile("s_waitcnt lgkmcnt(0)" ::: "memory");
; }
; __device__ __forceinline__ void convert_item(const P& p, int it, float* scr, int lane) {
;     ...
;     if (r < IT_WIN) transpose_item(p.w_in + (size_t)l * DM * INW, DM, INW, WSP(bf16_t, WS_WIN) + (size_t)l * INW * DM, 0, 0, scr, r, lane);
.LBB0_1188:
	s_andn2_b64 vcc, exec, s[6:7]
	s_cbranch_vccnz .LBB0_1161
	s_mul_i32 s7, s14, 0x3000000
	s_mul_hi_i32 s6, s14, 0x3000000
	s_waitcnt lgkmcnt(0)
	s_add_u32 s7, s44, s7
	s_addc_u32 s24, s45, s6
	s_mul_hi_i32 s6, s14, 0x1800000
	s_mul_i32 s14, s14, 0x1800000
	s_add_u32 s30, s17, s14
	s_addc_u32 s31, s18, s6
	s_mul_i32 s6, s22, 0x2aab
	s_lshr_b32 s14, s6, 31
	s_ashr_i32 s6, s6, 21
	s_add_i32 s6, s6, s14
	s_sext_i32_i16 s14, s6
	s_mulk_i32 s6, 0xc0
	s_sub_i32 s6, s22, s6
	s_sext_i32_i16 s15, s6
	s_lshl_b32 s6, s14, 6
	s_lshl_b32 s14, s15, 5
	s_ashr_i32 s15, s14, 31
	s_lshl_b64 s[22:23], s[14:15], 2
	s_add_u32 s22, s7, s22
	v_add_u32_e32 v5, s6, v1
	s_addc_u32 s23, s24, s23
	v_lshl_add_u64 v[54:55], s[22:23], 0, v[96:97]
	s_movk_i32 s7, 0x6000
	v_add_u32_e32 v28, 8, v5
	v_add_u32_e32 v34, 16, v5
	v_add_u32_e32 v36, 24, v5
	v_add_u32_e32 v42, 32, v5
	v_add_u32_e32 v44, 40, v5
	v_mad_i64_i32 v[26:27], s[22:23], v5, s7, v[54:55]
	v_mad_i64_i32 v[30:31], s[22:23], v28, s7, v[54:55]
	v_mad_i64_i32 v[34:35], s[22:23], v34, s7, v[54:55]
	v_mad_i64_i32 v[38:39], s[22:23], v36, s7, v[54:55]
	v_mad_i64_i32 v[42:43], s[22:23], v42, s7, v[54:55]
	v_mad_i64_i32 v[46:47], s[22:23], v44, s7, v[54:55]
	global_load_dwordx4 v[26:29], v[26:27], off nt
	s_nop 0
	global_load_dwordx4 v[30:33], v[30:31], off nt
	s_nop 0
	global_load_dwordx4 v[34:37], v[34:35], off nt
	s_nop 0
	global_load_dwordx4 v[38:41], v[38:39], off nt
	s_nop 0
	global_load_dwordx4 v[42:45], v[42:43], off nt
	s_nop 0
	global_load_dwordx4 v[46:49], v[46:47], off nt
	v_add_u32_e32 v50, 48, v5
	v_mad_i64_i32 v[50:51], s[22:23], v50, s7, v[54:55]
	global_load_dwordx4 v[50:53], v[50:51], off nt
	v_add_u32_e32 v5, 56, v5
	v_mad_i64_i32 v[54:55], s[22:23], v5, s7, v[54:55]
	global_load_dwordx4 v[54:57], v[54:55], off nt
	s_ashr_i32 s7, s6, 31
	s_lshl_b64 s[6:7], s[6:7], 1
	s_add_u32 s6, s30, s6
	v_mov_b32_e32 v5, v97
	s_addc_u32 s7, s31, s7
	v_lshl_add_u64 v[4:5], s[6:7], 0, v[4:5]
	s_movk_i32 s82, 0x6000
	s_waitcnt vmcnt(0)
	ds_write2_b32 v11, v26, v27 offset1:1
	ds_write2_b32 v11, v28, v29 offset0:2 offset1:3
	ds_write2_b32 v12, v30, v31 offset1:1
	ds_write2_b32 v13, v32, v33 offset1:1
	ds_write2_b32 v14, v34, v35 offset1:1
	ds_write2_b32 v15, v36, v37 offset1:1
	ds_write2_b32 v16, v38, v39 offset1:1
	ds_write2_b32 v17, v40, v41 offset1:1
	ds_write2_b32 v18, v42, v43 offset1:1
	ds_write2_b32 v19, v44, v45 offset1:1
	ds_write2_b32 v20, v46, v47 offset1:1
	ds_write2_b32 v21, v48, v49 offset1:1
	ds_write2_b32 v22, v50, v51 offset1:1
	ds_write2_b32 v23, v52, v53 offset1:1
	ds_write2_b32 v24, v54, v55 offset1:1
	ds_write2_b32 v25, v56, v57 offset1:1
	s_waitcnt lgkmcnt(0)
	ds_read2_b32 v[214:215], v10 offset1:33
	ds_read2_b32 v[222:223], v10 offset0:66 offset1:99
	ds_read2_b32 v[224:225], v10 offset0:132 offset1:165
	ds_read2_b32 v[226:227], v10 offset0:198 offset1:231
	ds_read2_b32 v[228:229], v10 offset0:8 offset1:41
	ds_read2_b32 v[230:231], v10 offset0:74 offset1:107
	ds_read2_b32 v[232:233], v10 offset0:140 offset1:173
	ds_read2_b32 v[234:235], v10 offset0:206 offset1:239
	s_waitcnt lgkmcnt(0)
	ds_read2_b32 v[236:237], v10 offset0:16 offset1:49
	ds_read2_b32 v[238:239], v10 offset0:82 offset1:115
	ds_read2_b32 v[240:241], v10 offset0:148 offset1:181
	ds_read2_b32 v[242:243], v10 offset0:214 offset1:247
	ds_read2_b32 v[244:245], v10 offset0:24 offset1:57
	ds_read2_b32 v[246:247], v10 offset0:90 offset1:123
	ds_read2_b32 v[248:249], v10 offset0:156 offset1:189
	ds_read2_b32 v[250:251], v10 offset0:222 offset1:255
	v_cvt_pk_bf16_f32 v12, v214, v215
	v_add_u32_e32 v16, s14, v1
	v_cvt_pk_bf16_f32 v13, v222, v223
	v_ashrrev_i32_e32 v17, 31, v16
	v_cvt_pk_bf16_f32 v14, v224, v225
	v_lshlrev_b64 v[16:17], 12, v[16:17]
	v_cvt_pk_bf16_f32 v15, v226, v227
	v_lshl_add_u64 v[16:17], v[4:5], 0, v[16:17]
	global_store_dwordx4 v[16:17], v[12:15], off nt
	s_nop 1
	s_nop 0
	v_cvt_pk_bf16_f32 v12, v228, v229
	v_add_u32_e32 v18, s14, v7
	v_ashrrev_i32_e32 v19, 31, v18
	v_lshlrev_b64 v[18:19], 12, v[18:19]
	v_cvt_pk_bf16_f32 v13, v230, v231
	v_lshl_add_u64 v[18:19], v[4:5], 0, v[18:19]
	v_cvt_pk_bf16_f32 v14, v232, v233
	v_cvt_pk_bf16_f32 v15, v234, v235
	global_store_dwordx4 v[18:19], v[12:15], off nt
	s_nop 1
	v_add_u32_e32 v18, s14, v8
	v_ashrrev_i32_e32 v19, 31, v18
	s_waitcnt lgkmcnt(0)
	v_cvt_pk_bf16_f32 v12, v236, v237
	v_lshlrev_b64 v[18:19], 12, v[18:19]
	v_cvt_pk_bf16_f32 v13, v238, v239
	v_lshl_add_u64 v[18:19], v[4:5], 0, v[18:19]
	v_cvt_pk_bf16_f32 v14, v240, v241
	v_cvt_pk_bf16_f32 v15, v242, v243
	global_store_dwordx4 v[18:19], v[12:15], off nt
	s_nop 1
	v_add_u32_e32 v18, s14, v9
	v_ashrrev_i32_e32 v19, 31, v18
	v_cvt_pk_bf16_f32 v12, v244, v245
	v_lshlrev_b64 v[18:19], 12, v[18:19]
	v_cvt_pk_bf16_f32 v13, v246, v247
	v_lshl_add_u64 v[4:5], v[4:5], 0, v[18:19]
	v_cvt_pk_bf16_f32 v14, v248, v249
	v_cvt_pk_bf16_f32 v15, v250, v251
	global_store_dwordx4 v[4:5], v[12:15], off nt
	s_nop 1
	s_waitcnt lgkmcnt(0)
	s_branch .LBB0_1161

; __device__ __forceinline__ unsigned pk2(float lo, float hi) { unsigned r; asm volatile("v_cvt_pk_bf16_f32 %0, %1, %2" : "=v"(r) : "v"(lo), "v"(hi)); return r; }
; __device__ __forceinline__ void transpose_item(const float* W, int K, int N, bf16_t* WT, int rstep, int roff, float* scr, int item, int lane) {
;   const int nblk = N / 32, kb = item / nblk, nb = item % nblk, k0 = 64 * kb, n0 = 32 * nb;
;   f32x4 v[8];
; #pragma unroll
;   for (int i = 0; i < 8; ++i) v[i] = __builtin_nontemporal_load((const f32x4*)(W + (size_t)(k0 + i * 8 + (lane >> 3)) * N + n0 + (lane & 7) * 4));
; #pragma unroll
;   for (int i = 0; i < 8; ++i) { float* d = scr + (i * 8 + (lane >> 3)) * 33 + (lane & 7) * 4; d[0] = v[i].x; d[1] = v[i].y; d[2] = v[i].z; d[3] = v[i].w; }
;   __builtin_amdgcn_wave_barrier(); asm volatile("s_waitcnt lgkmcnt(0)" ::: "memory");
;   const int c = lane & 7;
; #pragma unroll
;   for (int j = 0; j < 4; ++j) { const int nl = (lane >> 3) + 8 * j, n = n0 + nl; const float* s = scr + (8 * c) * 33 + nl;
;     u32x4 o; o.x = pk2(s[0 * 33], s[1 * 33]); o.y = pk2(s[2 * 33], s[3 * 33]); o.z = pk2(s[4 * 33], s[5 * 33]); o.w = pk2(s[6 * 33], s[7 * 33]);
;     const int row = n + (n >> 7) * rstep + roff;
;     __builtin_nontemporal_store(o, (u32x4*)(WT + (size_t)row * K + k0 + 8 * c)); }
;   __builtin_amdgcn_wave_barrier(); asm volatile("s_waitcnt lgkmcnt(0)" ::: "memory");
; }
; __device__ __forceinline__ void convert_item(const P& p, int it, float* scr, int lane) {
;     ...
;     else transpose_item(p.wd + (size_t)le * EFF * DM, EFF, DM, WSP(bf16_t, WS_WD) + (size_t)le * DM * EFF, 0, 0, scr, sub, lane);
.LBB0_1198:
	s_and_b32 s6, 0xffff, s19
	s_cmp_lg_u32 s6, 1
	s_mov_b64 s[6:7], -1
	s_cbranch_scc0 .LBB0_1200
	s_waitcnt lgkmcnt(0)
	s_add_u32 s21, s0, s14
	s_addc_u32 s24, s1, s15
	s_lshl_b64 s[22:23], s[64:65], 21
	s_add_u32 s7, s5, s22
	s_addc_u32 s19, s9, s23
	s_and_b32 s6, s18, 0x7e0
	s_and_b32 s20, s20, 0x1c0
	s_lshl_b32 s22, s6, 2
	v_add_u32_e32 v4, s20, v1
	s_add_u32 s22, s21, s22
	s_addc_u32 s23, s24, 0
	v_lshlrev_b32_e32 v96, 2, v0
	v_ashrrev_i32_e32 v5, 31, v4
	v_lshl_add_u64 v[12:13], s[22:23], 0, v[96:97]
	v_lshlrev_b64 v[4:5], 13, v[4:5]
	v_lshl_add_u64 v[4:5], v[12:13], 0, v[4:5]
	s_mov_b32 s21, 0x10000
	v_add_co_u32_e32 v16, vcc, s21, v4
	s_mov_b32 s21, 0x20000
	s_nop 0
	v_addc_co_u32_e32 v17, vcc, 0, v5, vcc
	global_load_dwordx4 v[12:15], v[4:5], off nt
	v_add_co_u32_e32 v20, vcc, s21, v4
	global_load_dwordx4 v[16:19], v[16:17], off nt
	s_nop 0
	v_addc_co_u32_e32 v21, vcc, 0, v5, vcc
	s_mov_b32 s21, 0x30000
	global_load_dwordx4 v[20:23], v[20:21], off nt
	v_add_co_u32_e32 v24, vcc, s21, v4
	s_mov_b32 s21, 0x40000
	s_nop 0
	v_addc_co_u32_e32 v25, vcc, 0, v5, vcc
	global_load_dwordx4 v[24:27], v[24:25], off nt
	v_add_co_u32_e32 v28, vcc, s21, v4
	s_mov_b32 s21, 0x50000
	s_nop 0
	v_addc_co_u32_e32 v29, vcc, 0, v5, vcc
	global_load_dwordx4 v[28:31], v[28:29], off nt
	v_add_co_u32_e32 v32, vcc, s21, v4
	s_mov_b32 s21, 0x60000
	s_nop 0
	v_addc_co_u32_e32 v33, vcc, 0, v5, vcc
	global_load_dwordx4 v[32:35], v[32:33], off nt
	v_add_co_u32_e32 v36, vcc, s21, v4
	s_mov_b32 s21, 0x70000
	s_nop 0
	v_addc_co_u32_e32 v37, vcc, 0, v5, vcc
	global_load_dwordx4 v[36:39], v[36:37], off nt
	v_add_co_u32_e32 v4, vcc, s21, v4
	s_lshl_b32 s20, s20, 1
	s_nop 0
	v_addc_co_u32_e32 v5, vcc, 0, v5, vcc
	global_load_dwordx4 v[40:43], v[4:5], off nt
	v_add_u32_e32 v4, v3, v6
	v_add_u32_e32 v5, 0x420, v4
	s_add_u32 s20, s7, s20
	s_addc_u32 s21, s19, 0
	v_lshlrev_b32_e32 v96, 1, v2
	s_waitcnt vmcnt(0)
	ds_write2_b32 v4, v12, v13 offset1:1
	ds_write2_b32 v4, v14, v15 offset0:2 offset1:3
	ds_write2_b32 v5, v16, v17 offset1:1
	v_add_u32_e32 v5, 0x428, v4
	ds_write2_b32 v5, v18, v19 offset1:1
	v_add_u32_e32 v5, 0x840, v4
	ds_write2_b32 v5, v20, v21 offset1:1
	v_add_u32_e32 v5, 0x848, v4
	ds_write2_b32 v5, v22, v23 offset1:1
	v_add_u32_e32 v5, 0xc60, v4
	v_add_u32_e32 v16, s6, v1
	v_ashrrev_i32_e32 v17, 31, v16
	ds_write2_b32 v5, v24, v25 offset1:1
	v_add_u32_e32 v5, 0xc68, v4
	ds_write2_b32 v5, v26, v27 offset1:1
	v_add_u32_e32 v5, 0x1080, v4
	v_lshlrev_b64 v[16:17], 10, v[16:17]
	ds_write2_b32 v5, v28, v29 offset1:1
	v_add_u32_e32 v5, 0x1088, v4
	ds_write2_b32 v5, v30, v31 offset1:1
	v_add_u32_e32 v5, 0x14a0, v4
	ds_write2_b32 v5, v32, v33 offset1:1
	v_add_u32_e32 v5, 0x14a8, v4
	ds_write2_b32 v5, v34, v35 offset1:1
	v_add_u32_e32 v5, 0x18c0, v4
	ds_write2_b32 v5, v36, v37 offset1:1
	v_add_u32_e32 v5, 0x18c8, v4
	ds_write2_b32 v5, v38, v39 offset1:1
	v_add_u32_e32 v5, 0x1ce0, v4
	v_add_u32_e32 v4, 0x1ce8, v4
	ds_write2_b32 v5, v40, v41 offset1:1
	ds_write2_b32 v4, v42, v43 offset1:1
	s_waitcnt lgkmcnt(0)
	ds_read2_b32 v[214:215], v10 offset1:33
	ds_read2_b32 v[222:223], v10 offset0:66 offset1:99
	ds_read2_b32 v[224:225], v10 offset0:132 offset1:165
	ds_read2_b32 v[226:227], v10 offset0:198 offset1:231
	ds_read2_b32 v[228:229], v10 offset0:8 offset1:41
	ds_read2_b32 v[230:231], v10 offset0:74 offset1:107
	ds_read2_b32 v[232:233], v10 offset0:140 offset1:173
	ds_read2_b32 v[234:235], v10 offset0:206 offset1:239
	s_waitcnt lgkmcnt(0)
	ds_read2_b32 v[236:237], v10 offset0:16 offset1:49
	ds_read2_b32 v[238:239], v10 offset0:82 offset1:115
	ds_read2_b32 v[240:241], v10 offset0:148 offset1:181
	ds_read2_b32 v[242:243], v10 offset0:214 offset1:247
	ds_read2_b32 v[244:245], v10 offset0:24 offset1:57
	ds_read2_b32 v[246:247], v10 offset0:90 offset1:123
	ds_read2_b32 v[248:249], v10 offset0:156 offset1:189
	ds_read2_b32 v[250:251], v10 offset0:222 offset1:255
	v_lshl_add_u64 v[4:5], s[20:21], 0, v[96:97]
	v_cvt_pk_bf16_f32 v12, v214, v215
	v_cvt_pk_bf16_f32 v13, v222, v223
	v_lshl_add_u64 v[16:17], v[4:5], 0, v[16:17]
	v_cvt_pk_bf16_f32 v14, v224, v225
	v_cvt_pk_bf16_f32 v15, v226, v227
	global_store_dwordx4 v[16:17], v[12:15], off nt
	s_nop 1
	v_add_u32_e32 v16, s6, v7
	v_ashrrev_i32_e32 v17, 31, v16
	v_cvt_pk_bf16_f32 v12, v228, v229
	v_lshlrev_b64 v[16:17], 10, v[16:17]
	v_cvt_pk_bf16_f32 v13, v230, v231
	v_lshl_add_u64 v[16:17], v[4:5], 0, v[16:17]
	v_cvt_pk_bf16_f32 v14, v232, v233
	v_cvt_pk_bf16_f32 v15, v234, v235
	global_store_dwordx4 v[16:17], v[12:15], off nt
	s_nop 1
	v_add_u32_e32 v16, s6, v8
	s_waitcnt lgkmcnt(0)
	v_ashrrev_i32_e32 v17, 31, v16
	v_cvt_pk_bf16_f32 v12, v236, v237
	v_lshlrev_b64 v[16:17], 10, v[16:17]
	v_cvt_pk_bf16_f32 v13, v238, v239
	v_lshl_add_u64 v[16:17], v[4:5], 0, v[16:17]
	v_cvt_pk_bf16_f32 v14, v240, v241
	v_cvt_pk_bf16_f32 v15, v242, v243
	global_store_dwordx4 v[16:17], v[12:15], off nt
	s_nop 1
	v_add_u32_e32 v16, s6, v9
	v_ashrrev_i32_e32 v17, 31, v16
	v_cvt_pk_bf16_f32 v12, v244, v245
	v_lshlrev_b64 v[16:17], 10, v[16:17]
	v_cvt_pk_bf16_f32 v13, v246, v247
	v_lshl_add_u64 v[4:5], v[4:5], 0, v[16:17]
	v_cvt_pk_bf16_f32 v14, v248, v249
	v_cvt_pk_bf16_f32 v15, v250, v251
	global_store_dwordx4 v[4:5], v[12:15], off nt
	s_nop 1
	s_waitcnt lgkmcnt(0)
	s_mov_b64 s[6:7], 0
; __device__ __forceinline__ unsigned pk2(float lo, float hi) { unsigned r; asm volatile("v_cvt_pk_bf16_f32 %0, %1, %2" : "=v"(r) : "v"(lo), "v"(hi)); return r; }
; __device__ __forceinline__ void transpose_item(const float* W, int K, int N, bf16_t* WT, int rstep, int roff, float* scr, int item, int lane) {
;     ...
;   for (int i = 0; i < 8; ++i) v[i] = __builtin_nontemporal_load((const f32x4*)(W + (size_t)(k0 + i * 8 + (lane >> 3)) * N + n0 + (lane & 7) * 4));
; #pragma unroll
;   for (int i = 0; i < 8; ++i) { float* d = scr + (i * 8 + (lane >> 3)) * 33 + (lane & 7) * 4; d[0] = v[i].x; d[1] = v[i].y; d[2] = v[i].z; d[3] = v[i].w; }
;   __builtin_amdgcn_wave_barrier(); asm volatile("s_waitcnt lgkmcnt(0)" ::: "memory");
;   const int c = lane & 7;
; #pragma unroll
;   for (int j = 0; j < 4; ++j) { const int nl = (lane >> 3) + 8 * j, n = n0 + nl; const float* s = scr + (8 * c) * 33 + nl;
;     u32x4 o; o.x = pk2(s[0 * 33], s[1 * 33]); o.y = pk2(s[2 * 33], s[3 * 33]); o.z = pk2(s[4 * 33], s[5 * 33]); o.w = pk2(s[6 * 33], s[7 * 33]);
;     const int row = n + (n >> 7) * rstep + roff;
;     __builtin_nontemporal_store(o, (u32x4*)(WT + (size_t)row * K + k0 + 8 * c)); }
.LBB0_1200:
	s_andn2_b64 vcc, exec, s[6:7]
	s_cbranch_vccnz .LBB0_1202
	s_waitcnt lgkmcnt(0)
	s_add_u32 s21, s50, s14
	s_addc_u32 s23, s51, s15
	s_add_u32 s7, s70, s14
	s_addc_u32 s19, s71, s15
	s_lshl_b32 s6, s17, 2
	s_and_b32 s20, s6, 0x7c0
	s_and_b32 s6, s18, 0x1e0
	s_lshl_b32 s22, s6, 2
	v_add_u32_e32 v4, s20, v1
	s_add_u32 s22, s21, s22
	s_addc_u32 s23, s23, 0
	v_lshlrev_b32_e32 v96, 2, v0
	v_ashrrev_i32_e32 v5, 31, v4
	v_lshl_add_u64 v[12:13], s[22:23], 0, v[96:97]
	v_lshlrev_b64 v[4:5], 11, v[4:5]
	v_lshl_add_u64 v[4:5], v[12:13], 0, v[4:5]
	s_movk_i32 s21, 0x4000
	v_add_co_u32_e32 v16, vcc, s21, v4
	s_mov_b32 s21, 0x8000
	s_nop 0
	v_addc_co_u32_e32 v17, vcc, 0, v5, vcc
	global_load_dwordx4 v[12:15], v[4:5], off nt
	v_add_co_u32_e32 v20, vcc, s21, v4
	global_load_dwordx4 v[16:19], v[16:17], off nt
	s_nop 0
	v_addc_co_u32_e32 v21, vcc, 0, v5, vcc
	s_mov_b32 s21, 0xc000
	global_load_dwordx4 v[20:23], v[20:21], off nt
	v_add_co_u32_e32 v24, vcc, s21, v4
	s_mov_b32 s21, 0x10000
	s_nop 0
	v_addc_co_u32_e32 v25, vcc, 0, v5, vcc
	global_load_dwordx4 v[24:27], v[24:25], off nt
	v_add_co_u32_e32 v28, vcc, s21, v4
	s_mov_b32 s21, 0x14000
	s_nop 0
	v_addc_co_u32_e32 v29, vcc, 0, v5, vcc
	global_load_dwordx4 v[28:31], v[28:29], off nt
	v_add_co_u32_e32 v32, vcc, s21, v4
	s_lshl_b32 s20, s20, 1
	s_nop 0
	v_addc_co_u32_e32 v33, vcc, 0, v5, vcc
	global_load_dwordx4 v[32:35], v[32:33], off nt
	v_add_co_u32_e32 v36, vcc, s93, v4
	v_add_u32_e32 v11, s6, v1
	s_nop 0
	v_addc_co_u32_e32 v37, vcc, 0, v5, vcc
	global_load_dwordx4 v[36:39], v[36:37], off nt
	v_add_co_u32_e32 v4, vcc, s96, v4
	s_add_u32 s20, s7, s20
	s_nop 0
	v_addc_co_u32_e32 v5, vcc, 0, v5, vcc
	global_load_dwordx4 v[40:43], v[4:5], off nt
	v_add_u32_e32 v4, v3, v6
	v_add_u32_e32 v5, 0x420, v4
	s_movk_i32 s7, 0x80
	s_addc_u32 s21, s19, 0
	v_lshlrev_b32_e32 v96, 1, v2
	s_waitcnt vmcnt(0)
	ds_write2_b32 v4, v12, v13 offset1:1
	ds_write2_b32 v4, v14, v15 offset0:2 offset1:3
	ds_write2_b32 v5, v16, v17 offset1:1
	v_add_u32_e32 v5, 0x428, v4
	ds_write2_b32 v5, v18, v19 offset1:1
	v_add_u32_e32 v5, 0x840, v4
	ds_write2_b32 v5, v20, v21 offset1:1
	v_add_u32_e32 v5, 0x848, v4
	ds_write2_b32 v5, v22, v23 offset1:1
	v_add_u32_e32 v5, 0xc60, v4
	ds_write2_b32 v5, v24, v25 offset1:1
	v_add_u32_e32 v5, 0xc68, v4
	ds_write2_b32 v5, v26, v27 offset1:1
	v_add_u32_e32 v5, 0x1080, v4
	ds_write2_b32 v5, v28, v29 offset1:1
	v_add_u32_e32 v5, 0x1088, v4
	ds_write2_b32 v5, v30, v31 offset1:1
	v_add_u32_e32 v5, 0x14a0, v4
	ds_write2_b32 v5, v32, v33 offset1:1
	v_add_u32_e32 v5, 0x14a8, v4
	ds_write2_b32 v5, v34, v35 offset1:1
	v_add_u32_e32 v5, 0x18c0, v4
	ds_write2_b32 v5, v36, v37 offset1:1
	v_add_u32_e32 v5, 0x18c8, v4
	ds_write2_b32 v5, v38, v39 offset1:1
	v_add_u32_e32 v5, 0x1ce0, v4
	v_add_u32_e32 v4, 0x1ce8, v4
	ds_write2_b32 v5, v40, v41 offset1:1
	ds_write2_b32 v4, v42, v43 offset1:1
	s_waitcnt lgkmcnt(0)
	ds_read2_b32 v[214:215], v10 offset1:33
	ds_read2_b32 v[222:223], v10 offset0:66 offset1:99
	ds_read2_b32 v[224:225], v10 offset0:132 offset1:165
	ds_read2_b32 v[226:227], v10 offset0:198 offset1:231
	ds_read2_b32 v[228:229], v10 offset0:8 offset1:41
	ds_read2_b32 v[230:231], v10 offset0:74 offset1:107
	ds_read2_b32 v[232:233], v10 offset0:140 offset1:173
	ds_read2_b32 v[234:235], v10 offset0:206 offset1:239
	s_waitcnt lgkmcnt(0)
	ds_read2_b32 v[236:237], v10 offset0:16 offset1:49
	ds_read2_b32 v[238:239], v10 offset0:82 offset1:115
	ds_read2_b32 v[240:241], v10 offset0:148 offset1:181
	ds_read2_b32 v[242:243], v10 offset0:214 offset1:247
	ds_read2_b32 v[244:245], v10 offset0:24 offset1:57
	ds_read2_b32 v[246:247], v10 offset0:90 offset1:123
	ds_read2_b32 v[248:249], v10 offset0:156 offset1:189
	ds_read2_b32 v[250:251], v10 offset0:222 offset1:255
	v_cvt_pk_bf16_f32 v12, v214, v215
	v_cvt_pk_bf16_f32 v13, v222, v223
	v_cvt_pk_bf16_f32 v14, v224, v225
	v_cvt_pk_bf16_f32 v15, v226, v227
	v_and_b32_e32 v16, 0xffffff80, v11
	v_add3_u32 v16, v11, v16, s7
	v_ashrrev_i32_e32 v17, 31, v16
	v_lshl_add_u64 v[4:5], s[20:21], 0, v[96:97]
	v_lshlrev_b64 v[16:17], 12, v[16:17]
	v_lshl_add_u64 v[16:17], v[4:5], 0, v[16:17]
	global_store_dwordx4 v[16:17], v[12:15], off nt
	s_nop 1
	v_add_u32_e32 v11, s6, v7
	v_cvt_pk_bf16_f32 v12, v228, v229
	v_cvt_pk_bf16_f32 v13, v230, v231
	v_cvt_pk_bf16_f32 v14, v232, v233
	v_cvt_pk_bf16_f32 v15, v234, v235
	v_and_b32_e32 v16, 0xffffff80, v11
	v_add3_u32 v16, v11, v16, s7
	v_ashrrev_i32_e32 v17, 31, v16
	v_lshlrev_b64 v[16:17], 12, v[16:17]
	v_lshl_add_u64 v[16:17], v[4:5], 0, v[16:17]
	global_store_dwordx4 v[16:17], v[12:15], off nt
	s_nop 1
	s_waitcnt lgkmcnt(0)
	v_add_u32_e32 v11, s6, v8
	v_cvt_pk_bf16_f32 v12, v236, v237
	v_cvt_pk_bf16_f32 v13, v238, v239
	v_cvt_pk_bf16_f32 v14, v240, v241
	v_cvt_pk_bf16_f32 v15, v242, v243
	v_and_b32_e32 v16, 0xffffff80, v11
	v_add3_u32 v16, v11, v16, s7
	v_ashrrev_i32_e32 v17, 31, v16
	v_lshlrev_b64 v[16:17], 12, v[16:17]
	v_lshl_add_u64 v[16:17], v[4:5], 0, v[16:17]
	global_store_dwordx4 v[16:17], v[12:15], off nt
	s_nop 1
	v_add_u32_e32 v11, s6, v9
	v_cvt_pk_bf16_f32 v12, v244, v245
	v_cvt_pk_bf16_f32 v13, v246, v247
	v_cvt_pk_bf16_f32 v14, v248, v249
	v_cvt_pk_bf16_f32 v15, v250, v251
	v_and_b32_e32 v16, 0xffffff80, v11
	v_add3_u32 v16, v11, v16, s7
	v_ashrrev_i32_e32 v17, 31, v16
	v_lshlrev_b64 v[16:17], 12, v[16:17]
	v_lshl_add_u64 v[4:5], v[4:5], 0, v[16:17]
	global_store_dwordx4 v[4:5], v[12:15], off nt
	s_nop 1
	s_waitcnt lgkmcnt(0)

; __device__ __forceinline__ unsigned pk2(float lo, float hi) { unsigned r; asm volatile("v_cvt_pk_bf16_f32 %0, %1, %2" : "=v"(r) : "v"(lo), "v"(hi)); return r; }
; __device__ __forceinline__ void transpose_item(const float* W, int K, int N, bf16_t* WT, int rstep, int roff, float* scr, int item, int lane) {
;     ...
;   for (int i = 0; i < 8; ++i) v[i] = __builtin_nontemporal_load((const f32x4*)(W + (size_t)(k0 + i * 8 + (lane >> 3)) * N + n0 + (lane & 7) * 4));
; #pragma unroll
;   for (int i = 0; i < 8; ++i) { float* d = scr + (i * 8 + (lane >> 3)) * 33 + (lane & 7) * 4; d[0] = v[i].x; d[1] = v[i].y; d[2] = v[i].z; d[3] = v[i].w; }
;   __builtin_amdgcn_wave_barrier(); asm volatile("s_waitcnt lgkmcnt(0)" ::: "memory");
;   const int c = lane & 7;
; #pragma unroll
;   for (int j = 0; j < 4; ++j) { const int nl = (lane >> 3) + 8 * j, n = n0 + nl; const float* s = scr + (8 * c) * 33 + nl;
;     u32x4 o; o.x = pk2(s[0 * 33], s[1 * 33]); o.y = pk2(s[2 * 33], s[3 * 33]); o.z = pk2(s[4 * 33], s[5 * 33]); o.w = pk2(s[6 * 33], s[7 * 33]);
;     const int row = n + (n >> 7) * rstep + roff;
;     __builtin_nontemporal_store(o, (u32x4*)(WT + (size_t)row * K + k0 + 8 * c)); }
.LBB0_1203:
	s_waitcnt lgkmcnt(0)
	s_add_u32 s19, s48, s14
	s_addc_u32 s20, s49, s15
	s_add_u32 s7, s70, s14
	s_addc_u32 s14, s71, s15
	s_lshl_b32 s6, s17, 2
	s_and_b32 s15, s6, 0x7c0
	s_and_b32 s6, s18, 0x1e0
	s_lshl_b32 s17, s6, 2
	v_add_u32_e32 v4, s15, v1
	s_add_u32 s18, s19, s17
	s_addc_u32 s19, s20, 0
	v_lshlrev_b32_e32 v96, 2, v0
	v_ashrrev_i32_e32 v5, 31, v4
	v_lshl_add_u64 v[12:13], s[18:19], 0, v[96:97]
	v_lshlrev_b64 v[4:5], 11, v[4:5]
	v_lshl_add_u64 v[4:5], v[12:13], 0, v[4:5]
	s_movk_i32 s17, 0x4000
	v_add_co_u32_e32 v16, vcc, s17, v4
	s_mov_b32 s17, 0x8000
	s_nop 0
	v_addc_co_u32_e32 v17, vcc, 0, v5, vcc
	global_load_dwordx4 v[12:15], v[4:5], off nt
	v_add_co_u32_e32 v20, vcc, s17, v4
	global_load_dwordx4 v[16:19], v[16:17], off nt
	s_nop 0
	v_addc_co_u32_e32 v21, vcc, 0, v5, vcc
	s_mov_b32 s17, 0xc000
	global_load_dwordx4 v[20:23], v[20:21], off nt
	v_add_co_u32_e32 v24, vcc, s17, v4
	s_mov_b32 s17, 0x10000
	s_nop 0
	v_addc_co_u32_e32 v25, vcc, 0, v5, vcc
	global_load_dwordx4 v[24:27], v[24:25], off nt
	v_add_co_u32_e32 v28, vcc, s17, v4
	s_mov_b32 s17, 0x14000
	s_nop 0
	v_addc_co_u32_e32 v29, vcc, 0, v5, vcc
	global_load_dwordx4 v[28:31], v[28:29], off nt
	v_add_co_u32_e32 v32, vcc, s17, v4
	v_add_u32_e32 v11, s6, v1
	s_nop 0
	v_addc_co_u32_e32 v33, vcc, 0, v5, vcc
	global_load_dwordx4 v[32:35], v[32:33], off nt
	v_add_co_u32_e32 v36, vcc, s93, v4
	s_lshl_b32 s15, s15, 1
	s_nop 0
	v_addc_co_u32_e32 v37, vcc, 0, v5, vcc
	global_load_dwordx4 v[36:39], v[36:37], off nt
	v_add_co_u32_e32 v4, vcc, s96, v4
	s_add_u32 s18, s7, s15
	s_nop 0
	v_addc_co_u32_e32 v5, vcc, 0, v5, vcc
	global_load_dwordx4 v[40:43], v[4:5], off nt
	v_add_u32_e32 v4, v3, v6
	v_add_u32_e32 v5, 0x420, v4
	s_addc_u32 s19, s14, 0
	v_lshlrev_b32_e32 v96, 1, v2
	s_waitcnt vmcnt(0)
	ds_write2_b32 v4, v12, v13 offset1:1
	ds_write2_b32 v4, v14, v15 offset0:2 offset1:3
	ds_write2_b32 v5, v16, v17 offset1:1
	v_add_u32_e32 v5, 0x428, v4
	ds_write2_b32 v5, v18, v19 offset1:1
	v_add_u32_e32 v5, 0x840, v4
	ds_write2_b32 v5, v20, v21 offset1:1
	v_add_u32_e32 v5, 0x848, v4
	ds_write2_b32 v5, v22, v23 offset1:1
	v_add_u32_e32 v5, 0xc60, v4
	ds_write2_b32 v5, v24, v25 offset1:1
	v_add_u32_e32 v5, 0xc68, v4
	ds_write2_b32 v5, v26, v27 offset1:1
	v_add_u32_e32 v5, 0x1080, v4
	ds_write2_b32 v5, v28, v29 offset1:1
	v_add_u32_e32 v5, 0x1088, v4
	ds_write2_b32 v5, v30, v31 offset1:1
	v_add_u32_e32 v5, 0x14a0, v4
	ds_write2_b32 v5, v32, v33 offset1:1
	v_add_u32_e32 v5, 0x14a8, v4
	ds_write2_b32 v5, v34, v35 offset1:1
	v_add_u32_e32 v5, 0x18c0, v4
	ds_write2_b32 v5, v36, v37 offset1:1
	v_add_u32_e32 v5, 0x18c8, v4
	ds_write2_b32 v5, v38, v39 offset1:1
	v_add_u32_e32 v5, 0x1ce0, v4
	v_add_u32_e32 v4, 0x1ce8, v4
	ds_write2_b32 v5, v40, v41 offset1:1
	ds_write2_b32 v4, v42, v43 offset1:1
	s_waitcnt lgkmcnt(0)
	ds_read2_b32 v[214:215], v10 offset1:33
	ds_read2_b32 v[222:223], v10 offset0:66 offset1:99
	ds_read2_b32 v[224:225], v10 offset0:132 offset1:165
	ds_read2_b32 v[226:227], v10 offset0:198 offset1:231
	ds_read2_b32 v[228:229], v10 offset0:8 offset1:41
	ds_read2_b32 v[230:231], v10 offset0:74 offset1:107
	ds_read2_b32 v[232:233], v10 offset0:140 offset1:173
	ds_read2_b32 v[234:235], v10 offset0:206 offset1:239
	s_waitcnt lgkmcnt(0)
	ds_read2_b32 v[236:237], v10 offset0:16 offset1:49
	ds_read2_b32 v[238:239], v10 offset0:82 offset1:115
	ds_read2_b32 v[240:241], v10 offset0:148 offset1:181
	ds_read2_b32 v[242:243], v10 offset0:214 offset1:247
	ds_read2_b32 v[244:245], v10 offset0:24 offset1:57
	ds_read2_b32 v[246:247], v10 offset0:90 offset1:123
	ds_read2_b32 v[248:249], v10 offset0:156 offset1:189
	ds_read2_b32 v[250:251], v10 offset0:222 offset1:255
	v_cvt_pk_bf16_f32 v12, v214, v215
	v_cvt_pk_bf16_f32 v13, v222, v223
	v_cvt_pk_bf16_f32 v14, v224, v225
	v_cvt_pk_bf16_f32 v15, v226, v227
	v_and_b32_e32 v16, 0xffffff80, v11
	v_add_u32_e32 v16, v16, v11
	v_ashrrev_i32_e32 v17, 31, v16
	v_lshl_add_u64 v[4:5], s[18:19], 0, v[96:97]
	v_lshlrev_b64 v[16:17], 12, v[16:17]
	v_lshl_add_u64 v[16:17], v[4:5], 0, v[16:17]
	global_store_dwordx4 v[16:17], v[12:15], off nt
	s_nop 1
	v_add_u32_e32 v11, s6, v7
	v_cvt_pk_bf16_f32 v12, v228, v229
	v_cvt_pk_bf16_f32 v13, v230, v231
	v_cvt_pk_bf16_f32 v14, v232, v233
	v_cvt_pk_bf16_f32 v15, v234, v235
	v_and_b32_e32 v16, 0xffffff80, v11
	v_add_u32_e32 v16, v16, v11
	v_ashrrev_i32_e32 v17, 31, v16
	v_lshlrev_b64 v[16:17], 12, v[16:17]
	v_lshl_add_u64 v[16:17], v[4:5], 0, v[16:17]
	global_store_dwordx4 v[16:17], v[12:15], off nt
	s_nop 1
	s_waitcnt lgkmcnt(0)
	v_add_u32_e32 v11, s6, v8
	v_cvt_pk_bf16_f32 v12, v236, v237
	v_cvt_pk_bf16_f32 v13, v238, v239
	v_cvt_pk_bf16_f32 v14, v240, v241
	v_cvt_pk_bf16_f32 v15, v242, v243
	v_and_b32_e32 v16, 0xffffff80, v11
	v_add_u32_e32 v16, v16, v11
	v_ashrrev_i32_e32 v17, 31, v16
	v_lshlrev_b64 v[16:17], 12, v[16:17]
	v_lshl_add_u64 v[16:17], v[4:5], 0, v[16:17]
	global_store_dwordx4 v[16:17], v[12:15], off nt
	s_nop 1
	v_add_u32_e32 v11, s6, v9
	v_cvt_pk_bf16_f32 v12, v244, v245
	v_cvt_pk_bf16_f32 v13, v246, v247
	v_cvt_pk_bf16_f32 v14, v248, v249
	v_cvt_pk_bf16_f32 v15, v250, v251
	v_and_b32_e32 v16, 0xffffff80, v11
	v_add_u32_e32 v16, v16, v11
	v_ashrrev_i32_e32 v17, 31, v16
	v_lshlrev_b64 v[16:17], 12, v[16:17]
	v_lshl_add_u64 v[4:5], v[4:5], 0, v[16:17]
	global_store_dwordx4 v[4:5], v[12:15], off nt
	s_nop 1
	s_waitcnt lgkmcnt(0)
	s_branch .LBB0_1195

; __device__ __forceinline__ unsigned pk2(float lo, float hi) { unsigned r; asm volatile("v_cvt_pk_bf16_f32 %0, %1, %2" : "=v"(r) : "v"(lo), "v"(hi)); return r; }
; __device__ __forceinline__ void transpose_item(const float* W, int K, int N, bf16_t* WT, int rstep, int roff, float* scr, int item, int lane) {
;     ...
;   for (int i = 0; i < 8; ++i) v[i] = __builtin_nontemporal_load((const f32x4*)(W + (size_t)(k0 + i * 8 + (lane >> 3)) * N + n0 + (lane & 7) * 4));
; #pragma unroll
;   for (int i = 0; i < 8; ++i) { float* d = scr + (i * 8 + (lane >> 3)) * 33 + (lane & 7) * 4; d[0] = v[i].x; d[1] = v[i].y; d[2] = v[i].z; d[3] = v[i].w; }
;   __builtin_amdgcn_wave_barrier(); asm volatile("s_waitcnt lgkmcnt(0)" ::: "memory");
;   const int c = lane & 7;
; #pragma unroll
;   for (int j = 0; j < 4; ++j) { const int nl = (lane >> 3) + 8 * j, n = n0 + nl; const float* s = scr + (8 * c) * 33 + nl;
;     u32x4 o; o.x = pk2(s[0 * 33], s[1 * 33]); o.y = pk2(s[2 * 33], s[3 * 33]); o.z = pk2(s[4 * 33], s[5 * 33]); o.w = pk2(s[6 * 33], s[7 * 33]);
;     const int row = n + (n >> 7) * rstep + roff;
;     __builtin_nontemporal_store(o, (u32x4*)(WT + (size_t)row * K + k0 + 8 * c)); }
; __device__ __forceinline__ void convert_item(const P& p, int it, float* scr, int lane) {
;     ...
;     const int idx = it - IT_DENSE, m = idx / IT_EXP, sub = idx % IT_EXP, le = m / 3, which = m % 3;
;     if (which == 0) transpose_item(p.wg + (size_t)le * DM * EFF, DM, EFF, WSP(bf16_t, WS_WGU) + (size_t)le * 1024 * DM, 128, 0, scr, sub, lane);
;     else if (which == 1) transpose_item(p.wu + (size_t)le * DM * EFF, DM, EFF, WSP(bf16_t, WS_WGU) + (size_t)le * 1024 * DM, 128, 128, scr, sub, lane);
;     else transpose_item(p.wd + (size_t)le * EFF * DM, EFF, DM, WSP(bf16_t, WS_WD) + (size_t)le * DM * EFF, 0, 0, scr, sub, lane);
.LBB0_1223:
	s_cmpk_gt_i32 s19, 0x3fff
	s_mov_b64 s[6:7], -1
	s_cbranch_scc0 .LBB0_1233
	s_add_i32 s6, s19, 0xffffc000
	s_lshr_b32 s7, s6, 9
	s_mul_hi_u32 s6, s6, 0xaaaaaaab
	s_lshr_b32 s64, s6, 10
	s_mul_hi_u32 s6, s7, 0x55555556
	s_mul_i32 s6, s6, 3
	s_and_b32 s20, s19, 0x1ff
	s_sub_i32 s22, s7, s6
	s_lshl_b64 s[12:13], s[64:65], 22
	s_lshl_b32 s21, s19, 5
	s_cmp_lt_i32 s22, 1
	s_mov_b64 s[6:7], -1
	s_cbranch_scc1 .LBB0_1230
	s_cmp_lg_u32 s22, 1
	s_cbranch_scc0 .LBB0_1227
	s_waitcnt lgkmcnt(0)
	s_add_u32 s24, s0, s12
	s_addc_u32 s31, s1, s13
	s_lshl_b64 s[22:23], s[64:65], 21
	s_add_u32 s7, s5, s22
	s_addc_u32 s22, s9, s23
	s_and_b32 s6, s21, 0x7e0
	s_and_b32 s23, s19, 0x1c0
	s_lshl_b32 s30, s6, 2
	v_add_u32_e32 v4, s23, v1
	s_add_u32 s30, s24, s30
	s_addc_u32 s31, s31, 0
	v_lshlrev_b32_e32 v96, 2, v0
	v_ashrrev_i32_e32 v5, 31, v4
	v_lshl_add_u64 v[12:13], s[30:31], 0, v[96:97]
	v_lshlrev_b64 v[4:5], 13, v[4:5]
	v_lshl_add_u64 v[4:5], v[12:13], 0, v[4:5]
	s_mov_b32 s24, 0x10000
	v_add_co_u32_e32 v16, vcc, s24, v4
	s_mov_b32 s24, 0x20000
	s_nop 0
	v_addc_co_u32_e32 v17, vcc, 0, v5, vcc
	global_load_dwordx4 v[12:15], v[4:5], off nt
	v_add_co_u32_e32 v20, vcc, s24, v4
	global_load_dwordx4 v[16:19], v[16:17], off nt
	s_nop 0
	v_addc_co_u32_e32 v21, vcc, 0, v5, vcc
	s_mov_b32 s24, 0x30000
	global_load_dwordx4 v[20:23], v[20:21], off nt
	v_add_co_u32_e32 v24, vcc, s24, v4
	s_mov_b32 s24, 0x40000
	s_nop 0
	v_addc_co_u32_e32 v25, vcc, 0, v5, vcc
	global_load_dwordx4 v[24:27], v[24:25], off nt
	v_add_co_u32_e32 v28, vcc, s24, v4
	s_mov_b32 s24, 0x50000
	s_nop 0
	v_addc_co_u32_e32 v29, vcc, 0, v5, vcc
	global_load_dwordx4 v[28:31], v[28:29], off nt
	v_add_co_u32_e32 v32, vcc, s24, v4
	s_mov_b32 s24, 0x60000
	s_nop 0
	v_addc_co_u32_e32 v33, vcc, 0, v5, vcc
	global_load_dwordx4 v[32:35], v[32:33], off nt
	v_add_co_u32_e32 v36, vcc, s24, v4
	s_mov_b32 s24, 0x70000
	s_nop 0
	v_addc_co_u32_e32 v37, vcc, 0, v5, vcc
	global_load_dwordx4 v[36:39], v[36:37], off nt
	v_add_co_u32_e32 v4, vcc, s24, v4
	s_lshl_b32 s23, s23, 1
	s_nop 0
	v_addc_co_u32_e32 v5, vcc, 0, v5, vcc
	global_load_dwordx4 v[40:43], v[4:5], off nt
	v_add_u32_e32 v4, v3, v6
	v_add_u32_e32 v5, 0x420, v4
	s_add_u32 s30, s7, s23
	s_addc_u32 s31, s22, 0
	v_lshlrev_b32_e32 v96, 1, v2
	s_waitcnt vmcnt(7)
	ds_write2_b32 v4, v12, v13 offset1:1
	ds_write2_b32 v4, v14, v15 offset0:2 offset1:3
	s_waitcnt vmcnt(6)
	ds_write2_b32 v5, v16, v17 offset1:1
	v_add_u32_e32 v5, 0x428, v4
	ds_write2_b32 v5, v18, v19 offset1:1
	v_add_u32_e32 v5, 0x840, v4
	s_waitcnt vmcnt(5)
	ds_write2_b32 v5, v20, v21 offset1:1
	v_add_u32_e32 v5, 0x848, v4
	ds_write2_b32 v5, v22, v23 offset1:1
	v_add_u32_e32 v5, 0xc60, v4
	v_add_u32_e32 v16, s6, v1
	v_ashrrev_i32_e32 v17, 31, v16
	s_waitcnt vmcnt(4)
	ds_write2_b32 v5, v24, v25 offset1:1
	v_add_u32_e32 v5, 0xc68, v4
	ds_write2_b32 v5, v26, v27 offset1:1
	v_add_u32_e32 v5, 0x1080, v4
	v_lshlrev_b64 v[16:17], 10, v[16:17]
	s_waitcnt vmcnt(3)
	ds_write2_b32 v5, v28, v29 offset1:1
	v_add_u32_e32 v5, 0x1088, v4
	ds_write2_b32 v5, v30, v31 offset1:1
	v_add_u32_e32 v5, 0x14a0, v4
	s_waitcnt vmcnt(2)
	ds_write2_b32 v5, v32, v33 offset1:1
	v_add_u32_e32 v5, 0x14a8, v4
	ds_write2_b32 v5, v34, v35 offset1:1
	v_add_u32_e32 v5, 0x18c0, v4
	s_waitcnt vmcnt(1)
	ds_write2_b32 v5, v36, v37 offset1:1
	v_add_u32_e32 v5, 0x18c8, v4
	ds_write2_b32 v5, v38, v39 offset1:1
	v_add_u32_e32 v5, 0x1ce0, v4
	v_add_u32_e32 v4, 0x1ce8, v4
	s_waitcnt vmcnt(0)
	ds_write2_b32 v5, v40, v41 offset1:1
	ds_write2_b32 v4, v42, v43 offset1:1
	s_waitcnt lgkmcnt(0)
	ds_read2_b32 v[214:215], v10 offset1:33
	ds_read2_b32 v[222:223], v10 offset0:66 offset1:99
	ds_read2_b32 v[224:225], v10 offset0:132 offset1:165
	ds_read2_b32 v[226:227], v10 offset0:198 offset1:231
	ds_read2_b32 v[228:229], v10 offset0:8 offset1:41
	ds_read2_b32 v[230:231], v10 offset0:74 offset1:107
	ds_read2_b32 v[232:233], v10 offset0:140 offset1:173
	ds_read2_b32 v[234:235], v10 offset0:206 offset1:239
	s_waitcnt lgkmcnt(0)
	ds_read2_b32 v[236:237], v10 offset0:16 offset1:49
	ds_read2_b32 v[238:239], v10 offset0:82 offset1:115
	ds_read2_b32 v[240:241], v10 offset0:148 offset1:181
	ds_read2_b32 v[242:243], v10 offset0:214 offset1:247
	ds_read2_b32 v[244:245], v10 offset0:24 offset1:57
	ds_read2_b32 v[246:247], v10 offset0:90 offset1:123
	ds_read2_b32 v[248:249], v10 offset0:156 offset1:189
	ds_read2_b32 v[250:251], v10 offset0:222 offset1:255
	v_lshl_add_u64 v[4:5], s[30:31], 0, v[96:97]
	v_cvt_pk_bf16_f32 v12, v214, v215
	v_cvt_pk_bf16_f32 v13, v222, v223
	v_lshl_add_u64 v[16:17], v[4:5], 0, v[16:17]
	v_cvt_pk_bf16_f32 v14, v224, v225
	v_cvt_pk_bf16_f32 v15, v226, v227
	global_store_dwordx4 v[16:17], v[12:15], off nt
	s_nop 1
	v_add_u32_e32 v16, s6, v7
	v_ashrrev_i32_e32 v17, 31, v16
	v_cvt_pk_bf16_f32 v12, v228, v229
	v_lshlrev_b64 v[16:17], 10, v[16:17]
	v_cvt_pk_bf16_f32 v13, v230, v231
	v_lshl_add_u64 v[16:17], v[4:5], 0, v[16:17]
	v_cvt_pk_bf16_f32 v14, v232, v233
	v_cvt_pk_bf16_f32 v15, v234, v235
	global_store_dwordx4 v[16:17], v[12:15], off nt
	s_nop 1
	v_add_u32_e32 v16, s6, v8
	s_waitcnt lgkmcnt(0)
	v_ashrrev_i32_e32 v17, 31, v16
	v_cvt_pk_bf16_f32 v12, v236, v237
	v_lshlrev_b64 v[16:17], 10, v[16:17]
	v_cvt_pk_bf16_f32 v13, v238, v239
	v_lshl_add_u64 v[16:17], v[4:5], 0, v[16:17]
	v_cvt_pk_bf16_f32 v14, v240, v241
	v_cvt_pk_bf16_f32 v15, v242, v243
	global_store_dwordx4 v[16:17], v[12:15], off nt
	s_nop 1
	v_add_u32_e32 v16, s6, v9
	v_ashrrev_i32_e32 v17, 31, v16
	v_cvt_pk_bf16_f32 v12, v244, v245
	v_lshlrev_b64 v[16:17], 10, v[16:17]
	v_cvt_pk_bf16_f32 v13, v246, v247
	v_lshl_add_u64 v[4:5], v[4:5], 0, v[16:17]
	v_cvt_pk_bf16_f32 v14, v248, v249
	v_cvt_pk_bf16_f32 v15, v250, v251
	global_store_dwordx4 v[4:5], v[12:15], off nt
	s_nop 1
	s_waitcnt lgkmcnt(0)
	s_mov_b64 s[6:7], 0
; __device__ __forceinline__ unsigned pk2(float lo, float hi) { unsigned r; asm volatile("v_cvt_pk_bf16_f32 %0, %1, %2" : "=v"(r) : "v"(lo), "v"(hi)); return r; }
; __device__ __forceinline__ void transpose_item(const float* W, int K, int N, bf16_t* WT, int rstep, int roff, float* scr, int item, int lane) {
;     ...
;   for (int i = 0; i < 8; ++i) v[i] = __builtin_nontemporal_load((const f32x4*)(W + (size_t)(k0 + i * 8 + (lane >> 3)) * N + n0 + (lane & 7) * 4));
; #pragma unroll
;   for (int i = 0; i < 8; ++i) { float* d = scr + (i * 8 + (lane >> 3)) * 33 + (lane & 7) * 4; d[0] = v[i].x; d[1] = v[i].y; d[2] = v[i].z; d[3] = v[i].w; }
;   __builtin_amdgcn_wave_barrier(); asm volatile("s_waitcnt lgkmcnt(0)" ::: "memory");
;   const int c = lane & 7;
; #pragma unroll
;   for (int j = 0; j < 4; ++j) { const int nl = (lane >> 3) + 8 * j, n = n0 + nl; const float* s = scr + (8 * c) * 33 + nl;
;     u32x4 o; o.x = pk2(s[0 * 33], s[1 * 33]); o.y = pk2(s[2 * 33], s[3 * 33]); o.z = pk2(s[4 * 33], s[5 * 33]); o.w = pk2(s[6 * 33], s[7 * 33]);
;     const int row = n + (n >> 7) * rstep + roff;
;     __builtin_nontemporal_store(o, (u32x4*)(WT + (size_t)row * K + k0 + 8 * c)); }
.LBB0_1227:
	s_andn2_b64 vcc, exec, s[6:7]
	s_cbranch_vccnz .LBB0_1229
	s_waitcnt lgkmcnt(0)
	s_add_u32 s24, s50, s12
	s_addc_u32 s31, s51, s13
	s_add_u32 s7, s70, s12
	s_addc_u32 s22, s71, s13
	s_lshl_b32 s6, s20, 2
	s_and_b32 s23, s6, 0x7c0
	s_and_b32 s6, s21, 0x1e0
	s_lshl_b32 s30, s6, 2
	v_add_u32_e32 v4, s23, v1
	s_add_u32 s30, s24, s30
	s_addc_u32 s31, s31, 0
	v_lshlrev_b32_e32 v96, 2, v0
	v_ashrrev_i32_e32 v5, 31, v4
	v_lshl_add_u64 v[12:13], s[30:31], 0, v[96:97]
	v_lshlrev_b64 v[4:5], 11, v[4:5]
	v_lshl_add_u64 v[4:5], v[12:13], 0, v[4:5]
	s_movk_i32 s24, 0x4000
	v_add_co_u32_e32 v16, vcc, s24, v4
	s_mov_b32 s24, 0x8000
	s_nop 0
	v_addc_co_u32_e32 v17, vcc, 0, v5, vcc
	global_load_dwordx4 v[12:15], v[4:5], off nt
	v_add_co_u32_e32 v20, vcc, s24, v4
	global_load_dwordx4 v[16:19], v[16:17], off nt
	s_nop 0
	v_addc_co_u32_e32 v21, vcc, 0, v5, vcc
	s_mov_b32 s24, 0xc000
	global_load_dwordx4 v[20:23], v[20:21], off nt
	v_add_co_u32_e32 v24, vcc, s24, v4
	s_mov_b32 s24, 0x10000
	s_nop 0
	v_addc_co_u32_e32 v25, vcc, 0, v5, vcc
	global_load_dwordx4 v[24:27], v[24:25], off nt
	v_add_co_u32_e32 v28, vcc, s24, v4
	s_mov_b32 s24, 0x14000
	s_nop 0
	v_addc_co_u32_e32 v29, vcc, 0, v5, vcc
	global_load_dwordx4 v[28:31], v[28:29], off nt
	v_add_co_u32_e32 v32, vcc, s24, v4
	s_lshl_b32 s23, s23, 1
	s_nop 0
	v_addc_co_u32_e32 v33, vcc, 0, v5, vcc
	global_load_dwordx4 v[32:35], v[32:33], off nt
	v_add_co_u32_e32 v36, vcc, s93, v4
	v_add_u32_e32 v11, s6, v1
	s_nop 0
	v_addc_co_u32_e32 v37, vcc, 0, v5, vcc
	global_load_dwordx4 v[36:39], v[36:37], off nt
	v_add_co_u32_e32 v4, vcc, s96, v4
	s_add_u32 s30, s7, s23
	s_nop 0
	v_addc_co_u32_e32 v5, vcc, 0, v5, vcc
	global_load_dwordx4 v[40:43], v[4:5], off nt
	v_add_u32_e32 v4, v3, v6
	v_add_u32_e32 v5, 0x420, v4
	s_movk_i32 s7, 0x80
	s_addc_u32 s31, s22, 0
	v_lshlrev_b32_e32 v96, 1, v2
	s_waitcnt vmcnt(7)
	ds_write2_b32 v4, v12, v13 offset1:1
	ds_write2_b32 v4, v14, v15 offset0:2 offset1:3
	s_waitcnt vmcnt(6)
	ds_write2_b32 v5, v16, v17 offset1:1
	v_add_u32_e32 v5, 0x428, v4
	ds_write2_b32 v5, v18, v19 offset1:1
	v_add_u32_e32 v5, 0x840, v4
	s_waitcnt vmcnt(5)
	ds_write2_b32 v5, v20, v21 offset1:1
	v_add_u32_e32 v5, 0x848, v4
	ds_write2_b32 v5, v22, v23 offset1:1
	v_add_u32_e32 v5, 0xc60, v4
	s_waitcnt vmcnt(4)
	ds_write2_b32 v5, v24, v25 offset1:1
	v_add_u32_e32 v5, 0xc68, v4
	ds_write2_b32 v5, v26, v27 offset1:1
	v_add_u32_e32 v5, 0x1080, v4
	s_waitcnt vmcnt(3)
	ds_write2_b32 v5, v28, v29 offset1:1
	v_add_u32_e32 v5, 0x1088, v4
	ds_write2_b32 v5, v30, v31 offset1:1
	v_add_u32_e32 v5, 0x14a0, v4
	s_waitcnt vmcnt(2)
	ds_write2_b32 v5, v32, v33 offset1:1
	v_add_u32_e32 v5, 0x14a8, v4
	ds_write2_b32 v5, v34, v35 offset1:1
	v_add_u32_e32 v5, 0x18c0, v4
	s_waitcnt vmcnt(1)
	ds_write2_b32 v5, v36, v37 offset1:1
	v_add_u32_e32 v5, 0x18c8, v4
	ds_write2_b32 v5, v38, v39 offset1:1
	v_add_u32_e32 v5, 0x1ce0, v4
	v_add_u32_e32 v4, 0x1ce8, v4
	s_waitcnt vmcnt(0)
	ds_write2_b32 v5, v40, v41 offset1:1
	ds_write2_b32 v4, v42, v43 offset1:1
	s_waitcnt lgkmcnt(0)
	ds_read2_b32 v[214:215], v10 offset1:33
	ds_read2_b32 v[222:223], v10 offset0:66 offset1:99
	ds_read2_b32 v[224:225], v10 offset0:132 offset1:165
	ds_read2_b32 v[226:227], v10 offset0:198 offset1:231
	ds_read2_b32 v[228:229], v10 offset0:8 offset1:41
	ds_read2_b32 v[230:231], v10 offset0:74 offset1:107
	ds_read2_b32 v[232:233], v10 offset0:140 offset1:173
	ds_read2_b32 v[234:235], v10 offset0:206 offset1:239
	s_waitcnt lgkmcnt(0)
	ds_read2_b32 v[236:237], v10 offset0:16 offset1:49
	ds_read2_b32 v[238:239], v10 offset0:82 offset1:115
	ds_read2_b32 v[240:241], v10 offset0:148 offset1:181
	ds_read2_b32 v[242:243], v10 offset0:214 offset1:247
	ds_read2_b32 v[244:245], v10 offset0:24 offset1:57
	ds_read2_b32 v[246:247], v10 offset0:90 offset1:123
	ds_read2_b32 v[248:249], v10 offset0:156 offset1:189
	ds_read2_b32 v[250:251], v10 offset0:222 offset1:255
	v_cvt_pk_bf16_f32 v12, v214, v215
	v_cvt_pk_bf16_f32 v13, v222, v223
	v_cvt_pk_bf16_f32 v14, v224, v225
	v_cvt_pk_bf16_f32 v15, v226, v227
	v_and_b32_e32 v16, 0xffffff80, v11
	v_add3_u32 v16, v11, v16, s7
	v_ashrrev_i32_e32 v17, 31, v16
	v_lshl_add_u64 v[4:5], s[30:31], 0, v[96:97]
	v_lshlrev_b64 v[16:17], 12, v[16:17]
	v_lshl_add_u64 v[16:17], v[4:5], 0, v[16:17]
	global_store_dwordx4 v[16:17], v[12:15], off nt
	s_nop 1
	v_add_u32_e32 v11, s6, v7
	v_cvt_pk_bf16_f32 v12, v228, v229
	v_cvt_pk_bf16_f32 v13, v230, v231
	v_cvt_pk_bf16_f32 v14, v232, v233
	v_cvt_pk_bf16_f32 v15, v234, v235
	v_and_b32_e32 v16, 0xffffff80, v11
	v_add3_u32 v16, v11, v16, s7
	v_ashrrev_i32_e32 v17, 31, v16
	v_lshlrev_b64 v[16:17], 12, v[16:17]
	v_lshl_add_u64 v[16:17], v[4:5], 0, v[16:17]
	global_store_dwordx4 v[16:17], v[12:15], off nt
	s_nop 1
	s_waitcnt lgkmcnt(0)
	v_add_u32_e32 v11, s6, v8
	v_cvt_pk_bf16_f32 v12, v236, v237
	v_cvt_pk_bf16_f32 v13, v238, v239
	v_cvt_pk_bf16_f32 v14, v240, v241
	v_cvt_pk_bf16_f32 v15, v242, v243
	v_and_b32_e32 v16, 0xffffff80, v11
	v_add3_u32 v16, v11, v16, s7
	v_ashrrev_i32_e32 v17, 31, v16
	v_lshlrev_b64 v[16:17], 12, v[16:17]
	v_lshl_add_u64 v[16:17], v[4:5], 0, v[16:17]
	global_store_dwordx4 v[16:17], v[12:15], off nt
	s_nop 1
	v_add_u32_e32 v11, s6, v9
	v_cvt_pk_bf16_f32 v12, v244, v245
	v_cvt_pk_bf16_f32 v13, v246, v247
	v_cvt_pk_bf16_f32 v14, v248, v249
	v_cvt_pk_bf16_f32 v15, v250, v251
	v_and_b32_e32 v16, 0xffffff80, v11
	v_add3_u32 v16, v11, v16, s7
	v_ashrrev_i32_e32 v17, 31, v16
	v_lshlrev_b64 v[16:17], 12, v[16:17]
	v_lshl_add_u64 v[4:5], v[4:5], 0, v[16:17]
	global_store_dwordx4 v[4:5], v[12:15], off nt
	s_nop 1
	s_waitcnt lgkmcnt(0)

; __device__ __forceinline__ unsigned pk2(float lo, float hi) { unsigned r; asm volatile("v_cvt_pk_bf16_f32 %0, %1, %2" : "=v"(r) : "v"(lo), "v"(hi)); return r; }
; __device__ __forceinline__ void transpose_item(const float* W, int K, int N, bf16_t* WT, int rstep, int roff, float* scr, int item, int lane) {
;     ...
;   for (int i = 0; i < 8; ++i) v[i] = __builtin_nontemporal_load((const f32x4*)(W + (size_t)(k0 + i * 8 + (lane >> 3)) * N + n0 + (lane & 7) * 4));
; #pragma unroll
;   for (int i = 0; i < 8; ++i) { float* d = scr + (i * 8 + (lane >> 3)) * 33 + (lane & 7) * 4; d[0] = v[i].x; d[1] = v[i].y; d[2] = v[i].z; d[3] = v[i].w; }
;   __builtin_amdgcn_wave_barrier(); asm volatile("s_waitcnt lgkmcnt(0)" ::: "memory");
;   const int c = lane & 7;
; #pragma unroll
;   for (int j = 0; j < 4; ++j) { const int nl = (lane >> 3) + 8 * j, n = n0 + nl; const float* s = scr + (8 * c) * 33 + nl;
;     u32x4 o; o.x = pk2(s[0 * 33], s[1 * 33]); o.y = pk2(s[2 * 33], s[3 * 33]); o.z = pk2(s[4 * 33], s[5 * 33]); o.w = pk2(s[6 * 33], s[7 * 33]);
;     const int row = n + (n >> 7) * rstep + roff;
;     __builtin_nontemporal_store(o, (u32x4*)(WT + (size_t)row * K + k0 + 8 * c)); }
.LBB0_1230:
	s_andn2_b64 vcc, exec, s[6:7]
	s_cbranch_vccnz .LBB0_1232
	s_waitcnt lgkmcnt(0)
	s_add_u32 s22, s48, s12
	s_addc_u32 s23, s49, s13
	s_add_u32 s7, s70, s12
	s_addc_u32 s12, s71, s13
	s_lshl_b32 s6, s20, 2
	s_and_b32 s13, s6, 0x7c0
	s_and_b32 s6, s21, 0x1e0
	s_lshl_b32 s20, s6, 2
	v_add_u32_e32 v4, s13, v1
	s_add_u32 s20, s22, s20
	s_addc_u32 s21, s23, 0
	v_lshlrev_b32_e32 v96, 2, v0
	v_ashrrev_i32_e32 v5, 31, v4
	v_lshl_add_u64 v[12:13], s[20:21], 0, v[96:97]
	v_lshlrev_b64 v[4:5], 11, v[4:5]
	v_lshl_add_u64 v[4:5], v[12:13], 0, v[4:5]
	s_movk_i32 s20, 0x4000
	v_add_co_u32_e32 v16, vcc, s20, v4
	s_mov_b32 s20, 0x8000
	s_nop 0
	v_addc_co_u32_e32 v17, vcc, 0, v5, vcc
	global_load_dwordx4 v[12:15], v[4:5], off nt
	v_add_co_u32_e32 v20, vcc, s20, v4
	global_load_dwordx4 v[16:19], v[16:17], off nt
	s_nop 0
	v_addc_co_u32_e32 v21, vcc, 0, v5, vcc
	s_mov_b32 s20, 0xc000
	global_load_dwordx4 v[20:23], v[20:21], off nt
	v_add_co_u32_e32 v24, vcc, s20, v4
	s_mov_b32 s20, 0x10000
	s_nop 0
	v_addc_co_u32_e32 v25, vcc, 0, v5, vcc
	global_load_dwordx4 v[24:27], v[24:25], off nt
	v_add_co_u32_e32 v28, vcc, s20, v4
	s_mov_b32 s20, 0x14000
	s_nop 0
	v_addc_co_u32_e32 v29, vcc, 0, v5, vcc
	global_load_dwordx4 v[28:31], v[28:29], off nt
	v_add_co_u32_e32 v32, vcc, s20, v4
	v_add_u32_e32 v11, s6, v1
	s_nop 0
	v_addc_co_u32_e32 v33, vcc, 0, v5, vcc
	global_load_dwordx4 v[32:35], v[32:33], off nt
	v_add_co_u32_e32 v36, vcc, s93, v4
	s_lshl_b32 s13, s13, 1
	s_nop 0
	v_addc_co_u32_e32 v37, vcc, 0, v5, vcc
	global_load_dwordx4 v[36:39], v[36:37], off nt
	v_add_co_u32_e32 v4, vcc, s96, v4
	s_add_u32 s20, s7, s13
	s_nop 0
	v_addc_co_u32_e32 v5, vcc, 0, v5, vcc
	global_load_dwordx4 v[40:43], v[4:5], off nt
	v_add_u32_e32 v4, v3, v6
	v_add_u32_e32 v5, 0x420, v4
	s_addc_u32 s21, s12, 0
	v_lshlrev_b32_e32 v96, 1, v2
	s_waitcnt vmcnt(7)
	ds_write2_b32 v4, v12, v13 offset1:1
	ds_write2_b32 v4, v14, v15 offset0:2 offset1:3
	s_waitcnt vmcnt(6)
	ds_write2_b32 v5, v16, v17 offset1:1
	v_add_u32_e32 v5, 0x428, v4
	ds_write2_b32 v5, v18, v19 offset1:1
	v_add_u32_e32 v5, 0x840, v4
	s_waitcnt vmcnt(5)
	ds_write2_b32 v5, v20, v21 offset1:1
	v_add_u32_e32 v5, 0x848, v4
	ds_write2_b32 v5, v22, v23 offset1:1
	v_add_u32_e32 v5, 0xc60, v4
	s_waitcnt vmcnt(4)
	ds_write2_b32 v5, v24, v25 offset1:1
	v_add_u32_e32 v5, 0xc68, v4
	ds_write2_b32 v5, v26, v27 offset1:1
	v_add_u32_e32 v5, 0x1080, v4
	s_waitcnt vmcnt(3)
	ds_write2_b32 v5, v28, v29 offset1:1
	v_add_u32_e32 v5, 0x1088, v4
	ds_write2_b32 v5, v30, v31 offset1:1
	v_add_u32_e32 v5, 0x14a0, v4
	s_waitcnt vmcnt(2)
	ds_write2_b32 v5, v32, v33 offset1:1
	v_add_u32_e32 v5, 0x14a8, v4
	ds_write2_b32 v5, v34, v35 offset1:1
	v_add_u32_e32 v5, 0x18c0, v4
	s_waitcnt vmcnt(1)
	ds_write2_b32 v5, v36, v37 offset1:1
	v_add_u32_e32 v5, 0x18c8, v4
	ds_write2_b32 v5, v38, v39 offset1:1
	v_add_u32_e32 v5, 0x1ce0, v4
	v_add_u32_e32 v4, 0x1ce8, v4
	s_waitcnt vmcnt(0)
	ds_write2_b32 v5, v40, v41 offset1:1
	ds_write2_b32 v4, v42, v43 offset1:1
	s_waitcnt lgkmcnt(0)
	ds_read2_b32 v[214:215], v10 offset1:33
	ds_read2_b32 v[222:223], v10 offset0:66 offset1:99
	ds_read2_b32 v[224:225], v10 offset0:132 offset1:165
	ds_read2_b32 v[226:227], v10 offset0:198 offset1:231
	ds_read2_b32 v[228:229], v10 offset0:8 offset1:41
	ds_read2_b32 v[230:231], v10 offset0:74 offset1:107
	ds_read2_b32 v[232:233], v10 offset0:140 offset1:173
	ds_read2_b32 v[234:235], v10 offset0:206 offset1:239
	s_waitcnt lgkmcnt(0)
	ds_read2_b32 v[236:237], v10 offset0:16 offset1:49
	ds_read2_b32 v[238:239], v10 offset0:82 offset1:115
	ds_read2_b32 v[240:241], v10 offset0:148 offset1:181
	ds_read2_b32 v[242:243], v10 offset0:214 offset1:247
	ds_read2_b32 v[244:245], v10 offset0:24 offset1:57
	ds_read2_b32 v[246:247], v10 offset0:90 offset1:123
	ds_read2_b32 v[248:249], v10 offset0:156 offset1:189
	ds_read2_b32 v[250:251], v10 offset0:222 offset1:255
	v_cvt_pk_bf16_f32 v12, v214, v215
	v_cvt_pk_bf16_f32 v13, v222, v223
	v_cvt_pk_bf16_f32 v14, v224, v225
	v_cvt_pk_bf16_f32 v15, v226, v227
	v_and_b32_e32 v16, 0xffffff80, v11
	v_add_u32_e32 v16, v16, v11
	v_ashrrev_i32_e32 v17, 31, v16
	v_lshl_add_u64 v[4:5], s[20:21], 0, v[96:97]
	v_lshlrev_b64 v[16:17], 12, v[16:17]
	v_lshl_add_u64 v[16:17], v[4:5], 0, v[16:17]
	global_store_dwordx4 v[16:17], v[12:15], off nt
	s_nop 1
	v_add_u32_e32 v11, s6, v7
	v_cvt_pk_bf16_f32 v12, v228, v229
	v_cvt_pk_bf16_f32 v13, v230, v231
	v_cvt_pk_bf16_f32 v14, v232, v233
	v_cvt_pk_bf16_f32 v15, v234, v235
	v_and_b32_e32 v16, 0xffffff80, v11
	v_add_u32_e32 v16, v16, v11
	v_ashrrev_i32_e32 v17, 31, v16
	v_lshlrev_b64 v[16:17], 12, v[16:17]
	v_lshl_add_u64 v[16:17], v[4:5], 0, v[16:17]
	global_store_dwordx4 v[16:17], v[12:15], off nt
	s_nop 1
	s_waitcnt lgkmcnt(0)
	v_add_u32_e32 v11, s6, v8
	v_cvt_pk_bf16_f32 v12, v236, v237
	v_cvt_pk_bf16_f32 v13, v238, v239
	v_cvt_pk_bf16_f32 v14, v240, v241
	v_cvt_pk_bf16_f32 v15, v242, v243
	v_and_b32_e32 v16, 0xffffff80, v11
	v_add_u32_e32 v16, v16, v11
	v_ashrrev_i32_e32 v17, 31, v16
	v_lshlrev_b64 v[16:17], 12, v[16:17]
	v_lshl_add_u64 v[16:17], v[4:5], 0, v[16:17]
	global_store_dwordx4 v[16:17], v[12:15], off nt
	s_nop 1
	v_add_u32_e32 v11, s6, v9
	v_cvt_pk_bf16_f32 v12, v244, v245
	v_cvt_pk_bf16_f32 v13, v246, v247
	v_cvt_pk_bf16_f32 v14, v248, v249
	v_cvt_pk_bf16_f32 v15, v250, v251
	v_and_b32_e32 v16, 0xffffff80, v11
	v_add_u32_e32 v16, v16, v11
	v_ashrrev_i32_e32 v17, 31, v16
	v_lshlrev_b64 v[16:17], 12, v[16:17]
	v_lshl_add_u64 v[4:5], v[4:5], 0, v[16:17]
	global_store_dwordx4 v[4:5], v[12:15], off nt
	s_nop 1
	s_waitcnt lgkmcnt(0)

; __device__ __forceinline__ unsigned pk2(float lo, float hi) { unsigned r; asm volatile("v_cvt_pk_bf16_f32 %0, %1, %2" : "=v"(r) : "v"(lo), "v"(hi)); return r; }
; __device__ __forceinline__ void transpose_item(const float* W, int K, int N, bf16_t* WT, int rstep, int roff, float* scr, int item, int lane) {
;     ...
;   for (int i = 0; i < 8; ++i) v[i] = __builtin_nontemporal_load((const f32x4*)(W + (size_t)(k0 + i * 8 + (lane >> 3)) * N + n0 + (lane & 7) * 4));
; #pragma unroll
;   for (int i = 0; i < 8; ++i) { float* d = scr + (i * 8 + (lane >> 3)) * 33 + (lane & 7) * 4; d[0] = v[i].x; d[1] = v[i].y; d[2] = v[i].z; d[3] = v[i].w; }
;   __builtin_amdgcn_wave_barrier(); asm volatile("s_waitcnt lgkmcnt(0)" ::: "memory");
;   const int c = lane & 7;
; #pragma unroll
;   for (int j = 0; j < 4; ++j) { const int nl = (lane >> 3) + 8 * j, n = n0 + nl; const float* s = scr + (8 * c) * 33 + nl;
;     u32x4 o; o.x = pk2(s[0 * 33], s[1 * 33]); o.y = pk2(s[2 * 33], s[3 * 33]); o.z = pk2(s[4 * 33], s[5 * 33]); o.w = pk2(s[6 * 33], s[7 * 33]);
;     const int row = n + (n >> 7) * rstep + roff;
;     __builtin_nontemporal_store(o, (u32x4*)(WT + (size_t)row * K + k0 + 8 * c)); }
; __device__ __forceinline__ void convert_item(const P& p, int it, float* scr, int lane) {
;     ...
;     const int l = it / (IT_WIN + IT_WOUT), r = it % (IT_WIN + IT_WOUT);
;     if (r < IT_WIN) transpose_item(p.w_in + (size_t)l * DM * INW, DM, INW, WSP(bf16_t, WS_WIN) + (size_t)l * INW * DM, 0, 0, scr, r, lane);
;     else transpose_item(p.w_out + (size_t)l * DM * DM, DM, DM, WSP(bf16_t, WS_WOUT) + (size_t)l * DM * DM, 0, 0, scr, r - IT_WIN, lane);
.LBB0_1233:
	s_and_b64 vcc, exec, s[6:7]
	s_cbranch_vccz .LBB0_1209
	s_ashr_i32 s6, s19, 31
	s_lshr_b32 s6, s6, 19
	s_add_i32 s6, s19, s6
	s_ashr_i32 s12, s6, 13
	s_and_b32 s6, s6, 0xffffe000
	s_sub_i32 s19, s19, s6
	s_ashr_i32 s13, s12, 31
	v_add_u32_e32 v11, v3, v6
	s_cmpk_gt_i32 s19, 0x17ff
	s_mov_b64 s[6:7], -1
	v_lshlrev_b32_e32 v96, 2, v0
	v_add_u32_e32 v12, 0x420, v11
	v_add_u32_e32 v13, 0x428, v11
	v_add_u32_e32 v14, 0x840, v11
	v_add_u32_e32 v15, 0x848, v11
	v_add_u32_e32 v16, 0xc60, v11
	v_add_u32_e32 v17, 0xc68, v11
	v_add_u32_e32 v18, 0x1080, v11
	v_add_u32_e32 v19, 0x1088, v11
	v_add_u32_e32 v20, 0x14a0, v11
	v_add_u32_e32 v21, 0x14a8, v11
	v_add_u32_e32 v22, 0x18c0, v11
	v_add_u32_e32 v23, 0x18c8, v11
	v_add_u32_e32 v24, 0x1ce0, v11
	v_add_u32_e32 v25, 0x1ce8, v11
	v_lshlrev_b32_e32 v4, 1, v2
	s_cbranch_scc0 .LBB0_1236
	s_lshl_b64 s[6:7], s[12:13], 24
	s_waitcnt lgkmcnt(0)
	s_add_u32 s20, s46, s6
	s_addc_u32 s21, s47, s7
	s_lshl_b64 s[6:7], s[12:13], 23
	s_add_u32 s13, s14, s6
	s_addc_u32 s22, s15, s7
	s_add_i32 s6, s19, 0xe800
	s_and_b32 s23, s6, 0xffc0
	s_lshl_b32 s6, s19, 5
	s_and_b32 s24, s6, 0x7e0
	s_lshl_b32 s6, s24, 2
	v_add_u32_e32 v26, s23, v1
	s_add_u32 s6, s20, s6
	s_addc_u32 s7, s21, 0
	v_ashrrev_i32_e32 v27, 31, v26
	v_lshl_add_u64 v[28:29], s[6:7], 0, v[96:97]
	v_lshlrev_b64 v[26:27], 13, v[26:27]
	v_lshl_add_u64 v[54:55], v[28:29], 0, v[26:27]
	s_mov_b32 s6, 0x10000
	v_add_co_u32_e32 v30, vcc, s6, v54
	s_mov_b32 s6, 0x20000
	s_nop 0
	v_addc_co_u32_e32 v31, vcc, 0, v55, vcc
	v_add_co_u32_e32 v34, vcc, s6, v54
	s_mov_b32 s6, 0x30000
	s_nop 0
	v_addc_co_u32_e32 v35, vcc, 0, v55, vcc
	v_add_co_u32_e32 v38, vcc, s6, v54
	s_mov_b32 s6, 0x40000
	s_nop 0
	v_addc_co_u32_e32 v39, vcc, 0, v55, vcc
	v_add_co_u32_e32 v42, vcc, s6, v54
	s_mov_b32 s6, 0x50000
	s_nop 0
	v_addc_co_u32_e32 v43, vcc, 0, v55, vcc
	v_add_co_u32_e32 v46, vcc, s6, v54
	global_load_dwordx4 v[26:29], v[54:55], off nt
	s_nop 0
	global_load_dwordx4 v[30:33], v[30:31], off nt
	v_addc_co_u32_e32 v47, vcc, 0, v55, vcc
	global_load_dwordx4 v[34:37], v[34:35], off nt
	s_nop 0
	global_load_dwordx4 v[38:41], v[38:39], off nt
	s_nop 0
	global_load_dwordx4 v[42:45], v[42:43], off nt
	s_nop 0
	global_load_dwordx4 v[46:49], v[46:47], off nt
	s_mov_b32 s6, 0x60000
	v_add_co_u32_e32 v50, vcc, s6, v54
	s_mov_b32 s6, 0x70000
	s_nop 0
	v_addc_co_u32_e32 v51, vcc, 0, v55, vcc
	global_load_dwordx4 v[50:53], v[50:51], off nt
	v_add_co_u32_e32 v54, vcc, s6, v54
	s_lshl_b32 s6, s23, 1
	s_nop 0
	v_addc_co_u32_e32 v55, vcc, 0, v55, vcc
	global_load_dwordx4 v[54:57], v[54:55], off nt
	s_add_u32 s6, s13, s6
	v_mov_b32_e32 v5, v97
	s_addc_u32 s7, s22, 0
	s_waitcnt vmcnt(7)
	ds_write2_b32 v11, v26, v27 offset1:1
	ds_write2_b32 v11, v28, v29 offset0:2 offset1:3
	s_waitcnt vmcnt(6)
	ds_write2_b32 v12, v30, v31 offset1:1
	ds_write2_b32 v13, v32, v33 offset1:1
	s_waitcnt vmcnt(5)
	ds_write2_b32 v14, v34, v35 offset1:1
	ds_write2_b32 v15, v36, v37 offset1:1
	s_waitcnt vmcnt(4)
	ds_write2_b32 v16, v38, v39 offset1:1
	ds_write2_b32 v17, v40, v41 offset1:1
	s_waitcnt vmcnt(3)
	ds_write2_b32 v18, v42, v43 offset1:1
	ds_write2_b32 v19, v44, v45 offset1:1
	s_waitcnt vmcnt(2)
	ds_write2_b32 v20, v46, v47 offset1:1
	ds_write2_b32 v21, v48, v49 offset1:1
	s_waitcnt vmcnt(1)
	ds_write2_b32 v22, v50, v51 offset1:1
	ds_write2_b32 v23, v52, v53 offset1:1
	s_waitcnt vmcnt(0)
	ds_write2_b32 v24, v54, v55 offset1:1
	ds_write2_b32 v25, v56, v57 offset1:1
	s_waitcnt lgkmcnt(0)
	ds_read2_b32 v[214:215], v10 offset1:33
	ds_read2_b32 v[222:223], v10 offset0:66 offset1:99
	ds_read2_b32 v[224:225], v10 offset0:132 offset1:165
	ds_read2_b32 v[226:227], v10 offset0:198 offset1:231
	ds_read2_b32 v[228:229], v10 offset0:8 offset1:41
	ds_read2_b32 v[230:231], v10 offset0:74 offset1:107
	ds_read2_b32 v[232:233], v10 offset0:140 offset1:173
	ds_read2_b32 v[234:235], v10 offset0:206 offset1:239
	s_waitcnt lgkmcnt(0)
	ds_read2_b32 v[236:237], v10 offset0:16 offset1:49
	ds_read2_b32 v[238:239], v10 offset0:82 offset1:115
	ds_read2_b32 v[240:241], v10 offset0:148 offset1:181
	ds_read2_b32 v[242:243], v10 offset0:214 offset1:247
	ds_read2_b32 v[244:245], v10 offset0:24 offset1:57
	ds_read2_b32 v[246:247], v10 offset0:90 offset1:123
	ds_read2_b32 v[248:249], v10 offset0:156 offset1:189
	ds_read2_b32 v[250:251], v10 offset0:222 offset1:255
	v_cvt_pk_bf16_f32 v26, v214, v215
	v_add_u32_e32 v30, s24, v1
	v_cvt_pk_bf16_f32 v27, v222, v223
	v_ashrrev_i32_e32 v31, 31, v30
	v_cvt_pk_bf16_f32 v28, v224, v225
	v_lshlrev_b64 v[30:31], 12, v[30:31]
	v_lshl_add_u64 v[34:35], s[6:7], 0, v[4:5]
	v_cvt_pk_bf16_f32 v29, v226, v227
	v_lshl_add_u64 v[30:31], v[34:35], 0, v[30:31]
	global_store_dwordx4 v[30:31], v[26:29], off nt
	s_nop 1
	s_mov_b64 s[6:7], 0
	v_cvt_pk_bf16_f32 v26, v228, v229
	v_add_u32_e32 v32, s24, v7
	v_ashrrev_i32_e32 v33, 31, v32
	v_lshlrev_b64 v[32:33], 12, v[32:33]
	v_cvt_pk_bf16_f32 v27, v230, v231
	v_lshl_add_u64 v[32:33], v[34:35], 0, v[32:33]
	v_cvt_pk_bf16_f32 v28, v232, v233
	v_cvt_pk_bf16_f32 v29, v234, v235
	global_store_dwordx4 v[32:33], v[26:29], off nt
	s_nop 1
	v_add_u32_e32 v32, s24, v8
	v_ashrrev_i32_e32 v33, 31, v32
	s_waitcnt lgkmcnt(0)
	v_cvt_pk_bf16_f32 v26, v236, v237
	v_lshlrev_b64 v[32:33], 12, v[32:33]
	v_cvt_pk_bf16_f32 v27, v238, v239
	v_lshl_add_u64 v[32:33], v[34:35], 0, v[32:33]
	v_cvt_pk_bf16_f32 v28, v240, v241
	v_cvt_pk_bf16_f32 v29, v242, v243
	global_store_dwordx4 v[32:33], v[26:29], off nt
	s_nop 1
	v_add_u32_e32 v32, s24, v9
	v_ashrrev_i32_e32 v33, 31, v32
	v_cvt_pk_bf16_f32 v26, v244, v245
	v_lshlrev_b64 v[32:33], 12, v[32:33]
	v_cvt_pk_bf16_f32 v27, v246, v247
	v_lshl_add_u64 v[32:33], v[34:35], 0, v[32:33]
	v_cvt_pk_bf16_f32 v28, v248, v249
	v_cvt_pk_bf16_f32 v29, v250, v251
	global_store_dwordx4 v[32:33], v[26:29], off nt
	s_nop 1
	s_waitcnt lgkmcnt(0)
; __device__ __forceinline__ unsigned pk2(float lo, float hi) { unsigned r; asm volatile("v_cvt_pk_bf16_f32 %0, %1, %2" : "=v"(r) : "v"(lo), "v"(hi)); return r; }
; __device__ __forceinline__ void transpose_item(const float* W, int K, int N, bf16_t* WT, int rstep, int roff, float* scr, int item, int lane) {
;     ...
;   for (int i = 0; i < 8; ++i) v[i] = __builtin_nontemporal_load((const f32x4*)(W + (size_t)(k0 + i * 8 + (lane >> 3)) * N + n0 + (lane & 7) * 4));
; #pragma unroll
;   for (int i = 0; i < 8; ++i) { float* d = scr + (i * 8 + (lane >> 3)) * 33 + (lane & 7) * 4; d[0] = v[i].x; d[1] = v[i].y; d[2] = v[i].z; d[3] = v[i].w; }
;   __builtin_amdgcn_wave_barrier(); asm volatile("s_waitcnt lgkmcnt(0)" ::: "memory");
;   const int c = lane & 7;
; #pragma unroll
;   for (int j = 0; j < 4; ++j) { const int nl = (lane >> 3) + 8 * j, n = n0 + nl; const float* s = scr + (8 * c) * 33 + nl;
;     u32x4 o; o.x = pk2(s[0 * 33], s[1 * 33]); o.y = pk2(s[2 * 33], s[3 * 33]); o.z = pk2(s[4 * 33], s[5 * 33]); o.w = pk2(s[6 * 33], s[7 * 33]);
;     const int row = n + (n >> 7) * rstep + roff;
;     __builtin_nontemporal_store(o, (u32x4*)(WT + (size_t)row * K + k0 + 8 * c)); }
; __device__ __forceinline__ void convert_item(const P& p, int it, float* scr, int lane) {
;     ...
;     if (r < IT_WIN) transpose_item(p.w_in + (size_t)l * DM * INW, DM, INW, WSP(bf16_t, WS_WIN) + (size_t)l * INW * DM, 0, 0, scr, r, lane);
.LBB0_1236:
	s_andn2_b64 vcc, exec, s[6:7]
	s_cbranch_vccnz .LBB0_1209
	s_mul_i32 s7, s12, 0x3000000
	s_mul_hi_i32 s6, s12, 0x3000000
	s_waitcnt lgkmcnt(0)
	s_add_u32 s7, s44, s7
	s_addc_u32 s22, s45, s6
	s_mul_hi_i32 s6, s12, 0x1800000
	s_mul_i32 s12, s12, 0x1800000
	s_add_u32 s23, s16, s12
	s_addc_u32 s24, s17, s6
	s_mul_i32 s6, s19, 0x2aab
	s_lshr_b32 s12, s6, 31
	s_ashr_i32 s6, s6, 21
	s_add_i32 s6, s6, s12
	s_sext_i32_i16 s12, s6
	s_mulk_i32 s6, 0xc0
	s_sub_i32 s6, s19, s6
	s_sext_i32_i16 s13, s6
	s_lshl_b32 s6, s12, 6
	s_lshl_b32 s12, s13, 5
	s_ashr_i32 s13, s12, 31
	s_lshl_b64 s[20:21], s[12:13], 2
	s_add_u32 s20, s7, s20
	v_add_u32_e32 v5, s6, v1
	s_addc_u32 s21, s22, s21
	v_lshl_add_u64 v[54:55], s[20:21], 0, v[96:97]
	s_movk_i32 s7, 0x6000
	v_add_u32_e32 v28, 8, v5
	v_add_u32_e32 v34, 16, v5
	v_add_u32_e32 v36, 24, v5
	v_add_u32_e32 v42, 32, v5
	v_add_u32_e32 v44, 40, v5
	v_mad_i64_i32 v[26:27], s[20:21], v5, s7, v[54:55]
	v_mad_i64_i32 v[30:31], s[20:21], v28, s7, v[54:55]
	v_mad_i64_i32 v[34:35], s[20:21], v34, s7, v[54:55]
	v_mad_i64_i32 v[38:39], s[20:21], v36, s7, v[54:55]
	v_mad_i64_i32 v[42:43], s[20:21], v42, s7, v[54:55]
	v_mad_i64_i32 v[46:47], s[20:21], v44, s7, v[54:55]
	global_load_dwordx4 v[26:29], v[26:27], off nt
	s_nop 0
	global_load_dwordx4 v[30:33], v[30:31], off nt
	s_nop 0
	global_load_dwordx4 v[34:37], v[34:35], off nt
	s_nop 0
	global_load_dwordx4 v[38:41], v[38:39], off nt
	s_nop 0
	global_load_dwordx4 v[42:45], v[42:43], off nt
	s_nop 0
	global_load_dwordx4 v[46:49], v[46:47], off nt
	v_add_u32_e32 v50, 48, v5
	v_mad_i64_i32 v[50:51], s[20:21], v50, s7, v[54:55]
	global_load_dwordx4 v[50:53], v[50:51], off nt
	v_add_u32_e32 v5, 56, v5
	v_mad_i64_i32 v[54:55], s[20:21], v5, s7, v[54:55]
	global_load_dwordx4 v[54:57], v[54:55], off nt
	s_ashr_i32 s7, s6, 31
	s_lshl_b64 s[6:7], s[6:7], 1
	s_add_u32 s6, s23, s6
	v_mov_b32_e32 v5, v97
	s_addc_u32 s7, s24, s7
	v_lshl_add_u64 v[4:5], s[6:7], 0, v[4:5]
	s_movk_i32 s82, 0x6000
	s_waitcnt vmcnt(7)
	ds_write2_b32 v11, v26, v27 offset1:1
	ds_write2_b32 v11, v28, v29 offset0:2 offset1:3
	s_waitcnt vmcnt(6)
	ds_write2_b32 v12, v30, v31 offset1:1
	ds_write2_b32 v13, v32, v33 offset1:1
	s_waitcnt vmcnt(5)
	ds_write2_b32 v14, v34, v35 offset1:1
	ds_write2_b32 v15, v36, v37 offset1:1
	s_waitcnt vmcnt(4)
	ds_write2_b32 v16, v38, v39 offset1:1
	ds_write2_b32 v17, v40, v41 offset1:1
	s_waitcnt vmcnt(3)
	ds_write2_b32 v18, v42, v43 offset1:1
	ds_write2_b32 v19, v44, v45 offset1:1
	s_waitcnt vmcnt(2)
	ds_write2_b32 v20, v46, v47 offset1:1
	ds_write2_b32 v21, v48, v49 offset1:1
	s_waitcnt vmcnt(1)
	ds_write2_b32 v22, v50, v51 offset1:1
	ds_write2_b32 v23, v52, v53 offset1:1
	s_waitcnt vmcnt(0)
	ds_write2_b32 v24, v54, v55 offset1:1
	ds_write2_b32 v25, v56, v57 offset1:1
	s_waitcnt lgkmcnt(0)
	ds_read2_b32 v[214:215], v10 offset1:33
	ds_read2_b32 v[222:223], v10 offset0:66 offset1:99
	ds_read2_b32 v[224:225], v10 offset0:132 offset1:165
	ds_read2_b32 v[226:227], v10 offset0:198 offset1:231
	ds_read2_b32 v[228:229], v10 offset0:8 offset1:41
	ds_read2_b32 v[230:231], v10 offset0:74 offset1:107
	ds_read2_b32 v[232:233], v10 offset0:140 offset1:173
	ds_read2_b32 v[234:235], v10 offset0:206 offset1:239
	s_waitcnt lgkmcnt(0)
	ds_read2_b32 v[236:237], v10 offset0:16 offset1:49
	ds_read2_b32 v[238:239], v10 offset0:82 offset1:115
	ds_read2_b32 v[240:241], v10 offset0:148 offset1:181
	ds_read2_b32 v[242:243], v10 offset0:214 offset1:247
	ds_read2_b32 v[244:245], v10 offset0:24 offset1:57
	ds_read2_b32 v[246:247], v10 offset0:90 offset1:123
	ds_read2_b32 v[248:249], v10 offset0:156 offset1:189
	ds_read2_b32 v[250:251], v10 offset0:222 offset1:255
	v_cvt_pk_bf16_f32 v12, v214, v215
	v_add_u32_e32 v16, s12, v1
	v_cvt_pk_bf16_f32 v13, v222, v223
	v_ashrrev_i32_e32 v17, 31, v16
	v_cvt_pk_bf16_f32 v14, v224, v225
	v_lshlrev_b64 v[16:17], 12, v[16:17]
	v_cvt_pk_bf16_f32 v15, v226, v227
	v_lshl_add_u64 v[16:17], v[4:5], 0, v[16:17]
	global_store_dwordx4 v[16:17], v[12:15], off nt
	s_nop 1
	s_nop 0
	v_cvt_pk_bf16_f32 v12, v228, v229
	v_add_u32_e32 v18, s12, v7
	v_ashrrev_i32_e32 v19, 31, v18
	v_lshlrev_b64 v[18:19], 12, v[18:19]
	v_cvt_pk_bf16_f32 v13, v230, v231
	v_lshl_add_u64 v[18:19], v[4:5], 0, v[18:19]
	v_cvt_pk_bf16_f32 v14, v232, v233
	v_cvt_pk_bf16_f32 v15, v234, v235
	global_store_dwordx4 v[18:19], v[12:15], off nt
	s_nop 1
	v_add_u32_e32 v18, s12, v8
	v_ashrrev_i32_e32 v19, 31, v18
	s_waitcnt lgkmcnt(0)
	v_cvt_pk_bf16_f32 v12, v236, v237
	v_lshlrev_b64 v[18:19], 12, v[18:19]
	v_cvt_pk_bf16_f32 v13, v238, v239
	v_lshl_add_u64 v[18:19], v[4:5], 0, v[18:19]
	v_cvt_pk_bf16_f32 v14, v240, v241
	v_cvt_pk_bf16_f32 v15, v242, v243
	global_store_dwordx4 v[18:19], v[12:15], off nt
	s_nop 1
	v_add_u32_e32 v18, s12, v9
	v_ashrrev_i32_e32 v19, 31, v18
	v_cvt_pk_bf16_f32 v12, v244, v245
	v_lshlrev_b64 v[18:19], 12, v[18:19]
	v_cvt_pk_bf16_f32 v13, v246, v247
	v_lshl_add_u64 v[4:5], v[4:5], 0, v[18:19]
	v_cvt_pk_bf16_f32 v14, v248, v249
	v_cvt_pk_bf16_f32 v15, v250, v251
	global_store_dwordx4 v[4:5], v[12:15], off nt
	s_nop 1
	s_waitcnt lgkmcnt(0)
	s_branch .LBB0_1209

; __device__ __forceinline__ unsigned pk2(float lo, float hi) { unsigned r; asm volatile("v_cvt_pk_bf16_f32 %0, %1, %2" : "=v"(r) : "v"(lo), "v"(hi)); return r; }
; __device__ __forceinline__ void transpose_item(const float* W, int K, int N, bf16_t* WT, int rstep, int roff, float* scr, int item, int lane) {
;     ...
;   for (int i = 0; i < 8; ++i) v[i] = __builtin_nontemporal_load((const f32x4*)(W + (size_t)(k0 + i * 8 + (lane >> 3)) * N + n0 + (lane & 7) * 4));
; #pragma unroll
;   for (int i = 0; i < 8; ++i) { float* d = scr + (i * 8 + (lane >> 3)) * 33 + (lane & 7) * 4; d[0] = v[i].x; d[1] = v[i].y; d[2] = v[i].z; d[3] = v[i].w; }
;   __builtin_amdgcn_wave_barrier(); asm volatile("s_waitcnt lgkmcnt(0)" ::: "memory");
;   const int c = lane & 7;
; #pragma unroll
;   for (int j = 0; j < 4; ++j) { const int nl = (lane >> 3) + 8 * j, n = n0 + nl; const float* s = scr + (8 * c) * 33 + nl;
;     u32x4 o; o.x = pk2(s[0 * 33], s[1 * 33]); o.y = pk2(s[2 * 33], s[3 * 33]); o.z = pk2(s[4 * 33], s[5 * 33]); o.w = pk2(s[6 * 33], s[7 * 33]);
;     const int row = n + (n >> 7) * rstep + roff;
;     __builtin_nontemporal_store(o, (u32x4*)(WT + (size_t)row * K + k0 + 8 * c)); }
; __device__ __forceinline__ void convert_item(const P& p, int it, float* scr, int lane) {
;     ...
;     const int idx = it - IT_DENSE, m = idx / IT_EXP, sub = idx % IT_EXP, le = m / 3, which = m % 3;
;     if (which == 0) transpose_item(p.wg + (size_t)le * DM * EFF, DM, EFF, WSP(bf16_t, WS_WGU) + (size_t)le * 1024 * DM, 128, 0, scr, sub, lane);
;     else if (which == 1) transpose_item(p.wu + (size_t)le * DM * EFF, DM, EFF, WSP(bf16_t, WS_WGU) + (size_t)le * 1024 * DM, 128, 128, scr, sub, lane);
;     else transpose_item(p.wd + (size_t)le * EFF * DM, EFF, DM, WSP(bf16_t, WS_WD) + (size_t)le * DM * EFF, 0, 0, scr, sub, lane);
.LBB0_1348:
	s_cmpk_gt_i32 s22, 0x3fff
	s_mov_b64 s[6:7], -1
	s_cbranch_scc0 .LBB0_1358
	s_add_i32 s6, s22, 0xffffc000
	s_lshr_b32 s7, s6, 9
	s_mul_hi_u32 s6, s6, 0xaaaaaaab
	s_lshr_b32 s64, s6, 10
	s_mul_hi_u32 s6, s7, 0x55555556
	s_mul_i32 s6, s6, 3
	s_and_b32 s23, s22, 0x1ff
	s_sub_i32 s30, s7, s6
	s_lshl_b64 s[12:13], s[64:65], 22
	s_lshl_b32 s24, s22, 5
	s_cmp_lt_i32 s30, 1
	s_mov_b64 s[6:7], -1
	s_cbranch_scc1 .LBB0_1355
	s_cmp_lg_u32 s30, 1
	s_cbranch_scc0 .LBB0_1352
	s_waitcnt lgkmcnt(0)
	s_add_u32 s34, s0, s12
	s_addc_u32 s35, s1, s13
	s_lshl_b64 s[30:31], s[64:65], 21
	s_add_u32 s7, s2, s30
	s_addc_u32 s30, s4, s31
	s_and_b32 s6, s24, 0x7e0
	s_and_b32 s31, s22, 0x1c0
	s_lshl_b32 s38, s6, 2
	v_add_u32_e32 v4, s31, v1
	s_add_u32 s34, s34, s38
	s_addc_u32 s35, s35, 0
	v_lshlrev_b32_e32 v96, 2, v0
	v_ashrrev_i32_e32 v5, 31, v4
	v_lshl_add_u64 v[12:13], s[34:35], 0, v[96:97]
	v_lshlrev_b64 v[4:5], 13, v[4:5]
	v_lshl_add_u64 v[4:5], v[12:13], 0, v[4:5]
	s_mov_b32 s34, 0x10000
	v_add_co_u32_e32 v16, vcc, s34, v4
	s_mov_b32 s34, 0x20000
	s_nop 0
	v_addc_co_u32_e32 v17, vcc, 0, v5, vcc
	global_load_dwordx4 v[12:15], v[4:5], off nt
	v_add_co_u32_e32 v20, vcc, s34, v4
	global_load_dwordx4 v[16:19], v[16:17], off nt
	s_nop 0
	v_addc_co_u32_e32 v21, vcc, 0, v5, vcc
	s_mov_b32 s34, 0x30000
	global_load_dwordx4 v[20:23], v[20:21], off nt
	v_add_co_u32_e32 v24, vcc, s34, v4
	s_mov_b32 s34, 0x40000
	s_nop 0
	v_addc_co_u32_e32 v25, vcc, 0, v5, vcc
	global_load_dwordx4 v[24:27], v[24:25], off nt
	v_add_co_u32_e32 v28, vcc, s34, v4
	s_mov_b32 s34, 0x50000
	s_nop 0
	v_addc_co_u32_e32 v29, vcc, 0, v5, vcc
	global_load_dwordx4 v[28:31], v[28:29], off nt
	v_add_co_u32_e32 v32, vcc, s34, v4
	s_mov_b32 s34, 0x60000
	s_nop 0
	v_addc_co_u32_e32 v33, vcc, 0, v5, vcc
	global_load_dwordx4 v[32:35], v[32:33], off nt
	v_add_co_u32_e32 v36, vcc, s34, v4
	s_mov_b32 s34, 0x70000
	s_nop 0
	v_addc_co_u32_e32 v37, vcc, 0, v5, vcc
	global_load_dwordx4 v[36:39], v[36:37], off nt
	v_add_co_u32_e32 v4, vcc, s34, v4
	s_lshl_b32 s31, s31, 1
	s_nop 0
	v_addc_co_u32_e32 v5, vcc, 0, v5, vcc
	global_load_dwordx4 v[40:43], v[4:5], off nt
	v_add_u32_e32 v4, v3, v6
	v_add_u32_e32 v5, 0x420, v4
	s_add_u32 s34, s7, s31
	s_addc_u32 s35, s30, 0
	v_lshlrev_b32_e32 v96, 1, v2
	s_waitcnt vmcnt(7)
	ds_write2_b32 v4, v12, v13 offset1:1
	ds_write2_b32 v4, v14, v15 offset0:2 offset1:3
	s_waitcnt vmcnt(6)
	ds_write2_b32 v5, v16, v17 offset1:1
	v_add_u32_e32 v5, 0x428, v4
	ds_write2_b32 v5, v18, v19 offset1:1
	v_add_u32_e32 v5, 0x840, v4
	s_waitcnt vmcnt(5)
	ds_write2_b32 v5, v20, v21 offset1:1
	v_add_u32_e32 v5, 0x848, v4
	ds_write2_b32 v5, v22, v23 offset1:1
	v_add_u32_e32 v5, 0xc60, v4
	v_add_u32_e32 v16, s6, v1
	v_ashrrev_i32_e32 v17, 31, v16
	s_waitcnt vmcnt(4)
	ds_write2_b32 v5, v24, v25 offset1:1
	v_add_u32_e32 v5, 0xc68, v4
	ds_write2_b32 v5, v26, v27 offset1:1
	v_add_u32_e32 v5, 0x1080, v4
	v_lshlrev_b64 v[16:17], 10, v[16:17]
	s_waitcnt vmcnt(3)
	ds_write2_b32 v5, v28, v29 offset1:1
	v_add_u32_e32 v5, 0x1088, v4
	ds_write2_b32 v5, v30, v31 offset1:1
	v_add_u32_e32 v5, 0x14a0, v4
	s_waitcnt vmcnt(2)
	ds_write2_b32 v5, v32, v33 offset1:1
	v_add_u32_e32 v5, 0x14a8, v4
	ds_write2_b32 v5, v34, v35 offset1:1
	v_add_u32_e32 v5, 0x18c0, v4
	s_waitcnt vmcnt(1)
	ds_write2_b32 v5, v36, v37 offset1:1
	v_add_u32_e32 v5, 0x18c8, v4
	ds_write2_b32 v5, v38, v39 offset1:1
	v_add_u32_e32 v5, 0x1ce0, v4
	v_add_u32_e32 v4, 0x1ce8, v4
	s_waitcnt vmcnt(0)
	ds_write2_b32 v5, v40, v41 offset1:1
	ds_write2_b32 v4, v42, v43 offset1:1
	s_waitcnt lgkmcnt(0)
	ds_read2_b32 v[214:215], v10 offset1:33
	ds_read2_b32 v[222:223], v10 offset0:66 offset1:99
	ds_read2_b32 v[224:225], v10 offset0:132 offset1:165
	ds_read2_b32 v[226:227], v10 offset0:198 offset1:231
	ds_read2_b32 v[228:229], v10 offset0:8 offset1:41
	ds_read2_b32 v[230:231], v10 offset0:74 offset1:107
	ds_read2_b32 v[232:233], v10 offset0:140 offset1:173
	ds_read2_b32 v[234:235], v10 offset0:206 offset1:239
	s_waitcnt lgkmcnt(0)
	ds_read2_b32 v[236:237], v10 offset0:16 offset1:49
	ds_read2_b32 v[238:239], v10 offset0:82 offset1:115
	ds_read2_b32 v[240:241], v10 offset0:148 offset1:181
	ds_read2_b32 v[242:243], v10 offset0:214 offset1:247
	ds_read2_b32 v[244:245], v10 offset0:24 offset1:57
	ds_read2_b32 v[246:247], v10 offset0:90 offset1:123
	ds_read2_b32 v[248:249], v10 offset0:156 offset1:189
	ds_read2_b32 v[250:251], v10 offset0:222 offset1:255
	v_lshl_add_u64 v[4:5], s[34:35], 0, v[96:97]
	v_cvt_pk_bf16_f32 v12, v214, v215
	v_cvt_pk_bf16_f32 v13, v222, v223
	v_lshl_add_u64 v[16:17], v[4:5], 0, v[16:17]
	v_cvt_pk_bf16_f32 v14, v224, v225
	v_cvt_pk_bf16_f32 v15, v226, v227
	global_store_dwordx4 v[16:17], v[12:15], off nt
	s_nop 1
	v_add_u32_e32 v16, s6, v7
	v_ashrrev_i32_e32 v17, 31, v16
	v_cvt_pk_bf16_f32 v12, v228, v229
	v_lshlrev_b64 v[16:17], 10, v[16:17]
	v_cvt_pk_bf16_f32 v13, v230, v231
	v_lshl_add_u64 v[16:17], v[4:5], 0, v[16:17]
	v_cvt_pk_bf16_f32 v14, v232, v233
	v_cvt_pk_bf16_f32 v15, v234, v235
	global_store_dwordx4 v[16:17], v[12:15], off nt
	s_nop 1
	v_add_u32_e32 v16, s6, v8
	s_waitcnt lgkmcnt(0)
	v_ashrrev_i32_e32 v17, 31, v16
	v_cvt_pk_bf16_f32 v12, v236, v237
	v_lshlrev_b64 v[16:17], 10, v[16:17]
	v_cvt_pk_bf16_f32 v13, v238, v239
	v_lshl_add_u64 v[16:17], v[4:5], 0, v[16:17]
	v_cvt_pk_bf16_f32 v14, v240, v241
	v_cvt_pk_bf16_f32 v15, v242, v243
	global_store_dwordx4 v[16:17], v[12:15], off nt
	s_nop 1
	v_add_u32_e32 v16, s6, v9
	v_ashrrev_i32_e32 v17, 31, v16
	v_cvt_pk_bf16_f32 v12, v244, v245
	v_lshlrev_b64 v[16:17], 10, v[16:17]
	v_cvt_pk_bf16_f32 v13, v246, v247
	v_lshl_add_u64 v[4:5], v[4:5], 0, v[16:17]
	v_cvt_pk_bf16_f32 v14, v248, v249
	v_cvt_pk_bf16_f32 v15, v250, v251
	global_store_dwordx4 v[4:5], v[12:15], off nt
	s_nop 1
	s_waitcnt lgkmcnt(0)
	s_mov_b64 s[6:7], 0
; __device__ __forceinline__ unsigned pk2(float lo, float hi) { unsigned r; asm volatile("v_cvt_pk_bf16_f32 %0, %1, %2" : "=v"(r) : "v"(lo), "v"(hi)); return r; }
; __device__ __forceinline__ void transpose_item(const float* W, int K, int N, bf16_t* WT, int rstep, int roff, float* scr, int item, int lane) {
;     ...
;   for (int i = 0; i < 8; ++i) v[i] = __builtin_nontemporal_load((const f32x4*)(W + (size_t)(k0 + i * 8 + (lane >> 3)) * N + n0 + (lane & 7) * 4));
; #pragma unroll
;   for (int i = 0; i < 8; ++i) { float* d = scr + (i * 8 + (lane >> 3)) * 33 + (lane & 7) * 4; d[0] = v[i].x; d[1] = v[i].y; d[2] = v[i].z; d[3] = v[i].w; }
;   __builtin_amdgcn_wave_barrier(); asm volatile("s_waitcnt lgkmcnt(0)" ::: "memory");
;   const int c = lane & 7;
; #pragma unroll
;   for (int j = 0; j < 4; ++j) { const int nl = (lane >> 3) + 8 * j, n = n0 + nl; const float* s = scr + (8 * c) * 33 + nl;
;     u32x4 o; o.x = pk2(s[0 * 33], s[1 * 33]); o.y = pk2(s[2 * 33], s[3 * 33]); o.z = pk2(s[4 * 33], s[5 * 33]); o.w = pk2(s[6 * 33], s[7 * 33]);
;     const int row = n + (n >> 7) * rstep + roff;
;     __builtin_nontemporal_store(o, (u32x4*)(WT + (size_t)row * K + k0 + 8 * c)); }
.LBB0_1352:
	s_andn2_b64 vcc, exec, s[6:7]
	s_cbranch_vccnz .LBB0_1354
	s_waitcnt lgkmcnt(0)
	s_add_u32 s34, s50, s12
	s_addc_u32 s35, s51, s13
	s_add_u32 s7, s14, s12
	s_addc_u32 s30, s15, s13
	s_lshl_b32 s6, s23, 2
	s_and_b32 s31, s6, 0x7c0
	s_and_b32 s6, s24, 0x1e0
	s_lshl_b32 s38, s6, 2
	v_add_u32_e32 v4, s31, v1
	s_add_u32 s34, s34, s38
	s_addc_u32 s35, s35, 0
	v_lshlrev_b32_e32 v96, 2, v0
	v_ashrrev_i32_e32 v5, 31, v4
	v_lshl_add_u64 v[12:13], s[34:35], 0, v[96:97]
	v_lshlrev_b64 v[4:5], 11, v[4:5]
	v_lshl_add_u64 v[4:5], v[12:13], 0, v[4:5]
	s_movk_i32 s34, 0x4000
	v_add_co_u32_e32 v16, vcc, s34, v4
	s_mov_b32 s34, 0x8000
	s_nop 0
	v_addc_co_u32_e32 v17, vcc, 0, v5, vcc
	global_load_dwordx4 v[12:15], v[4:5], off nt
	v_add_co_u32_e32 v20, vcc, s34, v4
	global_load_dwordx4 v[16:19], v[16:17], off nt
	s_nop 0
	v_addc_co_u32_e32 v21, vcc, 0, v5, vcc
	s_mov_b32 s34, 0xc000
	global_load_dwordx4 v[20:23], v[20:21], off nt
	v_add_co_u32_e32 v24, vcc, s34, v4
	s_mov_b32 s34, 0x10000
	s_nop 0
	v_addc_co_u32_e32 v25, vcc, 0, v5, vcc
	global_load_dwordx4 v[24:27], v[24:25], off nt
	v_add_co_u32_e32 v28, vcc, s34, v4
	s_mov_b32 s34, 0x14000
	s_nop 0
	v_addc_co_u32_e32 v29, vcc, 0, v5, vcc
	global_load_dwordx4 v[28:31], v[28:29], off nt
	v_add_co_u32_e32 v32, vcc, s34, v4
	s_lshl_b32 s31, s31, 1
	s_nop 0
	v_addc_co_u32_e32 v33, vcc, 0, v5, vcc
	global_load_dwordx4 v[32:35], v[32:33], off nt
	v_add_co_u32_e32 v36, vcc, s93, v4
	v_add_u32_e32 v11, s6, v1
	s_nop 0
	v_addc_co_u32_e32 v37, vcc, 0, v5, vcc
	global_load_dwordx4 v[36:39], v[36:37], off nt
	v_add_co_u32_e32 v4, vcc, s96, v4
	s_add_u32 s34, s7, s31
	s_nop 0
	v_addc_co_u32_e32 v5, vcc, 0, v5, vcc
	global_load_dwordx4 v[40:43], v[4:5], off nt
	v_add_u32_e32 v4, v3, v6
	v_add_u32_e32 v5, 0x420, v4
	s_movk_i32 s7, 0x80
	s_addc_u32 s35, s30, 0
	v_lshlrev_b32_e32 v96, 1, v2
	s_waitcnt vmcnt(7)
	ds_write2_b32 v4, v12, v13 offset1:1
	ds_write2_b32 v4, v14, v15 offset0:2 offset1:3
	s_waitcnt vmcnt(6)
	ds_write2_b32 v5, v16, v17 offset1:1
	v_add_u32_e32 v5, 0x428, v4
	ds_write2_b32 v5, v18, v19 offset1:1
	v_add_u32_e32 v5, 0x840, v4
	s_waitcnt vmcnt(5)
	ds_write2_b32 v5, v20, v21 offset1:1
	v_add_u32_e32 v5, 0x848, v4
	ds_write2_b32 v5, v22, v23 offset1:1
	v_add_u32_e32 v5, 0xc60, v4
	s_waitcnt vmcnt(4)
	ds_write2_b32 v5, v24, v25 offset1:1
	v_add_u32_e32 v5, 0xc68, v4
	ds_write2_b32 v5, v26, v27 offset1:1
	v_add_u32_e32 v5, 0x1080, v4
	s_waitcnt vmcnt(3)
	ds_write2_b32 v5, v28, v29 offset1:1
	v_add_u32_e32 v5, 0x1088, v4
	ds_write2_b32 v5, v30, v31 offset1:1
	v_add_u32_e32 v5, 0x14a0, v4
	s_waitcnt vmcnt(2)
	ds_write2_b32 v5, v32, v33 offset1:1
	v_add_u32_e32 v5, 0x14a8, v4
	ds_write2_b32 v5, v34, v35 offset1:1
	v_add_u32_e32 v5, 0x18c0, v4
	s_waitcnt vmcnt(1)
	ds_write2_b32 v5, v36, v37 offset1:1
	v_add_u32_e32 v5, 0x18c8, v4
	ds_write2_b32 v5, v38, v39 offset1:1
	v_add_u32_e32 v5, 0x1ce0, v4
	v_add_u32_e32 v4, 0x1ce8, v4
	s_waitcnt vmcnt(0)
	ds_write2_b32 v5, v40, v41 offset1:1
	ds_write2_b32 v4, v42, v43 offset1:1
	s_waitcnt lgkmcnt(0)
	ds_read2_b32 v[214:215], v10 offset1:33
	ds_read2_b32 v[222:223], v10 offset0:66 offset1:99
	ds_read2_b32 v[224:225], v10 offset0:132 offset1:165
	ds_read2_b32 v[226:227], v10 offset0:198 offset1:231
	ds_read2_b32 v[228:229], v10 offset0:8 offset1:41
	ds_read2_b32 v[230:231], v10 offset0:74 offset1:107
	ds_read2_b32 v[232:233], v10 offset0:140 offset1:173
	ds_read2_b32 v[234:235], v10 offset0:206 offset1:239
	s_waitcnt lgkmcnt(0)
	ds_read2_b32 v[236:237], v10 offset0:16 offset1:49
	ds_read2_b32 v[238:239], v10 offset0:82 offset1:115
	ds_read2_b32 v[240:241], v10 offset0:148 offset1:181
	ds_read2_b32 v[242:243], v10 offset0:214 offset1:247
	ds_read2_b32 v[244:245], v10 offset0:24 offset1:57
	ds_read2_b32 v[246:247], v10 offset0:90 offset1:123
	ds_read2_b32 v[248:249], v10 offset0:156 offset1:189
	ds_read2_b32 v[250:251], v10 offset0:222 offset1:255
	v_cvt_pk_bf16_f32 v12, v214, v215
	v_cvt_pk_bf16_f32 v13, v222, v223
	v_cvt_pk_bf16_f32 v14, v224, v225
	v_cvt_pk_bf16_f32 v15, v226, v227
	v_and_b32_e32 v16, 0xffffff80, v11
	v_add3_u32 v16, v11, v16, s7
	v_ashrrev_i32_e32 v17, 31, v16
	v_lshl_add_u64 v[4:5], s[34:35], 0, v[96:97]
	v_lshlrev_b64 v[16:17], 12, v[16:17]
	v_lshl_add_u64 v[16:17], v[4:5], 0, v[16:17]
	global_store_dwordx4 v[16:17], v[12:15], off nt
	s_nop 1
	v_add_u32_e32 v11, s6, v7
	v_cvt_pk_bf16_f32 v12, v228, v229
	v_cvt_pk_bf16_f32 v13, v230, v231
	v_cvt_pk_bf16_f32 v14, v232, v233
	v_cvt_pk_bf16_f32 v15, v234, v235
	v_and_b32_e32 v16, 0xffffff80, v11
	v_add3_u32 v16, v11, v16, s7
	v_ashrrev_i32_e32 v17, 31, v16
	v_lshlrev_b64 v[16:17], 12, v[16:17]
	v_lshl_add_u64 v[16:17], v[4:5], 0, v[16:17]
	global_store_dwordx4 v[16:17], v[12:15], off nt
	s_nop 1
	s_waitcnt lgkmcnt(0)
	v_add_u32_e32 v11, s6, v8
	v_cvt_pk_bf16_f32 v12, v236, v237
	v_cvt_pk_bf16_f32 v13, v238, v239
	v_cvt_pk_bf16_f32 v14, v240, v241
	v_cvt_pk_bf16_f32 v15, v242, v243
	v_and_b32_e32 v16, 0xffffff80, v11
	v_add3_u32 v16, v11, v16, s7
	v_ashrrev_i32_e32 v17, 31, v16
	v_lshlrev_b64 v[16:17], 12, v[16:17]
	v_lshl_add_u64 v[16:17], v[4:5], 0, v[16:17]
	global_store_dwordx4 v[16:17], v[12:15], off nt
	s_nop 1
	v_add_u32_e32 v11, s6, v9
	v_cvt_pk_bf16_f32 v12, v244, v245
	v_cvt_pk_bf16_f32 v13, v246, v247
	v_cvt_pk_bf16_f32 v14, v248, v249
	v_cvt_pk_bf16_f32 v15, v250, v251
	v_and_b32_e32 v16, 0xffffff80, v11
	v_add3_u32 v16, v11, v16, s7
	v_ashrrev_i32_e32 v17, 31, v16
	v_lshlrev_b64 v[16:17], 12, v[16:17]
	v_lshl_add_u64 v[4:5], v[4:5], 0, v[16:17]
	global_store_dwordx4 v[4:5], v[12:15], off nt
	s_nop 1
	s_waitcnt lgkmcnt(0)

; __device__ __forceinline__ unsigned pk2(float lo, float hi) { unsigned r; asm volatile("v_cvt_pk_bf16_f32 %0, %1, %2" : "=v"(r) : "v"(lo), "v"(hi)); return r; }
; __device__ __forceinline__ void transpose_item(const float* W, int K, int N, bf16_t* WT, int rstep, int roff, float* scr, int item, int lane) {
;     ...
;   for (int i = 0; i < 8; ++i) v[i] = __builtin_nontemporal_load((const f32x4*)(W + (size_t)(k0 + i * 8 + (lane >> 3)) * N + n0 + (lane & 7) * 4));
; #pragma unroll
;   for (int i = 0; i < 8; ++i) { float* d = scr + (i * 8 + (lane >> 3)) * 33 + (lane & 7) * 4; d[0] = v[i].x; d[1] = v[i].y; d[2] = v[i].z; d[3] = v[i].w; }
;   __builtin_amdgcn_wave_barrier(); asm volatile("s_waitcnt lgkmcnt(0)" ::: "memory");
;   const int c = lane & 7;
; #pragma unroll
;   for (int j = 0; j < 4; ++j) { const int nl = (lane >> 3) + 8 * j, n = n0 + nl; const float* s = scr + (8 * c) * 33 + nl;
;     u32x4 o; o.x = pk2(s[0 * 33], s[1 * 33]); o.y = pk2(s[2 * 33], s[3 * 33]); o.z = pk2(s[4 * 33], s[5 * 33]); o.w = pk2(s[6 * 33], s[7 * 33]);
;     const int row = n + (n >> 7) * rstep + roff;
;     __builtin_nontemporal_store(o, (u32x4*)(WT + (size_t)row * K + k0 + 8 * c)); }
.LBB0_1355:
	s_andn2_b64 vcc, exec, s[6:7]
	s_cbranch_vccnz .LBB0_1357
	s_waitcnt lgkmcnt(0)
	s_add_u32 s30, s48, s12
	s_addc_u32 s31, s49, s13
	s_add_u32 s7, s14, s12
	s_addc_u32 s12, s15, s13
	s_lshl_b32 s6, s23, 2
	s_and_b32 s13, s6, 0x7c0
	s_and_b32 s6, s24, 0x1e0
	s_lshl_b32 s23, s6, 2
	v_add_u32_e32 v4, s13, v1
	s_add_u32 s30, s30, s23
	s_addc_u32 s31, s31, 0
	v_lshlrev_b32_e32 v96, 2, v0
	v_ashrrev_i32_e32 v5, 31, v4
	v_lshl_add_u64 v[12:13], s[30:31], 0, v[96:97]
	v_lshlrev_b64 v[4:5], 11, v[4:5]
	v_lshl_add_u64 v[4:5], v[12:13], 0, v[4:5]
	s_movk_i32 s23, 0x4000
	v_add_co_u32_e32 v16, vcc, s23, v4
	s_mov_b32 s23, 0x8000
	s_nop 0
	v_addc_co_u32_e32 v17, vcc, 0, v5, vcc
	global_load_dwordx4 v[12:15], v[4:5], off nt
	v_add_co_u32_e32 v20, vcc, s23, v4
	global_load_dwordx4 v[16:19], v[16:17], off nt
	s_nop 0
	v_addc_co_u32_e32 v21, vcc, 0, v5, vcc
	s_mov_b32 s23, 0xc000
	global_load_dwordx4 v[20:23], v[20:21], off nt
	v_add_co_u32_e32 v24, vcc, s23, v4
	s_mov_b32 s23, 0x10000
	s_nop 0
	v_addc_co_u32_e32 v25, vcc, 0, v5, vcc
	global_load_dwordx4 v[24:27], v[24:25], off nt
	v_add_co_u32_e32 v28, vcc, s23, v4
	s_mov_b32 s23, 0x14000
	s_nop 0
	v_addc_co_u32_e32 v29, vcc, 0, v5, vcc
	global_load_dwordx4 v[28:31], v[28:29], off nt
	v_add_co_u32_e32 v32, vcc, s23, v4
	v_add_u32_e32 v11, s6, v1
	s_nop 0
	v_addc_co_u32_e32 v33, vcc, 0, v5, vcc
	global_load_dwordx4 v[32:35], v[32:33], off nt
	v_add_co_u32_e32 v36, vcc, s93, v4
	s_lshl_b32 s13, s13, 1
	s_nop 0
	v_addc_co_u32_e32 v37, vcc, 0, v5, vcc
	global_load_dwordx4 v[36:39], v[36:37], off nt
	v_add_co_u32_e32 v4, vcc, s96, v4
	s_add_u32 s30, s7, s13
	s_nop 0
	v_addc_co_u32_e32 v5, vcc, 0, v5, vcc
	global_load_dwordx4 v[40:43], v[4:5], off nt
	v_add_u32_e32 v4, v3, v6
	v_add_u32_e32 v5, 0x420, v4
	s_addc_u32 s31, s12, 0
	v_lshlrev_b32_e32 v96, 1, v2
	s_waitcnt vmcnt(7)
	ds_write2_b32 v4, v12, v13 offset1:1
	ds_write2_b32 v4, v14, v15 offset0:2 offset1:3
	s_waitcnt vmcnt(6)
	ds_write2_b32 v5, v16, v17 offset1:1
	v_add_u32_e32 v5, 0x428, v4
	ds_write2_b32 v5, v18, v19 offset1:1
	v_add_u32_e32 v5, 0x840, v4
	s_waitcnt vmcnt(5)
	ds_write2_b32 v5, v20, v21 offset1:1
	v_add_u32_e32 v5, 0x848, v4
	ds_write2_b32 v5, v22, v23 offset1:1
	v_add_u32_e32 v5, 0xc60, v4
	s_waitcnt vmcnt(4)
	ds_write2_b32 v5, v24, v25 offset1:1
	v_add_u32_e32 v5, 0xc68, v4
	ds_write2_b32 v5, v26, v27 offset1:1
	v_add_u32_e32 v5, 0x1080, v4
	s_waitcnt vmcnt(3)
	ds_write2_b32 v5, v28, v29 offset1:1
	v_add_u32_e32 v5, 0x1088, v4
	ds_write2_b32 v5, v30, v31 offset1:1
	v_add_u32_e32 v5, 0x14a0, v4
	s_waitcnt vmcnt(2)
	ds_write2_b32 v5, v32, v33 offset1:1
	v_add_u32_e32 v5, 0x14a8, v4
	ds_write2_b32 v5, v34, v35 offset1:1
	v_add_u32_e32 v5, 0x18c0, v4
	s_waitcnt vmcnt(1)
	ds_write2_b32 v5, v36, v37 offset1:1
	v_add_u32_e32 v5, 0x18c8, v4
	ds_write2_b32 v5, v38, v39 offset1:1
	v_add_u32_e32 v5, 0x1ce0, v4
	v_add_u32_e32 v4, 0x1ce8, v4
	s_waitcnt vmcnt(0)
	ds_write2_b32 v5, v40, v41 offset1:1
	ds_write2_b32 v4, v42, v43 offset1:1
	s_waitcnt lgkmcnt(0)
	ds_read2_b32 v[214:215], v10 offset1:33
	ds_read2_b32 v[222:223], v10 offset0:66 offset1:99
	ds_read2_b32 v[224:225], v10 offset0:132 offset1:165
	ds_read2_b32 v[226:227], v10 offset0:198 offset1:231
	ds_read2_b32 v[228:229], v10 offset0:8 offset1:41
	ds_read2_b32 v[230:231], v10 offset0:74 offset1:107
	ds_read2_b32 v[232:233], v10 offset0:140 offset1:173
	ds_read2_b32 v[234:235], v10 offset0:206 offset1:239
	s_waitcnt lgkmcnt(0)
	ds_read2_b32 v[236:237], v10 offset0:16 offset1:49
	ds_read2_b32 v[238:239], v10 offset0:82 offset1:115
	ds_read2_b32 v[240:241], v10 offset0:148 offset1:181
	ds_read2_b32 v[242:243], v10 offset0:214 offset1:247
	ds_read2_b32 v[244:245], v10 offset0:24 offset1:57
	ds_read2_b32 v[246:247], v10 offset0:90 offset1:123
	ds_read2_b32 v[248:249], v10 offset0:156 offset1:189
	ds_read2_b32 v[250:251], v10 offset0:222 offset1:255
	v_cvt_pk_bf16_f32 v12, v214, v215
	v_cvt_pk_bf16_f32 v13, v222, v223
	v_cvt_pk_bf16_f32 v14, v224, v225
	v_cvt_pk_bf16_f32 v15, v226, v227
	v_and_b32_e32 v16, 0xffffff80, v11
	v_add_u32_e32 v16, v16, v11
	v_ashrrev_i32_e32 v17, 31, v16
	v_lshl_add_u64 v[4:5], s[30:31], 0, v[96:97]
	v_lshlrev_b64 v[16:17], 12, v[16:17]
	v_lshl_add_u64 v[16:17], v[4:5], 0, v[16:17]
	global_store_dwordx4 v[16:17], v[12:15], off nt
	s_nop 1
	v_add_u32_e32 v11, s6, v7
	v_cvt_pk_bf16_f32 v12, v228, v229
	v_cvt_pk_bf16_f32 v13, v230, v231
	v_cvt_pk_bf16_f32 v14, v232, v233
	v_cvt_pk_bf16_f32 v15, v234, v235
	v_and_b32_e32 v16, 0xffffff80, v11
	v_add_u32_e32 v16, v16, v11
	v_ashrrev_i32_e32 v17, 31, v16
	v_lshlrev_b64 v[16:17], 12, v[16:17]
	v_lshl_add_u64 v[16:17], v[4:5], 0, v[16:17]
	global_store_dwordx4 v[16:17], v[12:15], off nt
	s_nop 1
	s_waitcnt lgkmcnt(0)
	v_add_u32_e32 v11, s6, v8
	v_cvt_pk_bf16_f32 v12, v236, v237
	v_cvt_pk_bf16_f32 v13, v238, v239
	v_cvt_pk_bf16_f32 v14, v240, v241
	v_cvt_pk_bf16_f32 v15, v242, v243
	v_and_b32_e32 v16, 0xffffff80, v11
	v_add_u32_e32 v16, v16, v11
	v_ashrrev_i32_e32 v17, 31, v16
	v_lshlrev_b64 v[16:17], 12, v[16:17]
	v_lshl_add_u64 v[16:17], v[4:5], 0, v[16:17]
	global_store_dwordx4 v[16:17], v[12:15], off nt
	s_nop 1
	v_add_u32_e32 v11, s6, v9
	v_cvt_pk_bf16_f32 v12, v244, v245
	v_cvt_pk_bf16_f32 v13, v246, v247
	v_cvt_pk_bf16_f32 v14, v248, v249
	v_cvt_pk_bf16_f32 v15, v250, v251
	v_and_b32_e32 v16, 0xffffff80, v11
	v_add_u32_e32 v16, v16, v11
	v_ashrrev_i32_e32 v17, 31, v16
	v_lshlrev_b64 v[16:17], 12, v[16:17]
	v_lshl_add_u64 v[4:5], v[4:5], 0, v[16:17]
	global_store_dwordx4 v[4:5], v[12:15], off nt
	s_nop 1
	s_waitcnt lgkmcnt(0)

; __device__ __forceinline__ unsigned pk2(float lo, float hi) { unsigned r; asm volatile("v_cvt_pk_bf16_f32 %0, %1, %2" : "=v"(r) : "v"(lo), "v"(hi)); return r; }
; __device__ __forceinline__ void transpose_item(const float* W, int K, int N, bf16_t* WT, int rstep, int roff, float* scr, int item, int lane) {
;     ...
;   for (int i = 0; i < 8; ++i) v[i] = __builtin_nontemporal_load((const f32x4*)(W + (size_t)(k0 + i * 8 + (lane >> 3)) * N + n0 + (lane & 7) * 4));
; #pragma unroll
;   for (int i = 0; i < 8; ++i) { float* d = scr + (i * 8 + (lane >> 3)) * 33 + (lane & 7) * 4; d[0] = v[i].x; d[1] = v[i].y; d[2] = v[i].z; d[3] = v[i].w; }
;   __builtin_amdgcn_wave_barrier(); asm volatile("s_waitcnt lgkmcnt(0)" ::: "memory");
;   const int c = lane & 7;
; #pragma unroll
;   for (int j = 0; j < 4; ++j) { const int nl = (lane >> 3) + 8 * j, n = n0 + nl; const float* s = scr + (8 * c) * 33 + nl;
;     u32x4 o; o.x = pk2(s[0 * 33], s[1 * 33]); o.y = pk2(s[2 * 33], s[3 * 33]); o.z = pk2(s[4 * 33], s[5 * 33]); o.w = pk2(s[6 * 33], s[7 * 33]);
;     const int row = n + (n >> 7) * rstep + roff;
;     __builtin_nontemporal_store(o, (u32x4*)(WT + (size_t)row * K + k0 + 8 * c)); }
; __device__ __forceinline__ void convert_item(const P& p, int it, float* scr, int lane) {
;     ...
;     const int l = it / (IT_WIN + IT_WOUT), r = it % (IT_WIN + IT_WOUT);
;     if (r < IT_WIN) transpose_item(p.w_in + (size_t)l * DM * INW, DM, INW, WSP(bf16_t, WS_WIN) + (size_t)l * INW * DM, 0, 0, scr, r, lane);
;     else transpose_item(p.w_out + (size_t)l * DM * DM, DM, DM, WSP(bf16_t, WS_WOUT) + (size_t)l * DM * DM, 0, 0, scr, r - IT_WIN, lane);
.LBB0_1358:
	s_and_b64 vcc, exec, s[6:7]
	s_cbranch_vccz .LBB0_1334
	s_ashr_i32 s6, s22, 31
	s_lshr_b32 s6, s6, 19
	s_add_i32 s6, s22, s6
	s_ashr_i32 s12, s6, 13
	s_and_b32 s6, s6, 0xffffe000
	s_sub_i32 s22, s22, s6
	s_ashr_i32 s13, s12, 31
	v_add_u32_e32 v11, v3, v6
	s_cmpk_gt_i32 s22, 0x17ff
	s_mov_b64 s[6:7], -1
	v_lshlrev_b32_e32 v96, 2, v0
	v_add_u32_e32 v12, 0x420, v11
	v_add_u32_e32 v13, 0x428, v11
	v_add_u32_e32 v14, 0x840, v11
	v_add_u32_e32 v15, 0x848, v11
	v_add_u32_e32 v16, 0xc60, v11
	v_add_u32_e32 v17, 0xc68, v11
	v_add_u32_e32 v18, 0x1080, v11
	v_add_u32_e32 v19, 0x1088, v11
	v_add_u32_e32 v20, 0x14a0, v11
	v_add_u32_e32 v21, 0x14a8, v11
	v_add_u32_e32 v22, 0x18c0, v11
	v_add_u32_e32 v23, 0x18c8, v11
	v_add_u32_e32 v24, 0x1ce0, v11
	v_add_u32_e32 v25, 0x1ce8, v11
	v_lshlrev_b32_e32 v4, 1, v2
	s_cbranch_scc0 .LBB0_1361
	s_lshl_b64 s[6:7], s[12:13], 24
	s_waitcnt lgkmcnt(0)
	s_add_u32 s23, s46, s6
	s_addc_u32 s24, s47, s7
	s_lshl_b64 s[6:7], s[12:13], 23
	s_add_u32 s13, s16, s6
	s_addc_u32 s30, s17, s7
	s_add_i32 s6, s22, 0xe800
	s_and_b32 s31, s6, 0xffc0
	s_lshl_b32 s6, s22, 5
	s_and_b32 s34, s6, 0x7e0
	s_lshl_b32 s6, s34, 2
	v_add_u32_e32 v26, s31, v1
	s_add_u32 s6, s23, s6
	s_addc_u32 s7, s24, 0
	v_ashrrev_i32_e32 v27, 31, v26
	v_lshl_add_u64 v[28:29], s[6:7], 0, v[96:97]
	v_lshlrev_b64 v[26:27], 13, v[26:27]
	v_lshl_add_u64 v[54:55], v[28:29], 0, v[26:27]
	s_mov_b32 s6, 0x10000
	v_add_co_u32_e32 v30, vcc, s6, v54
	s_mov_b32 s6, 0x20000
	s_nop 0
	v_addc_co_u32_e32 v31, vcc, 0, v55, vcc
	v_add_co_u32_e32 v34, vcc, s6, v54
	s_mov_b32 s6, 0x30000
	s_nop 0
	v_addc_co_u32_e32 v35, vcc, 0, v55, vcc
	v_add_co_u32_e32 v38, vcc, s6, v54
	s_mov_b32 s6, 0x40000
	s_nop 0
	v_addc_co_u32_e32 v39, vcc, 0, v55, vcc
	v_add_co_u32_e32 v42, vcc, s6, v54
	s_mov_b32 s6, 0x50000
	s_nop 0
	v_addc_co_u32_e32 v43, vcc, 0, v55, vcc
	v_add_co_u32_e32 v46, vcc, s6, v54
	global_load_dwordx4 v[26:29], v[54:55], off nt
	s_nop 0
	global_load_dwordx4 v[30:33], v[30:31], off nt
	v_addc_co_u32_e32 v47, vcc, 0, v55, vcc
	global_load_dwordx4 v[34:37], v[34:35], off nt
	s_nop 0
	global_load_dwordx4 v[38:41], v[38:39], off nt
	s_nop 0
	global_load_dwordx4 v[42:45], v[42:43], off nt
	s_nop 0
	global_load_dwordx4 v[46:49], v[46:47], off nt
	s_mov_b32 s6, 0x60000
	v_add_co_u32_e32 v50, vcc, s6, v54
	s_mov_b32 s6, 0x70000
	s_nop 0
	v_addc_co_u32_e32 v51, vcc, 0, v55, vcc
	global_load_dwordx4 v[50:53], v[50:51], off nt
	v_add_co_u32_e32 v54, vcc, s6, v54
	s_lshl_b32 s6, s31, 1
	s_nop 0
	v_addc_co_u32_e32 v55, vcc, 0, v55, vcc
	global_load_dwordx4 v[54:57], v[54:55], off nt
	s_add_u32 s6, s13, s6
	v_mov_b32_e32 v5, v97
	s_addc_u32 s7, s30, 0
	s_waitcnt vmcnt(7)
	ds_write2_b32 v11, v26, v27 offset1:1
	ds_write2_b32 v11, v28, v29 offset0:2 offset1:3
	s_waitcnt vmcnt(6)
	ds_write2_b32 v12, v30, v31 offset1:1
	ds_write2_b32 v13, v32, v33 offset1:1
	s_waitcnt vmcnt(5)
	ds_write2_b32 v14, v34, v35 offset1:1
	ds_write2_b32 v15, v36, v37 offset1:1
	s_waitcnt vmcnt(4)
	ds_write2_b32 v16, v38, v39 offset1:1
	ds_write2_b32 v17, v40, v41 offset1:1
	s_waitcnt vmcnt(3)
	ds_write2_b32 v18, v42, v43 offset1:1
	ds_write2_b32 v19, v44, v45 offset1:1
	s_waitcnt vmcnt(2)
	ds_write2_b32 v20, v46, v47 offset1:1
	ds_write2_b32 v21, v48, v49 offset1:1
	s_waitcnt vmcnt(1)
	ds_write2_b32 v22, v50, v51 offset1:1
	ds_write2_b32 v23, v52, v53 offset1:1
	s_waitcnt vmcnt(0)
	ds_write2_b32 v24, v54, v55 offset1:1
	ds_write2_b32 v25, v56, v57 offset1:1
	s_waitcnt lgkmcnt(0)
	ds_read2_b32 v[214:215], v10 offset1:33
	ds_read2_b32 v[222:223], v10 offset0:66 offset1:99
	ds_read2_b32 v[224:225], v10 offset0:132 offset1:165
	ds_read2_b32 v[226:227], v10 offset0:198 offset1:231
	ds_read2_b32 v[228:229], v10 offset0:8 offset1:41
	ds_read2_b32 v[230:231], v10 offset0:74 offset1:107
	ds_read2_b32 v[232:233], v10 offset0:140 offset1:173
	ds_read2_b32 v[234:235], v10 offset0:206 offset1:239
	s_waitcnt lgkmcnt(0)
	ds_read2_b32 v[236:237], v10 offset0:16 offset1:49
	ds_read2_b32 v[238:239], v10 offset0:82 offset1:115
	ds_read2_b32 v[240:241], v10 offset0:148 offset1:181
	ds_read2_b32 v[242:243], v10 offset0:214 offset1:247
	ds_read2_b32 v[244:245], v10 offset0:24 offset1:57
	ds_read2_b32 v[246:247], v10 offset0:90 offset1:123
	ds_read2_b32 v[248:249], v10 offset0:156 offset1:189
	ds_read2_b32 v[250:251], v10 offset0:222 offset1:255
	v_cvt_pk_bf16_f32 v26, v214, v215
	v_add_u32_e32 v30, s34, v1
	v_cvt_pk_bf16_f32 v27, v222, v223
	v_ashrrev_i32_e32 v31, 31, v30
	v_cvt_pk_bf16_f32 v28, v224, v225
	v_lshlrev_b64 v[30:31], 12, v[30:31]
	v_lshl_add_u64 v[34:35], s[6:7], 0, v[4:5]
	v_cvt_pk_bf16_f32 v29, v226, v227
	v_lshl_add_u64 v[30:31], v[34:35], 0, v[30:31]
	global_store_dwordx4 v[30:31], v[26:29], off nt
	s_nop 1
	s_mov_b64 s[6:7], 0
	v_cvt_pk_bf16_f32 v26, v228, v229
	v_add_u32_e32 v32, s34, v7
	v_ashrrev_i32_e32 v33, 31, v32
	v_lshlrev_b64 v[32:33], 12, v[32:33]
	v_cvt_pk_bf16_f32 v27, v230, v231
	v_lshl_add_u64 v[32:33], v[34:35], 0, v[32:33]
	v_cvt_pk_bf16_f32 v28, v232, v233
	v_cvt_pk_bf16_f32 v29, v234, v235
	global_store_dwordx4 v[32:33], v[26:29], off nt
	s_nop 1
	v_add_u32_e32 v32, s34, v8
	v_ashrrev_i32_e32 v33, 31, v32
	s_waitcnt lgkmcnt(0)
	v_cvt_pk_bf16_f32 v26, v236, v237
	v_lshlrev_b64 v[32:33], 12, v[32:33]
	v_cvt_pk_bf16_f32 v27, v238, v239
	v_lshl_add_u64 v[32:33], v[34:35], 0, v[32:33]
	v_cvt_pk_bf16_f32 v28, v240, v241
	v_cvt_pk_bf16_f32 v29, v242, v243
	global_store_dwordx4 v[32:33], v[26:29], off nt
	s_nop 1
	v_add_u32_e32 v32, s34, v9
	v_ashrrev_i32_e32 v33, 31, v32
	v_cvt_pk_bf16_f32 v26, v244, v245
	v_lshlrev_b64 v[32:33], 12, v[32:33]
	v_cvt_pk_bf16_f32 v27, v246, v247
	v_lshl_add_u64 v[32:33], v[34:35], 0, v[32:33]
	v_cvt_pk_bf16_f32 v28, v248, v249
	v_cvt_pk_bf16_f32 v29, v250, v251
	global_store_dwordx4 v[32:33], v[26:29], off nt
	s_nop 1
	s_waitcnt lgkmcnt(0)
; __device__ __forceinline__ unsigned pk2(float lo, float hi) { unsigned r; asm volatile("v_cvt_pk_bf16_f32 %0, %1, %2" : "=v"(r) : "v"(lo), "v"(hi)); return r; }
; __device__ __forceinline__ void transpose_item(const float* W, int K, int N, bf16_t* WT, int rstep, int roff, float* scr, int item, int lane) {
;     ...
;   for (int i = 0; i < 8; ++i) v[i] = __builtin_nontemporal_load((const f32x4*)(W + (size_t)(k0 + i * 8 + (lane >> 3)) * N + n0 + (lane & 7) * 4));
; #pragma unroll
;   for (int i = 0; i < 8; ++i) { float* d = scr + (i * 8 + (lane >> 3)) * 33 + (lane & 7) * 4; d[0] = v[i].x; d[1] = v[i].y; d[2] = v[i].z; d[3] = v[i].w; }
;   __builtin_amdgcn_wave_barrier(); asm volatile("s_waitcnt lgkmcnt(0)" ::: "memory");
;   const int c = lane & 7;
; #pragma unroll
;   for (int j = 0; j < 4; ++j) { const int nl = (lane >> 3) + 8 * j, n = n0 + nl; const float* s = scr + (8 * c) * 33 + nl;
;     u32x4 o; o.x = pk2(s[0 * 33], s[1 * 33]); o.y = pk2(s[2 * 33], s[3 * 33]); o.z = pk2(s[4 * 33], s[5 * 33]); o.w = pk2(s[6 * 33], s[7 * 33]);
;     const int row = n + (n >> 7) * rstep + roff;
;     __builtin_nontemporal_store(o, (u32x4*)(WT + (size_t)row * K + k0 + 8 * c)); }
; __device__ __forceinline__ void convert_item(const P& p, int it, float* scr, int lane) {
;     ...
;     if (r < IT_WIN) transpose_item(p.w_in + (size_t)l * DM * INW, DM, INW, WSP(bf16_t, WS_WIN) + (size_t)l * INW * DM, 0, 0, scr, r, lane);
.LBB0_1361:
	s_andn2_b64 vcc, exec, s[6:7]
	s_cbranch_vccnz .LBB0_1334
	s_mul_i32 s7, s12, 0x3000000
	s_mul_hi_i32 s6, s12, 0x3000000
	s_waitcnt lgkmcnt(0)
	s_add_u32 s7, s44, s7
	s_addc_u32 s24, s45, s6
	s_mul_hi_i32 s6, s12, 0x1800000
	s_mul_i32 s12, s12, 0x1800000
	s_add_u32 s30, s18, s12
	s_addc_u32 s31, s19, s6
	s_mul_i32 s6, s22, 0x2aab
	s_lshr_b32 s12, s6, 31
	s_ashr_i32 s6, s6, 21
	s_add_i32 s6, s6, s12
	s_sext_i32_i16 s12, s6
	s_mulk_i32 s6, 0xc0
	s_sub_i32 s6, s22, s6
	s_sext_i32_i16 s13, s6
	s_lshl_b32 s6, s12, 6
	s_lshl_b32 s12, s13, 5
	s_ashr_i32 s13, s12, 31
	s_lshl_b64 s[22:23], s[12:13], 2
	s_add_u32 s22, s7, s22
	v_add_u32_e32 v5, s6, v1
	s_addc_u32 s23, s24, s23
	v_lshl_add_u64 v[54:55], s[22:23], 0, v[96:97]
	s_movk_i32 s7, 0x6000
	v_add_u32_e32 v28, 8, v5
	v_add_u32_e32 v34, 16, v5
	v_add_u32_e32 v36, 24, v5
	v_add_u32_e32 v42, 32, v5
	v_add_u32_e32 v44, 40, v5
	v_mad_i64_i32 v[26:27], s[22:23], v5, s7, v[54:55]
	v_mad_i64_i32 v[30:31], s[22:23], v28, s7, v[54:55]
	v_mad_i64_i32 v[34:35], s[22:23], v34, s7, v[54:55]
	v_mad_i64_i32 v[38:39], s[22:23], v36, s7, v[54:55]
	v_mad_i64_i32 v[42:43], s[22:23], v42, s7, v[54:55]
	v_mad_i64_i32 v[46:47], s[22:23], v44, s7, v[54:55]
	global_load_dwordx4 v[26:29], v[26:27], off nt
	s_nop 0
	global_load_dwordx4 v[30:33], v[30:31], off nt
	s_nop 0
	global_load_dwordx4 v[34:37], v[34:35], off nt
	s_nop 0
	global_load_dwordx4 v[38:41], v[38:39], off nt
	s_nop 0
	global_load_dwordx4 v[42:45], v[42:43], off nt
	s_nop 0
	global_load_dwordx4 v[46:49], v[46:47], off nt
	v_add_u32_e32 v50, 48, v5
	v_mad_i64_i32 v[50:51], s[22:23], v50, s7, v[54:55]
	global_load_dwordx4 v[50:53], v[50:51], off nt
	v_add_u32_e32 v5, 56, v5
	v_mad_i64_i32 v[54:55], s[22:23], v5, s7, v[54:55]
	global_load_dwordx4 v[54:57], v[54:55], off nt
	s_ashr_i32 s7, s6, 31
	s_lshl_b64 s[6:7], s[6:7], 1
	s_add_u32 s6, s30, s6
	v_mov_b32_e32 v5, v97
	s_addc_u32 s7, s31, s7
	v_lshl_add_u64 v[4:5], s[6:7], 0, v[4:5]
	s_movk_i32 s82, 0x6000
	s_waitcnt vmcnt(7)
	ds_write2_b32 v11, v26, v27 offset1:1
	ds_write2_b32 v11, v28, v29 offset0:2 offset1:3
	s_waitcnt vmcnt(6)
	ds_write2_b32 v12, v30, v31 offset1:1
	ds_write2_b32 v13, v32, v33 offset1:1
	s_waitcnt vmcnt(5)
	ds_write2_b32 v14, v34, v35 offset1:1
	ds_write2_b32 v15, v36, v37 offset1:1
	s_waitcnt vmcnt(4)
	ds_write2_b32 v16, v38, v39 offset1:1
	ds_write2_b32 v17, v40, v41 offset1:1
	s_waitcnt vmcnt(3)
	ds_write2_b32 v18, v42, v43 offset1:1
	ds_write2_b32 v19, v44, v45 offset1:1
	s_waitcnt vmcnt(2)
	ds_write2_b32 v20, v46, v47 offset1:1
	ds_write2_b32 v21, v48, v49 offset1:1
	s_waitcnt vmcnt(1)
	ds_write2_b32 v22, v50, v51 offset1:1
	ds_write2_b32 v23, v52, v53 offset1:1
	s_waitcnt vmcnt(0)
	ds_write2_b32 v24, v54, v55 offset1:1
	ds_write2_b32 v25, v56, v57 offset1:1
	s_waitcnt lgkmcnt(0)
	ds_read2_b32 v[214:215], v10 offset1:33
	ds_read2_b32 v[222:223], v10 offset0:66 offset1:99
	ds_read2_b32 v[224:225], v10 offset0:132 offset1:165
	ds_read2_b32 v[226:227], v10 offset0:198 offset1:231
	ds_read2_b32 v[228:229], v10 offset0:8 offset1:41
	ds_read2_b32 v[230:231], v10 offset0:74 offset1:107
	ds_read2_b32 v[232:233], v10 offset0:140 offset1:173
	ds_read2_b32 v[234:235], v10 offset0:206 offset1:239
	s_waitcnt lgkmcnt(0)
	ds_read2_b32 v[236:237], v10 offset0:16 offset1:49
	ds_read2_b32 v[238:239], v10 offset0:82 offset1:115
	ds_read2_b32 v[240:241], v10 offset0:148 offset1:181
	ds_read2_b32 v[242:243], v10 offset0:214 offset1:247
	ds_read2_b32 v[244:245], v10 offset0:24 offset1:57
	ds_read2_b32 v[246:247], v10 offset0:90 offset1:123
	ds_read2_b32 v[248:249], v10 offset0:156 offset1:189
	ds_read2_b32 v[250:251], v10 offset0:222 offset1:255
	v_cvt_pk_bf16_f32 v12, v214, v215
	v_add_u32_e32 v16, s12, v1
	v_cvt_pk_bf16_f32 v13, v222, v223
	v_ashrrev_i32_e32 v17, 31, v16
	v_cvt_pk_bf16_f32 v14, v224, v225
	v_lshlrev_b64 v[16:17], 12, v[16:17]
	v_cvt_pk_bf16_f32 v15, v226, v227
	v_lshl_add_u64 v[16:17], v[4:5], 0, v[16:17]
	global_store_dwordx4 v[16:17], v[12:15], off nt
	s_nop 1
	s_nop 0
	v_cvt_pk_bf16_f32 v12, v228, v229
	v_add_u32_e32 v18, s12, v7
	v_ashrrev_i32_e32 v19, 31, v18
	v_lshlrev_b64 v[18:19], 12, v[18:19]
	v_cvt_pk_bf16_f32 v13, v230, v231
	v_lshl_add_u64 v[18:19], v[4:5], 0, v[18:19]
	v_cvt_pk_bf16_f32 v14, v232, v233
	v_cvt_pk_bf16_f32 v15, v234, v235
	global_store_dwordx4 v[18:19], v[12:15], off nt
	s_nop 1
	v_add_u32_e32 v18, s12, v8
	v_ashrrev_i32_e32 v19, 31, v18
	s_waitcnt lgkmcnt(0)
	v_cvt_pk_bf16_f32 v12, v236, v237
	v_lshlrev_b64 v[18:19], 12, v[18:19]
	v_cvt_pk_bf16_f32 v13, v238, v239
	v_lshl_add_u64 v[18:19], v[4:5], 0, v[18:19]
	v_cvt_pk_bf16_f32 v14, v240, v241
	v_cvt_pk_bf16_f32 v15, v242, v243
	global_store_dwordx4 v[18:19], v[12:15], off nt
	s_nop 1
	v_add_u32_e32 v18, s12, v9
	v_ashrrev_i32_e32 v19, 31, v18
	v_cvt_pk_bf16_f32 v12, v244, v245
	v_lshlrev_b64 v[18:19], 12, v[18:19]
	v_cvt_pk_bf16_f32 v13, v246, v247
	v_lshl_add_u64 v[4:5], v[4:5], 0, v[18:19]
	v_cvt_pk_bf16_f32 v14, v248, v249
	v_cvt_pk_bf16_f32 v15, v250, v251
	global_store_dwordx4 v[4:5], v[12:15], off nt
	s_nop 1
	s_waitcnt lgkmcnt(0)
	s_branch .LBB0_1334

; __device__ __forceinline__ unsigned pk2(float lo, float hi) { unsigned r; asm volatile("v_cvt_pk_bf16_f32 %0, %1, %2" : "=v"(r) : "v"(lo), "v"(hi)); return r; }
; __device__ __forceinline__ void transpose_item(const float* W, int K, int N, bf16_t* WT, int rstep, int roff, float* scr, int item, int lane) {
;     ...
;   for (int i = 0; i < 8; ++i) v[i] = __builtin_nontemporal_load((const f32x4*)(W + (size_t)(k0 + i * 8 + (lane >> 3)) * N + n0 + (lane & 7) * 4));
; #pragma unroll
;   for (int i = 0; i < 8; ++i) { float* d = scr + (i * 8 + (lane >> 3)) * 33 + (lane & 7) * 4; d[0] = v[i].x; d[1] = v[i].y; d[2] = v[i].z; d[3] = v[i].w; }
;   __builtin_amdgcn_wave_barrier(); asm volatile("s_waitcnt lgkmcnt(0)" ::: "memory");
;   const int c = lane & 7;
; #pragma unroll
;   for (int j = 0; j < 4; ++j) { const int nl = (lane >> 3) + 8 * j, n = n0 + nl; const float* s = scr + (8 * c) * 33 + nl;
;     u32x4 o; o.x = pk2(s[0 * 33], s[1 * 33]); o.y = pk2(s[2 * 33], s[3 * 33]); o.z = pk2(s[4 * 33], s[5 * 33]); o.w = pk2(s[6 * 33], s[7 * 33]);
;     const int row = n + (n >> 7) * rstep + roff;
;     __builtin_nontemporal_store(o, (u32x4*)(WT + (size_t)row * K + k0 + 8 * c)); }
; __device__ __forceinline__ void convert_item(const P& p, int it, float* scr, int lane) {
;     ...
;     const int idx = it - IT_DENSE, m = idx / IT_EXP, sub = idx % IT_EXP, le = m / 3, which = m % 3;
;     if (which == 0) transpose_item(p.wg + (size_t)le * DM * EFF, DM, EFF, WSP(bf16_t, WS_WGU) + (size_t)le * 1024 * DM, 128, 0, scr, sub, lane);
;     else if (which == 1) transpose_item(p.wu + (size_t)le * DM * EFF, DM, EFF, WSP(bf16_t, WS_WGU) + (size_t)le * 1024 * DM, 128, 128, scr, sub, lane);
;     else transpose_item(p.wd + (size_t)le * EFF * DM, EFF, DM, WSP(bf16_t, WS_WD) + (size_t)le * DM * EFF, 0, 0, scr, sub, lane);
.LBB0_1430:
	s_cmpk_gt_i32 s6, 0x3fff
	s_mov_b64 s[4:5], -1
	s_cbranch_scc0 .LBB0_1440
	s_add_i32 s4, s6, 0xffffc000
	s_lshr_b32 s5, s4, 9
	s_mul_i32 s4, s4, 0xaaab
	s_lshr_b32 s20, s4, 26
	s_mul_i32 s4, s5, 0xab
	s_bfe_u32 s4, s4, 0x70009
	s_mul_i32 s4, s4, 3
	s_sub_i32 s4, s5, s4
	s_and_b32 s7, s6, 0x1ff
	s_lshl_b32 s19, s20, 22
	s_lshl_b32 s18, s6, 5
	s_and_b32 s21, s4, 0xff
	s_cmp_lt_i32 s21, 1
	s_mov_b64 s[4:5], -1
	s_cbranch_scc1 .LBB0_1437
	s_and_b32 s4, 0xffff, s21
	s_cmp_lg_u32 s4, 1
	s_mov_b64 s[4:5], -1
	s_cbranch_scc0 .LBB0_1434
	s_add_u32 s22, s44, s19
	s_addc_u32 s23, s45, 0
	s_lshl_b32 s4, s20, 21
	s_add_u32 s5, s3, s4
	s_addc_u32 s20, s9, 0
	s_and_b32 s4, s18, 0x7e0
	s_and_b32 s21, s6, 0x1c0
	s_lshl_b32 s24, s4, 2
	v_add_u32_e32 v4, s21, v1
	s_add_u32 s22, s22, s24
	s_addc_u32 s23, s23, 0
	v_lshlrev_b32_e32 v96, 2, v0
	v_ashrrev_i32_e32 v5, 31, v4
	v_lshl_add_u64 v[12:13], s[22:23], 0, v[96:97]
	v_lshlrev_b64 v[4:5], 13, v[4:5]
	v_lshl_add_u64 v[4:5], v[12:13], 0, v[4:5]
	s_mov_b32 s22, 0x10000
	v_add_co_u32_e32 v16, vcc, s22, v4
	s_mov_b32 s22, 0x20000
	s_nop 0
	v_addc_co_u32_e32 v17, vcc, 0, v5, vcc
	global_load_dwordx4 v[12:15], v[4:5], off nt
	v_add_co_u32_e32 v20, vcc, s22, v4
	global_load_dwordx4 v[16:19], v[16:17], off nt
	s_nop 0
	v_addc_co_u32_e32 v21, vcc, 0, v5, vcc
	s_mov_b32 s22, 0x30000
	global_load_dwordx4 v[20:23], v[20:21], off nt
	v_add_co_u32_e32 v24, vcc, s22, v4
	s_mov_b32 s22, 0x40000
	s_nop 0
	v_addc_co_u32_e32 v25, vcc, 0, v5, vcc
	global_load_dwordx4 v[24:27], v[24:25], off nt
	v_add_co_u32_e32 v28, vcc, s22, v4
	s_mov_b32 s22, 0x50000
	s_nop 0
	v_addc_co_u32_e32 v29, vcc, 0, v5, vcc
	global_load_dwordx4 v[28:31], v[28:29], off nt
	v_add_co_u32_e32 v32, vcc, s22, v4
	s_mov_b32 s22, 0x60000
	s_nop 0
	v_addc_co_u32_e32 v33, vcc, 0, v5, vcc
	global_load_dwordx4 v[32:35], v[32:33], off nt
	v_add_co_u32_e32 v36, vcc, s22, v4
	s_mov_b32 s22, 0x70000
	s_nop 0
	v_addc_co_u32_e32 v37, vcc, 0, v5, vcc
	global_load_dwordx4 v[36:39], v[36:37], off nt
	v_add_co_u32_e32 v4, vcc, s22, v4
	s_lshl_b32 s21, s21, 1
	s_nop 0
	v_addc_co_u32_e32 v5, vcc, 0, v5, vcc
	global_load_dwordx4 v[40:43], v[4:5], off nt
	v_add_u32_e32 v4, v3, v6
	v_add_u32_e32 v5, 0x420, v4
	s_add_u32 s22, s5, s21
	s_addc_u32 s23, s20, 0
	v_lshlrev_b32_e32 v96, 1, v2
	s_waitcnt vmcnt(0)
	ds_write2_b32 v4, v12, v13 offset1:1
	ds_write2_b32 v4, v14, v15 offset0:2 offset1:3
	ds_write2_b32 v5, v16, v17 offset1:1
	v_add_u32_e32 v5, 0x428, v4
	ds_write2_b32 v5, v18, v19 offset1:1
	v_add_u32_e32 v5, 0x840, v4
	ds_write2_b32 v5, v20, v21 offset1:1
	v_add_u32_e32 v5, 0x848, v4
	ds_write2_b32 v5, v22, v23 offset1:1
	v_add_u32_e32 v5, 0xc60, v4
	v_add_u32_e32 v16, s4, v1
	v_ashrrev_i32_e32 v17, 31, v16
	ds_write2_b32 v5, v24, v25 offset1:1
	v_add_u32_e32 v5, 0xc68, v4
	ds_write2_b32 v5, v26, v27 offset1:1
	v_add_u32_e32 v5, 0x1080, v4
	v_lshlrev_b64 v[16:17], 10, v[16:17]
	ds_write2_b32 v5, v28, v29 offset1:1
	v_add_u32_e32 v5, 0x1088, v4
	ds_write2_b32 v5, v30, v31 offset1:1
	v_add_u32_e32 v5, 0x14a0, v4
	ds_write2_b32 v5, v32, v33 offset1:1
	v_add_u32_e32 v5, 0x14a8, v4
	ds_write2_b32 v5, v34, v35 offset1:1
	v_add_u32_e32 v5, 0x18c0, v4
	ds_write2_b32 v5, v36, v37 offset1:1
	v_add_u32_e32 v5, 0x18c8, v4
	ds_write2_b32 v5, v38, v39 offset1:1
	v_add_u32_e32 v5, 0x1ce0, v4
	v_add_u32_e32 v4, 0x1ce8, v4
	ds_write2_b32 v5, v40, v41 offset1:1
	ds_write2_b32 v4, v42, v43 offset1:1
	s_waitcnt lgkmcnt(0)
	ds_read2_b32 v[214:215], v10 offset1:33
	ds_read2_b32 v[222:223], v10 offset0:66 offset1:99
	ds_read2_b32 v[224:225], v10 offset0:132 offset1:165
	ds_read2_b32 v[226:227], v10 offset0:198 offset1:231
	ds_read2_b32 v[228:229], v10 offset0:8 offset1:41
	ds_read2_b32 v[230:231], v10 offset0:74 offset1:107
	ds_read2_b32 v[232:233], v10 offset0:140 offset1:173
	ds_read2_b32 v[234:235], v10 offset0:206 offset1:239
	s_waitcnt lgkmcnt(0)
	ds_read2_b32 v[236:237], v10 offset0:16 offset1:49
	ds_read2_b32 v[238:239], v10 offset0:82 offset1:115
	ds_read2_b32 v[240:241], v10 offset0:148 offset1:181
	ds_read2_b32 v[242:243], v10 offset0:214 offset1:247
	ds_read2_b32 v[244:245], v10 offset0:24 offset1:57
	ds_read2_b32 v[246:247], v10 offset0:90 offset1:123
	ds_read2_b32 v[248:249], v10 offset0:156 offset1:189
	ds_read2_b32 v[250:251], v10 offset0:222 offset1:255
	v_lshl_add_u64 v[4:5], s[22:23], 0, v[96:97]
	v_cvt_pk_bf16_f32 v12, v214, v215
	v_cvt_pk_bf16_f32 v13, v222, v223
	v_lshl_add_u64 v[16:17], v[4:5], 0, v[16:17]
	v_cvt_pk_bf16_f32 v14, v224, v225
	v_cvt_pk_bf16_f32 v15, v226, v227
	global_store_dwordx4 v[16:17], v[12:15], off nt
	s_nop 1
	v_add_u32_e32 v16, s4, v7
	v_ashrrev_i32_e32 v17, 31, v16
	v_cvt_pk_bf16_f32 v12, v228, v229
	v_lshlrev_b64 v[16:17], 10, v[16:17]
	v_cvt_pk_bf16_f32 v13, v230, v231
	v_lshl_add_u64 v[16:17], v[4:5], 0, v[16:17]
	v_cvt_pk_bf16_f32 v14, v232, v233
	v_cvt_pk_bf16_f32 v15, v234, v235
	global_store_dwordx4 v[16:17], v[12:15], off nt
	s_nop 1
	v_add_u32_e32 v16, s4, v8
	s_waitcnt lgkmcnt(0)
	v_ashrrev_i32_e32 v17, 31, v16
	v_cvt_pk_bf16_f32 v12, v236, v237
	v_lshlrev_b64 v[16:17], 10, v[16:17]
	v_cvt_pk_bf16_f32 v13, v238, v239
	v_lshl_add_u64 v[16:17], v[4:5], 0, v[16:17]
	v_cvt_pk_bf16_f32 v14, v240, v241
	v_cvt_pk_bf16_f32 v15, v242, v243
	global_store_dwordx4 v[16:17], v[12:15], off nt
	s_nop 1
	v_add_u32_e32 v16, s4, v9
	v_ashrrev_i32_e32 v17, 31, v16
	v_cvt_pk_bf16_f32 v12, v244, v245
	v_lshlrev_b64 v[16:17], 10, v[16:17]
	v_cvt_pk_bf16_f32 v13, v246, v247
	v_lshl_add_u64 v[4:5], v[4:5], 0, v[16:17]
	v_cvt_pk_bf16_f32 v14, v248, v249
	v_cvt_pk_bf16_f32 v15, v250, v251
	global_store_dwordx4 v[4:5], v[12:15], off nt
	s_nop 1
	s_waitcnt lgkmcnt(0)
	s_mov_b64 s[4:5], 0
; __device__ __forceinline__ unsigned pk2(float lo, float hi) { unsigned r; asm volatile("v_cvt_pk_bf16_f32 %0, %1, %2" : "=v"(r) : "v"(lo), "v"(hi)); return r; }
; __device__ __forceinline__ void transpose_item(const float* W, int K, int N, bf16_t* WT, int rstep, int roff, float* scr, int item, int lane) {
;     ...
;   for (int i = 0; i < 8; ++i) v[i] = __builtin_nontemporal_load((const f32x4*)(W + (size_t)(k0 + i * 8 + (lane >> 3)) * N + n0 + (lane & 7) * 4));
; #pragma unroll
;   for (int i = 0; i < 8; ++i) { float* d = scr + (i * 8 + (lane >> 3)) * 33 + (lane & 7) * 4; d[0] = v[i].x; d[1] = v[i].y; d[2] = v[i].z; d[3] = v[i].w; }
;   __builtin_amdgcn_wave_barrier(); asm volatile("s_waitcnt lgkmcnt(0)" ::: "memory");
;   const int c = lane & 7;
; #pragma unroll
;   for (int j = 0; j < 4; ++j) { const int nl = (lane >> 3) + 8 * j, n = n0 + nl; const float* s = scr + (8 * c) * 33 + nl;
;     u32x4 o; o.x = pk2(s[0 * 33], s[1 * 33]); o.y = pk2(s[2 * 33], s[3 * 33]); o.z = pk2(s[4 * 33], s[5 * 33]); o.w = pk2(s[6 * 33], s[7 * 33]);
;     const int row = n + (n >> 7) * rstep + roff;
;     __builtin_nontemporal_store(o, (u32x4*)(WT + (size_t)row * K + k0 + 8 * c)); }
.LBB0_1434:
	s_andn2_b64 vcc, exec, s[4:5]
	s_cbranch_vccnz .LBB0_1436
	s_add_u32 s22, s42, s19
	s_addc_u32 s23, s43, 0
	s_add_u32 s5, s1, s19
	s_addc_u32 s20, s2, 0
	s_lshl_b32 s4, s7, 2
	s_and_b32 s21, s4, 0x7c0
	s_and_b32 s4, s18, 0x1e0
	s_lshl_b32 s24, s4, 2
	v_add_u32_e32 v4, s21, v1
	s_add_u32 s22, s22, s24
	s_addc_u32 s23, s23, 0
	v_lshlrev_b32_e32 v96, 2, v0
	v_ashrrev_i32_e32 v5, 31, v4
	v_lshl_add_u64 v[12:13], s[22:23], 0, v[96:97]
	v_lshlrev_b64 v[4:5], 11, v[4:5]
	v_lshl_add_u64 v[4:5], v[12:13], 0, v[4:5]
	s_movk_i32 s22, 0x4000
	v_add_co_u32_e32 v16, vcc, s22, v4
	s_mov_b32 s22, 0x8000
	s_nop 0
	v_addc_co_u32_e32 v17, vcc, 0, v5, vcc
	global_load_dwordx4 v[12:15], v[4:5], off nt
	v_add_co_u32_e32 v20, vcc, s22, v4
	global_load_dwordx4 v[16:19], v[16:17], off nt
	s_nop 0
	v_addc_co_u32_e32 v21, vcc, 0, v5, vcc
	s_mov_b32 s22, 0xc000
	global_load_dwordx4 v[20:23], v[20:21], off nt
	v_add_co_u32_e32 v24, vcc, s22, v4
	s_mov_b32 s22, 0x10000
	s_nop 0
	v_addc_co_u32_e32 v25, vcc, 0, v5, vcc
	global_load_dwordx4 v[24:27], v[24:25], off nt
	v_add_co_u32_e32 v28, vcc, s22, v4
	s_mov_b32 s22, 0x14000
	s_nop 0
	v_addc_co_u32_e32 v29, vcc, 0, v5, vcc
	global_load_dwordx4 v[28:31], v[28:29], off nt
	v_add_co_u32_e32 v32, vcc, s22, v4
	s_lshl_b32 s21, s21, 1
	s_nop 0
	v_addc_co_u32_e32 v33, vcc, 0, v5, vcc
	global_load_dwordx4 v[32:35], v[32:33], off nt
	v_add_co_u32_e32 v36, vcc, s93, v4
	v_add_u32_e32 v11, s4, v1
	s_nop 0
	v_addc_co_u32_e32 v37, vcc, 0, v5, vcc
	global_load_dwordx4 v[36:39], v[36:37], off nt
	v_add_co_u32_e32 v4, vcc, s96, v4
	s_add_u32 s22, s5, s21
	s_nop 0
	v_addc_co_u32_e32 v5, vcc, 0, v5, vcc
	global_load_dwordx4 v[40:43], v[4:5], off nt
	v_add_u32_e32 v4, v3, v6
	v_add_u32_e32 v5, 0x420, v4
	s_movk_i32 s5, 0x80
	s_addc_u32 s23, s20, 0
	v_lshlrev_b32_e32 v96, 1, v2
	s_waitcnt vmcnt(0)
	ds_write2_b32 v4, v12, v13 offset1:1
	ds_write2_b32 v4, v14, v15 offset0:2 offset1:3
	ds_write2_b32 v5, v16, v17 offset1:1
	v_add_u32_e32 v5, 0x428, v4
	ds_write2_b32 v5, v18, v19 offset1:1
	v_add_u32_e32 v5, 0x840, v4
	ds_write2_b32 v5, v20, v21 offset1:1
	v_add_u32_e32 v5, 0x848, v4
	ds_write2_b32 v5, v22, v23 offset1:1
	v_add_u32_e32 v5, 0xc60, v4
	ds_write2_b32 v5, v24, v25 offset1:1
	v_add_u32_e32 v5, 0xc68, v4
	ds_write2_b32 v5, v26, v27 offset1:1
	v_add_u32_e32 v5, 0x1080, v4
	ds_write2_b32 v5, v28, v29 offset1:1
	v_add_u32_e32 v5, 0x1088, v4
	ds_write2_b32 v5, v30, v31 offset1:1
	v_add_u32_e32 v5, 0x14a0, v4
	ds_write2_b32 v5, v32, v33 offset1:1
	v_add_u32_e32 v5, 0x14a8, v4
	ds_write2_b32 v5, v34, v35 offset1:1
	v_add_u32_e32 v5, 0x18c0, v4
	ds_write2_b32 v5, v36, v37 offset1:1
	v_add_u32_e32 v5, 0x18c8, v4
	ds_write2_b32 v5, v38, v39 offset1:1
	v_add_u32_e32 v5, 0x1ce0, v4
	v_add_u32_e32 v4, 0x1ce8, v4
	ds_write2_b32 v5, v40, v41 offset1:1
	ds_write2_b32 v4, v42, v43 offset1:1
	s_waitcnt lgkmcnt(0)
	ds_read2_b32 v[214:215], v10 offset1:33
	ds_read2_b32 v[222:223], v10 offset0:66 offset1:99
	ds_read2_b32 v[224:225], v10 offset0:132 offset1:165
	ds_read2_b32 v[226:227], v10 offset0:198 offset1:231
	ds_read2_b32 v[228:229], v10 offset0:8 offset1:41
	ds_read2_b32 v[230:231], v10 offset0:74 offset1:107
	ds_read2_b32 v[232:233], v10 offset0:140 offset1:173
	ds_read2_b32 v[234:235], v10 offset0:206 offset1:239
	s_waitcnt lgkmcnt(0)
	ds_read2_b32 v[236:237], v10 offset0:16 offset1:49
	ds_read2_b32 v[238:239], v10 offset0:82 offset1:115
	ds_read2_b32 v[240:241], v10 offset0:148 offset1:181
	ds_read2_b32 v[242:243], v10 offset0:214 offset1:247
	ds_read2_b32 v[244:245], v10 offset0:24 offset1:57
	ds_read2_b32 v[246:247], v10 offset0:90 offset1:123
	ds_read2_b32 v[248:249], v10 offset0:156 offset1:189
	ds_read2_b32 v[250:251], v10 offset0:222 offset1:255
	v_cvt_pk_bf16_f32 v12, v214, v215
	v_cvt_pk_bf16_f32 v13, v222, v223
	v_cvt_pk_bf16_f32 v14, v224, v225
	v_cvt_pk_bf16_f32 v15, v226, v227
	v_and_b32_e32 v16, 0xffffff80, v11
	v_add3_u32 v16, v11, v16, s5
	v_ashrrev_i32_e32 v17, 31, v16
	v_lshl_add_u64 v[4:5], s[22:23], 0, v[96:97]
	v_lshlrev_b64 v[16:17], 12, v[16:17]
	v_lshl_add_u64 v[16:17], v[4:5], 0, v[16:17]
	global_store_dwordx4 v[16:17], v[12:15], off nt
	s_nop 1
	v_add_u32_e32 v11, s4, v7
	v_cvt_pk_bf16_f32 v12, v228, v229
	v_cvt_pk_bf16_f32 v13, v230, v231
	v_cvt_pk_bf16_f32 v14, v232, v233
	v_cvt_pk_bf16_f32 v15, v234, v235
	v_and_b32_e32 v16, 0xffffff80, v11
	v_add3_u32 v16, v11, v16, s5
	v_ashrrev_i32_e32 v17, 31, v16
	v_lshlrev_b64 v[16:17], 12, v[16:17]
	v_lshl_add_u64 v[16:17], v[4:5], 0, v[16:17]
	global_store_dwordx4 v[16:17], v[12:15], off nt
	s_nop 1
	s_waitcnt lgkmcnt(0)
	v_add_u32_e32 v11, s4, v8
	v_cvt_pk_bf16_f32 v12, v236, v237
	v_cvt_pk_bf16_f32 v13, v238, v239
	v_cvt_pk_bf16_f32 v14, v240, v241
	v_cvt_pk_bf16_f32 v15, v242, v243
	v_and_b32_e32 v16, 0xffffff80, v11
	v_add3_u32 v16, v11, v16, s5
	v_ashrrev_i32_e32 v17, 31, v16
	v_lshlrev_b64 v[16:17], 12, v[16:17]
	v_lshl_add_u64 v[16:17], v[4:5], 0, v[16:17]
	global_store_dwordx4 v[16:17], v[12:15], off nt
	s_nop 1
	v_add_u32_e32 v11, s4, v9
	v_cvt_pk_bf16_f32 v12, v244, v245
	v_cvt_pk_bf16_f32 v13, v246, v247
	v_cvt_pk_bf16_f32 v14, v248, v249
	v_cvt_pk_bf16_f32 v15, v250, v251
	v_and_b32_e32 v16, 0xffffff80, v11
	v_add3_u32 v16, v11, v16, s5
	v_ashrrev_i32_e32 v17, 31, v16
	v_lshlrev_b64 v[16:17], 12, v[16:17]
	v_lshl_add_u64 v[4:5], v[4:5], 0, v[16:17]
	global_store_dwordx4 v[4:5], v[12:15], off nt
	s_nop 1
	s_waitcnt lgkmcnt(0)

; __device__ __forceinline__ unsigned pk2(float lo, float hi) { unsigned r; asm volatile("v_cvt_pk_bf16_f32 %0, %1, %2" : "=v"(r) : "v"(lo), "v"(hi)); return r; }
; __device__ __forceinline__ void transpose_item(const float* W, int K, int N, bf16_t* WT, int rstep, int roff, float* scr, int item, int lane) {
;     ...
;   for (int i = 0; i < 8; ++i) v[i] = __builtin_nontemporal_load((const f32x4*)(W + (size_t)(k0 + i * 8 + (lane >> 3)) * N + n0 + (lane & 7) * 4));
; #pragma unroll
;   for (int i = 0; i < 8; ++i) { float* d = scr + (i * 8 + (lane >> 3)) * 33 + (lane & 7) * 4; d[0] = v[i].x; d[1] = v[i].y; d[2] = v[i].z; d[3] = v[i].w; }
;   __builtin_amdgcn_wave_barrier(); asm volatile("s_waitcnt lgkmcnt(0)" ::: "memory");
;   const int c = lane & 7;
; #pragma unroll
;   for (int j = 0; j < 4; ++j) { const int nl = (lane >> 3) + 8 * j, n = n0 + nl; const float* s = scr + (8 * c) * 33 + nl;
;     u32x4 o; o.x = pk2(s[0 * 33], s[1 * 33]); o.y = pk2(s[2 * 33], s[3 * 33]); o.z = pk2(s[4 * 33], s[5 * 33]); o.w = pk2(s[6 * 33], s[7 * 33]);
;     const int row = n + (n >> 7) * rstep + roff;
;     __builtin_nontemporal_store(o, (u32x4*)(WT + (size_t)row * K + k0 + 8 * c)); }
.LBB0_1437:
	s_andn2_b64 vcc, exec, s[4:5]
	s_cbranch_vccnz .LBB0_1439
	s_add_u32 s20, s40, s19
	s_addc_u32 s21, s41, 0
	s_add_u32 s5, s1, s19
	s_addc_u32 s19, s2, 0
	s_lshl_b32 s4, s7, 2
	s_and_b32 s7, s4, 0x7c0
	s_and_b32 s4, s18, 0x1e0
	s_lshl_b32 s18, s4, 2
	v_add_u32_e32 v4, s7, v1
	s_add_u32 s20, s20, s18
	s_addc_u32 s21, s21, 0
	v_lshlrev_b32_e32 v96, 2, v0
	v_ashrrev_i32_e32 v5, 31, v4
	v_lshl_add_u64 v[12:13], s[20:21], 0, v[96:97]
	v_lshlrev_b64 v[4:5], 11, v[4:5]
	v_lshl_add_u64 v[4:5], v[12:13], 0, v[4:5]
	s_movk_i32 s18, 0x4000
	v_add_co_u32_e32 v16, vcc, s18, v4
	s_mov_b32 s18, 0x8000
	s_nop 0
	v_addc_co_u32_e32 v17, vcc, 0, v5, vcc
	global_load_dwordx4 v[12:15], v[4:5], off nt
	v_add_co_u32_e32 v20, vcc, s18, v4
	global_load_dwordx4 v[16:19], v[16:17], off nt
	s_nop 0
	v_addc_co_u32_e32 v21, vcc, 0, v5, vcc
	s_mov_b32 s18, 0xc000
	global_load_dwordx4 v[20:23], v[20:21], off nt
	v_add_co_u32_e32 v24, vcc, s18, v4
	s_mov_b32 s18, 0x10000
	s_nop 0
	v_addc_co_u32_e32 v25, vcc, 0, v5, vcc
	global_load_dwordx4 v[24:27], v[24:25], off nt
	v_add_co_u32_e32 v28, vcc, s18, v4
	s_mov_b32 s18, 0x14000
	s_nop 0
	v_addc_co_u32_e32 v29, vcc, 0, v5, vcc
	global_load_dwordx4 v[28:31], v[28:29], off nt
	v_add_co_u32_e32 v32, vcc, s18, v4
	v_add_u32_e32 v11, s4, v1
	s_nop 0
	v_addc_co_u32_e32 v33, vcc, 0, v5, vcc
	global_load_dwordx4 v[32:35], v[32:33], off nt
	v_add_co_u32_e32 v36, vcc, s93, v4
	s_lshl_b32 s7, s7, 1
	s_nop 0
	v_addc_co_u32_e32 v37, vcc, 0, v5, vcc
	global_load_dwordx4 v[36:39], v[36:37], off nt
	v_add_co_u32_e32 v4, vcc, s96, v4
	s_add_u32 s18, s5, s7
	s_nop 0
	v_addc_co_u32_e32 v5, vcc, 0, v5, vcc
	global_load_dwordx4 v[40:43], v[4:5], off nt
	v_add_u32_e32 v4, v3, v6
	v_add_u32_e32 v5, 0x420, v4
	s_addc_u32 s19, s19, 0
	v_lshlrev_b32_e32 v96, 1, v2
	s_waitcnt vmcnt(0)
	ds_write2_b32 v4, v12, v13 offset1:1
	ds_write2_b32 v4, v14, v15 offset0:2 offset1:3
	ds_write2_b32 v5, v16, v17 offset1:1
	v_add_u32_e32 v5, 0x428, v4
	ds_write2_b32 v5, v18, v19 offset1:1
	v_add_u32_e32 v5, 0x840, v4
	ds_write2_b32 v5, v20, v21 offset1:1
	v_add_u32_e32 v5, 0x848, v4
	ds_write2_b32 v5, v22, v23 offset1:1
	v_add_u32_e32 v5, 0xc60, v4
	ds_write2_b32 v5, v24, v25 offset1:1
	v_add_u32_e32 v5, 0xc68, v4
	ds_write2_b32 v5, v26, v27 offset1:1
	v_add_u32_e32 v5, 0x1080, v4
	ds_write2_b32 v5, v28, v29 offset1:1
	v_add_u32_e32 v5, 0x1088, v4
	ds_write2_b32 v5, v30, v31 offset1:1
	v_add_u32_e32 v5, 0x14a0, v4
	ds_write2_b32 v5, v32, v33 offset1:1
	v_add_u32_e32 v5, 0x14a8, v4
	ds_write2_b32 v5, v34, v35 offset1:1
	v_add_u32_e32 v5, 0x18c0, v4
	ds_write2_b32 v5, v36, v37 offset1:1
	v_add_u32_e32 v5, 0x18c8, v4
	ds_write2_b32 v5, v38, v39 offset1:1
	v_add_u32_e32 v5, 0x1ce0, v4
	v_add_u32_e32 v4, 0x1ce8, v4
	ds_write2_b32 v5, v40, v41 offset1:1
	ds_write2_b32 v4, v42, v43 offset1:1
	s_waitcnt lgkmcnt(0)
	ds_read2_b32 v[214:215], v10 offset1:33
	ds_read2_b32 v[222:223], v10 offset0:66 offset1:99
	ds_read2_b32 v[224:225], v10 offset0:132 offset1:165
	ds_read2_b32 v[226:227], v10 offset0:198 offset1:231
	ds_read2_b32 v[228:229], v10 offset0:8 offset1:41
	ds_read2_b32 v[230:231], v10 offset0:74 offset1:107
	ds_read2_b32 v[232:233], v10 offset0:140 offset1:173
	ds_read2_b32 v[234:235], v10 offset0:206 offset1:239
	s_waitcnt lgkmcnt(0)
	ds_read2_b32 v[236:237], v10 offset0:16 offset1:49
	ds_read2_b32 v[238:239], v10 offset0:82 offset1:115
	ds_read2_b32 v[240:241], v10 offset0:148 offset1:181
	ds_read2_b32 v[242:243], v10 offset0:214 offset1:247
	ds_read2_b32 v[244:245], v10 offset0:24 offset1:57
	ds_read2_b32 v[246:247], v10 offset0:90 offset1:123
	ds_read2_b32 v[248:249], v10 offset0:156 offset1:189
	ds_read2_b32 v[250:251], v10 offset0:222 offset1:255
	v_cvt_pk_bf16_f32 v12, v214, v215
	v_cvt_pk_bf16_f32 v13, v222, v223
	v_cvt_pk_bf16_f32 v14, v224, v225
	v_cvt_pk_bf16_f32 v15, v226, v227
	v_and_b32_e32 v16, 0xffffff80, v11
	v_add_u32_e32 v16, v16, v11
	v_ashrrev_i32_e32 v17, 31, v16
	v_lshl_add_u64 v[4:5], s[18:19], 0, v[96:97]
	v_lshlrev_b64 v[16:17], 12, v[16:17]
	v_lshl_add_u64 v[16:17], v[4:5], 0, v[16:17]
	global_store_dwordx4 v[16:17], v[12:15], off nt
	s_nop 1
	v_add_u32_e32 v11, s4, v7
	v_cvt_pk_bf16_f32 v12, v228, v229
	v_cvt_pk_bf16_f32 v13, v230, v231
	v_cvt_pk_bf16_f32 v14, v232, v233
	v_cvt_pk_bf16_f32 v15, v234, v235
	v_and_b32_e32 v16, 0xffffff80, v11
	v_add_u32_e32 v16, v16, v11
	v_ashrrev_i32_e32 v17, 31, v16
	v_lshlrev_b64 v[16:17], 12, v[16:17]
	v_lshl_add_u64 v[16:17], v[4:5], 0, v[16:17]
	global_store_dwordx4 v[16:17], v[12:15], off nt
	s_nop 1
	s_waitcnt lgkmcnt(0)
	v_add_u32_e32 v11, s4, v8
	v_cvt_pk_bf16_f32 v12, v236, v237
	v_cvt_pk_bf16_f32 v13, v238, v239
	v_cvt_pk_bf16_f32 v14, v240, v241
	v_cvt_pk_bf16_f32 v15, v242, v243
	v_and_b32_e32 v16, 0xffffff80, v11
	v_add_u32_e32 v16, v16, v11
	v_ashrrev_i32_e32 v17, 31, v16
	v_lshlrev_b64 v[16:17], 12, v[16:17]
	v_lshl_add_u64 v[16:17], v[4:5], 0, v[16:17]
	global_store_dwordx4 v[16:17], v[12:15], off nt
	s_nop 1
	v_add_u32_e32 v11, s4, v9
	v_cvt_pk_bf16_f32 v12, v244, v245
	v_cvt_pk_bf16_f32 v13, v246, v247
	v_cvt_pk_bf16_f32 v14, v248, v249
	v_cvt_pk_bf16_f32 v15, v250, v251
	v_and_b32_e32 v16, 0xffffff80, v11
	v_add_u32_e32 v16, v16, v11
	v_ashrrev_i32_e32 v17, 31, v16
	v_lshlrev_b64 v[16:17], 12, v[16:17]
	v_lshl_add_u64 v[4:5], v[4:5], 0, v[16:17]
	global_store_dwordx4 v[4:5], v[12:15], off nt
	s_nop 1
	s_waitcnt lgkmcnt(0)

; __device__ __forceinline__ unsigned pk2(float lo, float hi) { unsigned r; asm volatile("v_cvt_pk_bf16_f32 %0, %1, %2" : "=v"(r) : "v"(lo), "v"(hi)); return r; }
; __device__ __forceinline__ void transpose_item(const float* W, int K, int N, bf16_t* WT, int rstep, int roff, float* scr, int item, int lane) {
;     ...
;   for (int i = 0; i < 8; ++i) v[i] = __builtin_nontemporal_load((const f32x4*)(W + (size_t)(k0 + i * 8 + (lane >> 3)) * N + n0 + (lane & 7) * 4));
; #pragma unroll
;   for (int i = 0; i < 8; ++i) { float* d = scr + (i * 8 + (lane >> 3)) * 33 + (lane & 7) * 4; d[0] = v[i].x; d[1] = v[i].y; d[2] = v[i].z; d[3] = v[i].w; }
;   __builtin_amdgcn_wave_barrier(); asm volatile("s_waitcnt lgkmcnt(0)" ::: "memory");
;   const int c = lane & 7;
; #pragma unroll
;   for (int j = 0; j < 4; ++j) { const int nl = (lane >> 3) + 8 * j, n = n0 + nl; const float* s = scr + (8 * c) * 33 + nl;
;     u32x4 o; o.x = pk2(s[0 * 33], s[1 * 33]); o.y = pk2(s[2 * 33], s[3 * 33]); o.z = pk2(s[4 * 33], s[5 * 33]); o.w = pk2(s[6 * 33], s[7 * 33]);
;     const int row = n + (n >> 7) * rstep + roff;
;     __builtin_nontemporal_store(o, (u32x4*)(WT + (size_t)row * K + k0 + 8 * c)); }
; __device__ __forceinline__ void convert_item(const P& p, int it, float* scr, int lane) {
;     ...
;     const int l = it / (IT_WIN + IT_WOUT), r = it % (IT_WIN + IT_WOUT);
;     if (r < IT_WIN) transpose_item(p.w_in + (size_t)l * DM * INW, DM, INW, WSP(bf16_t, WS_WIN) + (size_t)l * INW * DM, 0, 0, scr, r, lane);
;     else transpose_item(p.w_out + (size_t)l * DM * DM, DM, DM, WSP(bf16_t, WS_WOUT) + (size_t)l * DM * DM, 0, 0, scr, r - IT_WIN, lane);
.LBB0_1440:
	s_and_b64 vcc, exec, s[4:5]
	s_cbranch_vccz .LBB0_1424
	s_ashr_i32 s4, s6, 31
	s_lshr_b32 s4, s4, 19
	s_add_i32 s5, s6, s4
	s_ashr_i32 s4, s5, 13
	s_and_b32 s5, s5, 0xffffe000
	s_sub_i32 s18, s6, s5
	s_ashr_i32 s5, s4, 31
	v_add_u32_e32 v11, v3, v6
	s_cmpk_gt_i32 s18, 0x17ff
	s_mov_b64 s[6:7], -1
	v_lshlrev_b32_e32 v96, 2, v0
	v_add_u32_e32 v12, 0x420, v11
	v_add_u32_e32 v13, 0x428, v11
	v_add_u32_e32 v14, 0x840, v11
	v_add_u32_e32 v15, 0x848, v11
	v_add_u32_e32 v16, 0xc60, v11
	v_add_u32_e32 v17, 0xc68, v11
	v_add_u32_e32 v18, 0x1080, v11
	v_add_u32_e32 v19, 0x1088, v11
	v_add_u32_e32 v20, 0x14a0, v11
	v_add_u32_e32 v21, 0x14a8, v11
	v_add_u32_e32 v22, 0x18c0, v11
	v_add_u32_e32 v23, 0x18c8, v11
	v_add_u32_e32 v24, 0x1ce0, v11
	v_add_u32_e32 v25, 0x1ce8, v11
	v_lshlrev_b32_e32 v4, 1, v2
	s_cbranch_scc0 .LBB0_1443
	s_lshl_b64 s[6:7], s[4:5], 24
	s_add_u32 s19, s54, s6
	s_addc_u32 s20, s55, s7
	s_lshl_b64 s[6:7], s[4:5], 23
	s_add_u32 s5, s13, s6
	s_addc_u32 s21, s14, s7
	s_add_i32 s6, s18, 0xe800
	s_and_b32 s22, s6, 0xffc0
	s_lshl_b32 s6, s18, 5
	s_and_b32 s23, s6, 0x7e0
	s_lshl_b32 s6, s23, 2
	v_add_u32_e32 v26, s22, v1
	s_add_u32 s6, s19, s6
	s_addc_u32 s7, s20, 0
	v_ashrrev_i32_e32 v27, 31, v26
	v_lshl_add_u64 v[28:29], s[6:7], 0, v[96:97]
	v_lshlrev_b64 v[26:27], 13, v[26:27]
	v_lshl_add_u64 v[54:55], v[28:29], 0, v[26:27]
	s_mov_b32 s6, 0x10000
	v_add_co_u32_e32 v30, vcc, s6, v54
	s_mov_b32 s6, 0x20000
	s_nop 0
	v_addc_co_u32_e32 v31, vcc, 0, v55, vcc
	v_add_co_u32_e32 v34, vcc, s6, v54
	s_mov_b32 s6, 0x30000
	s_nop 0
	v_addc_co_u32_e32 v35, vcc, 0, v55, vcc
	v_add_co_u32_e32 v38, vcc, s6, v54
	s_mov_b32 s6, 0x40000
	s_nop 0
	v_addc_co_u32_e32 v39, vcc, 0, v55, vcc
	v_add_co_u32_e32 v42, vcc, s6, v54
	s_mov_b32 s6, 0x50000
	s_nop 0
	v_addc_co_u32_e32 v43, vcc, 0, v55, vcc
	v_add_co_u32_e32 v46, vcc, s6, v54
	global_load_dwordx4 v[26:29], v[54:55], off nt
	s_nop 0
	global_load_dwordx4 v[30:33], v[30:31], off nt
	v_addc_co_u32_e32 v47, vcc, 0, v55, vcc
	global_load_dwordx4 v[34:37], v[34:35], off nt
	s_nop 0
	global_load_dwordx4 v[38:41], v[38:39], off nt
	s_nop 0
	global_load_dwordx4 v[42:45], v[42:43], off nt
	s_nop 0
	global_load_dwordx4 v[46:49], v[46:47], off nt
	s_mov_b32 s6, 0x60000
	v_add_co_u32_e32 v50, vcc, s6, v54
	s_mov_b32 s6, 0x70000
	s_nop 0
	v_addc_co_u32_e32 v51, vcc, 0, v55, vcc
	global_load_dwordx4 v[50:53], v[50:51], off nt
	v_add_co_u32_e32 v54, vcc, s6, v54
	s_lshl_b32 s6, s22, 1
	s_nop 0
	v_addc_co_u32_e32 v55, vcc, 0, v55, vcc
	global_load_dwordx4 v[54:57], v[54:55], off nt
	s_add_u32 s6, s5, s6
	v_mov_b32_e32 v5, v97
	s_addc_u32 s7, s21, 0
	s_waitcnt vmcnt(0)
	ds_write2_b32 v11, v26, v27 offset1:1
	ds_write2_b32 v11, v28, v29 offset0:2 offset1:3
	ds_write2_b32 v12, v30, v31 offset1:1
	ds_write2_b32 v13, v32, v33 offset1:1
	ds_write2_b32 v14, v34, v35 offset1:1
	ds_write2_b32 v15, v36, v37 offset1:1
	ds_write2_b32 v16, v38, v39 offset1:1
	ds_write2_b32 v17, v40, v41 offset1:1
	ds_write2_b32 v18, v42, v43 offset1:1
	ds_write2_b32 v19, v44, v45 offset1:1
	ds_write2_b32 v20, v46, v47 offset1:1
	ds_write2_b32 v21, v48, v49 offset1:1
	ds_write2_b32 v22, v50, v51 offset1:1
	ds_write2_b32 v23, v52, v53 offset1:1
	ds_write2_b32 v24, v54, v55 offset1:1
	ds_write2_b32 v25, v56, v57 offset1:1
	s_waitcnt lgkmcnt(0)
	ds_read2_b32 v[214:215], v10 offset1:33
	ds_read2_b32 v[222:223], v10 offset0:66 offset1:99
	ds_read2_b32 v[224:225], v10 offset0:132 offset1:165
	ds_read2_b32 v[226:227], v10 offset0:198 offset1:231
	ds_read2_b32 v[228:229], v10 offset0:8 offset1:41
	ds_read2_b32 v[230:231], v10 offset0:74 offset1:107
	ds_read2_b32 v[232:233], v10 offset0:140 offset1:173
	ds_read2_b32 v[234:235], v10 offset0:206 offset1:239
	s_waitcnt lgkmcnt(0)
	ds_read2_b32 v[236:237], v10 offset0:16 offset1:49
	ds_read2_b32 v[238:239], v10 offset0:82 offset1:115
	ds_read2_b32 v[240:241], v10 offset0:148 offset1:181
	ds_read2_b32 v[242:243], v10 offset0:214 offset1:247
	ds_read2_b32 v[244:245], v10 offset0:24 offset1:57
	ds_read2_b32 v[246:247], v10 offset0:90 offset1:123
	ds_read2_b32 v[248:249], v10 offset0:156 offset1:189
	ds_read2_b32 v[250:251], v10 offset0:222 offset1:255
	v_cvt_pk_bf16_f32 v26, v214, v215
	v_add_u32_e32 v30, s23, v1
	v_cvt_pk_bf16_f32 v27, v222, v223
	v_ashrrev_i32_e32 v31, 31, v30
	v_cvt_pk_bf16_f32 v28, v224, v225
	v_lshlrev_b64 v[30:31], 12, v[30:31]
	v_lshl_add_u64 v[34:35], s[6:7], 0, v[4:5]
	v_cvt_pk_bf16_f32 v29, v226, v227
	v_lshl_add_u64 v[30:31], v[34:35], 0, v[30:31]
	global_store_dwordx4 v[30:31], v[26:29], off nt
	s_nop 1
	s_mov_b64 s[6:7], 0
	v_cvt_pk_bf16_f32 v26, v228, v229
	v_add_u32_e32 v32, s23, v7
	v_ashrrev_i32_e32 v33, 31, v32
	v_lshlrev_b64 v[32:33], 12, v[32:33]
	v_cvt_pk_bf16_f32 v27, v230, v231
	v_lshl_add_u64 v[32:33], v[34:35], 0, v[32:33]
	v_cvt_pk_bf16_f32 v28, v232, v233
	v_cvt_pk_bf16_f32 v29, v234, v235
	global_store_dwordx4 v[32:33], v[26:29], off nt
	s_nop 1
	v_add_u32_e32 v32, s23, v8
	v_ashrrev_i32_e32 v33, 31, v32
	s_waitcnt lgkmcnt(0)
	v_cvt_pk_bf16_f32 v26, v236, v237
	v_lshlrev_b64 v[32:33], 12, v[32:33]
	v_cvt_pk_bf16_f32 v27, v238, v239
	v_lshl_add_u64 v[32:33], v[34:35], 0, v[32:33]
	v_cvt_pk_bf16_f32 v28, v240, v241
	v_cvt_pk_bf16_f32 v29, v242, v243
	global_store_dwordx4 v[32:33], v[26:29], off nt
	s_nop 1
	v_add_u32_e32 v32, s23, v9
	v_ashrrev_i32_e32 v33, 31, v32
	v_cvt_pk_bf16_f32 v26, v244, v245
	v_lshlrev_b64 v[32:33], 12, v[32:33]
	v_cvt_pk_bf16_f32 v27, v246, v247
	v_lshl_add_u64 v[32:33], v[34:35], 0, v[32:33]
	v_cvt_pk_bf16_f32 v28, v248, v249
	v_cvt_pk_bf16_f32 v29, v250, v251
	global_store_dwordx4 v[32:33], v[26:29], off nt
	s_nop 1
	s_waitcnt lgkmcnt(0)
; __device__ __forceinline__ unsigned pk2(float lo, float hi) { unsigned r; asm volatile("v_cvt_pk_bf16_f32 %0, %1, %2" : "=v"(r) : "v"(lo), "v"(hi)); return r; }
; __device__ __forceinline__ void transpose_item(const float* W, int K, int N, bf16_t* WT, int rstep, int roff, float* scr, int item, int lane) {
;     ...
;   for (int i = 0; i < 8; ++i) v[i] = __builtin_nontemporal_load((const f32x4*)(W + (size_t)(k0 + i * 8 + (lane >> 3)) * N + n0 + (lane & 7) * 4));
; #pragma unroll
;   for (int i = 0; i < 8; ++i) { float* d = scr + (i * 8 + (lane >> 3)) * 33 + (lane & 7) * 4; d[0] = v[i].x; d[1] = v[i].y; d[2] = v[i].z; d[3] = v[i].w; }
;   __builtin_amdgcn_wave_barrier(); asm volatile("s_waitcnt lgkmcnt(0)" ::: "memory");
;   const int c = lane & 7;
; #pragma unroll
;   for (int j = 0; j < 4; ++j) { const int nl = (lane >> 3) + 8 * j, n = n0 + nl; const float* s = scr + (8 * c) * 33 + nl;
;     u32x4 o; o.x = pk2(s[0 * 33], s[1 * 33]); o.y = pk2(s[2 * 33], s[3 * 33]); o.z = pk2(s[4 * 33], s[5 * 33]); o.w = pk2(s[6 * 33], s[7 * 33]);
;     const int row = n + (n >> 7) * rstep + roff;
;     __builtin_nontemporal_store(o, (u32x4*)(WT + (size_t)row * K + k0 + 8 * c)); }
; __device__ __forceinline__ void convert_item(const P& p, int it, float* scr, int lane) {
;     ...
;     if (r < IT_WIN) transpose_item(p.w_in + (size_t)l * DM * INW, DM, INW, WSP(bf16_t, WS_WIN) + (size_t)l * INW * DM, 0, 0, scr, r, lane);
.LBB0_1443:
	s_andn2_b64 vcc, exec, s[6:7]
	s_cbranch_vccnz .LBB0_1424
	s_mul_i32 s6, s4, 0x3000000
	s_mul_hi_i32 s5, s4, 0x3000000
	s_add_u32 s7, s52, s6
	s_addc_u32 s20, s53, s5
	s_mul_hi_i32 s5, s4, 0x1800000
	s_mul_i32 s4, s4, 0x1800000
	s_add_u32 s21, s15, s4
	s_mul_i32 s4, s18, 0x2aab
	s_addc_u32 s22, s16, s5
	s_lshr_b32 s5, s4, 31
	s_ashr_i32 s4, s4, 21
	s_add_i32 s4, s4, s5
	s_sext_i32_i16 s5, s4
	s_mulk_i32 s4, 0xc0
	s_sub_i32 s4, s18, s4
	s_sext_i32_i16 s4, s4
	s_lshl_b32 s4, s4, 5
	s_lshl_b32 s6, s5, 6
	s_ashr_i32 s5, s4, 31
	s_lshl_b64 s[18:19], s[4:5], 2
	s_add_u32 s18, s7, s18
	v_add_u32_e32 v5, s6, v1
	s_addc_u32 s19, s20, s19
	v_lshl_add_u64 v[54:55], s[18:19], 0, v[96:97]
	s_movk_i32 s5, 0x6000
	v_add_u32_e32 v28, 8, v5
	v_add_u32_e32 v34, 16, v5
	v_add_u32_e32 v36, 24, v5
	v_add_u32_e32 v42, 32, v5
	v_add_u32_e32 v44, 40, v5
	v_mad_i64_i32 v[26:27], s[18:19], v5, s5, v[54:55]
	v_mad_i64_i32 v[30:31], s[18:19], v28, s5, v[54:55]
	v_mad_i64_i32 v[34:35], s[18:19], v34, s5, v[54:55]
	v_mad_i64_i32 v[38:39], s[18:19], v36, s5, v[54:55]
	v_mad_i64_i32 v[42:43], s[18:19], v42, s5, v[54:55]
	v_mad_i64_i32 v[46:47], s[18:19], v44, s5, v[54:55]
	global_load_dwordx4 v[26:29], v[26:27], off nt
	s_nop 0
	global_load_dwordx4 v[30:33], v[30:31], off nt
	s_nop 0
	global_load_dwordx4 v[34:37], v[34:35], off nt
	s_nop 0
	global_load_dwordx4 v[38:41], v[38:39], off nt
	s_nop 0
	global_load_dwordx4 v[42:45], v[42:43], off nt
	s_nop 0
	global_load_dwordx4 v[46:49], v[46:47], off nt
	v_add_u32_e32 v50, 48, v5
	v_mad_i64_i32 v[50:51], s[18:19], v50, s5, v[54:55]
	global_load_dwordx4 v[50:53], v[50:51], off nt
	v_add_u32_e32 v5, 56, v5
	v_mad_i64_i32 v[54:55], s[18:19], v5, s5, v[54:55]
	global_load_dwordx4 v[54:57], v[54:55], off nt
	s_ashr_i32 s7, s6, 31
	s_lshl_b64 s[6:7], s[6:7], 1
	s_add_u32 s6, s21, s6
	v_mov_b32_e32 v5, v97
	s_addc_u32 s7, s22, s7
	v_lshl_add_u64 v[4:5], s[6:7], 0, v[4:5]
	s_movk_i32 s82, 0x6000
	s_waitcnt vmcnt(0)
	ds_write2_b32 v11, v26, v27 offset1:1
	ds_write2_b32 v11, v28, v29 offset0:2 offset1:3
	ds_write2_b32 v12, v30, v31 offset1:1
	ds_write2_b32 v13, v32, v33 offset1:1
	ds_write2_b32 v14, v34, v35 offset1:1
	ds_write2_b32 v15, v36, v37 offset1:1
	ds_write2_b32 v16, v38, v39 offset1:1
	ds_write2_b32 v17, v40, v41 offset1:1
	ds_write2_b32 v18, v42, v43 offset1:1
	ds_write2_b32 v19, v44, v45 offset1:1
	ds_write2_b32 v20, v46, v47 offset1:1
	ds_write2_b32 v21, v48, v49 offset1:1
	ds_write2_b32 v22, v50, v51 offset1:1
	ds_write2_b32 v23, v52, v53 offset1:1
	ds_write2_b32 v24, v54, v55 offset1:1
	ds_write2_b32 v25, v56, v57 offset1:1
	s_waitcnt lgkmcnt(0)
	ds_read2_b32 v[214:215], v10 offset1:33
	ds_read2_b32 v[222:223], v10 offset0:66 offset1:99
	ds_read2_b32 v[224:225], v10 offset0:132 offset1:165
	ds_read2_b32 v[226:227], v10 offset0:198 offset1:231
	ds_read2_b32 v[228:229], v10 offset0:8 offset1:41
	ds_read2_b32 v[230:231], v10 offset0:74 offset1:107
	ds_read2_b32 v[232:233], v10 offset0:140 offset1:173
	ds_read2_b32 v[234:235], v10 offset0:206 offset1:239
	s_waitcnt lgkmcnt(0)
	ds_read2_b32 v[236:237], v10 offset0:16 offset1:49
	ds_read2_b32 v[238:239], v10 offset0:82 offset1:115
	ds_read2_b32 v[240:241], v10 offset0:148 offset1:181
	ds_read2_b32 v[242:243], v10 offset0:214 offset1:247
	ds_read2_b32 v[244:245], v10 offset0:24 offset1:57
	ds_read2_b32 v[246:247], v10 offset0:90 offset1:123
	ds_read2_b32 v[248:249], v10 offset0:156 offset1:189
	ds_read2_b32 v[250:251], v10 offset0:222 offset1:255
	v_cvt_pk_bf16_f32 v12, v214, v215
	v_add_u32_e32 v16, s4, v1
	v_cvt_pk_bf16_f32 v13, v222, v223
	v_ashrrev_i32_e32 v17, 31, v16
	v_cvt_pk_bf16_f32 v14, v224, v225
	v_lshlrev_b64 v[16:17], 12, v[16:17]
	v_cvt_pk_bf16_f32 v15, v226, v227
	v_lshl_add_u64 v[16:17], v[4:5], 0, v[16:17]
	global_store_dwordx4 v[16:17], v[12:15], off nt
	s_nop 1
	s_nop 0
	v_cvt_pk_bf16_f32 v12, v228, v229
	v_add_u32_e32 v18, s4, v7
	v_ashrrev_i32_e32 v19, 31, v18
	v_lshlrev_b64 v[18:19], 12, v[18:19]
	v_cvt_pk_bf16_f32 v13, v230, v231
	v_lshl_add_u64 v[18:19], v[4:5], 0, v[18:19]
	v_cvt_pk_bf16_f32 v14, v232, v233
	v_cvt_pk_bf16_f32 v15, v234, v235
	global_store_dwordx4 v[18:19], v[12:15], off nt
	s_nop 1
	v_add_u32_e32 v18, s4, v8
	v_ashrrev_i32_e32 v19, 31, v18
	s_waitcnt lgkmcnt(0)
	v_cvt_pk_bf16_f32 v12, v236, v237
	v_lshlrev_b64 v[18:19], 12, v[18:19]
	v_cvt_pk_bf16_f32 v13, v238, v239
	v_lshl_add_u64 v[18:19], v[4:5], 0, v[18:19]
	v_cvt_pk_bf16_f32 v14, v240, v241
	v_cvt_pk_bf16_f32 v15, v242, v243
	global_store_dwordx4 v[18:19], v[12:15], off nt
	s_nop 1
	v_add_u32_e32 v18, s4, v9
	v_ashrrev_i32_e32 v19, 31, v18
	v_cvt_pk_bf16_f32 v12, v244, v245
	v_lshlrev_b64 v[18:19], 12, v[18:19]
	v_cvt_pk_bf16_f32 v13, v246, v247
	v_lshl_add_u64 v[4:5], v[4:5], 0, v[18:19]
	v_cvt_pk_bf16_f32 v14, v248, v249
	v_cvt_pk_bf16_f32 v15, v250, v251
	global_store_dwordx4 v[4:5], v[12:15], off nt
	s_nop 1
	s_waitcnt lgkmcnt(0)
	s_branch .LBB0_1424
